# deleted the remaining 32 straight-line-redundant s_waitcnt lgkmcnt(0) (no LDS/SMEM op since the previous lgkmcnt(0)) on top of v62
# speedup vs baseline: 1.0032x; 1.0032x over previous
.LBB0_14:
	v_add_u32_e32 v28, s33, v71
	v_add_u32_e32 v4, 0x41, v28
	v_ashrrev_i32_e32 v29, 31, v28
	v_ashrrev_i32_e32 v5, 31, v4
	v_lshlrev_b64 v[0:1], 12, v[28:29]
	v_lshlrev_b64 v[4:5], 12, v[4:5]
	v_lshl_add_u64 v[0:1], v[72:73], 0, v[0:1]
	v_lshl_add_u64 v[4:5], v[72:73], 0, v[4:5]
	global_load_dwordx4 v[32:35], v[0:1], off sc0 sc1 nt
	global_load_dwordx4 v[8:11], v[4:5], off sc0 sc1 nt
	v_or_b32_e32 v0, 1, v28
	v_add_u32_e32 v4, 0x42, v28
	v_ashrrev_i32_e32 v1, 31, v0
	v_ashrrev_i32_e32 v5, 31, v4
	v_lshlrev_b64 v[0:1], 12, v[0:1]
	v_lshlrev_b64 v[4:5], 12, v[4:5]
	v_lshl_add_u64 v[0:1], v[72:73], 0, v[0:1]
	v_lshl_add_u64 v[4:5], v[72:73], 0, v[4:5]
	global_load_dwordx4 v[36:39], v[0:1], off sc0 sc1 nt
	global_load_dwordx4 v[16:19], v[4:5], off sc0 sc1 nt
	v_or_b32_e32 v0, 2, v28
	v_add_u32_e32 v4, 0x43, v28
	v_ashrrev_i32_e32 v1, 31, v0
	v_ashrrev_i32_e32 v5, 31, v4
	v_lshlrev_b64 v[0:1], 12, v[0:1]
	v_lshlrev_b64 v[4:5], 12, v[4:5]
	v_lshl_add_u64 v[0:1], v[72:73], 0, v[0:1]
	v_lshl_add_u64 v[4:5], v[72:73], 0, v[4:5]
	global_load_dwordx4 v[44:47], v[0:1], off sc0 sc1 nt
	global_load_dwordx4 v[24:27], v[4:5], off sc0 sc1 nt
	v_or_b32_e32 v0, 3, v28
	v_add_u32_e32 v4, 0x44, v28
	v_ashrrev_i32_e32 v1, 31, v0
	v_ashrrev_i32_e32 v5, 31, v4
	v_lshlrev_b64 v[0:1], 12, v[0:1]
	v_lshlrev_b64 v[4:5], 12, v[4:5]
	v_lshl_add_u64 v[0:1], v[72:73], 0, v[0:1]
	v_lshl_add_u64 v[4:5], v[72:73], 0, v[4:5]
	global_load_dwordx4 v[52:55], v[0:1], off sc0 sc1 nt
	v_add_u32_e32 v12, 0x45, v28
	global_load_dwordx4 v[4:7], v[4:5], off sc0 sc1 nt
	v_or_b32_e32 v0, 4, v28
	v_ashrrev_i32_e32 v1, 31, v0
	v_ashrrev_i32_e32 v13, 31, v12
	v_lshlrev_b64 v[0:1], 12, v[0:1]
	v_lshlrev_b64 v[12:13], 12, v[12:13]
	v_lshl_add_u64 v[0:1], v[72:73], 0, v[0:1]
	v_lshl_add_u64 v[12:13], v[72:73], 0, v[12:13]
	global_load_dwordx4 v[40:43], v[0:1], off sc0 sc1 nt
	v_add_u32_e32 v20, 0x46, v28
	global_load_dwordx4 v[12:15], v[12:13], off sc0 sc1 nt
	v_or_b32_e32 v0, 5, v28
	v_ashrrev_i32_e32 v1, 31, v0
	v_ashrrev_i32_e32 v21, 31, v20
	v_lshlrev_b64 v[0:1], 12, v[0:1]
	v_lshlrev_b64 v[20:21], 12, v[20:21]
	v_lshl_add_u64 v[0:1], v[72:73], 0, v[0:1]
	v_lshl_add_u64 v[20:21], v[72:73], 0, v[20:21]
	global_load_dwordx4 v[48:51], v[0:1], off sc0 sc1 nt
	v_mov_b32_e32 v128, 0
	global_load_dwordx4 v[20:23], v[20:21], off sc0 sc1 nt
	v_or_b32_e32 v0, 6, v28
	v_ashrrev_i32_e32 v1, 31, v0
	v_lshlrev_b64 v[0:1], 12, v[0:1]
	v_lshl_add_u64 v[0:1], v[72:73], 0, v[0:1]
	global_load_dwordx4 v[56:59], v[0:1], off sc0 sc1 nt
	v_or_b32_e32 v0, 7, v28
	v_ashrrev_i32_e32 v1, 31, v0
	v_lshlrev_b64 v[0:1], 12, v[0:1]
	v_lshl_add_u64 v[0:1], v[72:73], 0, v[0:1]
	global_load_dwordx4 v[60:63], v[0:1], off sc0 sc1 nt
	v_add_u32_e32 v0, 64, v28
	v_ashrrev_i32_e32 v1, 31, v0
	v_lshlrev_b64 v[0:1], 12, v[0:1]
	v_lshl_add_u64 v[0:1], v[72:73], 0, v[0:1]
	global_load_dwordx4 v[0:3], v[0:1], off sc0 sc1 nt
	v_add_u32_e32 v28, 0x47, v28
	v_ashrrev_i32_e32 v29, 31, v28
	v_lshlrev_b64 v[28:29], 12, v[28:29]
	v_lshl_add_u64 v[28:29], v[72:73], 0, v[28:29]
	global_load_dwordx4 v[28:31], v[28:29], off sc0 sc1 nt
	v_mov_b32_e32 v129, 0
	s_and_b64 vcc, exec, s[16:17]
	s_mov_b64 s[16:17], 0
	s_waitcnt vmcnt(15)
	v_mul_f32_e32 v32, 0x42000000, v32
	v_mul_f32_e32 v33, 0x42000000, v33
	v_mul_f32_e32 v34, 0x42000000, v34
	v_mul_f32_e32 v35, 0x42000000, v35
	s_waitcnt vmcnt(14)
	v_mul_f32_e32 v8, 0x42000000, v8
	s_waitcnt vmcnt(13)
	v_mul_f32_e32 v36, 0x42000000, v36
	v_cvt_pk_fp8_f32 v128, v32, v36
	s_waitcnt vmcnt(12)
	v_mul_f32_e32 v16, 0x42000000, v16
	s_waitcnt vmcnt(11)
	v_mul_f32_e32 v44, 0x42000000, v44
	s_waitcnt vmcnt(10)
	v_mul_f32_e32 v24, 0x42000000, v24
	s_waitcnt vmcnt(9)
	v_mul_f32_e32 v52, 0x42000000, v52
	v_cvt_pk_fp8_f32 v128, v44, v52 op_sel:[0,0,1]
	s_waitcnt vmcnt(7)
	v_mul_f32_e32 v32, 0x42000000, v40
	s_waitcnt vmcnt(5)
	v_mul_f32_e32 v36, 0x42000000, v48
	v_cvt_pk_fp8_f32 v129, v32, v36
	v_mul_f32_e32 v36, 0x42000000, v37
	v_mov_b32_e32 v32, 0
	v_cvt_pk_fp8_f32 v32, v33, v36
	v_mul_f32_e32 v37, 0x42000000, v45
	v_mul_f32_e32 v36, 0x42000000, v41
	s_waitcnt vmcnt(3)
	v_mul_f32_e32 v40, 0x42000000, v56
	v_mov_b32_e32 v33, 0
	v_mul_f32_e32 v41, 0x42000000, v57
	s_waitcnt vmcnt(2)
	v_mul_f32_e32 v44, 0x42000000, v60
	v_cvt_pk_fp8_f32 v129, v40, v44 op_sel:[0,0,1]
	v_mul_f32_e32 v44, 0x42000000, v53
	v_cvt_pk_fp8_f32 v32, v37, v44 op_sel:[0,0,1]
	v_mul_f32_e32 v37, 0x42000000, v49
	v_cvt_pk_fp8_f32 v33, v36, v37
	v_mul_f32_e32 v37, 0x42000000, v38
	v_mov_b32_e32 v36, 0
	v_cvt_pk_fp8_f32 v36, v34, v37
	v_mul_f32_e32 v44, 0x42000000, v61
	v_cvt_pk_fp8_f32 v33, v41, v44 op_sel:[0,0,1]
	v_mul_f32_e32 v38, 0x42000000, v46
	v_mul_f32_e32 v41, 0x42000000, v54
	v_cvt_pk_fp8_f32 v36, v38, v41 op_sel:[0,0,1]
	v_mul_f32_e32 v34, 0x42000000, v42
	v_mul_f32_e32 v38, 0x42000000, v50
	v_mov_b32_e32 v37, 0
	v_cvt_pk_fp8_f32 v37, v34, v38
	v_mul_f32_e32 v38, 0x42000000, v39
	v_mov_b32_e32 v34, 0
	v_cvt_pk_fp8_f32 v34, v35, v38
	v_mul_f32_e32 v41, 0x42000000, v58
	v_mul_f32_e32 v42, 0x42000000, v62
	v_cvt_pk_fp8_f32 v37, v41, v42 op_sel:[0,0,1]
	v_mul_f32_e32 v39, 0x42000000, v47
	v_mul_f32_e32 v41, 0x42000000, v55
	v_cvt_pk_fp8_f32 v34, v39, v41 op_sel:[0,0,1]
	v_mul_f32_e32 v38, 0x42000000, v43
	v_mul_f32_e32 v39, 0x42000000, v51
	v_mov_b32_e32 v35, 0
	v_cvt_pk_fp8_f32 v35, v38, v39
	s_waitcnt vmcnt(1)
	v_mul_f32_e32 v0, 0x42000000, v0
	v_mov_b32_e32 v38, 0
	v_cvt_pk_fp8_f32 v38, v0, v8
	v_mul_f32_e32 v0, 0x42000000, v4
	v_mul_f32_e32 v4, 0x42000000, v12
	v_mov_b32_e32 v39, 0
	v_cvt_pk_fp8_f32 v39, v0, v4
	v_mul_f32_e32 v1, 0x42000000, v1
	v_mul_f32_e32 v4, 0x42000000, v9
	v_mov_b32_e32 v0, 0
	v_cvt_pk_fp8_f32 v0, v1, v4
	v_mul_f32_e32 v4, 0x42000000, v5
	v_mul_f32_e32 v5, 0x42000000, v13
	v_mov_b32_e32 v1, 0
	v_cvt_pk_fp8_f32 v1, v4, v5
	v_mul_f32_e32 v8, 0x42000000, v20
	s_waitcnt vmcnt(0)
	v_mul_f32_e32 v12, 0x42000000, v28
	v_cvt_pk_fp8_f32 v39, v8, v12 op_sel:[0,0,1]
	v_mul_f32_e32 v8, 0x42000000, v17
	v_mul_f32_e32 v9, 0x42000000, v25
	v_cvt_pk_fp8_f32 v0, v8, v9 op_sel:[0,0,1]
	v_mul_f32_e32 v8, 0x42000000, v21
	v_mul_f32_e32 v9, 0x42000000, v29
	v_cvt_pk_fp8_f32 v1, v8, v9 op_sel:[0,0,1]
	v_add_u32_e32 v40, s33, v125
	v_mul_f32_e32 v4, 0x42000000, v18
	v_mul_f32_e32 v5, 0x42000000, v26
	ds_write2_b64 v40, v[32:33], v[0:1] offset0:34 offset1:42
	v_mul_f32_e32 v1, 0x42000000, v2
	v_mul_f32_e32 v2, 0x42000000, v10
	v_mov_b32_e32 v0, 0
	v_cvt_pk_fp8_f32 v0, v1, v2
	v_mul_f32_e32 v2, 0x42000000, v6
	v_mov_b32_e32 v1, 0
	v_mul_f32_e32 v6, 0x42000000, v30
	v_cvt_pk_fp8_f32 v0, v4, v5 op_sel:[0,0,1]
	v_mul_f32_e32 v4, 0x42000000, v14
	v_cvt_pk_fp8_f32 v1, v2, v4
	v_mul_f32_e32 v5, 0x42000000, v22
	v_mul_f32_e32 v2, 0x42000000, v11
	v_mul_f32_e32 v4, 0x42000000, v27
	v_cvt_pk_fp8_f32 v1, v5, v6 op_sel:[0,0,1]
	v_mul_f32_e32 v41, 0x42000000, v59
	v_mul_f32_e32 v42, 0x42000000, v63
	v_mul_f32_e32 v5, 0x42000000, v31
	ds_write2_b64 v40, v[36:37], v[0:1] offset0:68 offset1:76
	v_mul_f32_e32 v1, 0x42000000, v3
	v_mov_b32_e32 v0, 0
	v_cvt_pk_fp8_f32 v0, v1, v2
	v_mul_f32_e32 v3, 0x42000000, v19
	v_mul_f32_e32 v2, 0x42000000, v7
	v_mov_b32_e32 v1, 0
	v_cvt_pk_fp8_f32 v0, v3, v4 op_sel:[0,0,1]
	v_mul_f32_e32 v3, 0x42000000, v15
	v_cvt_pk_fp8_f32 v1, v2, v3
	v_mul_f32_e32 v4, 0x42000000, v23
	v_cvt_pk_fp8_f32 v35, v41, v42 op_sel:[0,0,1]
	v_cvt_pk_fp8_f32 v38, v16, v24 op_sel:[0,0,1]
	v_cvt_pk_fp8_f32 v1, v4, v5 op_sel:[0,0,1]
	s_movk_i32 s33, 0x80
	ds_write2_b64 v40, v[128:129], v[38:39] offset1:8
	ds_write2_b64 v40, v[34:35], v[0:1] offset0:102 offset1:110
	s_cbranch_vccnz .LBB0_14
	s_add_u32 s14, s18, s14
	s_waitcnt lgkmcnt(0)
	s_barrier
	v_add_u32_e32 v0, v77, v66
	s_addc_u32 s15, s19, s15
	ds_read_b128 v[0:3], v0
	v_add_u32_e32 v4, s2, v76
	s_add_u32 s14, s14, s31
	v_ashrrev_i32_e32 v5, 31, v4
	s_addc_u32 s15, s15, 0
	v_lshlrev_b64 v[4:5], 10, v[4:5]
	v_lshl_add_u64 v[4:5], s[14:15], 0, v[4:5]
	v_lshl_add_u64 v[8:9], v[4:5], 0, v[66:67]
	v_add_u32_e32 v4, v79, v66
	ds_read_b128 v[4:7], v4
	s_waitcnt lgkmcnt(1)
	global_store_dwordx4 v[8:9], v[0:3], off sc1
	s_nop 1
	v_add_u32_e32 v0, s2, v78
	v_ashrrev_i32_e32 v1, 31, v0
	v_lshlrev_b64 v[0:1], 10, v[0:1]
	v_lshl_add_u64 v[0:1], s[14:15], 0, v[0:1]
	v_lshl_add_u64 v[0:1], v[0:1], 0, v[66:67]
	s_waitcnt lgkmcnt(0)
	global_store_dwordx4 v[0:1], v[4:7], off sc1
	v_add_u32_e32 v0, v81, v66
	ds_read_b128 v[0:3], v0
	v_add_u32_e32 v4, s2, v80
	v_ashrrev_i32_e32 v5, 31, v4
	v_lshlrev_b64 v[4:5], 10, v[4:5]
	v_lshl_add_u64 v[4:5], s[14:15], 0, v[4:5]
	v_lshl_add_u64 v[8:9], v[4:5], 0, v[66:67]
	v_add_u32_e32 v4, v83, v66
	ds_read_b128 v[4:7], v4
	s_waitcnt lgkmcnt(1)
	global_store_dwordx4 v[8:9], v[0:3], off sc1
	s_nop 1
	v_add_u32_e32 v0, s2, v82
	v_ashrrev_i32_e32 v1, 31, v0
	v_lshlrev_b64 v[0:1], 10, v[0:1]
	v_lshl_add_u64 v[0:1], s[14:15], 0, v[0:1]
	v_lshl_add_u64 v[0:1], v[0:1], 0, v[66:67]
	s_waitcnt lgkmcnt(0)
	global_store_dwordx4 v[0:1], v[4:7], off sc1
	v_add_u32_e32 v0, v85, v66
	ds_read_b128 v[0:3], v0
	v_add_u32_e32 v4, s2, v84
	v_ashrrev_i32_e32 v5, 31, v4
	v_lshlrev_b64 v[4:5], 10, v[4:5]
	v_lshl_add_u64 v[4:5], s[14:15], 0, v[4:5]
	v_lshl_add_u64 v[8:9], v[4:5], 0, v[66:67]
	v_add_u32_e32 v4, v87, v66
	ds_read_b128 v[4:7], v4
	s_waitcnt lgkmcnt(1)
	global_store_dwordx4 v[8:9], v[0:3], off sc1
	s_nop 1
	v_add_u32_e32 v0, s2, v86
	v_ashrrev_i32_e32 v1, 31, v0
	v_lshlrev_b64 v[0:1], 10, v[0:1]
	v_lshl_add_u64 v[0:1], s[14:15], 0, v[0:1]
	v_lshl_add_u64 v[0:1], v[0:1], 0, v[66:67]
	s_waitcnt lgkmcnt(0)
	global_store_dwordx4 v[0:1], v[4:7], off sc1
	v_add_u32_e32 v0, v89, v66
	ds_read_b128 v[0:3], v0
	v_add_u32_e32 v4, s2, v88
	v_ashrrev_i32_e32 v5, 31, v4
	v_lshlrev_b64 v[4:5], 10, v[4:5]
	v_lshl_add_u64 v[4:5], s[14:15], 0, v[4:5]
	v_lshl_add_u64 v[8:9], v[4:5], 0, v[66:67]
	v_add_u32_e32 v4, v124, v66
	ds_read_b128 v[4:7], v4
	s_waitcnt lgkmcnt(1)
	global_store_dwordx4 v[8:9], v[0:3], off sc1
	s_nop 1
	v_add_u32_e32 v0, s2, v90
	v_ashrrev_i32_e32 v1, 31, v0
	v_lshlrev_b64 v[0:1], 10, v[0:1]
	v_lshl_add_u64 v[0:1], s[14:15], 0, v[0:1]
	v_lshl_add_u64 v[0:1], v[0:1], 0, v[66:67]
	s_waitcnt lgkmcnt(0)
	global_store_dwordx4 v[0:1], v[4:7], off sc1
	s_barrier

.LBB0_20:
	v_add_u32_e32 v28, s31, v71
	v_add_u32_e32 v4, 0x41, v28
	v_ashrrev_i32_e32 v29, 31, v28
	v_ashrrev_i32_e32 v5, 31, v4
	v_lshlrev_b64 v[0:1], 13, v[28:29]
	v_lshlrev_b64 v[4:5], 13, v[4:5]
	v_lshl_add_u64 v[0:1], v[72:73], 0, v[0:1]
	v_lshl_add_u64 v[4:5], v[72:73], 0, v[4:5]
	global_load_dwordx4 v[32:35], v[0:1], off sc0 sc1 nt
	global_load_dwordx4 v[8:11], v[4:5], off sc0 sc1 nt
	v_or_b32_e32 v0, 1, v28
	v_add_u32_e32 v4, 0x42, v28
	v_ashrrev_i32_e32 v1, 31, v0
	v_ashrrev_i32_e32 v5, 31, v4
	v_lshlrev_b64 v[0:1], 13, v[0:1]
	v_lshlrev_b64 v[4:5], 13, v[4:5]
	v_lshl_add_u64 v[0:1], v[72:73], 0, v[0:1]
	v_lshl_add_u64 v[4:5], v[72:73], 0, v[4:5]
	global_load_dwordx4 v[36:39], v[0:1], off sc0 sc1 nt
	global_load_dwordx4 v[16:19], v[4:5], off sc0 sc1 nt
	v_or_b32_e32 v0, 2, v28
	v_add_u32_e32 v4, 0x43, v28
	v_ashrrev_i32_e32 v1, 31, v0
	v_ashrrev_i32_e32 v5, 31, v4
	v_lshlrev_b64 v[0:1], 13, v[0:1]
	v_lshlrev_b64 v[4:5], 13, v[4:5]
	v_lshl_add_u64 v[0:1], v[72:73], 0, v[0:1]
	v_lshl_add_u64 v[4:5], v[72:73], 0, v[4:5]
	global_load_dwordx4 v[44:47], v[0:1], off sc0 sc1 nt
	global_load_dwordx4 v[24:27], v[4:5], off sc0 sc1 nt
	v_or_b32_e32 v0, 3, v28
	v_add_u32_e32 v4, 0x44, v28
	v_ashrrev_i32_e32 v1, 31, v0
	v_ashrrev_i32_e32 v5, 31, v4
	v_lshlrev_b64 v[0:1], 13, v[0:1]
	v_lshlrev_b64 v[4:5], 13, v[4:5]
	v_lshl_add_u64 v[0:1], v[72:73], 0, v[0:1]
	v_lshl_add_u64 v[4:5], v[72:73], 0, v[4:5]
	global_load_dwordx4 v[52:55], v[0:1], off sc0 sc1 nt
	v_add_u32_e32 v12, 0x45, v28
	global_load_dwordx4 v[4:7], v[4:5], off sc0 sc1 nt
	v_or_b32_e32 v0, 4, v28
	v_ashrrev_i32_e32 v1, 31, v0
	v_ashrrev_i32_e32 v13, 31, v12
	v_lshlrev_b64 v[0:1], 13, v[0:1]
	v_lshlrev_b64 v[12:13], 13, v[12:13]
	v_lshl_add_u64 v[0:1], v[72:73], 0, v[0:1]
	v_lshl_add_u64 v[12:13], v[72:73], 0, v[12:13]
	global_load_dwordx4 v[40:43], v[0:1], off sc0 sc1 nt
	v_add_u32_e32 v20, 0x46, v28
	global_load_dwordx4 v[12:15], v[12:13], off sc0 sc1 nt
	v_or_b32_e32 v0, 5, v28
	v_ashrrev_i32_e32 v1, 31, v0
	v_ashrrev_i32_e32 v21, 31, v20
	v_lshlrev_b64 v[0:1], 13, v[0:1]
	v_lshlrev_b64 v[20:21], 13, v[20:21]
	v_lshl_add_u64 v[0:1], v[72:73], 0, v[0:1]
	v_lshl_add_u64 v[20:21], v[72:73], 0, v[20:21]
	global_load_dwordx4 v[48:51], v[0:1], off sc0 sc1 nt
	v_mov_b32_e32 v128, 0
	global_load_dwordx4 v[20:23], v[20:21], off sc0 sc1 nt
	v_or_b32_e32 v0, 6, v28
	v_ashrrev_i32_e32 v1, 31, v0
	v_lshlrev_b64 v[0:1], 13, v[0:1]
	v_lshl_add_u64 v[0:1], v[72:73], 0, v[0:1]
	global_load_dwordx4 v[56:59], v[0:1], off sc0 sc1 nt
	v_or_b32_e32 v0, 7, v28
	v_ashrrev_i32_e32 v1, 31, v0
	v_lshlrev_b64 v[0:1], 13, v[0:1]
	v_lshl_add_u64 v[0:1], v[72:73], 0, v[0:1]
	global_load_dwordx4 v[60:63], v[0:1], off sc0 sc1 nt
	v_add_u32_e32 v0, 64, v28
	v_ashrrev_i32_e32 v1, 31, v0
	v_lshlrev_b64 v[0:1], 13, v[0:1]
	v_lshl_add_u64 v[0:1], v[72:73], 0, v[0:1]
	global_load_dwordx4 v[0:3], v[0:1], off sc0 sc1 nt
	v_add_u32_e32 v28, 0x47, v28
	v_ashrrev_i32_e32 v29, 31, v28
	v_lshlrev_b64 v[28:29], 13, v[28:29]
	v_lshl_add_u64 v[28:29], v[72:73], 0, v[28:29]
	global_load_dwordx4 v[28:31], v[28:29], off sc0 sc1 nt
	v_mov_b32_e32 v129, 0
	s_and_b64 vcc, exec, s[14:15]
	s_mov_b64 s[14:15], 0
	s_waitcnt vmcnt(15)
	v_mul_f32_e32 v32, 0x42000000, v32
	v_mul_f32_e32 v33, 0x42000000, v33
	v_mul_f32_e32 v34, 0x42000000, v34
	v_mul_f32_e32 v35, 0x42000000, v35
	s_waitcnt vmcnt(14)
	v_mul_f32_e32 v8, 0x42000000, v8
	s_waitcnt vmcnt(13)
	v_mul_f32_e32 v36, 0x42000000, v36
	v_cvt_pk_fp8_f32 v128, v32, v36
	s_waitcnt vmcnt(12)
	v_mul_f32_e32 v16, 0x42000000, v16
	s_waitcnt vmcnt(11)
	v_mul_f32_e32 v44, 0x42000000, v44
	s_waitcnt vmcnt(10)
	v_mul_f32_e32 v24, 0x42000000, v24
	s_waitcnt vmcnt(9)
	v_mul_f32_e32 v52, 0x42000000, v52
	v_cvt_pk_fp8_f32 v128, v44, v52 op_sel:[0,0,1]
	s_waitcnt vmcnt(7)
	v_mul_f32_e32 v32, 0x42000000, v40
	s_waitcnt vmcnt(5)
	v_mul_f32_e32 v36, 0x42000000, v48
	v_cvt_pk_fp8_f32 v129, v32, v36
	v_mul_f32_e32 v36, 0x42000000, v37
	v_mov_b32_e32 v32, 0
	v_cvt_pk_fp8_f32 v32, v33, v36
	v_mul_f32_e32 v37, 0x42000000, v45
	v_mul_f32_e32 v36, 0x42000000, v41
	s_waitcnt vmcnt(3)
	v_mul_f32_e32 v40, 0x42000000, v56
	v_mov_b32_e32 v33, 0
	v_mul_f32_e32 v41, 0x42000000, v57
	s_waitcnt vmcnt(2)
	v_mul_f32_e32 v44, 0x42000000, v60
	v_cvt_pk_fp8_f32 v129, v40, v44 op_sel:[0,0,1]
	v_mul_f32_e32 v44, 0x42000000, v53
	v_cvt_pk_fp8_f32 v32, v37, v44 op_sel:[0,0,1]
	v_mul_f32_e32 v37, 0x42000000, v49
	v_cvt_pk_fp8_f32 v33, v36, v37
	v_mul_f32_e32 v37, 0x42000000, v38
	v_mov_b32_e32 v36, 0
	v_cvt_pk_fp8_f32 v36, v34, v37
	v_mul_f32_e32 v44, 0x42000000, v61
	v_cvt_pk_fp8_f32 v33, v41, v44 op_sel:[0,0,1]
	v_mul_f32_e32 v38, 0x42000000, v46
	v_mul_f32_e32 v41, 0x42000000, v54
	v_cvt_pk_fp8_f32 v36, v38, v41 op_sel:[0,0,1]
	v_mul_f32_e32 v34, 0x42000000, v42
	v_mul_f32_e32 v38, 0x42000000, v50
	v_mov_b32_e32 v37, 0
	v_cvt_pk_fp8_f32 v37, v34, v38
	v_mul_f32_e32 v38, 0x42000000, v39
	v_mov_b32_e32 v34, 0
	v_cvt_pk_fp8_f32 v34, v35, v38
	v_mul_f32_e32 v41, 0x42000000, v58
	v_mul_f32_e32 v42, 0x42000000, v62
	v_cvt_pk_fp8_f32 v37, v41, v42 op_sel:[0,0,1]
	v_mul_f32_e32 v39, 0x42000000, v47
	v_mul_f32_e32 v41, 0x42000000, v55
	v_cvt_pk_fp8_f32 v34, v39, v41 op_sel:[0,0,1]
	v_mul_f32_e32 v38, 0x42000000, v43
	v_mul_f32_e32 v39, 0x42000000, v51
	v_mov_b32_e32 v35, 0
	v_cvt_pk_fp8_f32 v35, v38, v39
	s_waitcnt vmcnt(1)
	v_mul_f32_e32 v0, 0x42000000, v0
	v_mov_b32_e32 v38, 0
	v_cvt_pk_fp8_f32 v38, v0, v8
	v_mul_f32_e32 v0, 0x42000000, v4
	v_mul_f32_e32 v4, 0x42000000, v12
	v_mov_b32_e32 v39, 0
	v_cvt_pk_fp8_f32 v39, v0, v4
	v_mul_f32_e32 v1, 0x42000000, v1
	v_mul_f32_e32 v4, 0x42000000, v9
	v_mov_b32_e32 v0, 0
	v_cvt_pk_fp8_f32 v0, v1, v4
	v_mul_f32_e32 v4, 0x42000000, v5
	v_mul_f32_e32 v5, 0x42000000, v13
	v_mov_b32_e32 v1, 0
	v_cvt_pk_fp8_f32 v1, v4, v5
	v_mul_f32_e32 v8, 0x42000000, v20
	s_waitcnt vmcnt(0)
	v_mul_f32_e32 v12, 0x42000000, v28
	v_cvt_pk_fp8_f32 v39, v8, v12 op_sel:[0,0,1]
	v_mul_f32_e32 v8, 0x42000000, v17
	v_mul_f32_e32 v9, 0x42000000, v25
	v_cvt_pk_fp8_f32 v0, v8, v9 op_sel:[0,0,1]
	v_mul_f32_e32 v8, 0x42000000, v21
	v_mul_f32_e32 v9, 0x42000000, v29
	v_cvt_pk_fp8_f32 v1, v8, v9 op_sel:[0,0,1]
	v_add_u32_e32 v40, s31, v125
	v_mul_f32_e32 v4, 0x42000000, v18
	v_mul_f32_e32 v5, 0x42000000, v26
	ds_write2_b64 v40, v[32:33], v[0:1] offset0:34 offset1:42
	v_mul_f32_e32 v1, 0x42000000, v2
	v_mul_f32_e32 v2, 0x42000000, v10
	v_mov_b32_e32 v0, 0
	v_cvt_pk_fp8_f32 v0, v1, v2
	v_mul_f32_e32 v2, 0x42000000, v6
	v_mov_b32_e32 v1, 0
	v_mul_f32_e32 v6, 0x42000000, v30
	v_cvt_pk_fp8_f32 v0, v4, v5 op_sel:[0,0,1]
	v_mul_f32_e32 v4, 0x42000000, v14
	v_cvt_pk_fp8_f32 v1, v2, v4
	v_mul_f32_e32 v5, 0x42000000, v22
	v_mul_f32_e32 v2, 0x42000000, v11
	v_mul_f32_e32 v4, 0x42000000, v27
	v_cvt_pk_fp8_f32 v1, v5, v6 op_sel:[0,0,1]
	v_mul_f32_e32 v41, 0x42000000, v59
	v_mul_f32_e32 v42, 0x42000000, v63
	v_mul_f32_e32 v5, 0x42000000, v31
	ds_write2_b64 v40, v[36:37], v[0:1] offset0:68 offset1:76
	v_mul_f32_e32 v1, 0x42000000, v3
	v_mov_b32_e32 v0, 0
	v_cvt_pk_fp8_f32 v0, v1, v2
	v_mul_f32_e32 v3, 0x42000000, v19
	v_mul_f32_e32 v2, 0x42000000, v7
	v_mov_b32_e32 v1, 0
	v_cvt_pk_fp8_f32 v0, v3, v4 op_sel:[0,0,1]
	v_mul_f32_e32 v3, 0x42000000, v15
	v_cvt_pk_fp8_f32 v1, v2, v3
	v_mul_f32_e32 v4, 0x42000000, v23
	v_cvt_pk_fp8_f32 v35, v41, v42 op_sel:[0,0,1]
	v_cvt_pk_fp8_f32 v38, v16, v24 op_sel:[0,0,1]
	v_cvt_pk_fp8_f32 v1, v4, v5 op_sel:[0,0,1]
	s_movk_i32 s31, 0x80
	ds_write2_b64 v40, v[128:129], v[38:39] offset1:8
	ds_write2_b64 v40, v[34:35], v[0:1] offset0:102 offset1:110
	s_cbranch_vccnz .LBB0_20
	s_lshl_b64 s[14:15], s[2:3], 21
	s_add_u32 s2, s21, s14
	s_waitcnt lgkmcnt(0)
	s_barrier
	v_add_u32_e32 v0, v77, v66
	s_addc_u32 s15, s22, s15
	ds_read_b128 v[0:3], v0
	v_add_u32_e32 v4, s16, v76
	s_add_u32 s14, s2, s17
	v_ashrrev_i32_e32 v5, 31, v4
	s_addc_u32 s15, s15, 0
	v_lshlrev_b64 v[4:5], 10, v[4:5]
	v_lshl_add_u64 v[4:5], s[14:15], 0, v[4:5]
	v_lshl_add_u64 v[8:9], v[4:5], 0, v[66:67]
	v_add_u32_e32 v4, v79, v66
	ds_read_b128 v[4:7], v4
	s_waitcnt lgkmcnt(1)
	global_store_dwordx4 v[8:9], v[0:3], off sc1
	s_nop 1
	v_add_u32_e32 v0, s16, v78
	v_ashrrev_i32_e32 v1, 31, v0
	v_lshlrev_b64 v[0:1], 10, v[0:1]
	v_lshl_add_u64 v[0:1], s[14:15], 0, v[0:1]
	v_lshl_add_u64 v[0:1], v[0:1], 0, v[66:67]
	s_waitcnt lgkmcnt(0)
	global_store_dwordx4 v[0:1], v[4:7], off sc1
	v_add_u32_e32 v0, v81, v66
	ds_read_b128 v[0:3], v0
	v_add_u32_e32 v4, s16, v80
	v_ashrrev_i32_e32 v5, 31, v4
	v_lshlrev_b64 v[4:5], 10, v[4:5]
	v_lshl_add_u64 v[4:5], s[14:15], 0, v[4:5]
	v_lshl_add_u64 v[8:9], v[4:5], 0, v[66:67]
	v_add_u32_e32 v4, v83, v66
	ds_read_b128 v[4:7], v4
	s_waitcnt lgkmcnt(1)
	global_store_dwordx4 v[8:9], v[0:3], off sc1
	s_nop 1
	v_add_u32_e32 v0, s16, v82
	v_ashrrev_i32_e32 v1, 31, v0
	v_lshlrev_b64 v[0:1], 10, v[0:1]
	v_lshl_add_u64 v[0:1], s[14:15], 0, v[0:1]
	v_lshl_add_u64 v[0:1], v[0:1], 0, v[66:67]
	s_waitcnt lgkmcnt(0)
	global_store_dwordx4 v[0:1], v[4:7], off sc1
	v_add_u32_e32 v0, v85, v66
	ds_read_b128 v[0:3], v0
	v_add_u32_e32 v4, s16, v84
	v_ashrrev_i32_e32 v5, 31, v4
	v_lshlrev_b64 v[4:5], 10, v[4:5]
	v_lshl_add_u64 v[4:5], s[14:15], 0, v[4:5]
	v_lshl_add_u64 v[8:9], v[4:5], 0, v[66:67]
	v_add_u32_e32 v4, v87, v66
	ds_read_b128 v[4:7], v4
	s_waitcnt lgkmcnt(1)
	global_store_dwordx4 v[8:9], v[0:3], off sc1
	s_nop 1
	v_add_u32_e32 v0, s16, v86
	v_ashrrev_i32_e32 v1, 31, v0
	v_lshlrev_b64 v[0:1], 10, v[0:1]
	v_lshl_add_u64 v[0:1], s[14:15], 0, v[0:1]
	v_lshl_add_u64 v[0:1], v[0:1], 0, v[66:67]
	s_waitcnt lgkmcnt(0)
	global_store_dwordx4 v[0:1], v[4:7], off sc1
	v_add_u32_e32 v0, v89, v66
	ds_read_b128 v[0:3], v0
	v_add_u32_e32 v4, s16, v88
	v_ashrrev_i32_e32 v5, 31, v4
	v_lshlrev_b64 v[4:5], 10, v[4:5]
	v_lshl_add_u64 v[4:5], s[14:15], 0, v[4:5]
	v_lshl_add_u64 v[8:9], v[4:5], 0, v[66:67]
	v_add_u32_e32 v4, v124, v66
	ds_read_b128 v[4:7], v4
	s_waitcnt lgkmcnt(1)
	global_store_dwordx4 v[8:9], v[0:3], off sc1
	s_nop 1
	v_add_u32_e32 v0, s16, v90
	v_ashrrev_i32_e32 v1, 31, v0
	v_lshlrev_b64 v[0:1], 10, v[0:1]
	v_lshl_add_u64 v[0:1], s[14:15], 0, v[0:1]
	v_lshl_add_u64 v[0:1], v[0:1], 0, v[66:67]
	s_waitcnt lgkmcnt(0)
	global_store_dwordx4 v[0:1], v[4:7], off sc1
	s_barrier

.LBB0_25:
	v_lshl_add_u32 v32, s33, 6, v26
	v_or_b32_e32 v4, 1, v32
	v_ashrrev_i32_e32 v33, 31, v32
	v_ashrrev_i32_e32 v5, 31, v4
	s_or_b32 s34, s33, 1
	v_lshlrev_b64 v[0:1], 12, v[32:33]
	v_lshlrev_b64 v[4:5], 12, v[4:5]
	v_or_b32_e32 v8, 2, v32
	v_or_b32_e32 v12, 3, v32
	v_or_b32_e32 v16, 4, v32
	v_or_b32_e32 v20, 5, v32
	v_or_b32_e32 v28, 6, v32
	v_or_b32_e32 v32, 7, v32
	v_lshl_add_u32 v72, s34, 6, v26
	v_lshl_add_u64 v[0:1], v[24:25], 0, v[0:1]
	v_lshl_add_u64 v[4:5], v[24:25], 0, v[4:5]
	v_ashrrev_i32_e32 v9, 31, v8
	v_ashrrev_i32_e32 v13, 31, v12
	v_ashrrev_i32_e32 v17, 31, v16
	v_ashrrev_i32_e32 v21, 31, v20
	v_ashrrev_i32_e32 v29, 31, v28
	v_ashrrev_i32_e32 v33, 31, v32
	v_ashrrev_i32_e32 v73, 31, v72
	global_load_dwordx4 v[0:3], v[0:1], off sc0 sc1 nt
	v_lshlrev_b64 v[8:9], 12, v[8:9]
	global_load_dwordx4 v[4:7], v[4:5], off sc0 sc1 nt
	v_lshlrev_b64 v[12:13], 12, v[12:13]
	v_lshlrev_b64 v[16:17], 12, v[16:17]
	v_lshlrev_b64 v[20:21], 12, v[20:21]
	v_lshlrev_b64 v[28:29], 12, v[28:29]
	v_lshlrev_b64 v[32:33], 12, v[32:33]
	v_lshlrev_b64 v[36:37], 12, v[72:73]
	v_or_b32_e32 v40, 1, v72
	v_or_b32_e32 v44, 2, v72
	v_or_b32_e32 v48, 3, v72
	v_or_b32_e32 v52, 4, v72
	v_or_b32_e32 v56, 5, v72
	v_or_b32_e32 v60, 6, v72
	v_or_b32_e32 v72, 7, v72
	v_lshl_add_u64 v[8:9], v[24:25], 0, v[8:9]
	v_lshl_add_u64 v[12:13], v[24:25], 0, v[12:13]
	v_lshl_add_u64 v[16:17], v[24:25], 0, v[16:17]
	v_lshl_add_u64 v[20:21], v[24:25], 0, v[20:21]
	v_lshl_add_u64 v[28:29], v[24:25], 0, v[28:29]
	v_lshl_add_u64 v[32:33], v[24:25], 0, v[32:33]
	v_ashrrev_i32_e32 v41, 31, v40
	v_ashrrev_i32_e32 v45, 31, v44
	v_ashrrev_i32_e32 v49, 31, v48
	v_ashrrev_i32_e32 v53, 31, v52
	v_ashrrev_i32_e32 v57, 31, v56
	v_ashrrev_i32_e32 v61, 31, v60
	v_ashrrev_i32_e32 v73, 31, v72
	s_waitcnt vmcnt(0)
	v_cvt_pk_bf16_f32 v132, v0, v4
	v_lshl_add_u32 v4, s33, 7, v123
	global_load_dwordx4 v[8:11], v[8:9], off sc0 sc1 nt
	v_lshlrev_b64 v[40:41], 12, v[40:41]
	global_load_dwordx4 v[12:15], v[12:13], off sc0 sc1 nt
	v_lshlrev_b64 v[44:45], 12, v[44:45]
	global_load_dwordx4 v[16:19], v[16:17], off sc0 sc1 nt
	v_lshlrev_b64 v[48:49], 12, v[48:49]
	global_load_dwordx4 v[20:23], v[20:21], off sc0 sc1 nt
	v_lshlrev_b64 v[52:53], 12, v[52:53]
	global_load_dwordx4 v[28:31], v[28:29], off sc0 sc1 nt
	v_lshlrev_b64 v[56:57], 12, v[56:57]
	global_load_dwordx4 v[32:35], v[32:33], off sc0 sc1 nt
	v_lshlrev_b64 v[60:61], 12, v[60:61]
	v_lshlrev_b64 v[72:73], 12, v[72:73]
	s_waitcnt vmcnt(4)
	v_cvt_pk_bf16_f32 v133, v8, v12
	s_waitcnt vmcnt(2)
	v_cvt_pk_bf16_f32 v134, v16, v20
	s_waitcnt vmcnt(0)
	v_cvt_pk_bf16_f32 v135, v28, v32
	ds_write_b128 v4, v[132:135]
	v_cvt_pk_bf16_f32 v132, v1, v5
	v_lshl_add_u64 v[36:37], v[24:25], 0, v[36:37]
	v_lshl_add_u64 v[40:41], v[24:25], 0, v[40:41]
	v_lshl_add_u64 v[44:45], v[24:25], 0, v[44:45]
	v_lshl_add_u64 v[48:49], v[24:25], 0, v[48:49]
	v_lshl_add_u64 v[52:53], v[24:25], 0, v[52:53]
	v_lshl_add_u64 v[56:57], v[24:25], 0, v[56:57]
	v_lshl_add_u64 v[60:61], v[24:25], 0, v[60:61]
	v_lshl_add_u64 v[72:73], v[24:25], 0, v[72:73]
	v_cvt_pk_bf16_f32 v133, v9, v13
	v_cvt_pk_bf16_f32 v134, v17, v21
	v_cvt_pk_bf16_f32 v135, v29, v33
	ds_write_b128 v4, v[132:135] offset:528
	v_cvt_pk_bf16_f32 v132, v2, v6
	v_cvt_pk_bf16_f32 v0, v3, v7
	v_cvt_pk_bf16_f32 v1, v11, v15
	v_cvt_pk_bf16_f32 v2, v19, v23
	v_cvt_pk_bf16_f32 v3, v31, v35
	global_load_dwordx4 v[36:39], v[36:37], off sc0 sc1 nt
	v_cvt_pk_bf16_f32 v133, v10, v14
	global_load_dwordx4 v[40:43], v[40:41], off sc0 sc1 nt
	v_cvt_pk_bf16_f32 v134, v18, v22
	global_load_dwordx4 v[44:47], v[44:45], off sc0 sc1 nt
	v_cvt_pk_bf16_f32 v135, v30, v34
	global_load_dwordx4 v[48:51], v[48:49], off sc0 sc1 nt
	ds_write_b128 v4, v[132:135] offset:1056
	global_load_dwordx4 v[52:55], v[52:53], off sc0 sc1 nt
	ds_write_b128 v4, v[0:3] offset:1584
	global_load_dwordx4 v[56:59], v[56:57], off sc0 sc1 nt
	s_waitcnt vmcnt(4)
	v_cvt_pk_bf16_f32 v0, v36, v40
	global_load_dwordx4 v[60:63], v[60:61], off sc0 sc1 nt
	s_waitcnt vmcnt(3)
	v_cvt_pk_bf16_f32 v1, v44, v48
	global_load_dwordx4 v[128:131], v[72:73], off sc0 sc1 nt
	s_waitcnt vmcnt(2)
	v_cvt_pk_bf16_f32 v2, v52, v56
	s_waitcnt vmcnt(0)
	v_cvt_pk_bf16_f32 v3, v60, v128
	v_lshl_add_u32 v4, s34, 7, v123
	ds_write_b128 v4, v[0:3]
	v_cvt_pk_bf16_f32 v0, v37, v41
	v_cvt_pk_bf16_f32 v1, v45, v49
	v_cvt_pk_bf16_f32 v2, v53, v57
	v_cvt_pk_bf16_f32 v3, v61, v129
	ds_write_b128 v4, v[0:3] offset:528
	v_cvt_pk_bf16_f32 v0, v38, v42
	v_cvt_pk_bf16_f32 v1, v46, v50
	v_cvt_pk_bf16_f32 v2, v54, v58
	v_cvt_pk_bf16_f32 v3, v62, v130
	s_and_b64 vcc, exec, s[16:17]
	s_mov_b64 s[16:17], 0
	s_mov_b32 s33, 2
	ds_write_b128 v4, v[0:3] offset:1056
	v_cvt_pk_bf16_f32 v0, v39, v43
	v_cvt_pk_bf16_f32 v1, v47, v51
	v_cvt_pk_bf16_f32 v2, v55, v59
	v_cvt_pk_bf16_f32 v3, v63, v131
	ds_write_b128 v4, v[0:3] offset:1584
	s_cbranch_vccnz .LBB0_25
	s_lshl_b64 s[14:15], s[14:15], 1
	s_add_u32 s14, s23, s14
	s_waitcnt lgkmcnt(0)
	s_barrier
	s_addc_u32 s15, s24, s15
	s_lshl_b32 s16, s31, 1
	ds_read_b128 v[0:3], v92
	v_add_u32_e32 v4, s2, v91
	s_add_u32 s14, s14, s16
	v_ashrrev_i32_e32 v5, 31, v4
	s_addc_u32 s15, s15, 0
	v_lshlrev_b64 v[4:5], 11, v[4:5]
	v_lshl_add_u64 v[4:5], s[14:15], 0, v[4:5]
	v_mov_b32_e32 v71, v69
	v_lshl_add_u64 v[8:9], v[4:5], 0, v[70:71]
	ds_read_b128 v[4:7], v94
	s_waitcnt lgkmcnt(1)
	global_store_dwordx4 v[8:9], v[0:3], off sc1
	s_nop 1
	v_add_u32_e32 v0, s2, v93
	v_ashrrev_i32_e32 v1, 31, v0
	v_lshlrev_b64 v[0:1], 11, v[0:1]
	v_lshl_add_u64 v[0:1], s[14:15], 0, v[0:1]
	v_lshl_add_u64 v[0:1], v[0:1], 0, v[70:71]
	s_waitcnt lgkmcnt(0)
	global_store_dwordx4 v[0:1], v[4:7], off sc1
	ds_read_b128 v[0:3], v96
	s_nop 0
	v_add_u32_e32 v4, s2, v95
	v_ashrrev_i32_e32 v5, 31, v4
	v_lshlrev_b64 v[4:5], 11, v[4:5]
	v_lshl_add_u64 v[4:5], s[14:15], 0, v[4:5]
	v_lshl_add_u64 v[8:9], v[4:5], 0, v[70:71]
	ds_read_b128 v[4:7], v98
	s_waitcnt lgkmcnt(1)
	global_store_dwordx4 v[8:9], v[0:3], off sc1
	s_nop 1
	v_add_u32_e32 v0, s2, v97
	v_ashrrev_i32_e32 v1, 31, v0
	v_lshlrev_b64 v[0:1], 11, v[0:1]
	v_lshl_add_u64 v[0:1], s[14:15], 0, v[0:1]
	v_lshl_add_u64 v[0:1], v[0:1], 0, v[70:71]
	s_waitcnt lgkmcnt(0)
	global_store_dwordx4 v[0:1], v[4:7], off sc1
	ds_read_b128 v[0:3], v100
	s_nop 0
	v_add_u32_e32 v4, s2, v99
	v_ashrrev_i32_e32 v5, 31, v4
	v_lshlrev_b64 v[4:5], 11, v[4:5]
	v_lshl_add_u64 v[4:5], s[14:15], 0, v[4:5]
	v_lshl_add_u64 v[8:9], v[4:5], 0, v[70:71]
	ds_read_b128 v[4:7], v102
	s_waitcnt lgkmcnt(1)
	global_store_dwordx4 v[8:9], v[0:3], off sc1
	s_nop 1
	v_add_u32_e32 v0, s2, v101
	v_ashrrev_i32_e32 v1, 31, v0
	v_lshlrev_b64 v[0:1], 11, v[0:1]
	v_lshl_add_u64 v[0:1], s[14:15], 0, v[0:1]
	v_lshl_add_u64 v[0:1], v[0:1], 0, v[70:71]
	s_waitcnt lgkmcnt(0)
	global_store_dwordx4 v[0:1], v[4:7], off sc1
	ds_read_b128 v[0:3], v104
	s_nop 0
	v_add_u32_e32 v4, s2, v103
	v_ashrrev_i32_e32 v5, 31, v4
	v_lshlrev_b64 v[4:5], 11, v[4:5]
	v_lshl_add_u64 v[4:5], s[14:15], 0, v[4:5]
	v_lshl_add_u64 v[8:9], v[4:5], 0, v[70:71]
	ds_read_b128 v[4:7], v106
	s_waitcnt lgkmcnt(1)
	global_store_dwordx4 v[8:9], v[0:3], off sc1
	s_nop 1
	v_add_u32_e32 v0, s2, v105
	v_ashrrev_i32_e32 v1, 31, v0
	v_lshlrev_b64 v[0:1], 11, v[0:1]
	v_lshl_add_u64 v[0:1], s[14:15], 0, v[0:1]
	v_lshl_add_u64 v[0:1], v[0:1], 0, v[70:71]
	s_waitcnt lgkmcnt(0)
	global_store_dwordx4 v[0:1], v[4:7], off sc1
	ds_read_b128 v[0:3], v108
	s_nop 0
	v_add_u32_e32 v4, s2, v107
	v_ashrrev_i32_e32 v5, 31, v4
	v_lshlrev_b64 v[4:5], 11, v[4:5]
	v_lshl_add_u64 v[4:5], s[14:15], 0, v[4:5]
	v_lshl_add_u64 v[8:9], v[4:5], 0, v[70:71]
	ds_read_b128 v[4:7], v110
	s_waitcnt lgkmcnt(1)
	global_store_dwordx4 v[8:9], v[0:3], off sc1
	s_nop 1
	v_add_u32_e32 v0, s2, v109
	v_ashrrev_i32_e32 v1, 31, v0
	v_lshlrev_b64 v[0:1], 11, v[0:1]
	v_lshl_add_u64 v[0:1], s[14:15], 0, v[0:1]
	v_lshl_add_u64 v[0:1], v[0:1], 0, v[70:71]
	s_waitcnt lgkmcnt(0)
	global_store_dwordx4 v[0:1], v[4:7], off sc1
	ds_read_b128 v[0:3], v112
	s_nop 0
	v_add_u32_e32 v4, s2, v111
	v_ashrrev_i32_e32 v5, 31, v4
	v_lshlrev_b64 v[4:5], 11, v[4:5]
	v_lshl_add_u64 v[4:5], s[14:15], 0, v[4:5]
	v_lshl_add_u64 v[8:9], v[4:5], 0, v[70:71]
	ds_read_b128 v[4:7], v114
	s_waitcnt lgkmcnt(1)
	global_store_dwordx4 v[8:9], v[0:3], off sc1
	s_nop 1
	v_add_u32_e32 v0, s2, v113
	v_ashrrev_i32_e32 v1, 31, v0
	v_lshlrev_b64 v[0:1], 11, v[0:1]
	v_lshl_add_u64 v[0:1], s[14:15], 0, v[0:1]
	v_lshl_add_u64 v[0:1], v[0:1], 0, v[70:71]
	s_waitcnt lgkmcnt(0)
	global_store_dwordx4 v[0:1], v[4:7], off sc1
	ds_read_b128 v[0:3], v116
	s_nop 0
	v_add_u32_e32 v4, s2, v115
	v_ashrrev_i32_e32 v5, 31, v4
	v_lshlrev_b64 v[4:5], 11, v[4:5]
	v_lshl_add_u64 v[4:5], s[14:15], 0, v[4:5]
	v_lshl_add_u64 v[8:9], v[4:5], 0, v[70:71]
	ds_read_b128 v[4:7], v118
	s_waitcnt lgkmcnt(1)
	global_store_dwordx4 v[8:9], v[0:3], off sc1
	s_nop 1
	v_add_u32_e32 v0, s2, v117
	v_ashrrev_i32_e32 v1, 31, v0
	v_lshlrev_b64 v[0:1], 11, v[0:1]
	v_lshl_add_u64 v[0:1], s[14:15], 0, v[0:1]
	v_lshl_add_u64 v[0:1], v[0:1], 0, v[70:71]
	s_waitcnt lgkmcnt(0)
	global_store_dwordx4 v[0:1], v[4:7], off sc1
	ds_read_b128 v[0:3], v120
	s_nop 0
	v_add_u32_e32 v4, s2, v119
	v_ashrrev_i32_e32 v5, 31, v4
	v_lshlrev_b64 v[4:5], 11, v[4:5]
	v_lshl_add_u64 v[4:5], s[14:15], 0, v[4:5]
	v_lshl_add_u64 v[8:9], v[4:5], 0, v[70:71]
	ds_read_b128 v[4:7], v122
	s_waitcnt lgkmcnt(1)
	global_store_dwordx4 v[8:9], v[0:3], off sc1
	s_nop 1
	v_add_u32_e32 v0, s2, v121
	v_ashrrev_i32_e32 v1, 31, v0
	v_lshlrev_b64 v[0:1], 11, v[0:1]
	v_lshl_add_u64 v[0:1], s[14:15], 0, v[0:1]
	v_lshl_add_u64 v[0:1], v[0:1], 0, v[70:71]
	s_waitcnt lgkmcnt(0)
	global_store_dwordx4 v[0:1], v[4:7], off sc1
	s_barrier

.LBB0_30:
	v_add_u32_e32 v3, s31, v2
	v_mad_i64_i32 v[4:5], s[34:35], v3, s29, v[0:1]
	v_or_b32_e32 v8, 1, v3
	v_or_b32_e32 v9, 2, v3
	v_or_b32_e32 v10, 3, v3
	v_or_b32_e32 v11, 4, v3
	v_or_b32_e32 v12, 5, v3
	v_or_b32_e32 v13, 6, v3
	v_or_b32_e32 v14, 7, v3
	v_add_u32_e32 v15, 64, v3
	v_add_u32_e32 v16, 0x41, v3
	v_add_u32_e32 v17, 0x42, v3
	v_add_u32_e32 v18, 0x43, v3
	v_add_u32_e32 v19, 0x44, v3
	v_add_u32_e32 v26, 0x45, v3
	v_add_u32_e32 v27, 0x46, v3
	v_add_u32_e32 v3, 0x47, v3
	global_load_dwordx4 v[4:7], v[4:5], off sc0 sc1 nt
	v_mad_i64_i32 v[20:21], s[34:35], v8, s29, v[0:1]
	v_mad_i64_i32 v[22:23], s[34:35], v9, s29, v[0:1]
	v_mad_i64_i32 v[24:25], s[34:35], v10, s29, v[0:1]
	v_mad_i64_i32 v[28:29], s[34:35], v11, s29, v[0:1]
	v_mad_i64_i32 v[30:31], s[34:35], v12, s29, v[0:1]
	v_mad_i64_i32 v[32:33], s[34:35], v13, s29, v[0:1]
	v_mad_i64_i32 v[34:35], s[34:35], v14, s29, v[0:1]
	v_mad_i64_i32 v[36:37], s[34:35], v15, s29, v[0:1]
	v_mad_i64_i32 v[40:41], s[34:35], v16, s29, v[0:1]
	v_mad_i64_i32 v[44:45], s[34:35], v17, s29, v[0:1]
	v_mad_i64_i32 v[48:49], s[34:35], v18, s29, v[0:1]
	v_mad_i64_i32 v[52:53], s[34:35], v19, s29, v[0:1]
	v_mad_i64_i32 v[56:57], s[34:35], v26, s29, v[0:1]
	v_mad_i64_i32 v[60:61], s[34:35], v27, s29, v[0:1]
	v_mad_i64_i32 v[128:129], s[34:35], v3, s29, v[0:1]
	global_load_dwordx4 v[8:11], v[20:21], off sc0 sc1 nt
	global_load_dwordx4 v[12:15], v[22:23], off sc0 sc1 nt
	global_load_dwordx4 v[16:19], v[24:25], off sc0 sc1 nt
	s_nop 0
	global_load_dwordx4 v[20:23], v[28:29], off sc0 sc1 nt
	global_load_dwordx4 v[24:27], v[30:31], off sc0 sc1 nt
	s_nop 0
	global_load_dwordx4 v[28:31], v[32:33], off sc0 sc1 nt
	s_nop 0
	global_load_dwordx4 v[32:35], v[34:35], off sc0 sc1 nt
	s_nop 0
	global_load_dwordx4 v[36:39], v[36:37], off sc0 sc1 nt
	s_nop 0
	global_load_dwordx4 v[40:43], v[40:41], off sc0 sc1 nt
	s_nop 0
	global_load_dwordx4 v[44:47], v[44:45], off sc0 sc1 nt
	s_nop 0
	global_load_dwordx4 v[48:51], v[48:49], off sc0 sc1 nt
	s_nop 0
	global_load_dwordx4 v[52:55], v[52:53], off sc0 sc1 nt
	s_nop 0
	global_load_dwordx4 v[56:59], v[56:57], off sc0 sc1 nt
	s_nop 0
	global_load_dwordx4 v[60:63], v[60:61], off sc0 sc1 nt
	s_nop 0
	global_load_dwordx4 v[128:131], v[128:129], off sc0 sc1 nt
	v_mov_b32_e32 v72, 0
	v_mov_b32_e32 v73, 0
	v_mov_b32_e32 v138, 0
	v_mov_b32_e32 v139, 0
	v_mov_b32_e32 v132, 0
	v_mov_b32_e32 v133, 0
	v_mov_b32_e32 v140, 0
	v_mov_b32_e32 v141, 0
	v_mov_b32_e32 v134, 0
	v_mov_b32_e32 v135, 0
	v_mov_b32_e32 v142, 0
	v_mov_b32_e32 v143, 0
	v_mov_b32_e32 v136, 0
	v_mov_b32_e32 v137, 0
	v_mov_b32_e32 v144, 0
	v_mov_b32_e32 v145, 0
	v_add_u32_e32 v68, s31, v125
	s_movk_i32 s31, 0x80
	s_and_b64 vcc, exec, s[14:15]
	s_mov_b64 s[14:15], 0
	s_waitcnt vmcnt(15)
	v_mul_f32_e32 v3, 0x42000000, v4
	v_mul_f32_e32 v4, 0x42000000, v5
	v_mul_f32_e32 v5, 0x42000000, v6
	v_mul_f32_e32 v6, 0x42000000, v7
	s_waitcnt vmcnt(14)
	v_mul_f32_e32 v7, 0x42000000, v8
	v_mul_f32_e32 v8, 0x42000000, v9
	v_mul_f32_e32 v9, 0x42000000, v10
	v_mul_f32_e32 v10, 0x42000000, v11
	s_waitcnt vmcnt(13)
	v_mul_f32_e32 v11, 0x42000000, v12
	v_mul_f32_e32 v12, 0x42000000, v13
	v_mul_f32_e32 v13, 0x42000000, v14
	v_mul_f32_e32 v14, 0x42000000, v15
	s_waitcnt vmcnt(12)
	v_mul_f32_e32 v15, 0x42000000, v16
	v_mul_f32_e32 v16, 0x42000000, v17
	v_mul_f32_e32 v17, 0x42000000, v18
	v_mul_f32_e32 v18, 0x42000000, v19
	s_waitcnt vmcnt(11)
	v_mul_f32_e32 v19, 0x42000000, v20
	v_mul_f32_e32 v20, 0x42000000, v21
	v_mul_f32_e32 v21, 0x42000000, v22
	v_mul_f32_e32 v22, 0x42000000, v23
	s_waitcnt vmcnt(10)
	v_mul_f32_e32 v23, 0x42000000, v24
	v_mul_f32_e32 v24, 0x42000000, v25
	v_mul_f32_e32 v25, 0x42000000, v26
	v_mul_f32_e32 v26, 0x42000000, v27
	s_waitcnt vmcnt(9)
	v_mul_f32_e32 v27, 0x42000000, v28
	v_mul_f32_e32 v28, 0x42000000, v29
	v_mul_f32_e32 v29, 0x42000000, v30
	v_mul_f32_e32 v30, 0x42000000, v31
	s_waitcnt vmcnt(8)
	v_mul_f32_e32 v31, 0x42000000, v32
	v_mul_f32_e32 v32, 0x42000000, v33
	v_mul_f32_e32 v33, 0x42000000, v34
	v_mul_f32_e32 v34, 0x42000000, v35
	s_waitcnt vmcnt(7)
	v_mul_f32_e32 v35, 0x42000000, v36
	v_mul_f32_e32 v36, 0x42000000, v37
	v_mul_f32_e32 v37, 0x42000000, v38
	v_mul_f32_e32 v38, 0x42000000, v39
	s_waitcnt vmcnt(6)
	v_mul_f32_e32 v39, 0x42000000, v40
	v_mul_f32_e32 v40, 0x42000000, v41
	v_mul_f32_e32 v41, 0x42000000, v42
	v_mul_f32_e32 v42, 0x42000000, v43
	s_waitcnt vmcnt(5)
	v_mul_f32_e32 v43, 0x42000000, v44
	v_mul_f32_e32 v44, 0x42000000, v45
	v_mul_f32_e32 v45, 0x42000000, v46
	v_mul_f32_e32 v46, 0x42000000, v47
	s_waitcnt vmcnt(4)
	v_mul_f32_e32 v47, 0x42000000, v48
	v_mul_f32_e32 v48, 0x42000000, v49
	v_mul_f32_e32 v49, 0x42000000, v50
	v_mul_f32_e32 v50, 0x42000000, v51
	s_waitcnt vmcnt(3)
	v_mul_f32_e32 v51, 0x42000000, v52
	v_mul_f32_e32 v52, 0x42000000, v53
	v_mul_f32_e32 v53, 0x42000000, v54
	v_mul_f32_e32 v54, 0x42000000, v55
	s_waitcnt vmcnt(2)
	v_mul_f32_e32 v55, 0x42000000, v56
	v_mul_f32_e32 v56, 0x42000000, v57
	v_cvt_pk_fp8_f32 v72, v3, v7
	v_cvt_pk_fp8_f32 v73, v19, v23
	v_cvt_pk_fp8_f32 v138, v35, v39
	v_cvt_pk_fp8_f32 v139, v51, v55
	v_mul_f32_e32 v57, 0x42000000, v58
	v_cvt_pk_fp8_f32 v132, v4, v8
	v_cvt_pk_fp8_f32 v133, v20, v24
	v_cvt_pk_fp8_f32 v140, v36, v40
	v_cvt_pk_fp8_f32 v141, v52, v56
	v_mul_f32_e32 v58, 0x42000000, v59
	v_cvt_pk_fp8_f32 v134, v5, v9
	v_cvt_pk_fp8_f32 v135, v21, v25
	v_cvt_pk_fp8_f32 v142, v37, v41
	v_cvt_pk_fp8_f32 v143, v53, v57
	s_waitcnt vmcnt(1)
	v_mul_f32_e32 v59, 0x42000000, v60
	v_mul_f32_e32 v60, 0x42000000, v61
	v_mul_f32_e32 v61, 0x42000000, v62
	v_mul_f32_e32 v62, 0x42000000, v63
	s_waitcnt vmcnt(0)
	v_mul_f32_e32 v63, 0x42000000, v128
	v_cvt_pk_fp8_f32 v136, v6, v10
	v_cvt_pk_fp8_f32 v137, v22, v26
	v_cvt_pk_fp8_f32 v144, v38, v42
	v_cvt_pk_fp8_f32 v145, v54, v58
	v_mul_f32_e32 v71, 0x42000000, v129
	v_cvt_pk_fp8_f32 v72, v11, v15 op_sel:[0,0,1]
	v_cvt_pk_fp8_f32 v73, v27, v31 op_sel:[0,0,1]
	v_cvt_pk_fp8_f32 v138, v43, v47 op_sel:[0,0,1]
	v_cvt_pk_fp8_f32 v139, v59, v63 op_sel:[0,0,1]
	v_mul_f32_e32 v127, 0x42000000, v130
	v_cvt_pk_fp8_f32 v132, v12, v16 op_sel:[0,0,1]
	v_cvt_pk_fp8_f32 v133, v28, v32 op_sel:[0,0,1]
	v_cvt_pk_fp8_f32 v140, v44, v48 op_sel:[0,0,1]
	v_cvt_pk_fp8_f32 v141, v60, v71 op_sel:[0,0,1]
	v_mul_f32_e32 v128, 0x42000000, v131
	v_cvt_pk_fp8_f32 v134, v13, v17 op_sel:[0,0,1]
	v_cvt_pk_fp8_f32 v135, v29, v33 op_sel:[0,0,1]
	v_cvt_pk_fp8_f32 v142, v45, v49 op_sel:[0,0,1]
	v_cvt_pk_fp8_f32 v143, v61, v127 op_sel:[0,0,1]
	v_cvt_pk_fp8_f32 v136, v14, v18 op_sel:[0,0,1]
	v_cvt_pk_fp8_f32 v137, v30, v34 op_sel:[0,0,1]
	v_cvt_pk_fp8_f32 v144, v46, v50 op_sel:[0,0,1]
	v_cvt_pk_fp8_f32 v145, v62, v128 op_sel:[0,0,1]
	ds_write2_b64 v68, v[72:73], v[138:139] offset1:8
	ds_write2_b64 v68, v[132:133], v[140:141] offset0:34 offset1:42
	ds_write2_b64 v68, v[134:135], v[142:143] offset0:68 offset1:76
	ds_write2_b64 v68, v[136:137], v[144:145] offset0:102 offset1:110
	s_cbranch_vccnz .LBB0_30
	s_mul_i32 s15, s16, 0x280000
	s_mul_hi_i32 s14, s16, 0x280000
	s_add_u32 s15, s25, s15
	s_waitcnt lgkmcnt(0)
	s_barrier
	v_add_u32_e32 v0, v77, v66
	s_addc_u32 s16, s27, s14
	s_ashr_i32 s31, s17, 31
	ds_read_b128 v[0:3], v0
	v_add_u32_e32 v4, s2, v76
	s_add_u32 s14, s15, s17
	v_ashrrev_i32_e32 v5, 31, v4
	s_addc_u32 s15, s16, s31
	v_lshlrev_b64 v[4:5], 10, v[4:5]
	v_lshl_add_u64 v[4:5], s[14:15], 0, v[4:5]
	v_lshl_add_u64 v[8:9], v[4:5], 0, v[66:67]
	v_add_u32_e32 v4, v79, v66
	ds_read_b128 v[4:7], v4
	s_waitcnt lgkmcnt(1)
	global_store_dwordx4 v[8:9], v[0:3], off sc1
	s_nop 1
	v_add_u32_e32 v0, s2, v78
	v_ashrrev_i32_e32 v1, 31, v0
	v_lshlrev_b64 v[0:1], 10, v[0:1]
	v_lshl_add_u64 v[0:1], s[14:15], 0, v[0:1]
	v_lshl_add_u64 v[0:1], v[0:1], 0, v[66:67]
	s_waitcnt lgkmcnt(0)
	global_store_dwordx4 v[0:1], v[4:7], off sc1
	v_add_u32_e32 v0, v81, v66
	ds_read_b128 v[0:3], v0
	v_add_u32_e32 v4, s2, v80
	v_ashrrev_i32_e32 v5, 31, v4
	v_lshlrev_b64 v[4:5], 10, v[4:5]
	v_lshl_add_u64 v[4:5], s[14:15], 0, v[4:5]
	v_lshl_add_u64 v[8:9], v[4:5], 0, v[66:67]
	v_add_u32_e32 v4, v83, v66
	ds_read_b128 v[4:7], v4
	s_waitcnt lgkmcnt(1)
	global_store_dwordx4 v[8:9], v[0:3], off sc1
	s_nop 1
	v_add_u32_e32 v0, s2, v82
	v_ashrrev_i32_e32 v1, 31, v0
	v_lshlrev_b64 v[0:1], 10, v[0:1]
	v_lshl_add_u64 v[0:1], s[14:15], 0, v[0:1]
	v_lshl_add_u64 v[0:1], v[0:1], 0, v[66:67]
	s_waitcnt lgkmcnt(0)
	global_store_dwordx4 v[0:1], v[4:7], off sc1
	v_add_u32_e32 v0, v85, v66
	ds_read_b128 v[0:3], v0
	v_add_u32_e32 v4, s2, v84
	v_ashrrev_i32_e32 v5, 31, v4
	v_lshlrev_b64 v[4:5], 10, v[4:5]
	v_lshl_add_u64 v[4:5], s[14:15], 0, v[4:5]
	v_lshl_add_u64 v[8:9], v[4:5], 0, v[66:67]
	v_add_u32_e32 v4, v87, v66
	ds_read_b128 v[4:7], v4
	s_waitcnt lgkmcnt(1)
	global_store_dwordx4 v[8:9], v[0:3], off sc1
	s_nop 1
	v_add_u32_e32 v0, s2, v86
	v_ashrrev_i32_e32 v1, 31, v0
	v_lshlrev_b64 v[0:1], 10, v[0:1]
	v_lshl_add_u64 v[0:1], s[14:15], 0, v[0:1]
	v_lshl_add_u64 v[0:1], v[0:1], 0, v[66:67]
	s_waitcnt lgkmcnt(0)
	global_store_dwordx4 v[0:1], v[4:7], off sc1
	v_add_u32_e32 v0, v89, v66
	ds_read_b128 v[0:3], v0
	v_add_u32_e32 v4, s2, v88
	v_ashrrev_i32_e32 v5, 31, v4
	v_lshlrev_b64 v[4:5], 10, v[4:5]
	v_lshl_add_u64 v[4:5], s[14:15], 0, v[4:5]
	v_lshl_add_u64 v[8:9], v[4:5], 0, v[66:67]
	v_add_u32_e32 v4, v124, v66
	ds_read_b128 v[4:7], v4
	s_waitcnt lgkmcnt(1)
	global_store_dwordx4 v[8:9], v[0:3], off sc1
	s_nop 1
	v_add_u32_e32 v0, s2, v90
	v_ashrrev_i32_e32 v1, 31, v0
	v_lshlrev_b64 v[0:1], 10, v[0:1]
	v_lshl_add_u64 v[0:1], s[14:15], 0, v[0:1]
	v_lshl_add_u64 v[0:1], v[0:1], 0, v[66:67]
	s_waitcnt lgkmcnt(0)
	global_store_dwordx4 v[0:1], v[4:7], off sc1
	s_barrier
	s_branch .LBB0_8

.LBB0_340:
	v_readlane_b32 s0, v250, 4
	s_mov_b32 s0, s2
	v_writelane_b32 v255, s0, 33
	s_nop 1
	v_writelane_b32 v255, s1, 34
	s_mul_i32 s0, s2, 10
	s_add_i32 s4, s0, 3
	s_waitcnt lgkmcnt(0)
	s_mov_b32 s2, s100
	s_mov_b32 s1, s101
	s_cmp_le_i32 s2, s4
	s_cselect_b64 s[2:3], -1, 0
	s_cmp_lt_i32 s4, s1
	s_cselect_b64 s[4:5], -1, 0
	s_and_b64 s[2:3], s[2:3], s[4:5]
	v_writelane_b32 v255, s0, 35
	s_and_b64 vcc, exec, s[2:3]
	s_mov_b64 s[2:3], -1
	s_cbranch_vccnz .LBB0_342
	v_readlane_b32 s0, v255, 35
	s_add_i32 s22, s0, 4
	s_mov_b64 s[2:3], 0

.LBB0_506:
	v_readlane_b32 s0, v250, 4
	s_waitcnt vmcnt(0)
	s_waitcnt lgkmcnt(0)
	s_mov_b32 s1, s100
	s_cmp_le_i32 s1, s22
	s_cselect_b64 s[2:3], -1, 0
	s_mov_b32 s57, s101
	s_cmp_lt_i32 s22, s57
	s_cselect_b64 s[4:5], -1, 0
	s_and_b64 s[4:5], s[2:3], s[4:5]
	s_mov_b64 s[2:3], -1
	s_and_b64 vcc, exec, s[4:5]
	s_cbranch_vccnz .LBB0_508
	v_readlane_b32 s0, v255, 35
	s_add_i32 s1, s0, 5
	s_mov_b64 s[2:3], 0

.Lpeel_in:
	s_mov_b64 s[26:27], 0
	v_mov_b64_e32 v[178:179], v[174:175]
	v_mov_b64_e32 v[180:181], v[168:169]
	v_mov_b32_e32 v186, v176
	v_mov_b32_e32 v172, v170
	ds_read_b128 v[0:3], v193
	ds_read_b128 v[8:11], v193 offset:2048
	ds_read_b128 v[4:7], v195
	ds_read_b128 v[12:15], v195 offset:2048
	s_add_u32 s15, s24, 0x80
	s_addc_u32 s23, s25, 0
	s_and_b64 s[26:27], s[26:27], exec
	s_cselect_b32 s29, s19, s23
	s_cselect_b32 s28, s18, s15
	s_cselect_b32 s27, s17, s3
	s_cselect_b32 s26, s16, s2
	v_lshl_add_u64 v[16:17], s[24:25], 0, v[168:169]
	s_add_i32 m0, s47, 0xc000
	ds_read_b128 v[218:221], v192
	ds_read_b128 v[226:229], v192 offset:2048
	ds_read_b128 v[222:225], v194
	ds_read_b128 v[230:233], v194 offset:2048
	ds_read_b128 v[234:237], v192 offset:4096
	ds_read_b128 v[242:245], v192 offset:6144
	ds_read_b128 v[238:241], v194 offset:4096
	ds_read_b128 v[246:249], v194 offset:6144
	global_load_lds_dwordx4 v[16:17], off
	v_lshl_add_u64 v[16:17], s[24:25], 0, v[174:175]
	s_add_i32 m0, s47, 0xe000
	s_nop 0
	global_load_lds_dwordx4 v[16:17], off
	s_waitcnt lgkmcnt(8)
	s_barrier
	s_waitcnt lgkmcnt(0)
	s_setprio 1
	v_mfma_scale_f32_16x16x128_f8f6f4 v[156:159], v[0:7], v[218:225], 0, v191, v191 op_sel_hi:[0,0,0]
	v_mfma_scale_f32_16x16x128_f8f6f4 v[152:155], v[8:15], v[218:225], 0, v191, v191 op_sel_hi:[0,0,0]
	v_mfma_scale_f32_16x16x128_f8f6f4 v[148:151], v[0:7], v[226:233], 0, v191, v191 op_sel_hi:[0,0,0]
	v_mfma_scale_f32_16x16x128_f8f6f4 v[144:147], v[8:15], v[226:233], 0, v191, v191 op_sel_hi:[0,0,0]
	v_mfma_scale_f32_16x16x128_f8f6f4 v[140:143], v[0:7], v[234:241], 0, v191, v191 op_sel_hi:[0,0,0]
	v_mfma_scale_f32_16x16x128_f8f6f4 v[136:139], v[8:15], v[234:241], 0, v191, v191 op_sel_hi:[0,0,0]
	v_mfma_scale_f32_16x16x128_f8f6f4 v[132:135], v[0:7], v[242:249], 0, v191, v191 op_sel_hi:[0,0,0]
	v_mfma_scale_f32_16x16x128_f8f6f4 v[128:131], v[8:15], v[242:249], 0, v191, v191 op_sel_hi:[0,0,0]
	s_setprio 0
	s_barrier
	s_mov_b32 m0, s30
	v_lshl_add_u64 v[182:183], s[26:27], 0, v[162:163]
	ds_read_b128 v[16:19], v193 offset:16384
	ds_read_b128 v[24:27], v193 offset:18432
	ds_read_b128 v[20:23], v195 offset:16384
	ds_read_b128 v[28:31], v195 offset:18432
	global_load_lds_dwordx4 v[182:183], off
	v_lshl_add_u64 v[184:185], s[26:27], 0, v[164:165]
	s_mov_b32 m0, s46
	s_nop 0
	global_load_lds_dwordx4 v[184:185], off
	s_barrier
	s_waitcnt lgkmcnt(0)
	s_setprio 1
	v_mfma_scale_f32_16x16x128_f8f6f4 v[92:95], v[16:23], v[218:225], 0, v191, v191 op_sel_hi:[0,0,0]
	v_mfma_scale_f32_16x16x128_f8f6f4 v[88:91], v[24:31], v[218:225], 0, v191, v191 op_sel_hi:[0,0,0]
	v_mfma_scale_f32_16x16x128_f8f6f4 v[84:87], v[16:23], v[226:233], 0, v191, v191 op_sel_hi:[0,0,0]
	v_mfma_scale_f32_16x16x128_f8f6f4 v[80:83], v[24:31], v[226:233], 0, v191, v191 op_sel_hi:[0,0,0]
	v_mfma_scale_f32_16x16x128_f8f6f4 v[76:79], v[16:23], v[234:241], 0, v191, v191 op_sel_hi:[0,0,0]
	v_mfma_scale_f32_16x16x128_f8f6f4 v[72:75], v[24:31], v[234:241], 0, v191, v191 op_sel_hi:[0,0,0]
	v_mfma_scale_f32_16x16x128_f8f6f4 v[68:71], v[16:23], v[242:249], 0, v191, v191 op_sel_hi:[0,0,0]
	v_mfma_scale_f32_16x16x128_f8f6f4 v[64:67], v[24:31], v[242:249], 0, v191, v191 op_sel_hi:[0,0,0]
	s_setprio 0
	s_mov_b32 m0, s47
	s_barrier
	ds_read_b128 v[218:221], v192 offset:16384
	ds_read_b128 v[226:229], v192 offset:18432
	ds_read_b128 v[222:225], v194 offset:16384
	ds_read_b128 v[230:233], v194 offset:18432
	ds_read_b128 v[234:237], v192 offset:20480
	ds_read_b128 v[242:245], v192 offset:22528
	ds_read_b128 v[238:241], v194 offset:20480
	ds_read_b128 v[246:249], v194 offset:22528
	global_load_lds_dwordx4 v172, s[28:29]
	s_mov_b32 m0, s83
	v_mov_b32_e32 v187, v173
	global_load_lds_dwordx4 v186, s[28:29]
	s_barrier
	s_waitcnt lgkmcnt(0)
	v_lshl_add_u64 v[188:189], s[28:29], 0, v[172:173]
	v_lshl_add_u64 v[186:187], s[28:29], 0, v[186:187]
	s_setprio 1
	v_mfma_scale_f32_16x16x128_f8f6f4 v[124:127], v[0:7], v[218:225], 0, v191, v191 op_sel_hi:[0,0,0]
	v_mfma_scale_f32_16x16x128_f8f6f4 v[120:123], v[8:15], v[218:225], 0, v191, v191 op_sel_hi:[0,0,0]
	v_mfma_scale_f32_16x16x128_f8f6f4 v[116:119], v[0:7], v[226:233], 0, v191, v191 op_sel_hi:[0,0,0]
	v_mfma_scale_f32_16x16x128_f8f6f4 v[112:115], v[8:15], v[226:233], 0, v191, v191 op_sel_hi:[0,0,0]
	v_mfma_scale_f32_16x16x128_f8f6f4 v[108:111], v[0:7], v[234:241], 0, v191, v191 op_sel_hi:[0,0,0]
	v_mfma_scale_f32_16x16x128_f8f6f4 v[104:107], v[8:15], v[234:241], 0, v191, v191 op_sel_hi:[0,0,0]
	v_mfma_scale_f32_16x16x128_f8f6f4 v[100:103], v[0:7], v[242:249], 0, v191, v191 op_sel_hi:[0,0,0]
	v_mfma_scale_f32_16x16x128_f8f6f4 v[96:99], v[8:15], v[242:249], 0, v191, v191 op_sel_hi:[0,0,0]
	s_setprio 0
	s_barrier
	s_add_u32 s72, s26, 0x20000
	s_addc_u32 s73, s27, 0
	s_mov_b32 m0, s82
	v_lshl_add_u64 v[0:1], s[72:73], 0, v[162:163]
	global_load_lds_dwordx4 v[0:1], off
	v_lshl_add_u64 v[0:1], s[72:73], 0, v[164:165]
	s_mov_b32 m0, s80
	s_nop 0
	global_load_lds_dwordx4 v[0:1], off
	s_waitcnt vmcnt(6)
	s_barrier
	s_setprio 1
	v_mfma_scale_f32_16x16x128_f8f6f4 v[60:63], v[16:23], v[218:225], 0, v191, v191 op_sel_hi:[0,0,0]
	v_mfma_scale_f32_16x16x128_f8f6f4 v[56:59], v[24:31], v[218:225], 0, v191, v191 op_sel_hi:[0,0,0]
	v_mfma_scale_f32_16x16x128_f8f6f4 v[52:55], v[16:23], v[226:233], 0, v191, v191 op_sel_hi:[0,0,0]
	v_mfma_scale_f32_16x16x128_f8f6f4 v[48:51], v[24:31], v[226:233], 0, v191, v191 op_sel_hi:[0,0,0]
	v_mfma_scale_f32_16x16x128_f8f6f4 v[44:47], v[16:23], v[234:241], 0, v191, v191 op_sel_hi:[0,0,0]
	v_mfma_scale_f32_16x16x128_f8f6f4 v[40:43], v[24:31], v[234:241], 0, v191, v191 op_sel_hi:[0,0,0]
	v_mfma_scale_f32_16x16x128_f8f6f4 v[36:39], v[16:23], v[242:249], 0, v191, v191 op_sel_hi:[0,0,0]
	v_mfma_scale_f32_16x16x128_f8f6f4 v[32:35], v[24:31], v[242:249], 0, v191, v191 op_sel_hi:[0,0,0]
	s_setprio 0
	s_barrier
	ds_read_b128 v[0:3], v193 offset:32768
	ds_read_b128 v[8:11], v193 offset:34816
	ds_read_b128 v[4:7], v195 offset:32768
	ds_read_b128 v[12:15], v195 offset:34816
	s_mov_b32 m0, s81
	v_lshl_add_u64 v[180:181], s[28:29], 0, v[180:181]
	ds_read_b128 v[16:19], v192 offset:32768
	ds_read_b128 v[24:27], v192 offset:34816
	ds_read_b128 v[20:23], v194 offset:32768
	ds_read_b128 v[28:31], v194 offset:34816
	ds_read_b128 v[218:221], v192 offset:36864
	ds_read_b128 v[226:229], v192 offset:38912
	ds_read_b128 v[222:225], v194 offset:36864
	ds_read_b128 v[230:233], v194 offset:38912
	global_load_lds_dwordx4 v[180:181], off
	v_lshl_add_u64 v[178:179], s[28:29], 0, v[178:179]
	s_mov_b32 m0, s50
	s_nop 0
	global_load_lds_dwordx4 v[178:179], off
	s_waitcnt lgkmcnt(8)
	s_barrier
	s_waitcnt lgkmcnt(0)
	s_setprio 1
	v_mfma_scale_f32_16x16x128_f8f6f4 v[156:159], v[0:7], v[16:23], v[156:159], v191, v191 op_sel_hi:[0,0,0]
	v_mfma_scale_f32_16x16x128_f8f6f4 v[152:155], v[8:15], v[16:23], v[152:155], v191, v191 op_sel_hi:[0,0,0]
	v_mfma_scale_f32_16x16x128_f8f6f4 v[148:151], v[0:7], v[24:31], v[148:151], v191, v191 op_sel_hi:[0,0,0]
	v_mfma_scale_f32_16x16x128_f8f6f4 v[144:147], v[8:15], v[24:31], v[144:147], v191, v191 op_sel_hi:[0,0,0]
	v_mfma_scale_f32_16x16x128_f8f6f4 v[140:143], v[0:7], v[218:225], v[140:143], v191, v191 op_sel_hi:[0,0,0]
	v_mfma_scale_f32_16x16x128_f8f6f4 v[136:139], v[8:15], v[218:225], v[136:139], v191, v191 op_sel_hi:[0,0,0]
	v_mfma_scale_f32_16x16x128_f8f6f4 v[132:135], v[0:7], v[226:233], v[132:135], v191, v191 op_sel_hi:[0,0,0]
	v_mfma_scale_f32_16x16x128_f8f6f4 v[128:131], v[8:15], v[226:233], v[128:131], v191, v191 op_sel_hi:[0,0,0]
	s_setprio 0
	s_barrier
	s_mov_b32 m0, s51
	v_lshl_add_u64 v[178:179], v[182:183], 0, s[40:41]
	ds_read_b128 v[234:237], v193 offset:49152
	ds_read_b128 v[242:245], v193 offset:51200
	ds_read_b128 v[238:241], v195 offset:49152
	ds_read_b128 v[246:249], v195 offset:51200
	global_load_lds_dwordx4 v[178:179], off
	v_lshl_add_u64 v[178:179], v[184:185], 0, s[40:41]
	s_mov_b32 m0, s70
	s_nop 0
	global_load_lds_dwordx4 v[178:179], off
	s_barrier
	s_waitcnt lgkmcnt(0)
	s_setprio 1
	v_mfma_scale_f32_16x16x128_f8f6f4 v[92:95], v[234:241], v[16:23], v[92:95], v191, v191 op_sel_hi:[0,0,0]
	v_mfma_scale_f32_16x16x128_f8f6f4 v[88:91], v[242:249], v[16:23], v[88:91], v191, v191 op_sel_hi:[0,0,0]
	v_mfma_scale_f32_16x16x128_f8f6f4 v[84:87], v[234:241], v[24:31], v[84:87], v191, v191 op_sel_hi:[0,0,0]
	v_mfma_scale_f32_16x16x128_f8f6f4 v[80:83], v[242:249], v[24:31], v[80:83], v191, v191 op_sel_hi:[0,0,0]
	v_mfma_scale_f32_16x16x128_f8f6f4 v[76:79], v[234:241], v[218:225], v[76:79], v191, v191 op_sel_hi:[0,0,0]
	v_mfma_scale_f32_16x16x128_f8f6f4 v[72:75], v[242:249], v[218:225], v[72:75], v191, v191 op_sel_hi:[0,0,0]
	v_mfma_scale_f32_16x16x128_f8f6f4 v[68:71], v[234:241], v[226:233], v[68:71], v191, v191 op_sel_hi:[0,0,0]
	v_mfma_scale_f32_16x16x128_f8f6f4 v[64:67], v[242:249], v[226:233], v[64:67], v191, v191 op_sel_hi:[0,0,0]
	s_setprio 0
	s_mov_b32 m0, s71
	v_lshl_add_u64 v[188:189], v[188:189], 0, s[40:41]
	s_barrier
	ds_read_b128 v[16:19], v192 offset:49152
	ds_read_b128 v[24:27], v192 offset:51200
	ds_read_b128 v[20:23], v194 offset:49152
	ds_read_b128 v[28:31], v194 offset:51200
	ds_read_b128 v[178:181], v192 offset:53248
	ds_read_b128 v[218:221], v192 offset:55296
	ds_read_b128 v[182:185], v194 offset:53248
	ds_read_b128 v[222:225], v194 offset:55296
	global_load_lds_dwordx4 v[188:189], off
	v_lshl_add_u64 v[186:187], v[186:187], 0, s[40:41]
	s_mov_b32 m0, s87
	s_nop 0
	global_load_lds_dwordx4 v[186:187], off
	s_barrier
	s_waitcnt lgkmcnt(0)
	s_setprio 1
	v_mfma_scale_f32_16x16x128_f8f6f4 v[124:127], v[0:7], v[16:23], v[124:127], v191, v191 op_sel_hi:[0,0,0]
	v_mfma_scale_f32_16x16x128_f8f6f4 v[120:123], v[8:15], v[16:23], v[120:123], v191, v191 op_sel_hi:[0,0,0]
	v_mfma_scale_f32_16x16x128_f8f6f4 v[116:119], v[0:7], v[24:31], v[116:119], v191, v191 op_sel_hi:[0,0,0]
	v_mfma_scale_f32_16x16x128_f8f6f4 v[112:115], v[8:15], v[24:31], v[112:115], v191, v191 op_sel_hi:[0,0,0]
	v_mfma_scale_f32_16x16x128_f8f6f4 v[108:111], v[0:7], v[178:185], v[108:111], v191, v191 op_sel_hi:[0,0,0]
	v_mfma_scale_f32_16x16x128_f8f6f4 v[104:107], v[8:15], v[178:185], v[104:107], v191, v191 op_sel_hi:[0,0,0]
	v_mfma_scale_f32_16x16x128_f8f6f4 v[100:103], v[0:7], v[218:225], v[100:103], v191, v191 op_sel_hi:[0,0,0]
	v_mfma_scale_f32_16x16x128_f8f6f4 v[96:99], v[8:15], v[218:225], v[96:99], v191, v191 op_sel_hi:[0,0,0]
	s_setprio 0
	s_barrier
	s_add_u32 s26, s26, 0x20080
	s_addc_u32 s27, s27, 0
	s_mov_b32 m0, s1
	v_lshl_add_u64 v[0:1], s[26:27], 0, v[162:163]
	global_load_lds_dwordx4 v[0:1], off
	v_lshl_add_u64 v[0:1], s[26:27], 0, v[164:165]
	s_mov_b32 m0, s56
	s_nop 0
	global_load_lds_dwordx4 v[0:1], off
	s_waitcnt vmcnt(6)
	s_barrier
	s_setprio 1
	v_mfma_scale_f32_16x16x128_f8f6f4 v[60:63], v[234:241], v[16:23], v[60:63], v191, v191 op_sel_hi:[0,0,0]
	v_mfma_scale_f32_16x16x128_f8f6f4 v[56:59], v[242:249], v[16:23], v[56:59], v191, v191 op_sel_hi:[0,0,0]
	v_mfma_scale_f32_16x16x128_f8f6f4 v[52:55], v[234:241], v[24:31], v[52:55], v191, v191 op_sel_hi:[0,0,0]
	v_mfma_scale_f32_16x16x128_f8f6f4 v[48:51], v[242:249], v[24:31], v[48:51], v191, v191 op_sel_hi:[0,0,0]
	v_mfma_scale_f32_16x16x128_f8f6f4 v[44:47], v[234:241], v[178:185], v[44:47], v191, v191 op_sel_hi:[0,0,0]
	v_mfma_scale_f32_16x16x128_f8f6f4 v[40:43], v[242:249], v[178:185], v[40:43], v191, v191 op_sel_hi:[0,0,0]
	v_mfma_scale_f32_16x16x128_f8f6f4 v[36:39], v[234:241], v[218:225], v[36:39], v191, v191 op_sel_hi:[0,0,0]
	v_mfma_scale_f32_16x16x128_f8f6f4 v[32:35], v[242:249], v[218:225], v[32:35], v191, v191 op_sel_hi:[0,0,0]
	s_setprio 0
	s_add_i32 s13, s13, 2
	s_add_u32 s24, s24, 0x100
	s_addc_u32 s25, s25, 0
	s_add_u32 s2, s2, 0x100
	s_addc_u32 s3, s3, 0
	s_cmp_gt_u32 s13, 5
	s_barrier
	s_branch .LBB0_539
.LBB0_538:
	ds_read_b128 v[0:3], v193
	ds_read_b128 v[8:11], v193 offset:2048
	ds_read_b128 v[4:7], v195
	ds_read_b128 v[12:15], v195 offset:2048
	s_add_u32 s15, s24, 0x80
	s_addc_u32 s23, s25, 0
	s_and_b64 s[26:27], s[26:27], exec
	s_cselect_b32 s29, s19, s23
	s_cselect_b32 s28, s18, s15
	s_cselect_b32 s27, s17, s3
	s_cselect_b32 s26, s16, s2
	v_lshl_add_u64 v[16:17], s[24:25], 0, v[168:169]
	s_add_i32 m0, s47, 0xc000
	ds_read_b128 v[218:221], v192
	ds_read_b128 v[226:229], v192 offset:2048
	ds_read_b128 v[222:225], v194
	ds_read_b128 v[230:233], v194 offset:2048
	ds_read_b128 v[234:237], v192 offset:4096
	ds_read_b128 v[242:245], v192 offset:6144
	ds_read_b128 v[238:241], v194 offset:4096
	ds_read_b128 v[246:249], v194 offset:6144
	global_load_lds_dwordx4 v[16:17], off
	v_lshl_add_u64 v[16:17], s[24:25], 0, v[174:175]
	s_add_i32 m0, s47, 0xe000
	s_nop 0
	global_load_lds_dwordx4 v[16:17], off
	s_waitcnt lgkmcnt(8)
	s_barrier
	s_waitcnt lgkmcnt(0)
	s_setprio 1
	v_mfma_scale_f32_16x16x128_f8f6f4 v[156:159], v[0:7], v[218:225], v[156:159], v191, v191 op_sel_hi:[0,0,0]
	v_mfma_scale_f32_16x16x128_f8f6f4 v[152:155], v[8:15], v[218:225], v[152:155], v191, v191 op_sel_hi:[0,0,0]
	v_mfma_scale_f32_16x16x128_f8f6f4 v[148:151], v[0:7], v[226:233], v[148:151], v191, v191 op_sel_hi:[0,0,0]
	v_mfma_scale_f32_16x16x128_f8f6f4 v[144:147], v[8:15], v[226:233], v[144:147], v191, v191 op_sel_hi:[0,0,0]
	v_mfma_scale_f32_16x16x128_f8f6f4 v[140:143], v[0:7], v[234:241], v[140:143], v191, v191 op_sel_hi:[0,0,0]
	v_mfma_scale_f32_16x16x128_f8f6f4 v[136:139], v[8:15], v[234:241], v[136:139], v191, v191 op_sel_hi:[0,0,0]
	v_mfma_scale_f32_16x16x128_f8f6f4 v[132:135], v[0:7], v[242:249], v[132:135], v191, v191 op_sel_hi:[0,0,0]
	v_mfma_scale_f32_16x16x128_f8f6f4 v[128:131], v[8:15], v[242:249], v[128:131], v191, v191 op_sel_hi:[0,0,0]
	s_setprio 0
	s_barrier
	s_mov_b32 m0, s30
	v_lshl_add_u64 v[182:183], s[26:27], 0, v[162:163]
	ds_read_b128 v[16:19], v193 offset:16384
	ds_read_b128 v[24:27], v193 offset:18432
	ds_read_b128 v[20:23], v195 offset:16384
	ds_read_b128 v[28:31], v195 offset:18432
	global_load_lds_dwordx4 v[182:183], off
	v_lshl_add_u64 v[184:185], s[26:27], 0, v[164:165]
	s_mov_b32 m0, s46
	s_nop 0
	global_load_lds_dwordx4 v[184:185], off
	s_barrier
	s_waitcnt lgkmcnt(0)
	s_setprio 1
	v_mfma_scale_f32_16x16x128_f8f6f4 v[92:95], v[16:23], v[218:225], v[92:95], v191, v191 op_sel_hi:[0,0,0]
	v_mfma_scale_f32_16x16x128_f8f6f4 v[88:91], v[24:31], v[218:225], v[88:91], v191, v191 op_sel_hi:[0,0,0]
	v_mfma_scale_f32_16x16x128_f8f6f4 v[84:87], v[16:23], v[226:233], v[84:87], v191, v191 op_sel_hi:[0,0,0]
	v_mfma_scale_f32_16x16x128_f8f6f4 v[80:83], v[24:31], v[226:233], v[80:83], v191, v191 op_sel_hi:[0,0,0]
	v_mfma_scale_f32_16x16x128_f8f6f4 v[76:79], v[16:23], v[234:241], v[76:79], v191, v191 op_sel_hi:[0,0,0]
	v_mfma_scale_f32_16x16x128_f8f6f4 v[72:75], v[24:31], v[234:241], v[72:75], v191, v191 op_sel_hi:[0,0,0]
	v_mfma_scale_f32_16x16x128_f8f6f4 v[68:71], v[16:23], v[242:249], v[68:71], v191, v191 op_sel_hi:[0,0,0]
	v_mfma_scale_f32_16x16x128_f8f6f4 v[64:67], v[24:31], v[242:249], v[64:67], v191, v191 op_sel_hi:[0,0,0]
	s_setprio 0
	s_mov_b32 m0, s47
	s_barrier
	ds_read_b128 v[218:221], v192 offset:16384
	ds_read_b128 v[226:229], v192 offset:18432
	ds_read_b128 v[222:225], v194 offset:16384
	ds_read_b128 v[230:233], v194 offset:18432
	ds_read_b128 v[234:237], v192 offset:20480
	ds_read_b128 v[242:245], v192 offset:22528
	ds_read_b128 v[238:241], v194 offset:20480
	ds_read_b128 v[246:249], v194 offset:22528
	global_load_lds_dwordx4 v172, s[28:29]
	s_mov_b32 m0, s83
	v_mov_b32_e32 v187, v173
	global_load_lds_dwordx4 v186, s[28:29]
	s_barrier
	s_waitcnt lgkmcnt(0)
	v_lshl_add_u64 v[188:189], s[28:29], 0, v[172:173]
	v_lshl_add_u64 v[186:187], s[28:29], 0, v[186:187]
	s_setprio 1
	v_mfma_scale_f32_16x16x128_f8f6f4 v[124:127], v[0:7], v[218:225], v[124:127], v191, v191 op_sel_hi:[0,0,0]
	v_mfma_scale_f32_16x16x128_f8f6f4 v[120:123], v[8:15], v[218:225], v[120:123], v191, v191 op_sel_hi:[0,0,0]
	v_mfma_scale_f32_16x16x128_f8f6f4 v[116:119], v[0:7], v[226:233], v[116:119], v191, v191 op_sel_hi:[0,0,0]
	v_mfma_scale_f32_16x16x128_f8f6f4 v[112:115], v[8:15], v[226:233], v[112:115], v191, v191 op_sel_hi:[0,0,0]
	v_mfma_scale_f32_16x16x128_f8f6f4 v[108:111], v[0:7], v[234:241], v[108:111], v191, v191 op_sel_hi:[0,0,0]
	v_mfma_scale_f32_16x16x128_f8f6f4 v[104:107], v[8:15], v[234:241], v[104:107], v191, v191 op_sel_hi:[0,0,0]
	v_mfma_scale_f32_16x16x128_f8f6f4 v[100:103], v[0:7], v[242:249], v[100:103], v191, v191 op_sel_hi:[0,0,0]
	v_mfma_scale_f32_16x16x128_f8f6f4 v[96:99], v[8:15], v[242:249], v[96:99], v191, v191 op_sel_hi:[0,0,0]
	s_setprio 0
	s_barrier
	s_add_u32 s72, s26, 0x20000
	s_addc_u32 s73, s27, 0
	s_mov_b32 m0, s82
	v_lshl_add_u64 v[0:1], s[72:73], 0, v[162:163]
	global_load_lds_dwordx4 v[0:1], off
	v_lshl_add_u64 v[0:1], s[72:73], 0, v[164:165]
	s_mov_b32 m0, s80
	s_nop 0
	global_load_lds_dwordx4 v[0:1], off
	s_waitcnt vmcnt(6)
	s_barrier
	s_setprio 1
	v_mfma_scale_f32_16x16x128_f8f6f4 v[60:63], v[16:23], v[218:225], v[60:63], v191, v191 op_sel_hi:[0,0,0]
	v_mfma_scale_f32_16x16x128_f8f6f4 v[56:59], v[24:31], v[218:225], v[56:59], v191, v191 op_sel_hi:[0,0,0]
	v_mfma_scale_f32_16x16x128_f8f6f4 v[52:55], v[16:23], v[226:233], v[52:55], v191, v191 op_sel_hi:[0,0,0]
	v_mfma_scale_f32_16x16x128_f8f6f4 v[48:51], v[24:31], v[226:233], v[48:51], v191, v191 op_sel_hi:[0,0,0]
	v_mfma_scale_f32_16x16x128_f8f6f4 v[44:47], v[16:23], v[234:241], v[44:47], v191, v191 op_sel_hi:[0,0,0]
	v_mfma_scale_f32_16x16x128_f8f6f4 v[40:43], v[24:31], v[234:241], v[40:43], v191, v191 op_sel_hi:[0,0,0]
	v_mfma_scale_f32_16x16x128_f8f6f4 v[36:39], v[16:23], v[242:249], v[36:39], v191, v191 op_sel_hi:[0,0,0]
	v_mfma_scale_f32_16x16x128_f8f6f4 v[32:35], v[24:31], v[242:249], v[32:35], v191, v191 op_sel_hi:[0,0,0]
	s_setprio 0
	s_barrier
	ds_read_b128 v[0:3], v193 offset:32768
	ds_read_b128 v[8:11], v193 offset:34816
	ds_read_b128 v[4:7], v195 offset:32768
	ds_read_b128 v[12:15], v195 offset:34816
	s_mov_b32 m0, s81
	v_lshl_add_u64 v[180:181], s[28:29], 0, v[180:181]
	ds_read_b128 v[16:19], v192 offset:32768
	ds_read_b128 v[24:27], v192 offset:34816
	ds_read_b128 v[20:23], v194 offset:32768
	ds_read_b128 v[28:31], v194 offset:34816
	ds_read_b128 v[218:221], v192 offset:36864
	ds_read_b128 v[226:229], v192 offset:38912
	ds_read_b128 v[222:225], v194 offset:36864
	ds_read_b128 v[230:233], v194 offset:38912
	global_load_lds_dwordx4 v[180:181], off
	v_lshl_add_u64 v[178:179], s[28:29], 0, v[178:179]
	s_mov_b32 m0, s50
	s_nop 0
	global_load_lds_dwordx4 v[178:179], off
	s_waitcnt lgkmcnt(8)
	s_barrier
	s_waitcnt lgkmcnt(0)
	s_setprio 1
	v_mfma_scale_f32_16x16x128_f8f6f4 v[156:159], v[0:7], v[16:23], v[156:159], v191, v191 op_sel_hi:[0,0,0]
	v_mfma_scale_f32_16x16x128_f8f6f4 v[152:155], v[8:15], v[16:23], v[152:155], v191, v191 op_sel_hi:[0,0,0]
	v_mfma_scale_f32_16x16x128_f8f6f4 v[148:151], v[0:7], v[24:31], v[148:151], v191, v191 op_sel_hi:[0,0,0]
	v_mfma_scale_f32_16x16x128_f8f6f4 v[144:147], v[8:15], v[24:31], v[144:147], v191, v191 op_sel_hi:[0,0,0]
	v_mfma_scale_f32_16x16x128_f8f6f4 v[140:143], v[0:7], v[218:225], v[140:143], v191, v191 op_sel_hi:[0,0,0]
	v_mfma_scale_f32_16x16x128_f8f6f4 v[136:139], v[8:15], v[218:225], v[136:139], v191, v191 op_sel_hi:[0,0,0]
	v_mfma_scale_f32_16x16x128_f8f6f4 v[132:135], v[0:7], v[226:233], v[132:135], v191, v191 op_sel_hi:[0,0,0]
	v_mfma_scale_f32_16x16x128_f8f6f4 v[128:131], v[8:15], v[226:233], v[128:131], v191, v191 op_sel_hi:[0,0,0]
	s_setprio 0
	s_barrier
	s_mov_b32 m0, s51
	v_lshl_add_u64 v[178:179], v[182:183], 0, s[40:41]
	ds_read_b128 v[234:237], v193 offset:49152
	ds_read_b128 v[242:245], v193 offset:51200
	ds_read_b128 v[238:241], v195 offset:49152
	ds_read_b128 v[246:249], v195 offset:51200
	global_load_lds_dwordx4 v[178:179], off
	v_lshl_add_u64 v[178:179], v[184:185], 0, s[40:41]
	s_mov_b32 m0, s70
	s_nop 0
	global_load_lds_dwordx4 v[178:179], off
	s_barrier
	s_waitcnt lgkmcnt(0)
	s_setprio 1
	v_mfma_scale_f32_16x16x128_f8f6f4 v[92:95], v[234:241], v[16:23], v[92:95], v191, v191 op_sel_hi:[0,0,0]
	v_mfma_scale_f32_16x16x128_f8f6f4 v[88:91], v[242:249], v[16:23], v[88:91], v191, v191 op_sel_hi:[0,0,0]
	v_mfma_scale_f32_16x16x128_f8f6f4 v[84:87], v[234:241], v[24:31], v[84:87], v191, v191 op_sel_hi:[0,0,0]
	v_mfma_scale_f32_16x16x128_f8f6f4 v[80:83], v[242:249], v[24:31], v[80:83], v191, v191 op_sel_hi:[0,0,0]
	v_mfma_scale_f32_16x16x128_f8f6f4 v[76:79], v[234:241], v[218:225], v[76:79], v191, v191 op_sel_hi:[0,0,0]
	v_mfma_scale_f32_16x16x128_f8f6f4 v[72:75], v[242:249], v[218:225], v[72:75], v191, v191 op_sel_hi:[0,0,0]
	v_mfma_scale_f32_16x16x128_f8f6f4 v[68:71], v[234:241], v[226:233], v[68:71], v191, v191 op_sel_hi:[0,0,0]
	v_mfma_scale_f32_16x16x128_f8f6f4 v[64:67], v[242:249], v[226:233], v[64:67], v191, v191 op_sel_hi:[0,0,0]
	s_setprio 0
	s_mov_b32 m0, s71
	v_lshl_add_u64 v[188:189], v[188:189], 0, s[40:41]
	s_barrier
	ds_read_b128 v[16:19], v192 offset:49152
	ds_read_b128 v[24:27], v192 offset:51200
	ds_read_b128 v[20:23], v194 offset:49152
	ds_read_b128 v[28:31], v194 offset:51200
	ds_read_b128 v[178:181], v192 offset:53248
	ds_read_b128 v[218:221], v192 offset:55296
	ds_read_b128 v[182:185], v194 offset:53248
	ds_read_b128 v[222:225], v194 offset:55296
	global_load_lds_dwordx4 v[188:189], off
	v_lshl_add_u64 v[186:187], v[186:187], 0, s[40:41]
	s_mov_b32 m0, s87
	s_nop 0
	global_load_lds_dwordx4 v[186:187], off
	s_barrier
	s_waitcnt lgkmcnt(0)
	s_setprio 1
	v_mfma_scale_f32_16x16x128_f8f6f4 v[124:127], v[0:7], v[16:23], v[124:127], v191, v191 op_sel_hi:[0,0,0]
	v_mfma_scale_f32_16x16x128_f8f6f4 v[120:123], v[8:15], v[16:23], v[120:123], v191, v191 op_sel_hi:[0,0,0]
	v_mfma_scale_f32_16x16x128_f8f6f4 v[116:119], v[0:7], v[24:31], v[116:119], v191, v191 op_sel_hi:[0,0,0]
	v_mfma_scale_f32_16x16x128_f8f6f4 v[112:115], v[8:15], v[24:31], v[112:115], v191, v191 op_sel_hi:[0,0,0]
	v_mfma_scale_f32_16x16x128_f8f6f4 v[108:111], v[0:7], v[178:185], v[108:111], v191, v191 op_sel_hi:[0,0,0]
	v_mfma_scale_f32_16x16x128_f8f6f4 v[104:107], v[8:15], v[178:185], v[104:107], v191, v191 op_sel_hi:[0,0,0]
	v_mfma_scale_f32_16x16x128_f8f6f4 v[100:103], v[0:7], v[218:225], v[100:103], v191, v191 op_sel_hi:[0,0,0]
	v_mfma_scale_f32_16x16x128_f8f6f4 v[96:99], v[8:15], v[218:225], v[96:99], v191, v191 op_sel_hi:[0,0,0]
	s_setprio 0
	s_barrier
	s_add_u32 s26, s26, 0x20080
	s_addc_u32 s27, s27, 0
	s_mov_b32 m0, s1
	v_lshl_add_u64 v[0:1], s[26:27], 0, v[162:163]
	global_load_lds_dwordx4 v[0:1], off
	v_lshl_add_u64 v[0:1], s[26:27], 0, v[164:165]
	s_mov_b32 m0, s56
	s_nop 0
	global_load_lds_dwordx4 v[0:1], off
	s_waitcnt vmcnt(6)
	s_barrier
	s_setprio 1
	v_mfma_scale_f32_16x16x128_f8f6f4 v[60:63], v[234:241], v[16:23], v[60:63], v191, v191 op_sel_hi:[0,0,0]
	v_mfma_scale_f32_16x16x128_f8f6f4 v[56:59], v[242:249], v[16:23], v[56:59], v191, v191 op_sel_hi:[0,0,0]
	v_mfma_scale_f32_16x16x128_f8f6f4 v[52:55], v[234:241], v[24:31], v[52:55], v191, v191 op_sel_hi:[0,0,0]
	v_mfma_scale_f32_16x16x128_f8f6f4 v[48:51], v[242:249], v[24:31], v[48:51], v191, v191 op_sel_hi:[0,0,0]
	v_mfma_scale_f32_16x16x128_f8f6f4 v[44:47], v[234:241], v[178:185], v[44:47], v191, v191 op_sel_hi:[0,0,0]
	v_mfma_scale_f32_16x16x128_f8f6f4 v[40:43], v[242:249], v[178:185], v[40:43], v191, v191 op_sel_hi:[0,0,0]
	v_mfma_scale_f32_16x16x128_f8f6f4 v[36:39], v[234:241], v[218:225], v[36:39], v191, v191 op_sel_hi:[0,0,0]
	v_mfma_scale_f32_16x16x128_f8f6f4 v[32:35], v[242:249], v[218:225], v[32:35], v191, v191 op_sel_hi:[0,0,0]
	s_setprio 0
	s_add_i32 s13, s13, 2
	s_add_u32 s24, s24, 0x100
	s_addc_u32 s25, s25, 0
	s_add_u32 s2, s2, 0x100
	s_addc_u32 s3, s3, 0
	s_cmp_gt_u32 s13, 5
	s_barrier
	s_cbranch_scc1 .LBB0_541

.LBB0_579:
	s_waitcnt vmcnt(0)
	v_add_u32_e32 v12, s13, v88
	v_add_u32_e32 v4, 0x45, v12
	v_ashrrev_i32_e32 v13, 31, v12
	v_ashrrev_i32_e32 v5, 31, v4
	v_lshlrev_b64 v[0:1], 13, v[12:13]
	v_lshlrev_b64 v[4:5], 13, v[4:5]
	v_lshl_add_u64 v[0:1], v[64:65], 0, v[0:1]
	v_lshl_add_u64 v[4:5], v[64:65], 0, v[4:5]
	global_load_dwordx4 v[48:51], v[0:1], off nt
	v_add_u32_e32 v8, 0x46, v12
	global_load_dwordx4 v[4:7], v[4:5], off nt
	v_or_b32_e32 v0, 1, v12
	v_ashrrev_i32_e32 v1, 31, v0
	v_ashrrev_i32_e32 v9, 31, v8
	v_lshlrev_b64 v[0:1], 13, v[0:1]
	v_lshlrev_b64 v[8:9], 13, v[8:9]
	v_lshl_add_u64 v[0:1], v[64:65], 0, v[0:1]
	v_lshl_add_u64 v[8:9], v[64:65], 0, v[8:9]
	global_load_dwordx4 v[52:55], v[0:1], off nt
	global_load_dwordx4 v[8:11], v[8:9], off nt
	v_or_b32_e32 v0, 2, v12
	v_ashrrev_i32_e32 v1, 31, v0
	v_lshlrev_b64 v[0:1], 13, v[0:1]
	v_lshl_add_u64 v[0:1], v[64:65], 0, v[0:1]
	global_load_dwordx4 v[56:59], v[0:1], off nt
	v_or_b32_e32 v0, 3, v12
	v_ashrrev_i32_e32 v1, 31, v0
	v_lshlrev_b64 v[0:1], 13, v[0:1]
	v_lshl_add_u64 v[0:1], v[64:65], 0, v[0:1]
	global_load_dwordx4 v[60:63], v[0:1], off nt
	v_or_b32_e32 v0, 4, v12
	v_ashrrev_i32_e32 v1, 31, v0
	v_lshlrev_b64 v[0:1], 13, v[0:1]
	v_lshl_add_u64 v[0:1], v[64:65], 0, v[0:1]
	global_load_dwordx4 v[32:35], v[0:1], off nt
	v_or_b32_e32 v0, 5, v12
	v_ashrrev_i32_e32 v1, 31, v0
	v_lshlrev_b64 v[0:1], 13, v[0:1]
	v_lshl_add_u64 v[0:1], v[64:65], 0, v[0:1]
	global_load_dwordx4 v[36:39], v[0:1], off nt
	v_or_b32_e32 v0, 6, v12
	v_ashrrev_i32_e32 v1, 31, v0
	v_lshlrev_b64 v[0:1], 13, v[0:1]
	v_lshl_add_u64 v[0:1], v[64:65], 0, v[0:1]
	global_load_dwordx4 v[40:43], v[0:1], off nt
	v_or_b32_e32 v0, 7, v12
	v_ashrrev_i32_e32 v1, 31, v0
	v_lshlrev_b64 v[0:1], 13, v[0:1]
	v_lshl_add_u64 v[0:1], v[64:65], 0, v[0:1]
	global_load_dwordx4 v[44:47], v[0:1], off nt
	v_add_u32_e32 v0, 64, v12
	v_ashrrev_i32_e32 v1, 31, v0
	v_lshlrev_b64 v[0:1], 13, v[0:1]
	v_lshl_add_u64 v[0:1], v[64:65], 0, v[0:1]
	global_load_dwordx4 v[16:19], v[0:1], off nt
	v_add_u32_e32 v0, 0x41, v12
	v_ashrrev_i32_e32 v1, 31, v0
	v_lshlrev_b64 v[0:1], 13, v[0:1]
	v_lshl_add_u64 v[0:1], v[64:65], 0, v[0:1]
	global_load_dwordx4 v[20:23], v[0:1], off nt
	v_add_u32_e32 v0, 0x42, v12
	v_ashrrev_i32_e32 v1, 31, v0
	v_lshlrev_b64 v[0:1], 13, v[0:1]
	v_lshl_add_u64 v[0:1], v[64:65], 0, v[0:1]
	global_load_dwordx4 v[24:27], v[0:1], off nt
	v_add_u32_e32 v0, 0x43, v12
	v_ashrrev_i32_e32 v1, 31, v0
	v_lshlrev_b64 v[0:1], 13, v[0:1]
	v_lshl_add_u64 v[0:1], v[64:65], 0, v[0:1]
	global_load_dwordx4 v[28:31], v[0:1], off nt
	v_add_u32_e32 v0, 0x44, v12
	v_ashrrev_i32_e32 v1, 31, v0
	v_lshlrev_b64 v[0:1], 13, v[0:1]
	v_lshl_add_u64 v[0:1], v[64:65], 0, v[0:1]
	global_load_dwordx4 v[0:3], v[0:1], off nt
	v_add_u32_e32 v12, 0x47, v12
	v_ashrrev_i32_e32 v13, 31, v12
	v_lshlrev_b64 v[12:13], 13, v[12:13]
	v_lshl_add_u64 v[12:13], v[64:65], 0, v[12:13]
	global_load_dwordx4 v[12:15], v[12:13], off nt
	s_and_b64 vcc, exec, s[10:11]
	s_mov_b64 s[10:11], 0
	s_waitcnt vmcnt(15)
	v_mul_f32_e32 v48, 0x42000000, v48
	s_waitcnt vmcnt(14)
	v_mul_f32_e32 v4, 0x42000000, v4
	v_mul_f32_e32 v5, 0x42000000, v5
	s_waitcnt vmcnt(13)
	v_mul_f32_e32 v52, 0x42000000, v52
	v_cvt_pk_fp8_f32 v66, v48, v52
	s_waitcnt vmcnt(12)
	v_mul_f32_e32 v8, 0x42000000, v8
	s_waitcnt vmcnt(11)
	v_mul_f32_e32 v48, 0x42000000, v57
	v_mul_f32_e32 v56, 0x42000000, v56
	s_waitcnt vmcnt(10)
	v_mul_f32_e32 v60, 0x42000000, v60
	v_cvt_pk_fp8_f32 v66, v56, v60 op_sel:[0,0,1]
	s_waitcnt vmcnt(9)
	v_mul_f32_e32 v32, 0x42000000, v32
	s_waitcnt vmcnt(8)
	v_mul_f32_e32 v36, 0x42000000, v36
	v_cvt_pk_fp8_f32 v67, v32, v36
	v_mul_f32_e32 v32, 0x42000000, v49
	v_mul_f32_e32 v36, 0x42000000, v53
	v_mul_f32_e32 v49, 0x42000000, v61
	s_waitcnt vmcnt(7)
	v_mul_f32_e32 v40, 0x42000000, v40
	s_waitcnt vmcnt(6)
	v_mul_f32_e32 v44, 0x42000000, v44
	v_cvt_pk_fp8_f32 v67, v40, v44 op_sel:[0,0,1]
	v_cvt_pk_fp8_f32 v40, v32, v36
	v_mul_f32_e32 v32, 0x42000000, v33
	v_mul_f32_e32 v33, 0x42000000, v37
	v_mul_f32_e32 v36, 0x42000000, v41
	v_cvt_pk_fp8_f32 v41, v32, v33
	v_mul_f32_e32 v37, 0x42000000, v45
	v_mul_f32_e32 v32, 0x42000000, v50
	v_mul_f32_e32 v33, 0x42000000, v54
	v_cvt_pk_fp8_f32 v41, v36, v37 op_sel:[0,0,1]
	v_cvt_pk_fp8_f32 v36, v32, v33
	v_mul_f32_e32 v37, 0x42000000, v58
	v_mul_f32_e32 v45, 0x42000000, v62
	v_mul_f32_e32 v32, 0x42000000, v34
	v_cvt_pk_fp8_f32 v36, v37, v45 op_sel:[0,0,1]
	v_mul_f32_e32 v33, 0x42000000, v38
	v_cvt_pk_fp8_f32 v37, v32, v33
	v_mul_f32_e32 v34, 0x42000000, v42
	v_mul_f32_e32 v38, 0x42000000, v46
	v_mul_f32_e32 v33, 0x42000000, v51
	v_cvt_pk_fp8_f32 v37, v34, v38 op_sel:[0,0,1]
	v_mul_f32_e32 v34, 0x42000000, v55
	v_cvt_pk_fp8_f32 v32, v33, v34
	v_mul_f32_e32 v34, 0x42000000, v35
	v_mul_f32_e32 v35, 0x42000000, v39
	v_cvt_pk_fp8_f32 v33, v34, v35
	s_waitcnt vmcnt(1)
	v_mul_f32_e32 v0, 0x42000000, v0
	v_cvt_pk_fp8_f32 v35, v0, v4
	s_waitcnt vmcnt(0)
	v_mul_f32_e32 v12, 0x42000000, v12
	v_mul_f32_e32 v4, 0x42000000, v17
	v_cvt_pk_fp8_f32 v35, v8, v12 op_sel:[0,0,1]
	v_mul_f32_e32 v8, 0x42000000, v21
	v_cvt_pk_fp8_f32 v0, v4, v8
	v_mul_f32_e32 v4, 0x42000000, v1
	v_cvt_pk_fp8_f32 v1, v4, v5
	v_mul_f32_e32 v16, 0x42000000, v16
	v_mul_f32_e32 v20, 0x42000000, v20
	v_cvt_pk_fp8_f32 v34, v16, v20
	v_mul_f32_e32 v12, 0x42000000, v25
	v_mul_f32_e32 v16, 0x42000000, v29
	v_mul_f32_e32 v8, 0x42000000, v9
	v_mul_f32_e32 v9, 0x42000000, v13
	v_cvt_pk_fp8_f32 v40, v48, v49 op_sel:[0,0,1]
	v_cvt_pk_fp8_f32 v0, v12, v16 op_sel:[0,0,1]
	v_cvt_pk_fp8_f32 v1, v8, v9 op_sel:[0,0,1]
	v_add_u32_e32 v44, s13, v76
	v_mul_f32_e32 v4, 0x42000000, v22
	v_mul_f32_e32 v2, 0x42000000, v2
	ds_write2_b64 v44, v[40:41], v[0:1] offset0:34 offset1:42
	v_mul_f32_e32 v1, 0x42000000, v18
	v_cvt_pk_fp8_f32 v0, v1, v4
	v_mul_f32_e32 v4, 0x42000000, v6
	v_cvt_pk_fp8_f32 v1, v2, v4
	v_mul_f32_e32 v5, 0x42000000, v26
	v_mul_f32_e32 v8, 0x42000000, v30
	v_cvt_pk_fp8_f32 v0, v5, v8 op_sel:[0,0,1]
	v_mul_f32_e32 v5, 0x42000000, v10
	v_mul_f32_e32 v6, 0x42000000, v14
	v_cvt_pk_fp8_f32 v1, v5, v6 op_sel:[0,0,1]
	v_mul_f32_e32 v2, 0x42000000, v23
	v_mul_f32_e32 v38, 0x42000000, v59
	v_mul_f32_e32 v42, 0x42000000, v63
	ds_write2_b64 v44, v[36:37], v[0:1] offset0:68 offset1:76
	v_mul_f32_e32 v1, 0x42000000, v19
	v_cvt_pk_fp8_f32 v0, v1, v2
	v_mul_f32_e32 v2, 0x42000000, v3
	v_mul_f32_e32 v3, 0x42000000, v7
	v_cvt_pk_fp8_f32 v1, v2, v3
	v_mul_f32_e32 v4, 0x42000000, v27
	v_mul_f32_e32 v5, 0x42000000, v31
	v_cvt_pk_fp8_f32 v32, v38, v42 op_sel:[0,0,1]
	v_mul_f32_e32 v38, 0x42000000, v43
	v_mul_f32_e32 v39, 0x42000000, v47
	v_mul_f32_e32 v24, 0x42000000, v24
	v_mul_f32_e32 v28, 0x42000000, v28
	v_cvt_pk_fp8_f32 v0, v4, v5 op_sel:[0,0,1]
	v_mul_f32_e32 v4, 0x42000000, v11
	v_mul_f32_e32 v5, 0x42000000, v15
	v_cvt_pk_fp8_f32 v33, v38, v39 op_sel:[0,0,1]
	v_cvt_pk_fp8_f32 v34, v24, v28 op_sel:[0,0,1]
	v_cvt_pk_fp8_f32 v1, v4, v5 op_sel:[0,0,1]
	s_movk_i32 s13, 0x80
	ds_write2_b64 v44, v[66:67], v[34:35] offset1:8
	ds_write2_b64 v44, v[32:33], v[0:1] offset0:102 offset1:110
	s_cbranch_vccnz .LBB0_579
	s_lshl_b64 s[8:9], s[8:9], 21
	s_add_u32 s8, s95, s8
	s_addc_u32 s9, s97, s9
	s_lshl_b32 s2, s2, 8
	s_waitcnt lgkmcnt(0)
	s_barrier
	v_add_u32_e32 v88, v80, v172
	s_ashr_i32 s10, s3, 31
	ds_read_b128 v[0:3], v88
	v_add_u32_e32 v4, s2, v75
	s_add_u32 s8, s8, s3
	v_ashrrev_i32_e32 v5, 31, v4
	s_addc_u32 s9, s9, s10
	v_lshlrev_b64 v[4:5], 10, v[4:5]
	v_lshl_add_u64 v[4:5], s[8:9], 0, v[4:5]
	v_lshl_add_u64 v[4:5], v[4:5], 0, v[172:173]
	v_add_u32_e32 v89, v81, v172
	s_waitcnt lgkmcnt(0)
	global_store_dwordx4 v[4:5], v[0:3], off sc1
	ds_read_b128 v[0:3], v89
	v_add_u32_e32 v4, s2, v74
	v_ashrrev_i32_e32 v5, 31, v4
	v_lshlrev_b64 v[4:5], 10, v[4:5]
	v_lshl_add_u64 v[4:5], s[8:9], 0, v[4:5]
	v_lshl_add_u64 v[4:5], v[4:5], 0, v[172:173]
	v_add_u32_e32 v90, v82, v172
	s_waitcnt lgkmcnt(0)
	global_store_dwordx4 v[4:5], v[0:3], off sc1
	ds_read_b128 v[0:3], v90
	v_add_u32_e32 v4, s2, v73
	v_ashrrev_i32_e32 v5, 31, v4
	v_lshlrev_b64 v[4:5], 10, v[4:5]
	v_lshl_add_u64 v[4:5], s[8:9], 0, v[4:5]
	v_lshl_add_u64 v[4:5], v[4:5], 0, v[172:173]
	v_add_u32_e32 v91, v83, v172
	s_waitcnt lgkmcnt(0)
	global_store_dwordx4 v[4:5], v[0:3], off sc1
	ds_read_b128 v[0:3], v91
	v_add_u32_e32 v4, s2, v72
	v_ashrrev_i32_e32 v5, 31, v4
	v_lshlrev_b64 v[4:5], 10, v[4:5]
	v_lshl_add_u64 v[4:5], s[8:9], 0, v[4:5]
	v_lshl_add_u64 v[4:5], v[4:5], 0, v[172:173]
	v_add_u32_e32 v92, v84, v172
	s_waitcnt lgkmcnt(0)
	global_store_dwordx4 v[4:5], v[0:3], off sc1
	ds_read_b128 v[0:3], v92
	v_add_u32_e32 v4, s2, v71
	v_ashrrev_i32_e32 v5, 31, v4
	v_lshlrev_b64 v[4:5], 10, v[4:5]
	v_lshl_add_u64 v[4:5], s[8:9], 0, v[4:5]
	v_lshl_add_u64 v[4:5], v[4:5], 0, v[172:173]
	v_add_u32_e32 v93, v85, v172
	s_waitcnt lgkmcnt(0)
	global_store_dwordx4 v[4:5], v[0:3], off sc1
	ds_read_b128 v[0:3], v93
	v_add_u32_e32 v4, s2, v70
	v_ashrrev_i32_e32 v5, 31, v4
	v_lshlrev_b64 v[4:5], 10, v[4:5]
	v_lshl_add_u64 v[4:5], s[8:9], 0, v[4:5]
	v_lshl_add_u64 v[4:5], v[4:5], 0, v[172:173]
	v_add_u32_e32 v94, v86, v172
	s_waitcnt lgkmcnt(0)
	global_store_dwordx4 v[4:5], v[0:3], off sc1
	ds_read_b128 v[0:3], v94
	v_add_u32_e32 v4, s2, v69
	v_ashrrev_i32_e32 v5, 31, v4
	v_lshlrev_b64 v[4:5], 10, v[4:5]
	v_lshl_add_u64 v[4:5], s[8:9], 0, v[4:5]
	v_lshl_add_u64 v[4:5], v[4:5], 0, v[172:173]
	v_add_u32_e32 v95, v87, v172
	s_waitcnt lgkmcnt(0)
	global_store_dwordx4 v[4:5], v[0:3], off sc1
	ds_read_b128 v[0:3], v95
	v_add_u32_e32 v4, s2, v68
	v_ashrrev_i32_e32 v5, 31, v4
	v_lshlrev_b64 v[4:5], 10, v[4:5]
	v_lshl_add_u64 v[4:5], s[8:9], 0, v[4:5]
	v_lshl_add_u64 v[4:5], v[4:5], 0, v[172:173]
	s_waitcnt lgkmcnt(0)
	global_store_dwordx4 v[4:5], v[0:3], off sc1
	s_barrier
	s_movk_i32 s8, 0xff60
	s_mov_b64 s[2:3], 0
	s_and_b64 vcc, exec, s[6:7]
	s_cbranch_vccz .LBB0_578
	v_readlane_b32 s0, v250, 60
	s_add_i32 s2, s0, s1
	s_ashr_i32 s3, s2, 31
	v_readlane_b32 s8, v255, 19
	s_lshl_b64 s[4:5], s[2:3], 20
	s_lshl_b64 s[2:3], s[2:3], 22
	v_readlane_b32 s14, v255, 25
	v_readlane_b32 s0, v250, 61
	v_readlane_b32 s15, v255, 26
	s_add_u32 s2, s14, s2
	v_or_b32_e32 v0, s0, v77
	s_addc_u32 s3, s15, s3
	v_readlane_b32 s0, v250, 63
	v_ashrrev_i32_e32 v1, 31, v0
	v_lshl_add_u64 v[64:65], v[0:1], 2, s[2:3]
	v_add_u32_e32 v77, s0, v78
	s_mov_b32 s1, 0
	s_mov_b64 s[6:7], -1
	v_readlane_b32 s9, v255, 20
	v_readlane_b32 s10, v255, 21
	v_readlane_b32 s11, v255, 22
	v_readlane_b32 s12, v255, 23
	v_readlane_b32 s13, v255, 24
.LBB0_582:
	v_add_u32_e32 v12, s1, v77
	v_add_u32_e32 v4, 0x45, v12
	v_ashrrev_i32_e32 v13, 31, v12
	v_ashrrev_i32_e32 v5, 31, v4
	v_lshlrev_b64 v[0:1], 12, v[12:13]
	v_lshlrev_b64 v[4:5], 12, v[4:5]
	v_lshl_add_u64 v[0:1], v[64:65], 0, v[0:1]
	v_lshl_add_u64 v[4:5], v[64:65], 0, v[4:5]
	global_load_dwordx4 v[48:51], v[0:1], off nt
	v_add_u32_e32 v8, 0x46, v12
	global_load_dwordx4 v[4:7], v[4:5], off nt
	v_or_b32_e32 v0, 1, v12
	v_ashrrev_i32_e32 v1, 31, v0
	v_ashrrev_i32_e32 v9, 31, v8
	v_lshlrev_b64 v[0:1], 12, v[0:1]
	v_lshlrev_b64 v[8:9], 12, v[8:9]
	v_lshl_add_u64 v[0:1], v[64:65], 0, v[0:1]
	v_lshl_add_u64 v[8:9], v[64:65], 0, v[8:9]
	global_load_dwordx4 v[52:55], v[0:1], off nt
	global_load_dwordx4 v[8:11], v[8:9], off nt
	v_or_b32_e32 v0, 2, v12
	v_ashrrev_i32_e32 v1, 31, v0
	v_lshlrev_b64 v[0:1], 12, v[0:1]
	v_lshl_add_u64 v[0:1], v[64:65], 0, v[0:1]
	global_load_dwordx4 v[56:59], v[0:1], off nt
	v_or_b32_e32 v0, 3, v12
	v_ashrrev_i32_e32 v1, 31, v0
	v_lshlrev_b64 v[0:1], 12, v[0:1]
	v_lshl_add_u64 v[0:1], v[64:65], 0, v[0:1]
	global_load_dwordx4 v[60:63], v[0:1], off nt
	v_or_b32_e32 v0, 4, v12
	v_ashrrev_i32_e32 v1, 31, v0
	v_lshlrev_b64 v[0:1], 12, v[0:1]
	v_lshl_add_u64 v[0:1], v[64:65], 0, v[0:1]
	global_load_dwordx4 v[32:35], v[0:1], off nt
	v_or_b32_e32 v0, 5, v12
	v_ashrrev_i32_e32 v1, 31, v0
	v_lshlrev_b64 v[0:1], 12, v[0:1]
	v_lshl_add_u64 v[0:1], v[64:65], 0, v[0:1]
	global_load_dwordx4 v[36:39], v[0:1], off nt
	v_or_b32_e32 v0, 6, v12
	v_ashrrev_i32_e32 v1, 31, v0
	v_lshlrev_b64 v[0:1], 12, v[0:1]
	v_lshl_add_u64 v[0:1], v[64:65], 0, v[0:1]
	global_load_dwordx4 v[40:43], v[0:1], off nt
	v_or_b32_e32 v0, 7, v12
	v_ashrrev_i32_e32 v1, 31, v0
	v_lshlrev_b64 v[0:1], 12, v[0:1]
	v_lshl_add_u64 v[0:1], v[64:65], 0, v[0:1]
	global_load_dwordx4 v[44:47], v[0:1], off nt
	v_add_u32_e32 v0, 64, v12
	v_ashrrev_i32_e32 v1, 31, v0
	v_lshlrev_b64 v[0:1], 12, v[0:1]
	v_lshl_add_u64 v[0:1], v[64:65], 0, v[0:1]
	global_load_dwordx4 v[16:19], v[0:1], off nt
	v_add_u32_e32 v0, 0x41, v12
	v_ashrrev_i32_e32 v1, 31, v0
	v_lshlrev_b64 v[0:1], 12, v[0:1]
	v_lshl_add_u64 v[0:1], v[64:65], 0, v[0:1]
	global_load_dwordx4 v[20:23], v[0:1], off nt
	v_add_u32_e32 v0, 0x42, v12
	v_ashrrev_i32_e32 v1, 31, v0
	v_lshlrev_b64 v[0:1], 12, v[0:1]
	v_lshl_add_u64 v[0:1], v[64:65], 0, v[0:1]
	global_load_dwordx4 v[24:27], v[0:1], off nt
	v_add_u32_e32 v0, 0x43, v12
	v_ashrrev_i32_e32 v1, 31, v0
	v_lshlrev_b64 v[0:1], 12, v[0:1]
	v_lshl_add_u64 v[0:1], v[64:65], 0, v[0:1]
	global_load_dwordx4 v[28:31], v[0:1], off nt
	v_add_u32_e32 v0, 0x44, v12
	v_ashrrev_i32_e32 v1, 31, v0
	v_lshlrev_b64 v[0:1], 12, v[0:1]
	v_lshl_add_u64 v[0:1], v[64:65], 0, v[0:1]
	global_load_dwordx4 v[0:3], v[0:1], off nt
	v_add_u32_e32 v12, 0x47, v12
	v_ashrrev_i32_e32 v13, 31, v12
	v_lshlrev_b64 v[12:13], 12, v[12:13]
	v_lshl_add_u64 v[12:13], v[64:65], 0, v[12:13]
	global_load_dwordx4 v[12:15], v[12:13], off nt
	s_and_b64 vcc, exec, s[6:7]
	s_mov_b64 s[6:7], 0
	s_waitcnt vmcnt(15)
	v_mul_f32_e32 v48, 0x42000000, v48
	s_waitcnt vmcnt(14)
	v_mul_f32_e32 v4, 0x42000000, v4
	v_mul_f32_e32 v5, 0x42000000, v5
	s_waitcnt vmcnt(13)
	v_mul_f32_e32 v52, 0x42000000, v52
	v_cvt_pk_fp8_f32 v66, v48, v52
	s_waitcnt vmcnt(12)
	v_mul_f32_e32 v8, 0x42000000, v8
	s_waitcnt vmcnt(11)
	v_mul_f32_e32 v48, 0x42000000, v57
	v_mul_f32_e32 v56, 0x42000000, v56
	s_waitcnt vmcnt(10)
	v_mul_f32_e32 v60, 0x42000000, v60
	v_cvt_pk_fp8_f32 v66, v56, v60 op_sel:[0,0,1]
	s_waitcnt vmcnt(9)
	v_mul_f32_e32 v32, 0x42000000, v32
	s_waitcnt vmcnt(8)
	v_mul_f32_e32 v36, 0x42000000, v36
	v_cvt_pk_fp8_f32 v67, v32, v36
	v_mul_f32_e32 v32, 0x42000000, v49
	v_mul_f32_e32 v36, 0x42000000, v53
	v_mul_f32_e32 v49, 0x42000000, v61
	s_waitcnt vmcnt(7)
	v_mul_f32_e32 v40, 0x42000000, v40
	s_waitcnt vmcnt(6)
	v_mul_f32_e32 v44, 0x42000000, v44
	v_cvt_pk_fp8_f32 v67, v40, v44 op_sel:[0,0,1]
	v_cvt_pk_fp8_f32 v40, v32, v36
	v_mul_f32_e32 v32, 0x42000000, v33
	v_mul_f32_e32 v33, 0x42000000, v37
	v_mul_f32_e32 v36, 0x42000000, v41
	v_cvt_pk_fp8_f32 v41, v32, v33
	v_mul_f32_e32 v37, 0x42000000, v45
	v_mul_f32_e32 v32, 0x42000000, v50
	v_mul_f32_e32 v33, 0x42000000, v54
	v_cvt_pk_fp8_f32 v41, v36, v37 op_sel:[0,0,1]
	v_cvt_pk_fp8_f32 v36, v32, v33
	v_mul_f32_e32 v37, 0x42000000, v58
	v_mul_f32_e32 v45, 0x42000000, v62
	v_mul_f32_e32 v32, 0x42000000, v34
	v_cvt_pk_fp8_f32 v36, v37, v45 op_sel:[0,0,1]
	v_mul_f32_e32 v33, 0x42000000, v38
	v_cvt_pk_fp8_f32 v37, v32, v33
	v_mul_f32_e32 v34, 0x42000000, v42
	v_mul_f32_e32 v38, 0x42000000, v46
	v_mul_f32_e32 v33, 0x42000000, v51
	v_cvt_pk_fp8_f32 v37, v34, v38 op_sel:[0,0,1]
	v_mul_f32_e32 v34, 0x42000000, v55
	v_cvt_pk_fp8_f32 v32, v33, v34
	v_mul_f32_e32 v34, 0x42000000, v35
	v_mul_f32_e32 v35, 0x42000000, v39
	v_cvt_pk_fp8_f32 v33, v34, v35
	s_waitcnt vmcnt(1)
	v_mul_f32_e32 v0, 0x42000000, v0
	v_cvt_pk_fp8_f32 v35, v0, v4
	s_waitcnt vmcnt(0)
	v_mul_f32_e32 v12, 0x42000000, v12
	v_mul_f32_e32 v4, 0x42000000, v17
	v_cvt_pk_fp8_f32 v35, v8, v12 op_sel:[0,0,1]
	v_mul_f32_e32 v8, 0x42000000, v21
	v_cvt_pk_fp8_f32 v0, v4, v8
	v_mul_f32_e32 v4, 0x42000000, v1
	v_cvt_pk_fp8_f32 v1, v4, v5
	v_mul_f32_e32 v16, 0x42000000, v16
	v_mul_f32_e32 v20, 0x42000000, v20
	v_cvt_pk_fp8_f32 v34, v16, v20
	v_mul_f32_e32 v12, 0x42000000, v25
	v_mul_f32_e32 v16, 0x42000000, v29
	v_mul_f32_e32 v8, 0x42000000, v9
	v_mul_f32_e32 v9, 0x42000000, v13
	v_cvt_pk_fp8_f32 v40, v48, v49 op_sel:[0,0,1]
	v_cvt_pk_fp8_f32 v0, v12, v16 op_sel:[0,0,1]
	v_cvt_pk_fp8_f32 v1, v8, v9 op_sel:[0,0,1]
	v_add_u32_e32 v44, s1, v76
	v_mul_f32_e32 v4, 0x42000000, v22
	v_mul_f32_e32 v2, 0x42000000, v2
	ds_write2_b64 v44, v[40:41], v[0:1] offset0:34 offset1:42
	v_mul_f32_e32 v1, 0x42000000, v18
	v_cvt_pk_fp8_f32 v0, v1, v4
	v_mul_f32_e32 v4, 0x42000000, v6
	v_cvt_pk_fp8_f32 v1, v2, v4
	v_mul_f32_e32 v5, 0x42000000, v26
	v_mul_f32_e32 v8, 0x42000000, v30
	v_cvt_pk_fp8_f32 v0, v5, v8 op_sel:[0,0,1]
	v_mul_f32_e32 v5, 0x42000000, v10
	v_mul_f32_e32 v6, 0x42000000, v14
	v_cvt_pk_fp8_f32 v1, v5, v6 op_sel:[0,0,1]
	v_mul_f32_e32 v2, 0x42000000, v23
	v_mul_f32_e32 v38, 0x42000000, v59
	v_mul_f32_e32 v42, 0x42000000, v63
	ds_write2_b64 v44, v[36:37], v[0:1] offset0:68 offset1:76
	v_mul_f32_e32 v1, 0x42000000, v19
	v_cvt_pk_fp8_f32 v0, v1, v2
	v_mul_f32_e32 v2, 0x42000000, v3
	v_mul_f32_e32 v3, 0x42000000, v7
	v_cvt_pk_fp8_f32 v1, v2, v3
	v_mul_f32_e32 v4, 0x42000000, v27
	v_mul_f32_e32 v5, 0x42000000, v31
	v_cvt_pk_fp8_f32 v32, v38, v42 op_sel:[0,0,1]
	v_mul_f32_e32 v38, 0x42000000, v43
	v_mul_f32_e32 v39, 0x42000000, v47
	v_mul_f32_e32 v24, 0x42000000, v24
	v_mul_f32_e32 v28, 0x42000000, v28
	v_cvt_pk_fp8_f32 v0, v4, v5 op_sel:[0,0,1]
	v_mul_f32_e32 v4, 0x42000000, v11
	v_mul_f32_e32 v5, 0x42000000, v15
	v_cvt_pk_fp8_f32 v33, v38, v39 op_sel:[0,0,1]
	v_cvt_pk_fp8_f32 v34, v24, v28 op_sel:[0,0,1]
	v_cvt_pk_fp8_f32 v1, v4, v5 op_sel:[0,0,1]
	s_movk_i32 s1, 0x80
	ds_write2_b64 v44, v[66:67], v[34:35] offset1:8
	ds_write2_b64 v44, v[32:33], v[0:1] offset0:102 offset1:110
	s_cbranch_vccnz .LBB0_582
	v_readlane_b32 s0, v251, 0
	s_add_u32 s2, s0, s4
	v_readlane_b32 s0, v251, 2
	s_waitcnt lgkmcnt(0)
	s_barrier
	s_addc_u32 s3, s0, s5
	v_readlane_b32 s0, v250, 61
	ds_read_b128 v[0:3], v88
	s_nop 0
	v_add_u32_e32 v4, s0, v75
	v_ashrrev_i32_e32 v5, 31, v4
	v_lshlrev_b64 v[4:5], 10, v[4:5]
	v_lshl_add_u64 v[4:5], s[2:3], 0, v[4:5]
	v_lshl_add_u64 v[4:5], v[4:5], 0, v[172:173]
	s_waitcnt lgkmcnt(0)
	global_store_dwordx4 v[4:5], v[0:3], off sc1
	ds_read_b128 v[0:3], v89
	v_add_u32_e32 v4, s0, v74
	v_ashrrev_i32_e32 v5, 31, v4
	v_lshlrev_b64 v[4:5], 10, v[4:5]
	v_lshl_add_u64 v[4:5], s[2:3], 0, v[4:5]
	v_lshl_add_u64 v[4:5], v[4:5], 0, v[172:173]
	s_waitcnt lgkmcnt(0)
	global_store_dwordx4 v[4:5], v[0:3], off sc1
	ds_read_b128 v[0:3], v90
	v_add_u32_e32 v4, s0, v73
	v_ashrrev_i32_e32 v5, 31, v4
	v_lshlrev_b64 v[4:5], 10, v[4:5]
	v_lshl_add_u64 v[4:5], s[2:3], 0, v[4:5]
	v_lshl_add_u64 v[4:5], v[4:5], 0, v[172:173]
	s_waitcnt lgkmcnt(0)
	global_store_dwordx4 v[4:5], v[0:3], off sc1
	ds_read_b128 v[0:3], v91
	v_add_u32_e32 v4, s0, v72
	v_ashrrev_i32_e32 v5, 31, v4
	v_lshlrev_b64 v[4:5], 10, v[4:5]
	v_lshl_add_u64 v[4:5], s[2:3], 0, v[4:5]
	v_lshl_add_u64 v[4:5], v[4:5], 0, v[172:173]
	s_waitcnt lgkmcnt(0)
	global_store_dwordx4 v[4:5], v[0:3], off sc1
	ds_read_b128 v[0:3], v92
	v_add_u32_e32 v4, s0, v71
	v_ashrrev_i32_e32 v5, 31, v4
	v_lshlrev_b64 v[4:5], 10, v[4:5]
	v_lshl_add_u64 v[4:5], s[2:3], 0, v[4:5]
	v_lshl_add_u64 v[4:5], v[4:5], 0, v[172:173]
	s_waitcnt lgkmcnt(0)
	global_store_dwordx4 v[4:5], v[0:3], off sc1
	ds_read_b128 v[0:3], v93
	v_add_u32_e32 v4, s0, v70
	v_ashrrev_i32_e32 v5, 31, v4
	v_lshlrev_b64 v[4:5], 10, v[4:5]
	v_lshl_add_u64 v[4:5], s[2:3], 0, v[4:5]
	v_lshl_add_u64 v[4:5], v[4:5], 0, v[172:173]
	s_waitcnt lgkmcnt(0)
	global_store_dwordx4 v[4:5], v[0:3], off sc1
	ds_read_b128 v[0:3], v94
	v_add_u32_e32 v4, s0, v69
	v_ashrrev_i32_e32 v5, 31, v4
	v_lshlrev_b64 v[4:5], 10, v[4:5]
	v_lshl_add_u64 v[4:5], s[2:3], 0, v[4:5]
	v_lshl_add_u64 v[4:5], v[4:5], 0, v[172:173]
	s_waitcnt lgkmcnt(0)
	global_store_dwordx4 v[4:5], v[0:3], off sc1
	ds_read_b128 v[0:3], v95
	v_add_u32_e32 v4, s0, v68
	v_ashrrev_i32_e32 v5, 31, v4
	v_lshlrev_b64 v[4:5], 10, v[4:5]
	v_lshl_add_u64 v[4:5], s[2:3], 0, v[4:5]
	v_lshl_add_u64 v[4:5], v[4:5], 0, v[172:173]
	s_waitcnt lgkmcnt(0)
	global_store_dwordx4 v[4:5], v[0:3], off sc1
	s_barrier

.LBB0_638:
	v_readlane_b32 s0, v250, 4
	s_waitcnt lgkmcnt(0)
	s_mov_b32 s2, s100
	s_cmp_le_i32 s2, s1
	s_cselect_b64 s[2:3], -1, 0
	s_mov_b32 s65, s101
	s_cmp_lt_i32 s1, s65
	s_cselect_b64 s[4:5], -1, 0
	s_and_b64 s[4:5], s[2:3], s[4:5]
	s_mov_b64 s[2:3], -1
	s_and_b64 vcc, exec, s[4:5]
	s_cbranch_vccnz .LBB0_640
	v_readlane_b32 s0, v255, 35
	s_add_i32 s1, s0, 6
	s_mov_b64 s[2:3], 0

.LBB0_781:
	v_add_co_u32_e32 v136, vcc, s0, v118
	global_load_dwordx4 v[128:131], v[118:119], off
	s_nop 0
	v_addc_co_u32_e32 v137, vcc, 0, v119, vcc
	v_add_co_u32_e32 v156, vcc, s7, v118
	s_nop 1
	v_addc_co_u32_e32 v157, vcc, 0, v119, vcc
	v_add_co_u32_e32 v158, vcc, s67, v118
	global_load_dwordx4 v[132:135], v[136:137], off
	global_load_dwordx4 v[140:143], v[156:157], off
	v_addc_co_u32_e32 v159, vcc, 0, v119, vcc
	global_load_dwordx4 v[144:147], v[158:159], off
	ds_read_b128 v[148:151], v126
	ds_read_b128 v[152:155], v126 offset:16640
	s_waitcnt vmcnt(15) lgkmcnt(7)
	v_mfma_f32_16x16x32_bf16 v[100:103], v[28:31], v[68:71], v[100:103]
	s_waitcnt vmcnt(13)
	v_mfma_f32_16x16x32_bf16 v[96:99], v[40:43], v[68:71], v[96:99]
	s_waitcnt vmcnt(8)
	v_mfma_f32_16x16x32_bf16 v[92:95], v[52:55], v[68:71], v[92:95]
	v_mfma_f32_16x16x32_bf16 v[88:91], v[36:39], v[68:71], v[88:91]
	s_waitcnt lgkmcnt(5)
	v_mfma_f32_16x16x32_bf16 v[84:87], v[28:31], v[60:63], v[84:87]
	v_mfma_f32_16x16x32_bf16 v[80:83], v[40:43], v[60:63], v[80:83]
	v_mfma_f32_16x16x32_bf16 v[76:79], v[52:55], v[60:63], v[76:79]
	v_mfma_f32_16x16x32_bf16 v[72:75], v[36:39], v[60:63], v[72:75]
	global_load_dwordx4 v[28:31], v[118:119], off offset:1024
	global_load_dwordx4 v[40:43], v[136:137], off offset:1024
	global_load_dwordx4 v[52:55], v[156:157], off offset:1024
	global_load_dwordx4 v[36:39], v[158:159], off offset:1024
	ds_read_b128 v[68:71], v126 offset:64
	ds_read_b128 v[60:63], v126 offset:16704
	v_mfma_f32_16x16x32_bf16 v[100:103], v[8:11], v[64:67], v[100:103]
	v_mfma_f32_16x16x32_bf16 v[96:99], v[20:23], v[64:67], v[96:99]
	s_waitcnt vmcnt(10)
	v_mfma_f32_16x16x32_bf16 v[92:95], v[32:35], v[64:67], v[92:95]
	v_mfma_f32_16x16x32_bf16 v[88:91], v[24:27], v[64:67], v[88:91]
	s_waitcnt lgkmcnt(5)
	v_mfma_f32_16x16x32_bf16 v[84:87], v[8:11], v[56:59], v[84:87]
	v_mfma_f32_16x16x32_bf16 v[80:83], v[20:23], v[56:59], v[80:83]
	v_mfma_f32_16x16x32_bf16 v[76:79], v[32:35], v[56:59], v[76:79]
	v_mfma_f32_16x16x32_bf16 v[72:75], v[24:27], v[56:59], v[72:75]
	global_load_dwordx4 v[8:11], v[118:119], off offset:2048
	global_load_dwordx4 v[20:23], v[136:137], off offset:2048
	global_load_dwordx4 v[32:35], v[156:157], off offset:2048
	global_load_dwordx4 v[24:27], v[158:159], off offset:2048
	ds_read_b128 v[64:67], v126 offset:128
	ds_read_b128 v[56:59], v126 offset:16768
	v_mfma_f32_16x16x32_bf16 v[100:103], v[0:3], v[48:51], v[100:103]
	v_mfma_f32_16x16x32_bf16 v[96:99], v[4:7], v[48:51], v[96:99]
	s_waitcnt vmcnt(13)
	v_mfma_f32_16x16x32_bf16 v[92:95], v[16:19], v[48:51], v[92:95]
	s_waitcnt vmcnt(12)
	v_mfma_f32_16x16x32_bf16 v[88:91], v[12:15], v[48:51], v[88:91]
	s_waitcnt lgkmcnt(6)
	v_mfma_f32_16x16x32_bf16 v[84:87], v[0:3], v[44:47], v[84:87]
	v_mfma_f32_16x16x32_bf16 v[80:83], v[4:7], v[44:47], v[80:83]
	v_mfma_f32_16x16x32_bf16 v[76:79], v[16:19], v[44:47], v[76:79]
	v_mfma_f32_16x16x32_bf16 v[72:75], v[12:15], v[44:47], v[72:75]
	global_load_dwordx4 v[0:3], v[118:119], off offset:3072
	global_load_dwordx4 v[4:7], v[136:137], off offset:3072
	global_load_dwordx4 v[16:19], v[156:157], off offset:3072
	global_load_dwordx4 v[12:15], v[158:159], off offset:3072
	ds_read_b128 v[48:51], v126 offset:192
	ds_read_b128 v[44:47], v126 offset:16832
	s_waitcnt vmcnt(15) lgkmcnt(7)
	v_mfma_f32_16x16x32_bf16 v[100:103], v[128:131], v[148:151], v[100:103]
	s_waitcnt vmcnt(14)
	v_mfma_f32_16x16x32_bf16 v[96:99], v[132:135], v[148:151], v[96:99]
	s_waitcnt vmcnt(13)
	v_mfma_f32_16x16x32_bf16 v[92:95], v[140:143], v[148:151], v[92:95]
	s_waitcnt vmcnt(12)
	v_mfma_f32_16x16x32_bf16 v[88:91], v[144:147], v[148:151], v[88:91]
	s_waitcnt lgkmcnt(6)
	v_mfma_f32_16x16x32_bf16 v[84:87], v[128:131], v[152:155], v[84:87]
	v_mfma_f32_16x16x32_bf16 v[80:83], v[132:135], v[152:155], v[80:83]
	v_mfma_f32_16x16x32_bf16 v[76:79], v[140:143], v[152:155], v[76:79]
	v_mfma_f32_16x16x32_bf16 v[72:75], v[144:147], v[152:155], v[72:75]
	s_add_i32 s2, s2, 4
	v_lshl_add_u64 v[118:119], v[118:119], 0, s[52:53]
	s_cmp_lt_u32 s2, 8
	v_add_u32_e32 v126, 0x100, v126
	s_cbranch_scc1 .LBB0_781
	v_add_co_u32_e32 v118, vcc, 0x3000, v116
	s_nop 1
	v_addc_co_u32_e32 v119, vcc, 0, v117, vcc
	v_add_co_u32_e32 v130, vcc, 0x7000, v116
	s_nop 1
	v_addc_co_u32_e32 v131, vcc, 0, v117, vcc
	global_load_dwordx4 v[126:129], v[118:119], off offset:3072
	s_nop 0
	global_load_dwordx4 v[130:133], v[130:131], off offset:3072
	v_add_co_u32_e32 v118, vcc, 0xb000, v116
	s_nop 1
	v_addc_co_u32_e32 v119, vcc, 0, v117, vcc
	v_add_co_u32_e32 v134, vcc, 0xf000, v116
	s_nop 1
	v_addc_co_u32_e32 v135, vcc, 0, v117, vcc
	global_load_dwordx4 v[116:119], v[118:119], off offset:3072
	s_nop 0
	global_load_dwordx4 v[134:137], v[134:135], off offset:3072
	ds_read_b128 v[140:143], v125 offset:960
	ds_read_b128 v[144:147], v125 offset:17600
	s_waitcnt vmcnt(15) lgkmcnt(7)
	v_mfma_f32_16x16x32_bf16 v[100:103], v[28:31], v[68:71], v[100:103]
	s_waitcnt vmcnt(14)
	v_mfma_f32_16x16x32_bf16 v[96:99], v[40:43], v[68:71], v[96:99]
	s_waitcnt vmcnt(13)
	v_mfma_f32_16x16x32_bf16 v[92:95], v[52:55], v[68:71], v[92:95]
	s_waitcnt vmcnt(12)
	v_mfma_f32_16x16x32_bf16 v[68:71], v[36:39], v[68:71], v[88:91]
	s_waitcnt lgkmcnt(6)
	v_mfma_f32_16x16x32_bf16 v[28:31], v[28:31], v[60:63], v[84:87]
	v_mfma_f32_16x16x32_bf16 v[40:43], v[40:43], v[60:63], v[80:83]
	v_mfma_f32_16x16x32_bf16 v[52:55], v[52:55], v[60:63], v[76:79]
	v_mfma_f32_16x16x32_bf16 v[36:39], v[36:39], v[60:63], v[72:75]
	s_waitcnt vmcnt(11) lgkmcnt(5)
	v_mfma_f32_16x16x32_bf16 v[60:63], v[8:11], v[64:67], v[100:103]
	s_waitcnt vmcnt(10)
	v_mfma_f32_16x16x32_bf16 v[72:75], v[20:23], v[64:67], v[96:99]
	s_waitcnt vmcnt(9)
	v_mfma_f32_16x16x32_bf16 v[76:79], v[32:35], v[64:67], v[92:95]
	s_waitcnt vmcnt(8)
	v_mfma_f32_16x16x32_bf16 v[64:67], v[24:27], v[64:67], v[68:71]
	s_waitcnt lgkmcnt(4)
	v_mfma_f32_16x16x32_bf16 v[8:11], v[8:11], v[56:59], v[28:31]
	v_mfma_f32_16x16x32_bf16 v[20:23], v[20:23], v[56:59], v[40:43]
	v_mfma_f32_16x16x32_bf16 v[28:31], v[32:35], v[56:59], v[52:55]
	v_mfma_f32_16x16x32_bf16 v[24:27], v[24:27], v[56:59], v[36:39]
	s_waitcnt vmcnt(7) lgkmcnt(3)
	v_mfma_f32_16x16x32_bf16 v[32:35], v[0:3], v[48:51], v[60:63]
	s_waitcnt vmcnt(6)
	v_mfma_f32_16x16x32_bf16 v[36:39], v[4:7], v[48:51], v[72:75]
	s_waitcnt vmcnt(5)
	v_mfma_f32_16x16x32_bf16 v[40:43], v[16:19], v[48:51], v[76:79]
	s_waitcnt vmcnt(4)
	v_mfma_f32_16x16x32_bf16 v[48:51], v[12:15], v[48:51], v[64:67]
	s_waitcnt lgkmcnt(2)
	v_mfma_f32_16x16x32_bf16 v[0:3], v[0:3], v[44:47], v[8:11]
	v_mfma_f32_16x16x32_bf16 v[4:7], v[4:7], v[44:47], v[20:23]
	v_mfma_f32_16x16x32_bf16 v[8:11], v[16:19], v[44:47], v[28:31]
	v_mfma_f32_16x16x32_bf16 v[12:15], v[12:15], v[44:47], v[24:27]
	s_waitcnt vmcnt(3) lgkmcnt(1)
	v_mfma_f32_16x16x32_bf16 v[16:19], v[126:129], v[140:143], v[32:35]
	s_ashr_i32 s7, s6, 31
	s_add_i32 s4, s4, s37
	s_cmpk_lt_i32 s4, 0x90
	s_waitcnt vmcnt(2)
	v_mfma_f32_16x16x32_bf16 v[20:23], v[130:133], v[140:143], v[36:39]
	v_lshl_add_u64 v[32:33], v[110:111], 0, s[6:7]
	s_nop 1
	ds_bpermute_b32 v16, v123, v16
	ds_bpermute_b32 v17, v123, v17
	ds_bpermute_b32 v18, v123, v18
	ds_bpermute_b32 v19, v123, v19
	v_mov_b32_e32 v34, 0x240
	v_mad_i64_i32 v[32:33], s[2:3], s5, v34, v[32:33]
	v_lshlrev_b64 v[32:33], 10, v[32:33]
	v_lshl_add_u64 v[34:35], v[112:113], 0, v[32:33]
	v_readlane_b32 s2, v251, 33
	s_waitcnt lgkmcnt(0)
	global_store_dwordx4 v[34:35], v[16:19], off sc1
	ds_bpermute_b32 v16, v123, v20
	ds_bpermute_b32 v17, v123, v21
	ds_bpermute_b32 v18, v123, v22
	ds_bpermute_b32 v19, v123, v23
	v_readlane_b32 s3, v251, 34
	s_waitcnt vmcnt(2)
	v_mfma_f32_16x16x32_bf16 v[24:27], v[116:119], v[140:143], v[40:43]
	v_lshl_add_u64 v[20:21], s[2:3], 0, v[32:33]
	v_lshl_add_u64 v[20:21], v[20:21], 0, v[172:173]
	s_mov_b32 s2, 0x4b62b000
	v_add_co_u32_e32 v22, vcc, s2, v20
	s_waitcnt vmcnt(1)
	v_mfma_f32_16x16x32_bf16 v[28:31], v[134:137], v[140:143], v[48:51]
	v_addc_co_u32_e32 v23, vcc, 0, v21, vcc
	s_waitcnt lgkmcnt(0)
	global_store_dwordx4 v[22:23], v[16:19], off offset:1600 sc1
	ds_bpermute_b32 v16, v123, v24
	ds_bpermute_b32 v17, v123, v25
	ds_bpermute_b32 v18, v123, v26
	ds_bpermute_b32 v19, v123, v27
	v_mfma_f32_16x16x32_bf16 v[0:3], v[126:129], v[144:147], v[0:3]
	s_waitcnt lgkmcnt(0)
	global_store_dwordx4 v[22:23], v[16:19], off offset:1664 sc1
	ds_bpermute_b32 v16, v123, v28
	ds_bpermute_b32 v17, v123, v29
	ds_bpermute_b32 v18, v123, v30
	ds_bpermute_b32 v19, v123, v31
	s_nop 1
	ds_bpermute_b32 v0, v123, v0
	ds_bpermute_b32 v1, v123, v1
	ds_bpermute_b32 v2, v123, v2
	ds_bpermute_b32 v3, v123, v3
	v_mfma_f32_16x16x32_bf16 v[4:7], v[130:133], v[144:147], v[4:7]
	s_waitcnt lgkmcnt(4)
	global_store_dwordx4 v[22:23], v[16:19], off offset:1728 sc1
	s_nop 1
	v_add_co_u32_e32 v16, vcc, s0, v34
	v_mfma_f32_16x16x32_bf16 v[8:11], v[116:119], v[144:147], v[8:11]
	s_nop 0
	v_addc_co_u32_e32 v17, vcc, 0, v35, vcc
	s_waitcnt lgkmcnt(0)
	global_store_dwordx4 v[16:17], v[0:3], off sc1
	ds_bpermute_b32 v0, v123, v4
	ds_bpermute_b32 v1, v123, v5
	ds_bpermute_b32 v2, v123, v6
	ds_bpermute_b32 v3, v123, v7
	s_mov_b32 s0, 0x4b62f000
	v_add_co_u32_e32 v4, vcc, s0, v20
	v_mfma_f32_16x16x32_bf16 v[12:15], v[134:137], v[144:147], v[12:15]
	s_nop 0
	v_addc_co_u32_e32 v5, vcc, 0, v21, vcc
	s_waitcnt lgkmcnt(0)
	global_store_dwordx4 v[4:5], v[0:3], off offset:1600 sc1
	ds_bpermute_b32 v0, v123, v8
	ds_bpermute_b32 v1, v123, v9
	ds_bpermute_b32 v2, v123, v10
	ds_bpermute_b32 v3, v123, v11
	s_waitcnt lgkmcnt(0)
	global_store_dwordx4 v[4:5], v[0:3], off offset:1664 sc1
	ds_bpermute_b32 v0, v123, v12
	ds_bpermute_b32 v1, v123, v13
	ds_bpermute_b32 v2, v123, v14
	ds_bpermute_b32 v3, v123, v15
	s_waitcnt lgkmcnt(0)
	global_store_dwordx4 v[4:5], v[0:3], off offset:1728 sc1
	s_barrier
	s_cbranch_scc1 .LBB0_748

.LBB0_819:
	v_lshl_add_u64 v[136:137], s[6:7], 0, v[106:107]
	v_add_co_u32_e32 v140, vcc, s2, v136
	s_nop 1
	v_addc_co_u32_e32 v141, vcc, 0, v137, vcc
	v_add_co_u32_e32 v142, vcc, s3, v136
	global_load_dwordx4 v[112:115], v[136:137], off
	global_load_dwordx4 v[116:119], v[140:141], off
	v_addc_co_u32_e32 v143, vcc, 0, v137, vcc
	v_add_co_u32_e32 v144, vcc, s67, v136
	s_nop 1
	v_addc_co_u32_e32 v145, vcc, 0, v137, vcc
	global_load_dwordx4 v[120:123], v[142:143], off
	global_load_dwordx4 v[124:127], v[144:145], off
	ds_read_b128 v[128:131], v111
	ds_read_b128 v[132:135], v111 offset:16640
	s_waitcnt vmcnt(15) lgkmcnt(7)
	v_mfma_f32_16x16x32_bf16 v[100:103], v[28:31], v[68:71], v[100:103]
	s_waitcnt vmcnt(13)
	v_mfma_f32_16x16x32_bf16 v[96:99], v[40:43], v[68:71], v[96:99]
	s_waitcnt vmcnt(8)
	v_mfma_f32_16x16x32_bf16 v[92:95], v[44:47], v[68:71], v[92:95]
	v_mfma_f32_16x16x32_bf16 v[88:91], v[36:39], v[68:71], v[88:91]
	s_waitcnt lgkmcnt(5)
	v_mfma_f32_16x16x32_bf16 v[84:87], v[28:31], v[60:63], v[84:87]
	v_mfma_f32_16x16x32_bf16 v[80:83], v[40:43], v[60:63], v[80:83]
	v_mfma_f32_16x16x32_bf16 v[76:79], v[44:47], v[60:63], v[76:79]
	v_mfma_f32_16x16x32_bf16 v[72:75], v[36:39], v[60:63], v[72:75]
	global_load_dwordx4 v[28:31], v[136:137], off offset:1024
	global_load_dwordx4 v[40:43], v[140:141], off offset:1024
	global_load_dwordx4 v[44:47], v[142:143], off offset:1024
	global_load_dwordx4 v[36:39], v[144:145], off offset:1024
	ds_read_b128 v[68:71], v111 offset:64
	ds_read_b128 v[60:63], v111 offset:16704
	v_mfma_f32_16x16x32_bf16 v[100:103], v[8:11], v[64:67], v[100:103]
	v_mfma_f32_16x16x32_bf16 v[96:99], v[20:23], v[64:67], v[96:99]
	s_waitcnt vmcnt(10)
	v_mfma_f32_16x16x32_bf16 v[92:95], v[32:35], v[64:67], v[92:95]
	v_mfma_f32_16x16x32_bf16 v[88:91], v[24:27], v[64:67], v[88:91]
	s_waitcnt lgkmcnt(5)
	v_mfma_f32_16x16x32_bf16 v[84:87], v[8:11], v[56:59], v[84:87]
	v_mfma_f32_16x16x32_bf16 v[80:83], v[20:23], v[56:59], v[80:83]
	v_mfma_f32_16x16x32_bf16 v[76:79], v[32:35], v[56:59], v[76:79]
	v_mfma_f32_16x16x32_bf16 v[72:75], v[24:27], v[56:59], v[72:75]
	global_load_dwordx4 v[8:11], v[136:137], off offset:2048
	global_load_dwordx4 v[20:23], v[140:141], off offset:2048
	global_load_dwordx4 v[32:35], v[142:143], off offset:2048
	global_load_dwordx4 v[24:27], v[144:145], off offset:2048
	ds_read_b128 v[64:67], v111 offset:128
	ds_read_b128 v[56:59], v111 offset:16768
	v_mfma_f32_16x16x32_bf16 v[100:103], v[0:3], v[52:55], v[100:103]
	v_mfma_f32_16x16x32_bf16 v[96:99], v[4:7], v[52:55], v[96:99]
	s_waitcnt vmcnt(13)
	v_mfma_f32_16x16x32_bf16 v[92:95], v[16:19], v[52:55], v[92:95]
	s_waitcnt vmcnt(12)
	v_mfma_f32_16x16x32_bf16 v[88:91], v[12:15], v[52:55], v[88:91]
	s_waitcnt lgkmcnt(6)
	v_mfma_f32_16x16x32_bf16 v[84:87], v[0:3], v[48:51], v[84:87]
	v_mfma_f32_16x16x32_bf16 v[80:83], v[4:7], v[48:51], v[80:83]
	v_mfma_f32_16x16x32_bf16 v[76:79], v[16:19], v[48:51], v[76:79]
	v_mfma_f32_16x16x32_bf16 v[72:75], v[12:15], v[48:51], v[72:75]
	global_load_dwordx4 v[0:3], v[136:137], off offset:3072
	global_load_dwordx4 v[4:7], v[140:141], off offset:3072
	global_load_dwordx4 v[16:19], v[142:143], off offset:3072
	global_load_dwordx4 v[12:15], v[144:145], off offset:3072
	ds_read_b128 v[52:55], v111 offset:192
	ds_read_b128 v[48:51], v111 offset:16832
	s_waitcnt vmcnt(15) lgkmcnt(7)
	v_mfma_f32_16x16x32_bf16 v[100:103], v[112:115], v[128:131], v[100:103]
	s_waitcnt vmcnt(14)
	v_mfma_f32_16x16x32_bf16 v[96:99], v[116:119], v[128:131], v[96:99]
	s_waitcnt vmcnt(13)
	v_mfma_f32_16x16x32_bf16 v[92:95], v[120:123], v[128:131], v[92:95]
	s_waitcnt vmcnt(12)
	v_mfma_f32_16x16x32_bf16 v[88:91], v[124:127], v[128:131], v[88:91]
	s_waitcnt lgkmcnt(6)
	v_mfma_f32_16x16x32_bf16 v[84:87], v[112:115], v[132:135], v[84:87]
	v_mfma_f32_16x16x32_bf16 v[80:83], v[116:119], v[132:135], v[80:83]
	v_mfma_f32_16x16x32_bf16 v[76:79], v[120:123], v[132:135], v[76:79]
	v_mfma_f32_16x16x32_bf16 v[72:75], v[124:127], v[132:135], v[72:75]
	s_add_i32 s1, s1, 4
	s_add_u32 s6, s6, 0x1000
	s_addc_u32 s7, s7, 0
	s_cmp_lt_u32 s1, 8
	v_add_u32_e32 v111, 0x100, v111
	s_cbranch_scc1 .LBB0_819
	v_add_co_u32_e32 v106, vcc, 0x3000, v104
	s_nop 1
	v_addc_co_u32_e32 v107, vcc, 0, v105, vcc
	v_add_co_u32_e32 v116, vcc, 0x7000, v104
	s_nop 1
	v_addc_co_u32_e32 v117, vcc, 0, v105, vcc
	global_load_dwordx4 v[112:115], v[106:107], off offset:3072
	s_nop 0
	global_load_dwordx4 v[116:119], v[116:117], off offset:3072
	v_add_co_u32_e32 v106, vcc, 0xb000, v104
	s_nop 1
	v_addc_co_u32_e32 v107, vcc, 0, v105, vcc
	v_add_co_u32_e32 v120, vcc, 0xf000, v104
	s_nop 1
	v_addc_co_u32_e32 v121, vcc, 0, v105, vcc
	global_load_dwordx4 v[104:107], v[106:107], off offset:3072
	s_nop 0
	global_load_dwordx4 v[120:123], v[120:121], off offset:3072
	ds_read_b128 v[124:127], v110 offset:960
	ds_read_b128 v[128:131], v110 offset:17600
	s_waitcnt vmcnt(15) lgkmcnt(7)
	v_mfma_f32_16x16x32_bf16 v[100:103], v[28:31], v[68:71], v[100:103]
	s_waitcnt vmcnt(14)
	v_mfma_f32_16x16x32_bf16 v[96:99], v[40:43], v[68:71], v[96:99]
	s_waitcnt vmcnt(13)
	v_mfma_f32_16x16x32_bf16 v[92:95], v[44:47], v[68:71], v[92:95]
	s_waitcnt vmcnt(12)
	v_mfma_f32_16x16x32_bf16 v[68:71], v[36:39], v[68:71], v[88:91]
	s_waitcnt lgkmcnt(6)
	v_mfma_f32_16x16x32_bf16 v[28:31], v[28:31], v[60:63], v[84:87]
	v_mfma_f32_16x16x32_bf16 v[40:43], v[40:43], v[60:63], v[80:83]
	v_mfma_f32_16x16x32_bf16 v[44:47], v[44:47], v[60:63], v[76:79]
	v_mfma_f32_16x16x32_bf16 v[36:39], v[36:39], v[60:63], v[72:75]
	s_waitcnt vmcnt(11) lgkmcnt(5)
	v_mfma_f32_16x16x32_bf16 v[60:63], v[8:11], v[64:67], v[100:103]
	s_waitcnt vmcnt(10)
	v_mfma_f32_16x16x32_bf16 v[72:75], v[20:23], v[64:67], v[96:99]
	s_waitcnt vmcnt(9)
	v_mfma_f32_16x16x32_bf16 v[76:79], v[32:35], v[64:67], v[92:95]
	s_waitcnt vmcnt(8)
	v_mfma_f32_16x16x32_bf16 v[64:67], v[24:27], v[64:67], v[68:71]
	s_waitcnt lgkmcnt(4)
	v_mfma_f32_16x16x32_bf16 v[8:11], v[8:11], v[56:59], v[28:31]
	v_mfma_f32_16x16x32_bf16 v[20:23], v[20:23], v[56:59], v[40:43]
	v_mfma_f32_16x16x32_bf16 v[28:31], v[32:35], v[56:59], v[44:47]
	v_mfma_f32_16x16x32_bf16 v[24:27], v[24:27], v[56:59], v[36:39]
	s_waitcnt vmcnt(7) lgkmcnt(3)
	v_mfma_f32_16x16x32_bf16 v[32:35], v[0:3], v[52:55], v[60:63]
	s_waitcnt vmcnt(6)
	v_mfma_f32_16x16x32_bf16 v[36:39], v[4:7], v[52:55], v[72:75]
	s_waitcnt vmcnt(5)
	v_mfma_f32_16x16x32_bf16 v[40:43], v[16:19], v[52:55], v[76:79]
	s_waitcnt vmcnt(4)
	v_mfma_f32_16x16x32_bf16 v[44:47], v[12:15], v[52:55], v[64:67]
	s_waitcnt lgkmcnt(2)
	v_mfma_f32_16x16x32_bf16 v[0:3], v[0:3], v[48:51], v[8:11]
	v_mfma_f32_16x16x32_bf16 v[4:7], v[4:7], v[48:51], v[20:23]
	v_mfma_f32_16x16x32_bf16 v[8:11], v[16:19], v[48:51], v[28:31]
	v_mfma_f32_16x16x32_bf16 v[12:15], v[12:15], v[48:51], v[24:27]
	s_waitcnt vmcnt(3) lgkmcnt(1)
	v_mfma_f32_16x16x32_bf16 v[16:19], v[112:115], v[124:127], v[32:35]
	v_readlane_b32 s0, v251, 41
	v_readlane_b32 s1, v251, 42
	s_nop 0
	v_lshlrev_b32_e32 v32, 6, v108
	v_and_b32_e32 v32, 0xc0, v32
	v_add_u32_e32 v32, v32, v109
	s_waitcnt vmcnt(2)
	v_mfma_f32_16x16x32_bf16 v[20:23], v[116:119], v[124:127], v[36:39]
	v_lshrrev_b32_e32 v33, 2, v108
	s_nop 1
	v_and_or_b32 v36, v138, 12, v32
	v_ashrrev_i32_e32 v32, 2, v138
	v_and_or_b32 v32, v32, -4, v33
	v_ashrrev_i32_e32 v33, 31, v32
	ds_bpermute_b32 v16, v36, v16
	ds_bpermute_b32 v17, v36, v17
	ds_bpermute_b32 v18, v36, v18
	ds_bpermute_b32 v19, v36, v19
	v_lshl_add_u64 v[32:33], s[0:1], 0, v[32:33]
	v_readlane_b32 s0, v251, 31
	v_lshlrev_b64 v[32:33], 10, v[32:33]
	v_readlane_b32 s1, v251, 32
	v_lshlrev_b32_e32 v37, 4, v138
	v_and_b32_e32 v172, 48, v37
	v_lshl_add_u64 v[34:35], s[0:1], 0, v[32:33]
	v_lshl_add_u64 v[34:35], v[34:35], 0, v[172:173]
	v_readlane_b32 s0, v251, 33
	s_waitcnt lgkmcnt(0)
	global_store_dwordx4 v[34:35], v[16:19], off sc1
	ds_bpermute_b32 v16, v36, v20
	ds_bpermute_b32 v17, v36, v21
	ds_bpermute_b32 v18, v36, v22
	ds_bpermute_b32 v19, v36, v23
	v_readlane_b32 s1, v251, 34
	s_waitcnt vmcnt(2)
	v_mfma_f32_16x16x32_bf16 v[24:27], v[104:107], v[124:127], v[40:43]
	v_lshl_add_u64 v[20:21], s[0:1], 0, v[32:33]
	v_lshl_add_u64 v[20:21], v[20:21], 0, v[172:173]
	s_mov_b32 s0, 0x4b62b000
	v_add_co_u32_e32 v22, vcc, s0, v20
	s_waitcnt vmcnt(1)
	v_mfma_f32_16x16x32_bf16 v[28:31], v[120:123], v[124:127], v[44:47]
	v_addc_co_u32_e32 v23, vcc, 0, v21, vcc
	s_waitcnt lgkmcnt(0)
	global_store_dwordx4 v[22:23], v[16:19], off offset:1600 sc1
	ds_bpermute_b32 v16, v36, v24
	ds_bpermute_b32 v17, v36, v25
	ds_bpermute_b32 v18, v36, v26
	ds_bpermute_b32 v19, v36, v27
	v_mfma_f32_16x16x32_bf16 v[0:3], v[112:115], v[128:131], v[0:3]
	s_mov_b32 s0, 0x4b62f000
	s_waitcnt lgkmcnt(0)
	global_store_dwordx4 v[22:23], v[16:19], off offset:1664 sc1
	ds_bpermute_b32 v16, v36, v28
	ds_bpermute_b32 v17, v36, v29
	ds_bpermute_b32 v18, v36, v30
	ds_bpermute_b32 v19, v36, v31
	s_nop 0
	ds_bpermute_b32 v0, v36, v0
	ds_bpermute_b32 v1, v36, v1
	ds_bpermute_b32 v2, v36, v2
	ds_bpermute_b32 v3, v36, v3
	v_mfma_f32_16x16x32_bf16 v[4:7], v[116:119], v[128:131], v[4:7]
	s_waitcnt lgkmcnt(4)
	global_store_dwordx4 v[22:23], v[16:19], off offset:1728 sc1
	s_nop 1
	v_add_co_u32_e32 v16, vcc, s2, v34
	v_mfma_f32_16x16x32_bf16 v[8:11], v[104:107], v[128:131], v[8:11]
	s_nop 0
	v_addc_co_u32_e32 v17, vcc, 0, v35, vcc
	s_waitcnt lgkmcnt(0)
	global_store_dwordx4 v[16:17], v[0:3], off sc1
	ds_bpermute_b32 v0, v36, v4
	ds_bpermute_b32 v1, v36, v5
	ds_bpermute_b32 v2, v36, v6
	ds_bpermute_b32 v3, v36, v7
	v_add_co_u32_e32 v4, vcc, s0, v20
	v_mfma_f32_16x16x32_bf16 v[12:15], v[120:123], v[128:131], v[12:15]
	s_nop 0
	v_addc_co_u32_e32 v5, vcc, 0, v21, vcc
	s_waitcnt lgkmcnt(0)
	global_store_dwordx4 v[4:5], v[0:3], off offset:1600 sc1
	ds_bpermute_b32 v0, v36, v8
	ds_bpermute_b32 v1, v36, v9
	ds_bpermute_b32 v2, v36, v10
	ds_bpermute_b32 v3, v36, v11
	s_waitcnt lgkmcnt(0)
	global_store_dwordx4 v[4:5], v[0:3], off offset:1664 sc1
	ds_bpermute_b32 v0, v36, v12
	ds_bpermute_b32 v1, v36, v13
	ds_bpermute_b32 v2, v36, v14
	ds_bpermute_b32 v3, v36, v15
	s_waitcnt lgkmcnt(0)
	global_store_dwordx4 v[4:5], v[0:3], off offset:1728 sc1
	s_barrier

.LBB0_875:
	v_readlane_b32 s0, v250, 4
	s_waitcnt lgkmcnt(0)
	s_mov_b32 s2, s100
	s_cmp_le_i32 s2, s1
	s_cselect_b64 s[2:3], -1, 0
	s_mov_b32 s4, s101
	s_cmp_lt_i32 s1, s4
	s_cselect_b64 s[6:7], -1, 0
	s_and_b64 s[6:7], s[2:3], s[6:7]
	s_mov_b64 s[2:3], -1
	s_and_b64 vcc, exec, s[6:7]
	s_cbranch_vccnz .LBB0_877
	v_readlane_b32 s0, v255, 35
	s_add_i32 s1, s0, 7
	s_mov_b64 s[2:3], 0

.LBB0_1051:
	v_readlane_b32 s0, v250, 4
	s_waitcnt lgkmcnt(0)
	s_mov_b32 s2, s100
	s_cmp_le_i32 s2, s1
	s_cselect_b64 s[2:3], -1, 0
	s_mov_b32 s28, s101
	s_cmp_lt_i32 s1, s28
	s_cselect_b64 s[4:5], -1, 0
	s_and_b64 s[4:5], s[2:3], s[4:5]
	s_mov_b64 s[2:3], -1
	s_and_b64 vcc, exec, s[4:5]
	s_cbranch_vccnz .LBB0_1053
	v_readlane_b32 s0, v255, 35
	s_add_i32 s1, s0, 8
	s_mov_b64 s[2:3], 0

.LBB0_1056:
	v_sub_f32_e32 v85, v221, v160
	v_mul_f32_e32 v85, 0x3fb8aa3b, v85
	v_exp_f32_e32 v86, v85
	v_add_f32_e32 v85, v160, v220
	v_mul_f32_e32 v85, 0xbfb8aa3b, v85
	v_exp_f32_e32 v87, v85
	s_waitcnt lgkmcnt(0)
	v_sub_f32_e32 v84, v236, v225
	v_mul_f32_e32 v89, 0x3fb8aa3b, v84
	v_pk_add_f32 v[84:85], v[156:157], v[158:159]
	v_pk_fma_f32 v[26:27], v[86:87], v[74:75], v[26:27] op_sel_hi:[0,1,1]
	v_fmac_f32_e32 v85, v86, v84
	v_max_f32_e64 v84, |v85|, v87
	v_rcp_f32_e32 v88, v84
	v_pk_fma_f32 v[72:73], v[86:87], v[72:73], v[24:25] op_sel_hi:[0,1,1]
	v_pk_fma_f32 v[22:23], v[86:87], v[70:71], v[22:23] op_sel_hi:[0,1,1]
	v_pk_fma_f32 v[20:21], v[86:87], v[68:69], v[20:21] op_sel_hi:[0,1,1]
	v_add_u32_e32 v68, s1, v177
	v_pk_fma_f32 v[24:25], v[88:89], v[26:27], 0 op_sel_hi:[0,1,0]
	v_pk_fma_f32 v[26:27], v[88:89], v[72:73], 0 op_sel_hi:[0,1,0]
	v_pk_fma_f32 v[72:73], v[88:89], v[22:23], 0 op_sel_hi:[0,1,0]
	v_pk_fma_f32 v[74:75], v[88:89], v[20:21], 0 op_sel_hi:[0,1,0]
	v_pk_fma_f32 v[22:23], v[86:87], v[66:67], v[18:19] op_sel_hi:[0,1,1]
	ds_read_b128 v[18:21], v68 offset:384
	v_pk_fma_f32 v[16:17], v[86:87], v[64:65], v[16:17] op_sel_hi:[0,1,1]
	ds_read_b128 v[64:67], v68 offset:400
	v_pk_fma_f32 v[34:35], v[86:87], v[78:79], v[34:35] op_sel_hi:[0,1,1]
	v_pk_fma_f32 v[78:79], v[88:89], v[16:17], 0 op_sel_hi:[0,1,0]
	s_waitcnt lgkmcnt(1)
	v_fma_f32 v69, v18, v223, 0
	v_fmac_f32_e32 v69, v19, v224
	v_fmac_f32_e32 v69, v20, v232
	v_fmac_f32_e32 v69, v21, v234
	ds_read_b128 v[16:19], v68 offset:512
	s_waitcnt lgkmcnt(1)
	v_fmac_f32_e32 v69, v64, v235
	v_pk_fma_f32 v[76:77], v[86:87], v[76:77], v[32:33] op_sel_hi:[0,1,1]
	v_fmac_f32_e32 v69, v65, v230
	v_pk_fma_f32 v[32:33], v[88:89], v[34:35], 0 op_sel_hi:[0,1,0]
	v_pk_fma_f32 v[34:35], v[88:89], v[76:77], 0 op_sel_hi:[0,1,0]
	v_pk_fma_f32 v[76:77], v[88:89], v[22:23], 0 op_sel_hi:[0,1,0]
	v_fmac_f32_e32 v69, v66, v231
	ds_read_b128 v[20:23], v68 offset:528
	v_fmac_f32_e32 v69, v67, v233
	s_waitcnt lgkmcnt(1)
	v_fmac_f32_e32 v69, v16, v226
	v_fmac_f32_e32 v69, v17, v227
	v_fmac_f32_e32 v69, v18, v228
	v_fmac_f32_e32 v69, v19, v229
	s_waitcnt lgkmcnt(0)
	v_pk_mul_f32 v[16:17], v[20:21], v[148:149]
	v_pk_mul_f32 v[20:21], v[22:23], v[152:153]
	v_add_f32_e32 v16, v69, v16
	v_add_f32_e32 v64, v16, v17
	ds_read_b128 v[16:19], v68 offset:640
	v_add_f32_e32 v20, v64, v20
	v_add_f32_e32 v64, v20, v21
	ds_read_b128 v[20:23], v68 offset:656
	v_pk_fma_f32 v[30:31], v[86:87], v[82:83], v[30:31] op_sel_hi:[0,1,1]
	s_waitcnt lgkmcnt(1)
	v_pk_mul_f32 v[16:17], v[16:17], v[150:151]
	v_pk_fma_f32 v[82:83], v[86:87], v[48:49], v[12:13] op_sel_hi:[0,1,1]
	v_add_f32_e32 v16, v64, v16
	v_add_f32_e32 v64, v16, v17
	v_pk_mul_f32 v[16:17], v[18:19], v[154:155]
	s_waitcnt lgkmcnt(0)
	v_pk_mul_f32 v[20:21], v[20:21], v[144:145]
	v_add_f32_e32 v16, v64, v16
	v_add_f32_e32 v64, v16, v17
	ds_read_b128 v[16:19], v219 offset:19968
	v_add_f32_e32 v20, v64, v20
	ds_read_b128 v[64:67], v219 offset:20032
	v_add_f32_e32 v68, v20, v21
	v_pk_mul_f32 v[20:21], v[22:23], v[146:147]
	s_waitcnt lgkmcnt(1)
	v_mfma_f32_16x16x32_bf16 v[16:19], v[16:19], v[8:11], 0
	v_add_f32_e32 v20, v68, v20
	v_add_f32_e32 v160, v20, v21
	ds_read_b128 v[20:23], v219 offset:20096
	ds_read_b128 v[68:71], v219 offset:23296
	s_waitcnt lgkmcnt(2)
	v_mfma_f32_16x16x32_bf16 v[16:19], v[64:67], v[4:7], v[16:19]
	v_fma_f32 v64, v86, v50, v14
	v_fma_f32 v65, v86, v51, v15
	ds_read_b128 v[12:15], v219 offset:23360
	v_pk_fma_f32 v[80:81], v[86:87], v[80:81], v[28:29] op_sel_hi:[0,1,1]
	s_waitcnt lgkmcnt(2)
	v_mfma_f32_16x16x32_bf16 v[16:19], v[20:23], v[0:3], v[16:19]
	ds_read_b128 v[20:23], v219 offset:23424
	v_pk_fma_f32 v[28:29], v[88:89], v[30:31], 0 op_sel_hi:[0,1,0]
	v_pk_fma_f32 v[30:31], v[88:89], v[80:81], 0 op_sel_hi:[0,1,0]
	s_waitcnt lgkmcnt(2)
	v_mfma_f32_16x16x32_bf16 v[48:51], v[68:71], v[8:11], 0
	ds_swizzle_b32 v80, v160 offset:swizzle(SWAP,16)
	ds_swizzle_b32 v81, v161 offset:swizzle(SWAP,16)
	v_pk_fma_f32 v[144:145], v[88:89], v[64:65], 0 op_sel_hi:[0,1,0]
	ds_read_b128 v[64:67], v219 offset:26624
	s_waitcnt lgkmcnt(4)
	v_mfma_f32_16x16x32_bf16 v[12:15], v[12:15], v[4:7], v[48:51]
	v_exp_f32_e32 v84, v89
	s_waitcnt lgkmcnt(1)
	v_pk_add_f32 v[80:81], v[160:161], v[80:81]
	ds_bpermute_b32 v86, v178, v80
	ds_read_b128 v[48:51], v219 offset:26688
	ds_bpermute_b32 v87, v178, v81
	v_mfma_f32_16x16x32_bf16 v[12:15], v[20:23], v[0:3], v[12:15]
	v_add_f32_e32 v20, v225, v222
	v_mul_f32_e32 v68, 0xbfb8aa3b, v20
	v_exp_f32_e32 v85, v68
	s_waitcnt lgkmcnt(3)
	v_mfma_f32_16x16x32_bf16 v[64:67], v[64:67], v[8:11], 0
	ds_read_b128 v[20:23], v219 offset:26752
	ds_read_b128 v[68:71], v219 offset:29952
	s_waitcnt lgkmcnt(2)
	v_pk_add_f32 v[80:81], v[80:81], v[86:87]
	v_mfma_f32_16x16x32_bf16 v[48:51], v[48:51], v[4:7], v[64:67]
	v_fmac_f32_e32 v81, v84, v80
	v_pk_fma_f32 v[82:83], v[88:89], v[82:83], 0 op_sel_hi:[0,1,0]
	v_pk_fma_f32 v[62:63], v[84:85], v[18:19], v[62:63] op_sel_hi:[0,1,1]
	v_max_f32_e64 v64, |v81|, v85
	v_rcp_f32_e32 v80, v64
	ds_read_b128 v[64:67], v219 offset:30016
	v_pk_fma_f32 v[60:61], v[84:85], v[16:17], v[60:61] op_sel_hi:[0,1,1]
	ds_read_b128 v[16:19], v219 offset:30080
	s_waitcnt lgkmcnt(3)
	v_mfma_f32_16x16x32_bf16 v[20:23], v[20:23], v[0:3], v[48:51]
	v_fma_f32 v58, v84, v14, v58
	v_fma_f32 v59, v84, v15, v59
	v_pk_fma_f32 v[56:57], v[84:85], v[12:13], v[56:57] op_sel_hi:[0,1,1]
	ds_read_b128 v[12:15], v219 offset:33344
	s_waitcnt lgkmcnt(3)
	v_mfma_f32_16x16x32_bf16 v[48:51], v[68:71], v[8:11], 0
	v_fma_f32 v68, v80, v62, v144
	v_fma_f32 v69, v80, v63, v145
	v_pk_fma_f32 v[70:71], v[80:81], v[60:61], v[82:83] op_sel_hi:[0,1,1]
	ds_read_b128 v[60:63], v219 offset:33280
	s_waitcnt lgkmcnt(3)
	v_mfma_f32_16x16x32_bf16 v[48:51], v[64:67], v[4:7], v[48:51]
	v_fma_f32 v64, v80, v58, v76
	v_fma_f32 v65, v80, v59, v77
	v_pk_fma_f32 v[66:67], v[80:81], v[56:57], v[78:79] op_sel_hi:[0,1,1]
	v_pk_fma_f32 v[54:55], v[84:85], v[22:23], v[54:55] op_sel_hi:[0,1,1]
	s_waitcnt lgkmcnt(2)
	v_mfma_f32_16x16x32_bf16 v[16:19], v[16:19], v[0:3], v[48:51]
	v_fma_f32 v52, v84, v20, v52
	v_fma_f32 v53, v84, v21, v53
	ds_read_b128 v[20:23], v219 offset:36608
	s_mov_b32 s0, 0x800000
	ds_read_b128 v[48:51], v219 offset:33408
	s_waitcnt lgkmcnt(2)
	v_mfma_f32_16x16x32_bf16 v[56:59], v[60:63], v[8:11], 0
	s_nop 0
	v_fma_f32 v44, v84, v16, v44
	v_fma_f32 v45, v84, v17, v45
	v_readlane_b32 s2, v253, 3
	v_readlane_b32 s3, v253, 4
	v_mfma_f32_16x16x32_bf16 v[12:15], v[12:15], v[4:7], v[56:59]
	s_waitcnt lgkmcnt(0)
	v_mfma_f32_16x16x32_bf16 v[48:51], v[48:51], v[0:3], v[12:15]
	s_nop 0
	v_fma_f32 v56, v80, v54, v72
	v_fma_f32 v57, v80, v55, v73
	v_pk_fma_f32 v[58:59], v[80:81], v[52:53], v[74:75] op_sel_hi:[0,1,1]
	ds_read_b128 v[52:55], v219 offset:36672
	s_nop 0
	ds_read_b128 v[14:17], v219 offset:36736
	v_pk_fma_f32 v[12:13], v[84:85], v[18:19], v[46:47] op_sel_hi:[0,1,1]
	v_mfma_f32_16x16x32_bf16 v[18:21], v[20:23], v[8:11], 0
	v_fma_f32 v10, v84, v50, v42
	v_fma_f32 v11, v84, v51, v43
	v_pk_fma_f32 v[8:9], v[80:81], v[12:13], v[24:25] op_sel_hi:[0,1,1]
	v_pk_fma_f32 v[12:13], v[80:81], v[44:45], v[26:27] op_sel_hi:[0,1,1]
	s_waitcnt lgkmcnt(1)
	v_mfma_f32_16x16x32_bf16 v[18:21], v[52:55], v[4:7], v[18:21]
	v_fma_f32 v4, v80, v10, v32
	v_fma_f32 v5, v80, v11, v33
	v_pk_fma_f32 v[6:7], v[84:85], v[48:49], v[40:41] op_sel_hi:[0,1,1]
	v_pk_fma_f32 v[6:7], v[80:81], v[6:7], v[34:35] op_sel_hi:[0,1,1]
	s_waitcnt lgkmcnt(0)
	v_mfma_f32_16x16x32_bf16 v[0:3], v[14:17], v[0:3], v[18:21]
	v_mov_b32_e32 v14, v71
	v_mov_b32_e32 v15, v67
	v_pk_mul_f32 v[14:15], v[14:15], v[14:15]
	v_mov_b32_e32 v16, v59
	v_mov_b32_e32 v17, v13
	s_nop 2
	v_pk_fma_f32 v[2:3], v[84:85], v[2:3], v[38:39] op_sel_hi:[0,1,1]
	v_pk_fma_f32 v[10:11], v[84:85], v[0:1], v[36:37] op_sel_hi:[0,1,1]
	v_pk_fma_f32 v[0:1], v[80:81], v[2:3], v[28:29] op_sel_hi:[0,1,1]
	v_pk_fma_f32 v[2:3], v[80:81], v[10:11], v[30:31] op_sel_hi:[0,1,1]
	v_mov_b32_e32 v10, v70
	v_mov_b32_e32 v11, v66
	v_pk_fma_f32 v[10:11], v[10:11], v[10:11], v[14:15]
	v_mov_b32_e32 v14, v68
	v_mov_b32_e32 v15, v64
	v_pk_fma_f32 v[10:11], v[14:15], v[14:15], v[10:11]
	v_mov_b32_e32 v14, v69
	v_mov_b32_e32 v15, v65
	v_pk_fma_f32 v[10:11], v[14:15], v[14:15], v[10:11]
	v_mov_b32_e32 v14, v58
	v_mov_b32_e32 v15, v12
	v_pk_mul_f32 v[16:17], v[16:17], v[16:17]
	v_mov_b32_e32 v18, v7
	v_pk_fma_f32 v[14:15], v[14:15], v[14:15], v[16:17]
	v_mov_b32_e32 v16, v56
	v_mov_b32_e32 v17, v8
	v_pk_fma_f32 v[14:15], v[16:17], v[16:17], v[14:15]
	v_mov_b32_e32 v16, v57
	v_mov_b32_e32 v17, v9
	v_mov_b32_e32 v19, v3
	v_pk_fma_f32 v[14:15], v[16:17], v[16:17], v[14:15]
	v_mov_b32_e32 v16, v6
	v_mov_b32_e32 v17, v2
	v_pk_mul_f32 v[18:19], v[18:19], v[18:19]
	v_add_f32_e32 v10, v10, v11
	v_pk_fma_f32 v[16:17], v[16:17], v[16:17], v[18:19]
	v_mov_b32_e32 v18, v4
	v_mov_b32_e32 v19, v0
	v_pk_fma_f32 v[16:17], v[18:19], v[18:19], v[16:17]
	v_mov_b32_e32 v18, v5
	v_mov_b32_e32 v19, v1
	v_add_f32_e32 v10, v10, v14
	v_pk_fma_f32 v[16:17], v[18:19], v[18:19], v[16:17]
	v_add_f32_e32 v10, v10, v15
	v_add_f32_e32 v10, v10, v16
	v_add_f32_e32 v10, v10, v17
	ds_swizzle_b32 v11, v10 offset:swizzle(SWAP,16)
	v_lshlrev_b32_e32 v18, 16, v142
	v_and_b32_e32 v19, 0xffff0000, v142
	v_mul_f32_e32 v18, 0xbfb8aa3b, v18
	v_mul_f32_e32 v19, 0xbfb8aa3b, v19
	s_waitcnt lgkmcnt(0)
	v_add_f32_e32 v10, v10, v11
	ds_bpermute_b32 v11, v178, v10
	v_lshlrev_b32_e32 v23, 16, v143
	v_exp_f32_e32 v18, v18
	v_exp_f32_e32 v19, v19
	v_and_b32_e32 v24, 0xffff0000, v143
	s_waitcnt lgkmcnt(0)
	v_add_f32_e32 v10, v10, v11
	v_fmamk_f32 v10, v10, 0x3c2aaaab, v198
	v_mul_f32_e32 v11, 0x4b800000, v10
	v_cmp_gt_f32_e32 vcc, s0, v10
	v_mul_f32_e32 v23, 0xbfb8aa3b, v23
	v_exp_f32_e32 v23, v23
	v_cndmask_b32_e32 v10, v10, v11, vcc
	v_rsq_f32_e32 v10, v10
	v_mul_f32_e32 v24, 0xbfb8aa3b, v24
	v_exp_f32_e32 v24, v24
	v_add_f32_e32 v18, 1.0, v18
	v_mul_f32_e32 v11, 0x45800000, v10
	v_cndmask_b32_e32 v22, v10, v11, vcc
	v_mul_f32_e32 v20, v70, v22
	v_mul_f32_e32 v21, v71, v22
	ds_bpermute_b32 v20, v183, v20
	ds_bpermute_b32 v25, v183, v21
	v_add_f32_e32 v19, 1.0, v19
	ds_read_b128 v[14:17], v184
	v_mul_f32_e32 v21, v68, v22
	v_rcp_f32_e32 v18, v18
	v_rcp_f32_e32 v28, v19
	ds_bpermute_b32 v26, v183, v21
	v_mul_f32_e32 v21, v69, v22
	v_add_f32_e32 v23, 1.0, v23
	ds_bpermute_b32 v27, v183, v21
	v_rcp_f32_e32 v23, v23
	v_add_f32_e32 v24, 1.0, v24
	v_rcp_f32_e32 v24, v24
	s_waitcnt lgkmcnt(4)
	v_mul_f32_e32 v29, v18, v20
	v_add_u32_e32 v18, 64, v184
	s_waitcnt lgkmcnt(3)
	v_mul_f32_e32 v25, v28, v25
	v_lshlrev_b64 v[10:11], 11, v[140:141]
	ds_read_b128 v[18:21], v18
	s_waitcnt lgkmcnt(3)
	v_mul_f32_e32 v14, v14, v29
	v_mul_f32_e32 v15, v15, v25
	v_cvt_pk_bf16_f32 v14, v14, v15
	s_waitcnt lgkmcnt(2)
	v_mul_f32_e32 v15, v23, v26
	v_lshl_add_u64 v[10:11], s[2:3], 0, v[10:11]
	v_mul_f32_e32 v15, v16, v15
	s_waitcnt lgkmcnt(1)
	v_mul_f32_e32 v16, v24, v27
	v_lshl_add_u64 v[10:11], s[22:23], 1, v[10:11]
	v_mul_f32_e32 v16, v17, v16
	v_cvt_pk_bf16_f32 v15, v15, v16
	v_lshl_add_u64 v[10:11], v[10:11], 0, v[172:173]
	global_store_dwordx2 v[10:11], v[14:15], off
	v_lshlrev_b32_e32 v14, 16, v138
	v_and_b32_e32 v15, 0xffff0000, v138
	v_mul_f32_e32 v14, 0xbfb8aa3b, v14
	v_mul_f32_e32 v15, 0xbfb8aa3b, v15
	v_exp_f32_e32 v14, v14
	v_exp_f32_e32 v15, v15
	v_lshlrev_b32_e32 v16, 16, v139
	v_and_b32_e32 v17, 0xffff0000, v139
	v_mul_f32_e32 v23, v66, v22
	v_mul_f32_e32 v24, v67, v22
	ds_bpermute_b32 v23, v183, v23
	ds_bpermute_b32 v24, v183, v24
	v_add_f32_e32 v14, 1.0, v14
	v_add_f32_e32 v15, 1.0, v15
	v_mul_f32_e32 v16, 0xbfb8aa3b, v16
	v_mul_f32_e32 v17, 0xbfb8aa3b, v17
	v_rcp_f32_e32 v14, v14
	v_rcp_f32_e32 v15, v15
	v_exp_f32_e32 v16, v16
	v_exp_f32_e32 v17, v17
	v_mul_f32_e32 v25, v64, v22
	v_mul_f32_e32 v26, v65, v22
	ds_bpermute_b32 v25, v183, v25
	ds_bpermute_b32 v26, v183, v26
	s_waitcnt lgkmcnt(3)
	v_mul_f32_e32 v14, v14, v23
	s_waitcnt lgkmcnt(2)
	v_mul_f32_e32 v15, v15, v24
	v_add_f32_e32 v16, 1.0, v16
	v_add_f32_e32 v17, 1.0, v17
	v_mul_f32_e32 v14, v18, v14
	v_mul_f32_e32 v15, v19, v15
	v_rcp_f32_e32 v16, v16
	v_rcp_f32_e32 v17, v17
	v_lshlrev_b32_e32 v18, 16, v136
	v_and_b32_e32 v19, 0xffff0000, v136
	v_mul_f32_e32 v18, 0xbfb8aa3b, v18
	v_mul_f32_e32 v19, 0xbfb8aa3b, v19
	v_lshlrev_b32_e32 v23, 16, v137
	v_exp_f32_e32 v18, v18
	v_exp_f32_e32 v19, v19
	v_and_b32_e32 v24, 0xffff0000, v137
	v_mul_f32_e32 v23, 0xbfb8aa3b, v23
	v_cvt_pk_bf16_f32 v14, v14, v15
	s_waitcnt lgkmcnt(1)
	v_mul_f32_e32 v15, v16, v25
	s_waitcnt lgkmcnt(0)
	v_mul_f32_e32 v16, v17, v26
	v_exp_f32_e32 v23, v23
	v_mul_f32_e32 v24, 0xbfb8aa3b, v24
	v_mul_f32_e32 v15, v20, v15
	v_mul_f32_e32 v16, v21, v16
	v_mul_f32_e32 v20, v58, v22
	v_mul_f32_e32 v21, v59, v22
	v_exp_f32_e32 v24, v24
	v_cvt_pk_bf16_f32 v15, v15, v16
	ds_bpermute_b32 v20, v183, v20
	ds_bpermute_b32 v25, v183, v21
	v_add_f32_e32 v18, 1.0, v18
	v_add_f32_e32 v19, 1.0, v19
	global_store_dwordx2 v[10:11], v[14:15], off offset:32
	ds_read_b128 v[14:17], v185
	v_mul_f32_e32 v21, v56, v22
	v_rcp_f32_e32 v18, v18
	v_rcp_f32_e32 v28, v19
	ds_bpermute_b32 v26, v183, v21
	v_mul_f32_e32 v21, v57, v22
	v_add_f32_e32 v23, 1.0, v23
	ds_bpermute_b32 v27, v183, v21
	v_rcp_f32_e32 v23, v23
	v_add_f32_e32 v24, 1.0, v24
	v_rcp_f32_e32 v24, v24
	s_waitcnt lgkmcnt(4)
	v_mul_f32_e32 v29, v18, v20
	s_waitcnt lgkmcnt(3)
	v_mul_f32_e32 v25, v28, v25
	ds_read_b128 v[18:21], v186
	s_waitcnt lgkmcnt(3)
	v_mul_f32_e32 v14, v14, v29
	v_mul_f32_e32 v15, v15, v25
	v_cvt_pk_bf16_f32 v14, v14, v15
	s_waitcnt lgkmcnt(2)
	v_mul_f32_e32 v15, v23, v26
	v_mul_f32_e32 v15, v16, v15
	s_waitcnt lgkmcnt(1)
	v_mul_f32_e32 v16, v24, v27
	v_mul_f32_e32 v16, v17, v16
	v_cvt_pk_bf16_f32 v15, v15, v16
	global_store_dwordx2 v[10:11], v[14:15], off offset:64
	v_lshlrev_b32_e32 v14, 16, v134
	v_and_b32_e32 v15, 0xffff0000, v134
	v_mul_f32_e32 v8, v8, v22
	ds_bpermute_b32 v23, v183, v8
	v_mul_f32_e32 v8, 0xbfb8aa3b, v14
	v_mul_f32_e32 v14, 0xbfb8aa3b, v15
	v_exp_f32_e32 v8, v8
	v_exp_f32_e32 v14, v14
	v_mul_f32_e32 v12, v12, v22
	v_mul_f32_e32 v13, v13, v22
	ds_bpermute_b32 v12, v183, v12
	ds_bpermute_b32 v13, v183, v13
	v_add_f32_e32 v8, 1.0, v8
	v_add_f32_e32 v14, 1.0, v14
	v_rcp_f32_e32 v8, v8
	v_rcp_f32_e32 v14, v14
	v_and_b32_e32 v17, 0xffff0000, v135
	v_lshlrev_b32_e32 v16, 16, v135
	s_waitcnt lgkmcnt(1)
	v_mul_f32_e32 v8, v8, v12
	s_waitcnt lgkmcnt(0)
	v_mul_f32_e32 v12, v14, v13
	v_mul_f32_e32 v14, 0xbfb8aa3b, v17
	v_mul_f32_e32 v13, 0xbfb8aa3b, v16
	v_exp_f32_e32 v14, v14
	v_exp_f32_e32 v13, v13
	v_mul_f32_e32 v9, v9, v22
	ds_bpermute_b32 v9, v183, v9
	v_add_f32_e32 v14, 1.0, v14
	v_add_f32_e32 v13, 1.0, v13
	v_rcp_f32_e32 v14, v14
	v_rcp_f32_e32 v13, v13
	v_mul_f32_e32 v8, v18, v8
	v_mul_f32_e32 v12, v19, v12
	s_waitcnt lgkmcnt(0)
	v_mul_f32_e32 v9, v14, v9
	v_cvt_pk_bf16_f32 v8, v8, v12
	v_mul_f32_e32 v12, v13, v23
	v_mul_f32_e32 v9, v21, v9
	v_mul_f32_e32 v12, v20, v12
	v_cvt_pk_bf16_f32 v9, v12, v9
	global_store_dwordx2 v[10:11], v[8:9], off offset:96
	s_waitcnt vmcnt(5)
	v_and_b32_e32 v9, 0xffff0000, v130
	v_mul_f32_e32 v7, v7, v22
	v_lshlrev_b32_e32 v8, 16, v130
	ds_bpermute_b32 v18, v183, v7
	v_mul_f32_e32 v4, v4, v22
	v_mul_f32_e32 v7, 0xbfb8aa3b, v9
	ds_bpermute_b32 v19, v183, v4
	v_mul_f32_e32 v4, 0xbfb8aa3b, v8
	v_exp_f32_e32 v7, v7
	v_exp_f32_e32 v4, v4
	v_mul_f32_e32 v5, v5, v22
	v_lshlrev_b32_e32 v16, 16, v131
	v_and_b32_e32 v17, 0xffff0000, v131
	v_mul_f32_e32 v6, v6, v22
	ds_bpermute_b32 v9, v183, v5
	v_add_f32_e32 v5, 1.0, v7
	ds_read_b128 v[12:15], v187
	ds_bpermute_b32 v6, v183, v6
	v_add_f32_e32 v4, 1.0, v4
	v_rcp_f32_e32 v8, v5
	v_mul_f32_e32 v16, 0xbfb8aa3b, v16
	v_mul_f32_e32 v17, 0xbfb8aa3b, v17
	v_rcp_f32_e32 v4, v4
	v_exp_f32_e32 v16, v16
	v_exp_f32_e32 v17, v17
	s_waitcnt lgkmcnt(4)
	v_mul_f32_e32 v8, v8, v18
	s_waitcnt lgkmcnt(0)
	v_mul_f32_e32 v20, v4, v6
	ds_read_b128 v[4:7], v188
	v_mul_f32_e32 v8, v13, v8
	v_add_f32_e32 v13, 1.0, v16
	v_add_f32_e32 v16, 1.0, v17
	v_rcp_f32_e32 v16, v16
	v_rcp_f32_e32 v13, v13
	v_mul_f32_e32 v12, v12, v20
	v_cvt_pk_bf16_f32 v8, v12, v8
	v_mul_f32_e32 v9, v16, v9
	v_mul_f32_e32 v12, v13, v19
	v_mul_f32_e32 v9, v15, v9
	v_mul_f32_e32 v12, v14, v12
	v_cvt_pk_bf16_f32 v9, v12, v9
	global_store_dwordx2 v[10:11], v[8:9], off offset:128
	s_waitcnt vmcnt(5)
	v_lshlrev_b32_e32 v8, 16, v128
	v_mul_f32_e32 v0, v0, v22
	ds_bpermute_b32 v14, v183, v0
	v_mul_f32_e32 v0, 0xbfb8aa3b, v8
	v_and_b32_e32 v9, 0xffff0000, v128
	v_exp_f32_e32 v0, v0
	v_mul_f32_e32 v8, 0xbfb8aa3b, v9
	v_exp_f32_e32 v8, v8
	v_mul_f32_e32 v2, v2, v22
	ds_bpermute_b32 v2, v183, v2
	v_add_f32_e32 v0, 1.0, v0
	v_mul_f32_e32 v3, v3, v22
	v_rcp_f32_e32 v0, v0
	ds_bpermute_b32 v3, v183, v3
	v_add_f32_e32 v8, 1.0, v8
	v_rcp_f32_e32 v8, v8
	v_and_b32_e32 v13, 0xffff0000, v129
	s_waitcnt lgkmcnt(1)
	v_mul_f32_e32 v0, v0, v2
	v_lshlrev_b32_e32 v12, 16, v129
	v_mul_f32_e32 v0, v4, v0
	v_mul_f32_e32 v4, 0xbfb8aa3b, v13
	s_waitcnt lgkmcnt(0)
	v_mul_f32_e32 v2, v8, v3
	v_mul_f32_e32 v3, 0xbfb8aa3b, v12
	v_exp_f32_e32 v4, v4
	v_exp_f32_e32 v3, v3
	v_mul_f32_e32 v1, v1, v22
	ds_bpermute_b32 v1, v183, v1
	v_add_f32_e32 v4, 1.0, v4
	v_add_f32_e32 v3, 1.0, v3
	v_rcp_f32_e32 v4, v4
	v_rcp_f32_e32 v3, v3
	v_mul_f32_e32 v2, v5, v2
	v_cvt_pk_bf16_f32 v0, v0, v2
	s_waitcnt lgkmcnt(0)
	v_mul_f32_e32 v1, v4, v1
	v_mul_f32_e32 v2, v3, v14
	v_mul_f32_e32 v1, v7, v1
	v_mul_f32_e32 v2, v6, v2
	v_cvt_pk_bf16_f32 v1, v2, v1
	global_store_dwordx2 v[10:11], v[0:1], off offset:160
	s_barrier

.LBB0_1102:
	s_or_b64 exec, exec, s[2:3]
	s_waitcnt vmcnt(11)
	v_fmac_f32_e32 v105, v104, v152
	v_fmac_f32_e32 v55, v108, v152
	v_fmac_f32_e32 v53, v114, v152
	v_fmac_f32_e32 v51, v118, v152
	v_fmac_f32_e32 v49, v120, v152
	v_fmac_f32_e32 v47, v122, v152
	v_fmac_f32_e32 v45, v124, v152
	v_fmac_f32_e32 v31, v128, v152
	v_fmac_f32_e32 v29, v130, v152
	v_fmac_f32_e32 v107, v134, v152
	v_fmac_f32_e32 v111, v136, v152
	v_fmac_f32_e32 v113, v140, v152
	v_fmac_f32_e32 v117, v142, v152
	v_fmac_f32_e32 v127, v144, v152
	v_fmac_f32_e32 v139, v146, v152
	v_fmac_f32_e32 v149, v150, v152
	ds_write_b32 v75, v105
	ds_write_b32 v77, v55
	ds_write_b32 v79, v53
	ds_write_b32 v81, v51
	ds_write_b32 v83, v49
	ds_write_b32 v85, v47
	ds_write_b32 v87, v45
	ds_write_b32 v89, v31
	ds_write_b32 v91, v29
	ds_write_b32 v93, v107
	ds_write_b32 v95, v111
	ds_write_b32 v97, v113
	ds_write_b32 v99, v117
	ds_write_b32 v101, v127
	ds_write_b32 v153, v139
	ds_write_b32 v154, v149
	s_waitcnt lgkmcnt(0)
	s_barrier
	ds_read_b128 v[28:31], v71 offset:16384
	ds_read_b128 v[44:47], v71
	ds_read_b128 v[48:51], v71 offset:16
	ds_read_b128 v[52:55], v71 offset:16400
	s_mov_b32 s0, 0x800000
	s_and_b32 s2, s10, 0xffff
	s_waitcnt lgkmcnt(2)
	v_pk_add_f32 v[28:29], v[44:45], v[28:29]
	v_pk_add_f32 v[30:31], v[46:47], v[30:31]
	v_pk_mul_f32 v[44:45], v[28:29], v[28:29]
	v_pk_mul_f32 v[46:47], v[30:31], v[30:31]
	v_add_f32_e32 v44, v44, v45
	s_waitcnt lgkmcnt(0)
	v_pk_add_f32 v[48:49], v[48:49], v[52:53]
	v_add_f32_e32 v44, v44, v46
	v_pk_mul_f32 v[52:53], v[48:49], v[48:49]
	v_add_f32_e32 v44, v44, v47
	v_pk_add_f32 v[50:51], v[50:51], v[54:55]
	v_add_f32_e32 v44, v44, v52
	v_pk_mul_f32 v[54:55], v[50:51], v[50:51]
	v_add_f32_e32 v44, v44, v53
	v_add_f32_e32 v44, v44, v54
	v_add_f32_e32 v44, v44, v55
	s_mul_i32 s2, s2, 0xaaab
	s_lshr_b32 s2, s2, 18
	v_add_f32_dpp v44, v44, v44 quad_perm:[1,0,3,2] row_mask:0xf bank_mask:0xf bound_ctrl:1
	s_mul_i32 s3, s2, 0xe39
	s_lshr_b32 s3, s3, 17
	v_add_f32_dpp v44, v44, v44 quad_perm:[2,3,0,1] row_mask:0xf bank_mask:0xf bound_ctrl:1
	s_mul_i32 s3, s3, 36
	s_bfe_u32 s12, s10, 0xd0003
	v_add_f32_dpp v44, v44, v44 row_half_mirror row_mask:0xf bank_mask:0xf bound_ctrl:1
	v_fmamk_f32 v44, v44, 0x3c800000, v198
	v_mul_f32_e32 v45, 0x4b800000, v44
	v_cmp_gt_f32_e32 vcc, s0, v44
	s_sub_i32 s3, s2, s3
	s_mulk_i32 s12, 0x12f7
	v_cndmask_b32_e32 v44, v44, v45, vcc
	v_rsq_f32_e32 v44, v44
	s_and_b32 s11, s3, 0xffff
	s_lshr_b32 s12, s12, 17
	s_lshl_b32 s3, s3, 6
	v_mul_f32_e32 v45, 0x45800000, v44
	v_cndmask_b32_e32 v44, v44, v45, vcc
	s_waitcnt vmcnt(10)
	v_lshlrev_b32_e32 v45, 16, v0
	v_and_b32_e32 v0, 0xffff0000, v0
	v_mul_f32_e32 v28, v28, v45
	v_mul_f32_e32 v0, v29, v0
	v_mul_f32_e32 v28, v28, v44
	v_mul_f32_e32 v0, v0, v44
	s_waitcnt vmcnt(8)
	v_mul_f32_e32 v8, v8, v28
	v_mul_f32_e32 v0, v9, v0
	v_cvt_pk_bf16_f32 v0, v8, v0
	v_lshlrev_b32_e32 v8, 16, v1
	v_and_b32_e32 v1, 0xffff0000, v1
	v_mul_f32_e32 v8, v30, v8
	v_mul_f32_e32 v1, v31, v1
	v_mul_f32_e32 v8, v8, v44
	v_mul_f32_e32 v1, v1, v44
	v_mul_f32_e32 v8, v10, v8
	v_mul_f32_e32 v1, v11, v1
	v_cvt_pk_bf16_f32 v1, v8, v1
	v_lshlrev_b32_e32 v8, 16, v2
	v_and_b32_e32 v2, 0xffff0000, v2
	v_mul_f32_e32 v8, v48, v8
	v_mul_f32_e32 v2, v49, v2
	v_mul_f32_e32 v8, v8, v44
	v_mul_f32_e32 v2, v2, v44
	v_mul_f32_e32 v4, v4, v8
	v_mul_f32_e32 v2, v5, v2
	s_lshl_b32 s13, s12, 8
	s_lshl_b32 s12, s12, 11
	s_and_b32 s3, s3, 0xffc0
	v_cvt_pk_bf16_f32 v2, v4, v2
	v_lshlrev_b32_e32 v4, 16, v3
	v_and_b32_e32 v3, 0xffff0000, v3
	s_addk_i32 s12, 0x800
	s_add_i32 s14, s3, 0xffffff00
	v_mul_f32_e32 v4, v50, v4
	v_mul_f32_e32 v3, v51, v3
	s_cmp_lt_u32 s11, 4
	v_mul_f32_e32 v4, v4, v44
	v_mul_f32_e32 v3, v3, v44
	s_cselect_b32 s11, s13, s12
	s_cselect_b32 s3, s3, s14
	v_mul_f32_e32 v4, v6, v4
	v_mul_f32_e32 v3, v7, v3
	s_add_i32 s3, s3, s11
	v_cvt_pk_bf16_f32 v3, v4, v3
	s_mul_i32 s2, s2, 6
	v_add_u32_e32 v4, s3, v65
	s_sub_i32 s2, s10, s2
	v_ashrrev_i32_e32 v5, 31, v4
	v_lshlrev_b64 v[4:5], 11, v[4:5]
	s_lshl_b32 s2, s2, 7
	v_lshl_add_u64 v[4:5], s[60:61], 0, v[4:5]
	s_and_b32 s44, s2, 0x1ff80
	v_lshl_add_u64 v[4:5], v[4:5], 0, s[44:45]
	v_lshl_add_u64 v[4:5], v[4:5], 0, v[172:173]
	v_add_co_u32_e32 v4, vcc, 0x4ccab000, v4
	s_waitcnt vmcnt(0)
	v_mov_b64_e32 v[8:9], v[40:41]
	v_addc_co_u32_e32 v5, vcc, 0, v5, vcc
	global_store_dwordx4 v[4:5], v[0:3], off offset:2304 sc1
	s_barrier
	v_mov_b64_e32 v[4:5], v[36:37]
	v_mov_b64_e32 v[0:1], v[32:33]
	v_mov_b64_e32 v[30:31], v[26:27]
	v_mov_b64_e32 v[46:47], v[22:23]
	v_mov_b64_e32 v[50:51], v[18:19]
	v_mov_b64_e32 v[54:55], v[14:15]
	s_cmp_lt_i32 s1, 0
	s_mov_b32 s10, s1
	v_mov_b64_e32 v[6:7], v[38:39]
	v_mov_b64_e32 v[10:11], v[42:43]
	v_mov_b64_e32 v[2:3], v[34:35]
	v_mov_b32_e32 v152, v103
	v_mov_b64_e32 v[28:29], v[24:25]
	v_mov_b64_e32 v[44:45], v[20:21]
	v_mov_b64_e32 v[48:49], v[16:17]
	v_mov_b64_e32 v[52:53], v[12:13]
	s_cbranch_scc1 .LBB0_1113

.LBB0_1141:
	v_add_co_u32_e32 v160, vcc, s3, v144
	global_load_dwordx4 v[156:159], v[144:145], off
	s_nop 0
	v_addc_co_u32_e32 v161, vcc, 0, v145, vcc
	v_add_co_u32_e32 v190, vcc, s67, v144
	s_nop 1
	v_addc_co_u32_e32 v191, vcc, 0, v145, vcc
	v_add_co_u32_e32 v192, vcc, s0, v144
	global_load_dwordx4 v[164:167], v[160:161], off
	global_load_dwordx4 v[168:171], v[190:191], off
	v_addc_co_u32_e32 v193, vcc, 0, v145, vcc
	global_load_dwordx4 v[174:177], v[192:193], off
	ds_read_b128 v[178:181], v155 offset:24832
	ds_read_b128 v[182:185], v155
	ds_read_b128 v[186:189], v155 offset:49664
	s_waitcnt vmcnt(15) lgkmcnt(4)
	v_mfma_f32_16x16x32_bf16 v[128:131], v[28:31], v[80:83], v[128:131]
	s_waitcnt vmcnt(13)
	v_mfma_f32_16x16x32_bf16 v[124:127], v[44:47], v[80:83], v[124:127]
	s_waitcnt vmcnt(8)
	v_mfma_f32_16x16x32_bf16 v[120:123], v[56:59], v[80:83], v[120:123]
	v_mfma_f32_16x16x32_bf16 v[116:119], v[40:43], v[80:83], v[116:119]
	v_mfma_f32_16x16x32_bf16 v[112:115], v[28:31], v[76:79], v[112:115]
	v_mfma_f32_16x16x32_bf16 v[108:111], v[44:47], v[76:79], v[108:111]
	v_mfma_f32_16x16x32_bf16 v[104:107], v[56:59], v[76:79], v[104:107]
	v_mfma_f32_16x16x32_bf16 v[100:103], v[40:43], v[76:79], v[100:103]
	v_mfma_f32_16x16x32_bf16 v[96:99], v[28:31], v[68:71], v[96:99]
	v_mfma_f32_16x16x32_bf16 v[92:95], v[44:47], v[68:71], v[92:95]
	v_mfma_f32_16x16x32_bf16 v[88:91], v[56:59], v[68:71], v[88:91]
	v_mfma_f32_16x16x32_bf16 v[84:87], v[40:43], v[68:71], v[84:87]
	global_load_dwordx4 v[28:31], v[144:145], off offset:1024
	global_load_dwordx4 v[44:47], v[160:161], off offset:1024
	global_load_dwordx4 v[56:59], v[190:191], off offset:1024
	global_load_dwordx4 v[40:43], v[192:193], off offset:1024
	ds_read_b128 v[76:79], v155 offset:24896
	ds_read_b128 v[80:83], v155 offset:64
	ds_read_b128 v[68:71], v155 offset:49728
	v_mfma_f32_16x16x32_bf16 v[128:131], v[16:19], v[72:75], v[128:131]
	v_mfma_f32_16x16x32_bf16 v[124:127], v[20:23], v[72:75], v[124:127]
	s_waitcnt vmcnt(10)
	v_mfma_f32_16x16x32_bf16 v[120:123], v[36:39], v[72:75], v[120:123]
	v_mfma_f32_16x16x32_bf16 v[116:119], v[24:27], v[72:75], v[116:119]
	v_mfma_f32_16x16x32_bf16 v[112:115], v[16:19], v[64:67], v[112:115]
	v_mfma_f32_16x16x32_bf16 v[108:111], v[20:23], v[64:67], v[108:111]
	v_mfma_f32_16x16x32_bf16 v[104:107], v[36:39], v[64:67], v[104:107]
	v_mfma_f32_16x16x32_bf16 v[100:103], v[24:27], v[64:67], v[100:103]
	v_mfma_f32_16x16x32_bf16 v[96:99], v[16:19], v[52:55], v[96:99]
	v_mfma_f32_16x16x32_bf16 v[92:95], v[20:23], v[52:55], v[92:95]
	v_mfma_f32_16x16x32_bf16 v[88:91], v[36:39], v[52:55], v[88:91]
	v_mfma_f32_16x16x32_bf16 v[84:87], v[24:27], v[52:55], v[84:87]
	global_load_dwordx4 v[16:19], v[144:145], off offset:2048
	global_load_dwordx4 v[20:23], v[160:161], off offset:2048
	global_load_dwordx4 v[36:39], v[190:191], off offset:2048
	global_load_dwordx4 v[24:27], v[192:193], off offset:2048
	ds_read_b128 v[64:67], v155 offset:24960
	ds_read_b128 v[72:75], v155 offset:128
	ds_read_b128 v[52:55], v155 offset:49792
	v_mfma_f32_16x16x32_bf16 v[128:131], v[0:3], v[60:63], v[128:131]
	v_mfma_f32_16x16x32_bf16 v[124:127], v[4:7], v[60:63], v[124:127]
	s_waitcnt vmcnt(13)
	v_mfma_f32_16x16x32_bf16 v[120:123], v[12:15], v[60:63], v[120:123]
	s_waitcnt vmcnt(12)
	v_mfma_f32_16x16x32_bf16 v[116:119], v[8:11], v[60:63], v[116:119]
	v_mfma_f32_16x16x32_bf16 v[112:115], v[0:3], v[48:51], v[112:115]
	v_mfma_f32_16x16x32_bf16 v[108:111], v[4:7], v[48:51], v[108:111]
	v_mfma_f32_16x16x32_bf16 v[104:107], v[12:15], v[48:51], v[104:107]
	v_mfma_f32_16x16x32_bf16 v[100:103], v[8:11], v[48:51], v[100:103]
	s_waitcnt lgkmcnt(9)
	v_mfma_f32_16x16x32_bf16 v[96:99], v[0:3], v[32:35], v[96:99]
	v_mfma_f32_16x16x32_bf16 v[92:95], v[4:7], v[32:35], v[92:95]
	v_mfma_f32_16x16x32_bf16 v[88:91], v[12:15], v[32:35], v[88:91]
	v_mfma_f32_16x16x32_bf16 v[84:87], v[8:11], v[32:35], v[84:87]
	global_load_dwordx4 v[0:3], v[144:145], off offset:3072
	global_load_dwordx4 v[4:7], v[160:161], off offset:3072
	global_load_dwordx4 v[12:15], v[190:191], off offset:3072
	global_load_dwordx4 v[8:11], v[192:193], off offset:3072
	ds_read_b128 v[48:51], v155 offset:25024
	ds_read_b128 v[60:63], v155 offset:192
	ds_read_b128 v[32:35], v155 offset:49856
	s_waitcnt vmcnt(15) lgkmcnt(10)
	v_mfma_f32_16x16x32_bf16 v[128:131], v[156:159], v[182:185], v[128:131]
	s_waitcnt vmcnt(14)
	v_mfma_f32_16x16x32_bf16 v[124:127], v[164:167], v[182:185], v[124:127]
	s_waitcnt vmcnt(13)
	v_mfma_f32_16x16x32_bf16 v[120:123], v[168:171], v[182:185], v[120:123]
	s_waitcnt vmcnt(12)
	v_mfma_f32_16x16x32_bf16 v[116:119], v[174:177], v[182:185], v[116:119]
	v_mfma_f32_16x16x32_bf16 v[112:115], v[156:159], v[178:181], v[112:115]
	v_mfma_f32_16x16x32_bf16 v[108:111], v[164:167], v[178:181], v[108:111]
	v_mfma_f32_16x16x32_bf16 v[104:107], v[168:171], v[178:181], v[104:107]
	v_mfma_f32_16x16x32_bf16 v[100:103], v[174:177], v[178:181], v[100:103]
	s_waitcnt lgkmcnt(9)
	v_mfma_f32_16x16x32_bf16 v[96:99], v[156:159], v[186:189], v[96:99]
	v_mfma_f32_16x16x32_bf16 v[92:95], v[164:167], v[186:189], v[92:95]
	v_mfma_f32_16x16x32_bf16 v[88:91], v[168:171], v[186:189], v[88:91]
	v_mfma_f32_16x16x32_bf16 v[84:87], v[174:177], v[186:189], v[84:87]
	s_add_i32 s2, s2, 4
	v_lshl_add_u64 v[144:145], v[144:145], 0, s[52:53]
	s_cmp_lt_u32 s2, 16
	v_add_u32_e32 v155, 0x100, v155
	s_cbranch_scc1 .LBB0_1141
	v_add_co_u32_e32 v144, vcc, 0x5000, v142
	s_nop 1
	v_addc_co_u32_e32 v145, vcc, 0, v143, vcc
	v_add_co_u32_e32 v160, vcc, 0xb000, v142
	s_nop 1
	v_addc_co_u32_e32 v161, vcc, 0, v143, vcc
	global_load_dwordx4 v[156:159], v[144:145], off offset:3072
	global_load_dwordx4 v[164:167], v[160:161], off offset:3072
	v_add_co_u32_e32 v144, vcc, 0x11000, v142
	s_nop 1
	v_addc_co_u32_e32 v145, vcc, 0, v143, vcc
	v_add_co_u32_e32 v160, vcc, 0x17000, v142
	s_nop 1
	v_addc_co_u32_e32 v161, vcc, 0, v143, vcc
	global_load_dwordx4 v[142:145], v[144:145], off offset:3072
	s_nop 0
	global_load_dwordx4 v[168:171], v[160:161], off offset:3072
	ds_read_b128 v[174:177], v154 offset:26304
	ds_read_b128 v[178:181], v154 offset:1472
	ds_read_b128 v[182:185], v154 offset:51136
	s_waitcnt vmcnt(15) lgkmcnt(10)
	v_mfma_f32_16x16x32_bf16 v[128:131], v[28:31], v[80:83], v[128:131]
	s_waitcnt vmcnt(14)
	v_mfma_f32_16x16x32_bf16 v[124:127], v[44:47], v[80:83], v[124:127]
	s_waitcnt vmcnt(13)
	v_mfma_f32_16x16x32_bf16 v[120:123], v[56:59], v[80:83], v[120:123]
	s_waitcnt vmcnt(12)
	v_mfma_f32_16x16x32_bf16 v[80:83], v[40:43], v[80:83], v[116:119]
	v_mfma_f32_16x16x32_bf16 v[112:115], v[28:31], v[76:79], v[112:115]
	v_mfma_f32_16x16x32_bf16 v[108:111], v[44:47], v[76:79], v[108:111]
	v_mfma_f32_16x16x32_bf16 v[104:107], v[56:59], v[76:79], v[104:107]
	v_mfma_f32_16x16x32_bf16 v[76:79], v[40:43], v[76:79], v[100:103]
	s_waitcnt lgkmcnt(9)
	v_mfma_f32_16x16x32_bf16 v[28:31], v[28:31], v[68:71], v[96:99]
	v_mfma_f32_16x16x32_bf16 v[44:47], v[44:47], v[68:71], v[92:95]
	v_mfma_f32_16x16x32_bf16 v[56:59], v[56:59], v[68:71], v[88:91]
	v_mfma_f32_16x16x32_bf16 v[40:43], v[40:43], v[68:71], v[84:87]
	s_waitcnt vmcnt(11) lgkmcnt(7)
	v_mfma_f32_16x16x32_bf16 v[68:71], v[16:19], v[72:75], v[128:131]
	s_waitcnt vmcnt(10)
	v_mfma_f32_16x16x32_bf16 v[84:87], v[20:23], v[72:75], v[124:127]
	s_waitcnt vmcnt(9)
	v_mfma_f32_16x16x32_bf16 v[88:91], v[36:39], v[72:75], v[120:123]
	s_waitcnt vmcnt(8)
	v_mfma_f32_16x16x32_bf16 v[72:75], v[24:27], v[72:75], v[80:83]
	v_mfma_f32_16x16x32_bf16 v[80:83], v[16:19], v[64:67], v[112:115]
	v_mfma_f32_16x16x32_bf16 v[92:95], v[20:23], v[64:67], v[108:111]
	v_mfma_f32_16x16x32_bf16 v[96:99], v[36:39], v[64:67], v[104:107]
	v_mfma_f32_16x16x32_bf16 v[64:67], v[24:27], v[64:67], v[76:79]
	s_waitcnt lgkmcnt(6)
	v_mfma_f32_16x16x32_bf16 v[16:19], v[16:19], v[52:55], v[28:31]
	v_mfma_f32_16x16x32_bf16 v[20:23], v[20:23], v[52:55], v[44:47]
	v_mfma_f32_16x16x32_bf16 v[28:31], v[36:39], v[52:55], v[56:59]
	v_mfma_f32_16x16x32_bf16 v[24:27], v[24:27], v[52:55], v[40:43]
	s_waitcnt vmcnt(7) lgkmcnt(4)
	v_mfma_f32_16x16x32_bf16 v[36:39], v[0:3], v[60:63], v[68:71]
	s_waitcnt vmcnt(6)
	v_mfma_f32_16x16x32_bf16 v[40:43], v[4:7], v[60:63], v[84:87]
	s_waitcnt vmcnt(5)
	v_mfma_f32_16x16x32_bf16 v[44:47], v[12:15], v[60:63], v[88:91]
	s_waitcnt vmcnt(4)
	v_mfma_f32_16x16x32_bf16 v[52:55], v[8:11], v[60:63], v[72:75]
	v_mfma_f32_16x16x32_bf16 v[56:59], v[0:3], v[48:51], v[80:83]
	v_mfma_f32_16x16x32_bf16 v[60:63], v[4:7], v[48:51], v[92:95]
	v_mfma_f32_16x16x32_bf16 v[68:71], v[12:15], v[48:51], v[96:99]
	v_mfma_f32_16x16x32_bf16 v[48:51], v[8:11], v[48:51], v[64:67]
	s_waitcnt lgkmcnt(3)
	v_mfma_f32_16x16x32_bf16 v[0:3], v[0:3], v[32:35], v[16:19]
	v_mfma_f32_16x16x32_bf16 v[4:7], v[4:7], v[32:35], v[20:23]
	v_mfma_f32_16x16x32_bf16 v[64:67], v[12:15], v[32:35], v[28:31]
	v_mfma_f32_16x16x32_bf16 v[72:75], v[8:11], v[32:35], v[24:27]
	s_waitcnt vmcnt(3) lgkmcnt(1)
	v_mfma_f32_16x16x32_bf16 v[76:79], v[156:159], v[178:181], v[36:39]
	s_mov_b32 s14, 0x38e38e39
	s_movk_i32 s15, 0x7f8
	v_readlane_b32 s0, v253, 14
	s_waitcnt vmcnt(0)
	v_mfma_f32_16x16x32_bf16 v[16:19], v[168:171], v[174:177], v[48:51]
	v_readlane_b32 s2, v253, 9
	v_readlane_b32 s8, v253, 26
	v_readlane_b32 s9, v253, 27
	v_pk_mul_f32 v[50:51], v[76:77], v[76:77]
	v_pk_mul_f32 v[48:49], v[78:79], v[78:79]
	v_pk_mul_f32 v[50:51], v[76:77], v[50:51]
	v_pk_mul_f32 v[48:49], v[78:79], v[48:49]
	v_pk_fma_f32 v[50:51], v[50:51], s[42:43], v[76:77] op_sel_hi:[1,0,1]
	v_pk_fma_f32 v[48:49], v[48:49], s[42:43], v[78:79] op_sel_hi:[1,0,1]
	v_pk_mul_f32 v[50:51], v[50:51], s[96:97] op_sel_hi:[1,0]
	v_mfma_f32_16x16x32_bf16 v[36:39], v[142:145], v[178:181], v[44:47]
	v_exp_f32_e32 v50, v50
	v_exp_f32_e32 v51, v51
	v_pk_mul_f32 v[48:49], v[48:49], s[96:97] op_sel_hi:[1,0]
	v_add_u32_e32 v44, s7, v152
	v_mul_hi_i32 v45, v44, s14
	v_exp_f32_e32 v48, v48
	v_exp_f32_e32 v49, v49
	v_lshrrev_b32_e32 v46, 31, v45
	v_ashrrev_i32_e32 v45, 4, v45
	v_add_u32_e32 v45, v45, v46
	v_mul_lo_u32 v46, v45, s72
	v_pk_add_f32 v[50:51], v[50:51], 1.0 op_sel_hi:[1,0]
	v_sub_u32_e32 v46, v44, v46
	v_lshlrev_b32_e32 v47, 11, v45
	v_rcp_f32_e32 v50, v50
	v_rcp_f32_e32 v51, v51
	v_pk_add_f32 v[48:49], v[48:49], 1.0 op_sel_hi:[1,0]
	v_mfma_f32_16x16x32_bf16 v[32:35], v[168:171], v[178:181], v[52:55]
	v_cmp_gt_i32_e32 vcc, 8, v46
	v_rcp_f32_e32 v48, v48
	v_rcp_f32_e32 v49, v49
	v_add3_u32 v52, v46, v47, s15
	v_lshlrev_b32_e32 v46, 5, v46
	v_lshl_add_u32 v45, v45, 8, v46
	v_add_u32_e32 v46, s0, v45
	v_add_u32_e32 v47, s2, v52
	v_cndmask_b32_e32 v46, v47, v46, vcc
	v_pk_mul_f32 v[50:51], v[76:77], v[50:51]
	v_pk_mul_f32 v[48:49], v[78:79], v[48:49]
	v_cvt_pk_bf16_f32 v47, v50, v51
	ds_bpermute_b32 v50, v151, v47
	v_cvt_pk_bf16_f32 v47, v48, v49
	ds_bpermute_b32 v51, v151, v47
	v_ashrrev_i32_e32 v47, 31, v46
	v_mfma_f32_16x16x32_bf16 v[40:43], v[164:167], v[178:181], v[40:43]
	v_lshlrev_b64 v[46:47], 9, v[46:47]
	v_lshl_add_u64 v[46:47], s[8:9], 0, v[46:47]
	s_lshl_b64 s[4:5], s[4:5], 1
	v_lshl_add_u64 v[46:47], v[46:47], 0, s[4:5]
	v_lshl_add_u64 v[46:47], v[46:47], 0, v[172:173]
	s_waitcnt lgkmcnt(0)
	global_store_dwordx2 v[46:47], v[50:51], off
	s_nop 0
	v_pk_mul_f32 v[50:51], v[40:41], v[40:41]
	v_pk_mul_f32 v[48:49], v[42:43], v[42:43]
	v_pk_mul_f32 v[50:51], v[40:41], v[50:51]
	v_pk_mul_f32 v[48:49], v[42:43], v[48:49]
	v_pk_fma_f32 v[50:51], v[50:51], s[42:43], v[40:41] op_sel_hi:[1,0,1]
	v_pk_fma_f32 v[48:49], v[48:49], s[42:43], v[42:43] op_sel_hi:[1,0,1]
	v_pk_mul_f32 v[50:51], v[50:51], s[96:97] op_sel_hi:[1,0]
	v_pk_mul_f32 v[48:49], v[48:49], s[96:97] op_sel_hi:[1,0]
	v_exp_f32_e32 v50, v50
	v_exp_f32_e32 v51, v51
	v_exp_f32_e32 v48, v48
	v_exp_f32_e32 v49, v49
	v_readlane_b32 s3, v253, 10
	v_pk_add_f32 v[50:51], v[50:51], 1.0 op_sel_hi:[1,0]
	v_readlane_b32 s7, v253, 11
	v_rcp_f32_e32 v50, v50
	v_rcp_f32_e32 v51, v51
	v_pk_add_f32 v[48:49], v[48:49], 1.0 op_sel_hi:[1,0]
	v_add_u32_e32 v46, s3, v45
	v_rcp_f32_e32 v48, v48
	v_rcp_f32_e32 v49, v49
	v_add_u32_e32 v47, s7, v52
	v_pk_mul_f32 v[40:41], v[40:41], v[50:51]
	v_cndmask_b32_e32 v46, v47, v46, vcc
	v_pk_mul_f32 v[42:43], v[42:43], v[48:49]
	v_cvt_pk_bf16_f32 v40, v40, v41
	ds_bpermute_b32 v40, v151, v40
	v_cvt_pk_bf16_f32 v41, v42, v43
	ds_bpermute_b32 v41, v151, v41
	v_ashrrev_i32_e32 v47, 31, v46
	v_lshlrev_b64 v[42:43], 9, v[46:47]
	v_lshl_add_u64 v[42:43], s[8:9], 0, v[42:43]
	v_lshl_add_u64 v[42:43], v[42:43], 0, s[4:5]
	v_lshl_add_u64 v[42:43], v[42:43], 0, v[172:173]
	v_pk_mul_f32 v[46:47], v[36:37], v[36:37]
	s_waitcnt lgkmcnt(0)
	global_store_dwordx2 v[42:43], v[40:41], off
	v_pk_mul_f32 v[42:43], v[38:39], v[38:39]
	v_pk_mul_f32 v[46:47], v[36:37], v[46:47]
	v_pk_mul_f32 v[42:43], v[38:39], v[42:43]
	v_pk_fma_f32 v[46:47], v[46:47], s[42:43], v[36:37] op_sel_hi:[1,0,1]
	v_pk_fma_f32 v[42:43], v[42:43], s[42:43], v[38:39] op_sel_hi:[1,0,1]
	v_pk_mul_f32 v[46:47], v[46:47], s[96:97] op_sel_hi:[1,0]
	v_pk_mul_f32 v[42:43], v[42:43], s[96:97] op_sel_hi:[1,0]
	v_exp_f32_e32 v46, v46
	v_exp_f32_e32 v47, v47
	v_exp_f32_e32 v42, v42
	v_exp_f32_e32 v43, v43
	v_readlane_b32 s10, v253, 12
	v_pk_add_f32 v[46:47], v[46:47], 1.0 op_sel_hi:[1,0]
	v_readlane_b32 s11, v253, 13
	v_rcp_f32_e32 v46, v46
	v_rcp_f32_e32 v47, v47
	v_pk_add_f32 v[42:43], v[42:43], 1.0 op_sel_hi:[1,0]
	v_add_u32_e32 v40, s10, v45
	v_rcp_f32_e32 v42, v42
	v_rcp_f32_e32 v43, v43
	v_add_u32_e32 v41, s11, v52
	v_pk_mul_f32 v[36:37], v[36:37], v[46:47]
	v_cndmask_b32_e32 v40, v41, v40, vcc
	v_pk_mul_f32 v[38:39], v[38:39], v[42:43]
	v_cvt_pk_bf16_f32 v36, v36, v37
	ds_bpermute_b32 v36, v151, v36
	v_cvt_pk_bf16_f32 v37, v38, v39
	ds_bpermute_b32 v37, v151, v37
	v_ashrrev_i32_e32 v41, 31, v40
	v_lshlrev_b64 v[38:39], 9, v[40:41]
	v_lshl_add_u64 v[38:39], s[8:9], 0, v[38:39]
	v_lshl_add_u64 v[38:39], v[38:39], 0, s[4:5]
	v_lshl_add_u64 v[38:39], v[38:39], 0, v[172:173]
	v_pk_mul_f32 v[40:41], v[32:33], v[32:33]
	s_waitcnt lgkmcnt(0)
	global_store_dwordx2 v[38:39], v[36:37], off
	v_pk_mul_f32 v[38:39], v[34:35], v[34:35]
	v_pk_mul_f32 v[40:41], v[32:33], v[40:41]
	v_pk_mul_f32 v[38:39], v[34:35], v[38:39]
	v_pk_fma_f32 v[40:41], v[40:41], s[42:43], v[32:33] op_sel_hi:[1,0,1]
	v_pk_fma_f32 v[38:39], v[38:39], s[42:43], v[34:35] op_sel_hi:[1,0,1]
	v_pk_mul_f32 v[40:41], v[40:41], s[96:97] op_sel_hi:[1,0]
	v_pk_mul_f32 v[38:39], v[38:39], s[96:97] op_sel_hi:[1,0]
	v_exp_f32_e32 v40, v40
	v_exp_f32_e32 v41, v41
	v_exp_f32_e32 v38, v38
	v_exp_f32_e32 v39, v39
	v_readlane_b32 s12, v253, 15
	v_pk_add_f32 v[40:41], v[40:41], 1.0 op_sel_hi:[1,0]
	v_readlane_b32 s13, v253, 16
	v_rcp_f32_e32 v40, v40
	v_rcp_f32_e32 v41, v41
	v_pk_add_f32 v[38:39], v[38:39], 1.0 op_sel_hi:[1,0]
	v_add_u32_e32 v36, s12, v45
	v_rcp_f32_e32 v38, v38
	v_rcp_f32_e32 v39, v39
	v_add_u32_e32 v37, s13, v52
	v_pk_mul_f32 v[32:33], v[32:33], v[40:41]
	v_cndmask_b32_e32 v36, v37, v36, vcc
	v_pk_mul_f32 v[34:35], v[34:35], v[38:39]
	v_cvt_pk_bf16_f32 v32, v32, v33
	ds_bpermute_b32 v32, v151, v32
	v_cvt_pk_bf16_f32 v33, v34, v35
	ds_bpermute_b32 v33, v151, v33
	v_ashrrev_i32_e32 v37, 31, v36
	v_lshlrev_b64 v[34:35], 9, v[36:37]
	v_lshl_add_u64 v[34:35], s[8:9], 0, v[34:35]
	v_lshl_add_u64 v[34:35], v[34:35], 0, s[4:5]
	v_lshl_add_u64 v[34:35], v[34:35], 0, v[172:173]
	s_waitcnt lgkmcnt(0)
	global_store_dwordx2 v[34:35], v[32:33], off
	v_add_u32_e32 v32, 16, v44
	v_mfma_f32_16x16x32_bf16 v[28:31], v[156:159], v[174:177], v[56:59]
	v_mul_hi_i32 v33, v32, s14
	v_lshrrev_b32_e32 v34, 31, v33
	v_ashrrev_i32_e32 v33, 4, v33
	v_add_u32_e32 v33, v33, v34
	v_mul_lo_u32 v34, v33, s72
	v_sub_u32_e32 v32, v32, v34
	v_lshlrev_b32_e32 v34, 11, v33
	s_nop 0
	v_pk_mul_f32 v[36:37], v[28:29], v[28:29]
	v_add3_u32 v38, v32, v34, s15
	v_pk_mul_f32 v[34:35], v[30:31], v[30:31]
	v_pk_mul_f32 v[36:37], v[28:29], v[36:37]
	v_pk_mul_f32 v[34:35], v[30:31], v[34:35]
	v_pk_fma_f32 v[36:37], v[36:37], s[42:43], v[28:29] op_sel_hi:[1,0,1]
	v_pk_fma_f32 v[34:35], v[34:35], s[42:43], v[30:31] op_sel_hi:[1,0,1]
	v_pk_mul_f32 v[36:37], v[36:37], s[96:97] op_sel_hi:[1,0]
	v_pk_mul_f32 v[34:35], v[34:35], s[96:97] op_sel_hi:[1,0]
	v_exp_f32_e32 v36, v36
	v_exp_f32_e32 v37, v37
	v_exp_f32_e32 v34, v34
	v_exp_f32_e32 v35, v35
	v_cmp_gt_i32_e32 vcc, 8, v32
	v_pk_add_f32 v[36:37], v[36:37], 1.0 op_sel_hi:[1,0]
	v_lshlrev_b32_e32 v32, 5, v32
	v_rcp_f32_e32 v36, v36
	v_rcp_f32_e32 v37, v37
	v_pk_add_f32 v[34:35], v[34:35], 1.0 op_sel_hi:[1,0]
	v_lshl_add_u32 v39, v33, 8, v32
	v_rcp_f32_e32 v34, v34
	v_rcp_f32_e32 v35, v35
	v_add_u32_e32 v32, s0, v39
	v_add_u32_e32 v33, s2, v38
	v_pk_mul_f32 v[28:29], v[28:29], v[36:37]
	v_cndmask_b32_e32 v32, v33, v32, vcc
	v_pk_mul_f32 v[30:31], v[30:31], v[34:35]
	v_cvt_pk_bf16_f32 v28, v28, v29
	v_mfma_f32_16x16x32_bf16 v[24:27], v[164:167], v[174:177], v[60:63]
	v_cvt_pk_bf16_f32 v29, v30, v31
	ds_bpermute_b32 v28, v151, v28
	ds_bpermute_b32 v29, v151, v29
	v_ashrrev_i32_e32 v33, 31, v32
	v_lshlrev_b64 v[30:31], 9, v[32:33]
	v_lshl_add_u64 v[30:31], s[8:9], 0, v[30:31]
	v_lshl_add_u64 v[30:31], v[30:31], 0, s[4:5]
	v_lshl_add_u64 v[30:31], v[30:31], 0, v[172:173]
	s_nop 0
	v_pk_mul_f32 v[32:33], v[24:25], v[24:25]
	s_waitcnt lgkmcnt(0)
	global_store_dwordx2 v[30:31], v[28:29], off
	v_pk_mul_f32 v[30:31], v[26:27], v[26:27]
	v_pk_mul_f32 v[32:33], v[24:25], v[32:33]
	v_pk_mul_f32 v[30:31], v[26:27], v[30:31]
	v_pk_fma_f32 v[32:33], v[32:33], s[42:43], v[24:25] op_sel_hi:[1,0,1]
	v_pk_fma_f32 v[30:31], v[30:31], s[42:43], v[26:27] op_sel_hi:[1,0,1]
	v_pk_mul_f32 v[32:33], v[32:33], s[96:97] op_sel_hi:[1,0]
	v_pk_mul_f32 v[30:31], v[30:31], s[96:97] op_sel_hi:[1,0]
	v_exp_f32_e32 v32, v32
	v_exp_f32_e32 v33, v33
	v_exp_f32_e32 v30, v30
	v_exp_f32_e32 v31, v31
	v_add_u32_e32 v28, s3, v39
	v_pk_add_f32 v[32:33], v[32:33], 1.0 op_sel_hi:[1,0]
	v_add_u32_e32 v29, s7, v38
	v_rcp_f32_e32 v32, v32
	v_rcp_f32_e32 v33, v33
	v_pk_add_f32 v[30:31], v[30:31], 1.0 op_sel_hi:[1,0]
	v_cndmask_b32_e32 v28, v29, v28, vcc
	v_rcp_f32_e32 v30, v30
	v_rcp_f32_e32 v31, v31
	v_pk_mul_f32 v[24:25], v[24:25], v[32:33]
	v_mfma_f32_16x16x32_bf16 v[20:23], v[142:145], v[174:177], v[68:71]
	v_cvt_pk_bf16_f32 v24, v24, v25
	v_mul_f32_e64 v26, v26, v30
	v_mul_f32_e64 v27, v27, v31
	ds_bpermute_b32 v24, v151, v24
	v_cvt_pk_bf16_f32 v25, v26, v27
	ds_bpermute_b32 v25, v151, v25
	v_ashrrev_i32_e32 v29, 31, v28
	v_lshlrev_b64 v[26:27], 9, v[28:29]
	v_lshl_add_u64 v[26:27], s[8:9], 0, v[26:27]
	v_lshl_add_u64 v[26:27], v[26:27], 0, s[4:5]
	v_lshl_add_u64 v[26:27], v[26:27], 0, v[172:173]
	v_pk_mul_f32 v[28:29], v[20:21], v[20:21]
	s_waitcnt lgkmcnt(0)
	global_store_dwordx2 v[26:27], v[24:25], off
	v_pk_mul_f32 v[26:27], v[22:23], v[22:23]
	v_pk_mul_f32 v[28:29], v[20:21], v[28:29]
	v_pk_mul_f32 v[26:27], v[22:23], v[26:27]
	v_pk_fma_f32 v[28:29], v[28:29], s[42:43], v[20:21] op_sel_hi:[1,0,1]
	v_pk_fma_f32 v[26:27], v[26:27], s[42:43], v[22:23] op_sel_hi:[1,0,1]
	v_pk_mul_f32 v[28:29], v[28:29], s[96:97] op_sel_hi:[1,0]
	v_pk_mul_f32 v[26:27], v[26:27], s[96:97] op_sel_hi:[1,0]
	v_exp_f32_e32 v28, v28
	v_exp_f32_e32 v29, v29
	v_exp_f32_e32 v26, v26
	v_exp_f32_e32 v27, v27
	v_add_u32_e32 v24, s10, v39
	v_pk_add_f32 v[28:29], v[28:29], 1.0 op_sel_hi:[1,0]
	v_add_u32_e32 v25, s11, v38
	v_rcp_f32_e32 v28, v28
	v_rcp_f32_e32 v29, v29
	v_pk_add_f32 v[26:27], v[26:27], 1.0 op_sel_hi:[1,0]
	v_cndmask_b32_e32 v24, v25, v24, vcc
	v_rcp_f32_e32 v26, v26
	v_rcp_f32_e32 v27, v27
	v_pk_mul_f32 v[20:21], v[20:21], v[28:29]
	v_ashrrev_i32_e32 v25, 31, v24
	v_cvt_pk_bf16_f32 v20, v20, v21
	v_pk_mul_f32 v[22:23], v[22:23], v[26:27]
	ds_bpermute_b32 v20, v151, v20
	v_cvt_pk_bf16_f32 v21, v22, v23
	ds_bpermute_b32 v21, v151, v21
	v_lshlrev_b64 v[22:23], 9, v[24:25]
	v_lshl_add_u64 v[22:23], s[8:9], 0, v[22:23]
	v_lshl_add_u64 v[22:23], v[22:23], 0, s[4:5]
	v_lshl_add_u64 v[22:23], v[22:23], 0, v[172:173]
	v_pk_mul_f32 v[24:25], v[16:17], v[16:17]
	s_waitcnt lgkmcnt(0)
	global_store_dwordx2 v[22:23], v[20:21], off
	v_pk_mul_f32 v[22:23], v[18:19], v[18:19]
	v_pk_mul_f32 v[24:25], v[16:17], v[24:25]
	v_pk_mul_f32 v[22:23], v[18:19], v[22:23]
	v_pk_fma_f32 v[24:25], v[24:25], s[42:43], v[16:17] op_sel_hi:[1,0,1]
	v_pk_fma_f32 v[22:23], v[22:23], s[42:43], v[18:19] op_sel_hi:[1,0,1]
	v_pk_mul_f32 v[24:25], v[24:25], s[96:97] op_sel_hi:[1,0]
	v_pk_mul_f32 v[22:23], v[22:23], s[96:97] op_sel_hi:[1,0]
	v_exp_f32_e32 v24, v24
	v_exp_f32_e32 v25, v25
	v_exp_f32_e32 v22, v22
	v_exp_f32_e32 v23, v23
	v_add_u32_e32 v20, s12, v39
	v_pk_add_f32 v[24:25], v[24:25], 1.0 op_sel_hi:[1,0]
	v_add_u32_e32 v21, s13, v38
	v_rcp_f32_e32 v24, v24
	v_rcp_f32_e32 v25, v25
	v_pk_add_f32 v[22:23], v[22:23], 1.0 op_sel_hi:[1,0]
	v_cndmask_b32_e32 v20, v21, v20, vcc
	v_rcp_f32_e32 v22, v22
	v_rcp_f32_e32 v23, v23
	v_pk_mul_f32 v[16:17], v[16:17], v[24:25]
	v_ashrrev_i32_e32 v21, 31, v20
	v_cvt_pk_bf16_f32 v16, v16, v17
	v_pk_mul_f32 v[18:19], v[18:19], v[22:23]
	ds_bpermute_b32 v16, v151, v16
	v_cvt_pk_bf16_f32 v17, v18, v19
	ds_bpermute_b32 v17, v151, v17
	v_lshlrev_b64 v[18:19], 9, v[20:21]
	v_lshl_add_u64 v[18:19], s[8:9], 0, v[18:19]
	v_lshl_add_u64 v[18:19], v[18:19], 0, s[4:5]
	v_lshl_add_u64 v[18:19], v[18:19], 0, v[172:173]
	s_waitcnt lgkmcnt(0)
	global_store_dwordx2 v[18:19], v[16:17], off
	v_add_u32_e32 v16, 32, v44
	v_mfma_f32_16x16x32_bf16 v[12:15], v[156:159], v[182:185], v[0:3]
	v_mul_hi_i32 v17, v16, s14
	v_lshrrev_b32_e32 v18, 31, v17
	v_ashrrev_i32_e32 v17, 4, v17
	v_add_u32_e32 v17, v17, v18
	v_mul_lo_u32 v18, v17, s72
	v_sub_u32_e32 v16, v16, v18
	v_lshlrev_b32_e32 v18, 11, v17
	s_nop 0
	v_pk_mul_f32 v[20:21], v[12:13], v[12:13]
	v_add3_u32 v22, v16, v18, s15
	v_pk_mul_f32 v[18:19], v[14:15], v[14:15]
	v_pk_mul_f32 v[20:21], v[12:13], v[20:21]
	v_pk_mul_f32 v[18:19], v[14:15], v[18:19]
	v_pk_fma_f32 v[20:21], v[20:21], s[42:43], v[12:13] op_sel_hi:[1,0,1]
	v_pk_fma_f32 v[18:19], v[18:19], s[42:43], v[14:15] op_sel_hi:[1,0,1]
	v_pk_mul_f32 v[20:21], v[20:21], s[96:97] op_sel_hi:[1,0]
	v_pk_mul_f32 v[18:19], v[18:19], s[96:97] op_sel_hi:[1,0]
	v_exp_f32_e32 v20, v20
	v_exp_f32_e32 v21, v21
	v_exp_f32_e32 v18, v18
	v_exp_f32_e32 v19, v19
	v_cmp_gt_i32_e32 vcc, 8, v16
	v_pk_add_f32 v[20:21], v[20:21], 1.0 op_sel_hi:[1,0]
	v_lshlrev_b32_e32 v16, 5, v16
	v_rcp_f32_e32 v20, v20
	v_rcp_f32_e32 v21, v21
	v_pk_add_f32 v[18:19], v[18:19], 1.0 op_sel_hi:[1,0]
	v_lshl_add_u32 v23, v17, 8, v16
	v_rcp_f32_e32 v18, v18
	v_rcp_f32_e32 v19, v19
	v_add_u32_e32 v16, s0, v23
	v_add_u32_e32 v17, s2, v22
	v_pk_mul_f32 v[12:13], v[12:13], v[20:21]
	v_cndmask_b32_e32 v16, v17, v16, vcc
	v_pk_mul_f32 v[14:15], v[14:15], v[18:19]
	v_cvt_pk_bf16_f32 v12, v12, v13
	v_mfma_f32_16x16x32_bf16 v[8:11], v[164:167], v[182:185], v[4:7]
	v_cvt_pk_bf16_f32 v13, v14, v15
	ds_bpermute_b32 v12, v151, v12
	ds_bpermute_b32 v13, v151, v13
	v_ashrrev_i32_e32 v17, 31, v16
	v_lshlrev_b64 v[14:15], 9, v[16:17]
	v_lshl_add_u64 v[14:15], s[8:9], 0, v[14:15]
	v_lshl_add_u64 v[14:15], v[14:15], 0, s[4:5]
	v_lshl_add_u64 v[14:15], v[14:15], 0, v[172:173]
	s_nop 0
	v_pk_mul_f32 v[16:17], v[8:9], v[8:9]
	s_waitcnt lgkmcnt(0)
	global_store_dwordx2 v[14:15], v[12:13], off
	v_pk_mul_f32 v[14:15], v[10:11], v[10:11]
	v_pk_mul_f32 v[16:17], v[8:9], v[16:17]
	v_pk_mul_f32 v[14:15], v[10:11], v[14:15]
	v_pk_fma_f32 v[16:17], v[16:17], s[42:43], v[8:9] op_sel_hi:[1,0,1]
	v_pk_fma_f32 v[14:15], v[14:15], s[42:43], v[10:11] op_sel_hi:[1,0,1]
	v_pk_mul_f32 v[16:17], v[16:17], s[96:97] op_sel_hi:[1,0]
	v_pk_mul_f32 v[14:15], v[14:15], s[96:97] op_sel_hi:[1,0]
	v_exp_f32_e32 v16, v16
	v_exp_f32_e32 v17, v17
	v_exp_f32_e32 v14, v14
	v_exp_f32_e32 v15, v15
	v_add_u32_e32 v12, s3, v23
	v_pk_add_f32 v[16:17], v[16:17], 1.0 op_sel_hi:[1,0]
	v_add_u32_e32 v13, s7, v22
	v_rcp_f32_e32 v16, v16
	v_rcp_f32_e32 v17, v17
	v_pk_add_f32 v[14:15], v[14:15], 1.0 op_sel_hi:[1,0]
	v_cndmask_b32_e32 v12, v13, v12, vcc
	v_rcp_f32_e32 v14, v14
	v_rcp_f32_e32 v15, v15
	v_pk_mul_f32 v[8:9], v[8:9], v[16:17]
	v_mfma_f32_16x16x32_bf16 v[4:7], v[142:145], v[182:185], v[64:67]
	v_cvt_pk_bf16_f32 v8, v8, v9
	v_mul_f32_e64 v10, v10, v14
	v_mul_f32_e64 v11, v11, v15
	ds_bpermute_b32 v8, v151, v8
	v_cvt_pk_bf16_f32 v9, v10, v11
	ds_bpermute_b32 v9, v151, v9
	v_ashrrev_i32_e32 v13, 31, v12
	v_lshlrev_b64 v[10:11], 9, v[12:13]
	v_lshl_add_u64 v[10:11], s[8:9], 0, v[10:11]
	v_lshl_add_u64 v[10:11], v[10:11], 0, s[4:5]
	v_lshl_add_u64 v[10:11], v[10:11], 0, v[172:173]
	v_pk_mul_f32 v[12:13], v[4:5], v[4:5]
	s_waitcnt lgkmcnt(0)
	global_store_dwordx2 v[10:11], v[8:9], off
	v_pk_mul_f32 v[10:11], v[6:7], v[6:7]
	v_pk_mul_f32 v[12:13], v[4:5], v[12:13]
	v_pk_mul_f32 v[10:11], v[6:7], v[10:11]
	v_pk_fma_f32 v[12:13], v[12:13], s[42:43], v[4:5] op_sel_hi:[1,0,1]
	v_pk_fma_f32 v[10:11], v[10:11], s[42:43], v[6:7] op_sel_hi:[1,0,1]
	v_pk_mul_f32 v[12:13], v[12:13], s[96:97] op_sel_hi:[1,0]
	v_pk_mul_f32 v[10:11], v[10:11], s[96:97] op_sel_hi:[1,0]
	v_exp_f32_e32 v12, v12
	v_exp_f32_e32 v13, v13
	v_exp_f32_e32 v10, v10
	v_exp_f32_e32 v11, v11
	v_add_u32_e32 v8, s10, v23
	v_pk_add_f32 v[12:13], v[12:13], 1.0 op_sel_hi:[1,0]
	v_add_u32_e32 v9, s11, v22
	v_rcp_f32_e32 v12, v12
	v_rcp_f32_e32 v13, v13
	v_pk_add_f32 v[10:11], v[10:11], 1.0 op_sel_hi:[1,0]
	v_cndmask_b32_e32 v8, v9, v8, vcc
	v_rcp_f32_e32 v10, v10
	v_rcp_f32_e32 v11, v11
	v_pk_mul_f32 v[4:5], v[4:5], v[12:13]
	v_mfma_f32_16x16x32_bf16 v[0:3], v[168:171], v[182:185], v[72:75]
	v_cvt_pk_bf16_f32 v4, v4, v5
	v_mul_f32_e64 v6, v6, v10
	v_mul_f32_e64 v7, v7, v11
	ds_bpermute_b32 v4, v151, v4
	v_cvt_pk_bf16_f32 v5, v6, v7
	ds_bpermute_b32 v5, v151, v5
	v_ashrrev_i32_e32 v9, 31, v8
	v_lshlrev_b64 v[6:7], 9, v[8:9]
	v_lshl_add_u64 v[6:7], s[8:9], 0, v[6:7]
	v_lshl_add_u64 v[6:7], v[6:7], 0, s[4:5]
	v_lshl_add_u64 v[6:7], v[6:7], 0, v[172:173]
	v_pk_mul_f32 v[8:9], v[0:1], v[0:1]
	s_waitcnt lgkmcnt(0)
	global_store_dwordx2 v[6:7], v[4:5], off
	v_pk_mul_f32 v[6:7], v[2:3], v[2:3]
	v_pk_mul_f32 v[8:9], v[0:1], v[8:9]
	v_pk_mul_f32 v[6:7], v[2:3], v[6:7]
	v_pk_fma_f32 v[8:9], v[8:9], s[42:43], v[0:1] op_sel_hi:[1,0,1]
	v_pk_fma_f32 v[6:7], v[6:7], s[42:43], v[2:3] op_sel_hi:[1,0,1]
	v_pk_mul_f32 v[8:9], v[8:9], s[96:97] op_sel_hi:[1,0]
	v_pk_mul_f32 v[6:7], v[6:7], s[96:97] op_sel_hi:[1,0]
	v_exp_f32_e32 v8, v8
	v_exp_f32_e32 v9, v9
	v_exp_f32_e32 v6, v6
	v_exp_f32_e32 v7, v7
	v_add_u32_e32 v4, s12, v23
	v_pk_add_f32 v[8:9], v[8:9], 1.0 op_sel_hi:[1,0]
	v_add_u32_e32 v5, s13, v22
	v_rcp_f32_e32 v8, v8
	v_rcp_f32_e32 v9, v9
	v_pk_add_f32 v[6:7], v[6:7], 1.0 op_sel_hi:[1,0]
	v_cndmask_b32_e32 v4, v5, v4, vcc
	v_rcp_f32_e32 v6, v6
	v_rcp_f32_e32 v7, v7
	v_pk_mul_f32 v[0:1], v[0:1], v[8:9]
	v_ashrrev_i32_e32 v5, 31, v4
	v_cvt_pk_bf16_f32 v0, v0, v1
	v_pk_mul_f32 v[2:3], v[2:3], v[6:7]
	ds_bpermute_b32 v0, v151, v0
	v_cvt_pk_bf16_f32 v1, v2, v3
	ds_bpermute_b32 v1, v151, v1
	v_lshlrev_b64 v[2:3], 9, v[4:5]
	v_lshl_add_u64 v[2:3], s[8:9], 0, v[2:3]
	v_lshl_add_u64 v[2:3], v[2:3], 0, s[4:5]
	v_lshl_add_u64 v[2:3], v[2:3], 0, v[172:173]
	s_waitcnt lgkmcnt(0)
	global_store_dwordx2 v[2:3], v[0:1], off
	s_barrier
	s_add_i32 s6, s6, s37
	s_cmpk_lt_i32 s6, 0xc0
	s_cbranch_scc1 .LBB0_1116

.LBB0_1171:
	v_lshl_add_u64 v[174:175], s[4:5], 0, v[136:137]
	s_mov_b32 s2, 0x323f8000
	v_add_co_u32_e32 v142, vcc, s2, v174
	s_mov_b32 s2, 0x323fe000
	s_nop 0
	v_addc_co_u32_e32 v143, vcc, 0, v175, vcc
	v_add_co_u32_e32 v146, vcc, s2, v174
	s_mov_b32 s2, 0x32404000
	s_nop 0
	v_addc_co_u32_e32 v147, vcc, 0, v175, vcc
	v_add_co_u32_e32 v150, vcc, s2, v174
	s_mov_b32 s2, 0x3240a000
	s_nop 0
	v_addc_co_u32_e32 v151, vcc, 0, v175, vcc
	v_add_co_u32_e32 v154, vcc, s2, v174
	global_load_dwordx4 v[142:145], v[142:143], off offset:3072
	s_nop 0
	global_load_dwordx4 v[146:149], v[146:147], off offset:3072
	v_addc_co_u32_e32 v155, vcc, 0, v175, vcc
	global_load_dwordx4 v[150:153], v[150:151], off offset:3072
	s_nop 0
	global_load_dwordx4 v[154:157], v[154:155], off offset:3072
	ds_read_b128 v[158:161], v140 offset:24832
	ds_read_b128 v[164:167], v140
	ds_read_b128 v[168:171], v140 offset:49664
	s_waitcnt vmcnt(15) lgkmcnt(4)
	v_mfma_f32_16x16x32_bf16 v[128:131], v[36:39], v[80:83], v[128:131]
	s_waitcnt vmcnt(13)
	v_mfma_f32_16x16x32_bf16 v[124:127], v[48:51], v[80:83], v[124:127]
	s_waitcnt vmcnt(8)
	v_mfma_f32_16x16x32_bf16 v[120:123], v[68:71], v[80:83], v[120:123]
	v_mfma_f32_16x16x32_bf16 v[116:119], v[60:63], v[80:83], v[116:119]
	v_mfma_f32_16x16x32_bf16 v[112:115], v[36:39], v[76:79], v[112:115]
	v_mfma_f32_16x16x32_bf16 v[108:111], v[48:51], v[76:79], v[108:111]
	v_mfma_f32_16x16x32_bf16 v[104:107], v[68:71], v[76:79], v[104:107]
	v_mfma_f32_16x16x32_bf16 v[100:103], v[60:63], v[76:79], v[100:103]
	v_mfma_f32_16x16x32_bf16 v[96:99], v[36:39], v[72:75], v[96:99]
	v_mfma_f32_16x16x32_bf16 v[92:95], v[48:51], v[72:75], v[92:95]
	v_mfma_f32_16x16x32_bf16 v[88:91], v[68:71], v[72:75], v[88:91]
	v_mfma_f32_16x16x32_bf16 v[84:87], v[60:63], v[72:75], v[84:87]
	s_mov_b32 s2, 0x323f9000
	v_add_co_u32_e32 v176, vcc, s2, v174
	s_mov_b32 s2, 0x323ff000
	s_nop 0
	v_addc_co_u32_e32 v177, vcc, 0, v175, vcc
	v_add_co_u32_e32 v178, vcc, s2, v174
	s_mov_b32 s2, 0x32405000
	s_nop 0
	v_addc_co_u32_e32 v179, vcc, 0, v175, vcc
	v_add_co_u32_e32 v180, vcc, s2, v174
	s_mov_b32 s2, 0x3240b000
	s_nop 0
	v_addc_co_u32_e32 v181, vcc, 0, v175, vcc
	v_add_co_u32_e32 v174, vcc, s2, v174
	global_load_dwordx4 v[36:39], v[176:177], off
	global_load_dwordx4 v[48:51], v[178:179], off
	v_addc_co_u32_e32 v175, vcc, 0, v175, vcc
	global_load_dwordx4 v[68:71], v[180:181], off
	global_load_dwordx4 v[60:63], v[174:175], off
	ds_read_b128 v[76:79], v140 offset:24896
	ds_read_b128 v[80:83], v140 offset:64
	ds_read_b128 v[72:75], v140 offset:49728
	v_mfma_f32_16x16x32_bf16 v[128:131], v[16:19], v[64:67], v[128:131]
	v_mfma_f32_16x16x32_bf16 v[124:127], v[20:23], v[64:67], v[124:127]
	s_waitcnt vmcnt(10)
	v_mfma_f32_16x16x32_bf16 v[120:123], v[28:31], v[64:67], v[120:123]
	v_mfma_f32_16x16x32_bf16 v[116:119], v[24:27], v[64:67], v[116:119]
	v_mfma_f32_16x16x32_bf16 v[112:115], v[16:19], v[56:59], v[112:115]
	v_mfma_f32_16x16x32_bf16 v[108:111], v[20:23], v[56:59], v[108:111]
	v_mfma_f32_16x16x32_bf16 v[104:107], v[28:31], v[56:59], v[104:107]
	v_mfma_f32_16x16x32_bf16 v[100:103], v[24:27], v[56:59], v[100:103]
	v_mfma_f32_16x16x32_bf16 v[96:99], v[16:19], v[44:47], v[96:99]
	v_mfma_f32_16x16x32_bf16 v[92:95], v[20:23], v[44:47], v[92:95]
	v_mfma_f32_16x16x32_bf16 v[88:91], v[28:31], v[44:47], v[88:91]
	v_mfma_f32_16x16x32_bf16 v[84:87], v[24:27], v[44:47], v[84:87]
	global_load_dwordx4 v[16:19], v[176:177], off offset:1024
	global_load_dwordx4 v[20:23], v[178:179], off offset:1024
	global_load_dwordx4 v[28:31], v[180:181], off offset:1024
	global_load_dwordx4 v[24:27], v[174:175], off offset:1024
	ds_read_b128 v[56:59], v140 offset:24960
	ds_read_b128 v[64:67], v140 offset:128
	ds_read_b128 v[44:47], v140 offset:49792
	v_mfma_f32_16x16x32_bf16 v[128:131], v[0:3], v[52:55], v[128:131]
	v_mfma_f32_16x16x32_bf16 v[124:127], v[4:7], v[52:55], v[124:127]
	s_waitcnt vmcnt(13)
	v_mfma_f32_16x16x32_bf16 v[120:123], v[12:15], v[52:55], v[120:123]
	s_waitcnt vmcnt(12)
	v_mfma_f32_16x16x32_bf16 v[116:119], v[8:11], v[52:55], v[116:119]
	v_mfma_f32_16x16x32_bf16 v[112:115], v[0:3], v[40:43], v[112:115]
	v_mfma_f32_16x16x32_bf16 v[108:111], v[4:7], v[40:43], v[108:111]
	v_mfma_f32_16x16x32_bf16 v[104:107], v[12:15], v[40:43], v[104:107]
	v_mfma_f32_16x16x32_bf16 v[100:103], v[8:11], v[40:43], v[100:103]
	s_waitcnt lgkmcnt(9)
	v_mfma_f32_16x16x32_bf16 v[96:99], v[0:3], v[32:35], v[96:99]
	v_mfma_f32_16x16x32_bf16 v[92:95], v[4:7], v[32:35], v[92:95]
	v_mfma_f32_16x16x32_bf16 v[88:91], v[12:15], v[32:35], v[88:91]
	v_mfma_f32_16x16x32_bf16 v[84:87], v[8:11], v[32:35], v[84:87]
	global_load_dwordx4 v[0:3], v[176:177], off offset:2048
	global_load_dwordx4 v[4:7], v[178:179], off offset:2048
	global_load_dwordx4 v[12:15], v[180:181], off offset:2048
	global_load_dwordx4 v[8:11], v[174:175], off offset:2048
	ds_read_b128 v[40:43], v140 offset:25024
	ds_read_b128 v[52:55], v140 offset:192
	ds_read_b128 v[32:35], v140 offset:49856
	s_waitcnt vmcnt(15) lgkmcnt(10)
	v_mfma_f32_16x16x32_bf16 v[128:131], v[142:145], v[164:167], v[128:131]
	s_waitcnt vmcnt(14)
	v_mfma_f32_16x16x32_bf16 v[124:127], v[146:149], v[164:167], v[124:127]
	s_waitcnt vmcnt(13)
	v_mfma_f32_16x16x32_bf16 v[120:123], v[150:153], v[164:167], v[120:123]
	s_waitcnt vmcnt(12)
	v_mfma_f32_16x16x32_bf16 v[116:119], v[154:157], v[164:167], v[116:119]
	v_mfma_f32_16x16x32_bf16 v[112:115], v[142:145], v[158:161], v[112:115]
	v_mfma_f32_16x16x32_bf16 v[108:111], v[146:149], v[158:161], v[108:111]
	v_mfma_f32_16x16x32_bf16 v[104:107], v[150:153], v[158:161], v[104:107]
	v_mfma_f32_16x16x32_bf16 v[100:103], v[154:157], v[158:161], v[100:103]
	s_waitcnt lgkmcnt(9)
	v_mfma_f32_16x16x32_bf16 v[96:99], v[142:145], v[168:171], v[96:99]
	v_mfma_f32_16x16x32_bf16 v[92:95], v[146:149], v[168:171], v[92:95]
	v_mfma_f32_16x16x32_bf16 v[88:91], v[150:153], v[168:171], v[88:91]
	v_mfma_f32_16x16x32_bf16 v[84:87], v[154:157], v[168:171], v[84:87]
	s_add_i32 s1, s1, 4
	s_add_u32 s4, s4, 0x1000
	s_addc_u32 s5, s5, 0
	s_cmp_lt_u32 s1, 16
	v_add_u32_e32 v140, 0x100, v140
	s_cbranch_scc1 .LBB0_1171
	v_add_co_u32_e32 v136, vcc, 0x5000, v134
	s_nop 1
	v_addc_co_u32_e32 v137, vcc, 0, v135, vcc
	v_add_co_u32_e32 v144, vcc, 0xb000, v134
	s_nop 1
	v_addc_co_u32_e32 v145, vcc, 0, v135, vcc
	global_load_dwordx4 v[140:143], v[136:137], off offset:3072
	s_nop 0
	global_load_dwordx4 v[144:147], v[144:145], off offset:3072
	v_add_co_u32_e32 v136, vcc, 0x11000, v134
	s_nop 1
	v_addc_co_u32_e32 v137, vcc, 0, v135, vcc
	v_add_co_u32_e32 v148, vcc, 0x17000, v134
	s_nop 1
	v_addc_co_u32_e32 v149, vcc, 0, v135, vcc
	global_load_dwordx4 v[134:137], v[136:137], off offset:3072
	s_nop 0
	global_load_dwordx4 v[148:151], v[148:149], off offset:3072
	ds_read_b128 v[152:155], v139 offset:26304
	ds_read_b128 v[156:159], v139 offset:1472
	ds_read_b128 v[164:167], v139 offset:51136
	s_waitcnt vmcnt(15) lgkmcnt(10)
	v_mfma_f32_16x16x32_bf16 v[128:131], v[36:39], v[80:83], v[128:131]
	s_waitcnt vmcnt(14)
	v_mfma_f32_16x16x32_bf16 v[124:127], v[48:51], v[80:83], v[124:127]
	s_waitcnt vmcnt(13)
	v_mfma_f32_16x16x32_bf16 v[120:123], v[68:71], v[80:83], v[120:123]
	s_waitcnt vmcnt(12)
	v_mfma_f32_16x16x32_bf16 v[80:83], v[60:63], v[80:83], v[116:119]
	v_mfma_f32_16x16x32_bf16 v[112:115], v[36:39], v[76:79], v[112:115]
	v_mfma_f32_16x16x32_bf16 v[108:111], v[48:51], v[76:79], v[108:111]
	v_mfma_f32_16x16x32_bf16 v[104:107], v[68:71], v[76:79], v[104:107]
	v_mfma_f32_16x16x32_bf16 v[76:79], v[60:63], v[76:79], v[100:103]
	s_waitcnt lgkmcnt(9)
	v_mfma_f32_16x16x32_bf16 v[36:39], v[36:39], v[72:75], v[96:99]
	v_mfma_f32_16x16x32_bf16 v[48:51], v[48:51], v[72:75], v[92:95]
	v_mfma_f32_16x16x32_bf16 v[68:71], v[68:71], v[72:75], v[88:91]
	v_mfma_f32_16x16x32_bf16 v[60:63], v[60:63], v[72:75], v[84:87]
	s_waitcnt vmcnt(11) lgkmcnt(7)
	v_mfma_f32_16x16x32_bf16 v[72:75], v[16:19], v[64:67], v[128:131]
	s_waitcnt vmcnt(10)
	v_mfma_f32_16x16x32_bf16 v[84:87], v[20:23], v[64:67], v[124:127]
	s_waitcnt vmcnt(9)
	v_mfma_f32_16x16x32_bf16 v[88:91], v[28:31], v[64:67], v[120:123]
	s_waitcnt vmcnt(8)
	v_mfma_f32_16x16x32_bf16 v[64:67], v[24:27], v[64:67], v[80:83]
	v_mfma_f32_16x16x32_bf16 v[80:83], v[16:19], v[56:59], v[112:115]
	v_mfma_f32_16x16x32_bf16 v[92:95], v[20:23], v[56:59], v[108:111]
	v_mfma_f32_16x16x32_bf16 v[96:99], v[28:31], v[56:59], v[104:107]
	v_mfma_f32_16x16x32_bf16 v[56:59], v[24:27], v[56:59], v[76:79]
	s_waitcnt lgkmcnt(6)
	v_mfma_f32_16x16x32_bf16 v[16:19], v[16:19], v[44:47], v[36:39]
	v_mfma_f32_16x16x32_bf16 v[20:23], v[20:23], v[44:47], v[48:51]
	v_mfma_f32_16x16x32_bf16 v[28:31], v[28:31], v[44:47], v[68:71]
	v_mfma_f32_16x16x32_bf16 v[24:27], v[24:27], v[44:47], v[60:63]
	s_waitcnt vmcnt(7) lgkmcnt(4)
	v_mfma_f32_16x16x32_bf16 v[36:39], v[0:3], v[52:55], v[72:75]
	s_waitcnt vmcnt(6)
	v_mfma_f32_16x16x32_bf16 v[44:47], v[4:7], v[52:55], v[84:87]
	s_waitcnt vmcnt(5)
	v_mfma_f32_16x16x32_bf16 v[48:51], v[12:15], v[52:55], v[88:91]
	s_waitcnt vmcnt(4)
	v_mfma_f32_16x16x32_bf16 v[52:55], v[8:11], v[52:55], v[64:67]
	v_mfma_f32_16x16x32_bf16 v[60:63], v[0:3], v[40:43], v[80:83]
	v_mfma_f32_16x16x32_bf16 v[64:67], v[4:7], v[40:43], v[92:95]
	v_mfma_f32_16x16x32_bf16 v[68:71], v[12:15], v[40:43], v[96:99]
	v_mfma_f32_16x16x32_bf16 v[56:59], v[8:11], v[40:43], v[56:59]
	s_waitcnt lgkmcnt(3)
	v_mfma_f32_16x16x32_bf16 v[0:3], v[0:3], v[32:35], v[16:19]
	v_mfma_f32_16x16x32_bf16 v[4:7], v[4:7], v[32:35], v[20:23]
	v_mfma_f32_16x16x32_bf16 v[72:75], v[12:15], v[32:35], v[28:31]
	v_mfma_f32_16x16x32_bf16 v[76:79], v[8:11], v[32:35], v[24:27]
	s_waitcnt vmcnt(2) lgkmcnt(1)
	v_mfma_f32_16x16x32_bf16 v[40:43], v[144:147], v[156:159], v[44:47]
	v_readlane_b32 s0, v254, 30
	s_mov_b32 s10, 0x38e38e39
	s_movk_i32 s11, 0x7f8
	v_ashrrev_i32_e32 v45, 2, v162
	v_lshrrev_b32_e32 v46, 2, v133
	v_and_or_b32 v45, v45, -4, v46
	v_add_u32_e32 v45, s0, v45
	v_mfma_f32_16x16x32_bf16 v[80:83], v[140:143], v[156:159], v[36:39]
	v_mul_hi_i32 v46, v45, s10
	v_lshrrev_b32_e32 v47, 31, v46
	v_ashrrev_i32_e32 v46, 4, v46
	v_add_u32_e32 v46, v46, v47
	v_mul_lo_u32 v47, v46, s72
	s_waitcnt vmcnt(1)
	v_mfma_f32_16x16x32_bf16 v[36:39], v[134:137], v[156:159], v[48:51]
	v_sub_u32_e32 v47, v45, v47
	v_lshlrev_b32_e32 v44, 6, v133
	v_cmp_gt_i32_e32 vcc, 8, v47
	v_lshlrev_b32_e32 v48, 11, v46
	v_pk_mul_f32 v[50:51], v[80:81], v[80:81]
	s_waitcnt vmcnt(0)
	v_mfma_f32_16x16x32_bf16 v[32:35], v[148:151], v[156:159], v[52:55]
	v_mul_f32_e64 v50, v80, v50
	v_mul_f32_e64 v51, v81, v51
	v_and_b32_e32 v44, 0xc0, v44
	v_pk_fma_f32 v[50:51], v[50:51], s[42:43], v[80:81] op_sel_hi:[1,0,1]
	v_add3_u32 v52, v47, v48, s11
	v_pk_mul_f32 v[48:49], v[82:83], v[82:83]
	v_pk_mul_f32 v[50:51], v[50:51], s[96:97] op_sel_hi:[1,0]
	v_pk_mul_f32 v[48:49], v[82:83], v[48:49]
	v_exp_f32_e32 v50, v50
	v_pk_fma_f32 v[48:49], v[48:49], s[42:43], v[82:83] op_sel_hi:[1,0,1]
	v_exp_f32_e32 v51, v51
	v_pk_mul_f32 v[48:49], v[48:49], s[96:97] op_sel_hi:[1,0]
	v_lshlrev_b32_e32 v47, 5, v47
	v_exp_f32_e32 v48, v48
	v_exp_f32_e32 v49, v49
	v_pk_add_f32 v[50:51], v[50:51], 1.0 op_sel_hi:[1,0]
	v_lshl_add_u32 v53, v46, 8, v47
	v_rcp_f32_e32 v50, v50
	v_rcp_f32_e32 v51, v51
	v_pk_add_f32 v[48:49], v[48:49], 1.0 op_sel_hi:[1,0]
	v_readlane_b32 s0, v253, 14
	v_rcp_f32_e32 v48, v48
	v_rcp_f32_e32 v49, v49
	v_readlane_b32 s1, v253, 9
	v_add_u32_e32 v44, v44, v138
	v_add_u32_e32 v46, s0, v53
	v_add_u32_e32 v47, s1, v52
	v_and_or_b32 v44, v162, 12, v44
	v_cndmask_b32_e32 v46, v47, v46, vcc
	v_pk_mul_f32 v[50:51], v[80:81], v[50:51]
	v_pk_mul_f32 v[48:49], v[82:83], v[48:49]
	v_cvt_pk_bf16_f32 v47, v50, v51
	ds_bpermute_b32 v50, v44, v47
	v_cvt_pk_bf16_f32 v47, v48, v49
	ds_bpermute_b32 v51, v44, v47
	v_ashrrev_i32_e32 v47, 31, v46
	v_readlane_b32 s8, v253, 28
	v_lshlrev_b64 v[46:47], 9, v[46:47]
	v_readlane_b32 s9, v253, 29
	v_and_b32_e32 v172, 24, v132
	v_pk_mul_f32 v[48:49], v[42:43], v[42:43]
	v_lshl_add_u64 v[46:47], s[8:9], 0, v[46:47]
	v_lshl_add_u64 v[46:47], v[46:47], 0, v[172:173]
	s_waitcnt lgkmcnt(0)
	global_store_dwordx2 v[46:47], v[50:51], off
	v_pk_mul_f32 v[50:51], v[40:41], v[40:41]
	v_pk_mul_f32 v[48:49], v[42:43], v[48:49]
	v_pk_mul_f32 v[50:51], v[40:41], v[50:51]
	v_pk_fma_f32 v[48:49], v[48:49], s[42:43], v[42:43] op_sel_hi:[1,0,1]
	v_pk_fma_f32 v[50:51], v[50:51], s[42:43], v[40:41] op_sel_hi:[1,0,1]
	v_pk_mul_f32 v[48:49], v[48:49], s[96:97] op_sel_hi:[1,0]
	v_pk_mul_f32 v[50:51], v[50:51], s[96:97] op_sel_hi:[1,0]
	v_exp_f32_e32 v48, v48
	v_exp_f32_e32 v50, v50
	v_exp_f32_e32 v51, v51
	v_exp_f32_e32 v49, v49
	v_readlane_b32 s2, v253, 10
	v_readlane_b32 s3, v253, 11
	v_pk_add_f32 v[50:51], v[50:51], 1.0 op_sel_hi:[1,0]
	v_pk_add_f32 v[48:49], v[48:49], 1.0 op_sel_hi:[1,0]
	v_rcp_f32_e32 v50, v50
	v_rcp_f32_e32 v51, v51
	v_rcp_f32_e32 v48, v48
	v_rcp_f32_e32 v49, v49
	v_add_u32_e32 v46, s2, v53
	v_pk_mul_f32 v[40:41], v[40:41], v[50:51]
	v_add_u32_e32 v47, s3, v52
	v_pk_mul_f32 v[42:43], v[42:43], v[48:49]
	v_cvt_pk_bf16_f32 v40, v40, v41
	v_cndmask_b32_e32 v46, v47, v46, vcc
	v_cvt_pk_bf16_f32 v41, v42, v43
	ds_bpermute_b32 v40, v44, v40
	ds_bpermute_b32 v41, v44, v41
	v_ashrrev_i32_e32 v47, 31, v46
	v_lshlrev_b64 v[42:43], 9, v[46:47]
	v_lshl_add_u64 v[42:43], s[8:9], 0, v[42:43]
	v_lshl_add_u64 v[42:43], v[42:43], 0, v[172:173]
	v_pk_mul_f32 v[46:47], v[36:37], v[36:37]
	s_waitcnt lgkmcnt(0)
	global_store_dwordx2 v[42:43], v[40:41], off
	v_pk_mul_f32 v[42:43], v[38:39], v[38:39]
	v_pk_mul_f32 v[46:47], v[36:37], v[46:47]
	v_pk_mul_f32 v[42:43], v[38:39], v[42:43]
	v_pk_fma_f32 v[46:47], v[46:47], s[42:43], v[36:37] op_sel_hi:[1,0,1]
	v_pk_fma_f32 v[42:43], v[42:43], s[42:43], v[38:39] op_sel_hi:[1,0,1]
	v_pk_mul_f32 v[46:47], v[46:47], s[96:97] op_sel_hi:[1,0]
	v_pk_mul_f32 v[42:43], v[42:43], s[96:97] op_sel_hi:[1,0]
	v_exp_f32_e32 v46, v46
	v_exp_f32_e32 v47, v47
	v_exp_f32_e32 v42, v42
	v_exp_f32_e32 v43, v43
	v_readlane_b32 s4, v253, 12
	v_pk_add_f32 v[46:47], v[46:47], 1.0 op_sel_hi:[1,0]
	v_readlane_b32 s5, v253, 13
	v_rcp_f32_e32 v46, v46
	v_rcp_f32_e32 v47, v47
	v_pk_add_f32 v[42:43], v[42:43], 1.0 op_sel_hi:[1,0]
	v_add_u32_e32 v40, s4, v53
	v_rcp_f32_e32 v42, v42
	v_rcp_f32_e32 v43, v43
	v_pk_mul_f32 v[36:37], v[36:37], v[46:47]
	v_add_u32_e32 v41, s5, v52
	v_cvt_pk_bf16_f32 v36, v36, v37
	v_pk_mul_f32 v[38:39], v[38:39], v[42:43]
	v_cndmask_b32_e32 v40, v41, v40, vcc
	v_cvt_pk_bf16_f32 v37, v38, v39
	ds_bpermute_b32 v36, v44, v36
	ds_bpermute_b32 v37, v44, v37
	v_ashrrev_i32_e32 v41, 31, v40
	v_lshlrev_b64 v[38:39], 9, v[40:41]
	v_lshl_add_u64 v[38:39], s[8:9], 0, v[38:39]
	v_lshl_add_u64 v[38:39], v[38:39], 0, v[172:173]
	v_pk_mul_f32 v[40:41], v[32:33], v[32:33]
	s_waitcnt lgkmcnt(0)
	global_store_dwordx2 v[38:39], v[36:37], off
	v_pk_mul_f32 v[38:39], v[34:35], v[34:35]
	v_pk_mul_f32 v[40:41], v[32:33], v[40:41]
	v_pk_mul_f32 v[38:39], v[34:35], v[38:39]
	v_pk_fma_f32 v[40:41], v[40:41], s[42:43], v[32:33] op_sel_hi:[1,0,1]
	v_pk_fma_f32 v[38:39], v[38:39], s[42:43], v[34:35] op_sel_hi:[1,0,1]
	v_pk_mul_f32 v[40:41], v[40:41], s[96:97] op_sel_hi:[1,0]
	v_pk_mul_f32 v[38:39], v[38:39], s[96:97] op_sel_hi:[1,0]
	v_exp_f32_e32 v40, v40
	v_exp_f32_e32 v41, v41
	v_exp_f32_e32 v38, v38
	v_exp_f32_e32 v39, v39
	v_readlane_b32 s6, v253, 15
	v_pk_add_f32 v[40:41], v[40:41], 1.0 op_sel_hi:[1,0]
	v_readlane_b32 s7, v253, 16
	v_rcp_f32_e32 v40, v40
	v_rcp_f32_e32 v41, v41
	v_pk_add_f32 v[38:39], v[38:39], 1.0 op_sel_hi:[1,0]
	v_add_u32_e32 v36, s6, v53
	v_rcp_f32_e32 v38, v38
	v_rcp_f32_e32 v39, v39
	v_pk_mul_f32 v[32:33], v[32:33], v[40:41]
	v_add_u32_e32 v37, s7, v52
	v_cvt_pk_bf16_f32 v32, v32, v33
	v_pk_mul_f32 v[34:35], v[34:35], v[38:39]
	v_cndmask_b32_e32 v36, v37, v36, vcc
	v_cvt_pk_bf16_f32 v33, v34, v35
	ds_bpermute_b32 v32, v44, v32
	ds_bpermute_b32 v33, v44, v33
	v_ashrrev_i32_e32 v37, 31, v36
	v_lshlrev_b64 v[34:35], 9, v[36:37]
	v_lshl_add_u64 v[34:35], s[8:9], 0, v[34:35]
	v_lshl_add_u64 v[34:35], v[34:35], 0, v[172:173]
	s_waitcnt lgkmcnt(0)
	global_store_dwordx2 v[34:35], v[32:33], off
	v_add_u32_e32 v32, 16, v45
	v_mfma_f32_16x16x32_bf16 v[28:31], v[140:143], v[152:155], v[60:63]
	v_mul_hi_i32 v33, v32, s10
	v_lshrrev_b32_e32 v34, 31, v33
	v_ashrrev_i32_e32 v33, 4, v33
	v_add_u32_e32 v33, v33, v34
	v_mul_lo_u32 v34, v33, s72
	v_sub_u32_e32 v32, v32, v34
	v_lshlrev_b32_e32 v34, 11, v33
	s_nop 0
	v_pk_mul_f32 v[36:37], v[28:29], v[28:29]
	v_add3_u32 v38, v32, v34, s11
	v_pk_mul_f32 v[34:35], v[30:31], v[30:31]
	v_pk_mul_f32 v[36:37], v[28:29], v[36:37]
	v_pk_mul_f32 v[34:35], v[30:31], v[34:35]
	v_pk_fma_f32 v[36:37], v[36:37], s[42:43], v[28:29] op_sel_hi:[1,0,1]
	v_pk_fma_f32 v[34:35], v[34:35], s[42:43], v[30:31] op_sel_hi:[1,0,1]
	v_pk_mul_f32 v[36:37], v[36:37], s[96:97] op_sel_hi:[1,0]
	v_pk_mul_f32 v[34:35], v[34:35], s[96:97] op_sel_hi:[1,0]
	v_exp_f32_e32 v36, v36
	v_exp_f32_e32 v37, v37
	v_exp_f32_e32 v34, v34
	v_exp_f32_e32 v35, v35
	v_cmp_gt_i32_e32 vcc, 8, v32
	v_pk_add_f32 v[36:37], v[36:37], 1.0 op_sel_hi:[1,0]
	v_lshlrev_b32_e32 v32, 5, v32
	v_rcp_f32_e32 v36, v36
	v_rcp_f32_e32 v37, v37
	v_pk_add_f32 v[34:35], v[34:35], 1.0 op_sel_hi:[1,0]
	v_lshl_add_u32 v39, v33, 8, v32
	v_rcp_f32_e32 v34, v34
	v_rcp_f32_e32 v35, v35
	v_pk_mul_f32 v[28:29], v[28:29], v[36:37]
	v_add_u32_e32 v32, s0, v39
	v_add_u32_e32 v33, s1, v38
	v_pk_mul_f32 v[30:31], v[30:31], v[34:35]
	v_cvt_pk_bf16_f32 v28, v28, v29
	v_mfma_f32_16x16x32_bf16 v[24:27], v[144:147], v[152:155], v[64:67]
	v_cvt_pk_bf16_f32 v29, v30, v31
	v_cndmask_b32_e32 v32, v33, v32, vcc
	ds_bpermute_b32 v28, v44, v28
	ds_bpermute_b32 v29, v44, v29
	v_ashrrev_i32_e32 v33, 31, v32
	v_lshlrev_b64 v[30:31], 9, v[32:33]
	v_lshl_add_u64 v[30:31], s[8:9], 0, v[30:31]
	v_lshl_add_u64 v[30:31], v[30:31], 0, v[172:173]
	s_nop 0
	v_pk_mul_f32 v[32:33], v[24:25], v[24:25]
	s_waitcnt lgkmcnt(0)
	global_store_dwordx2 v[30:31], v[28:29], off
	v_pk_mul_f32 v[30:31], v[26:27], v[26:27]
	v_pk_mul_f32 v[32:33], v[24:25], v[32:33]
	v_pk_mul_f32 v[30:31], v[26:27], v[30:31]
	v_pk_fma_f32 v[32:33], v[32:33], s[42:43], v[24:25] op_sel_hi:[1,0,1]
	v_pk_fma_f32 v[30:31], v[30:31], s[42:43], v[26:27] op_sel_hi:[1,0,1]
	v_pk_mul_f32 v[32:33], v[32:33], s[96:97] op_sel_hi:[1,0]
	v_pk_mul_f32 v[30:31], v[30:31], s[96:97] op_sel_hi:[1,0]
	v_exp_f32_e32 v32, v32
	v_exp_f32_e32 v33, v33
	v_exp_f32_e32 v30, v30
	v_exp_f32_e32 v31, v31
	v_add_u32_e32 v28, s2, v39
	v_pk_add_f32 v[32:33], v[32:33], 1.0 op_sel_hi:[1,0]
	v_add_u32_e32 v29, s3, v38
	v_rcp_f32_e32 v32, v32
	v_rcp_f32_e32 v33, v33
	v_pk_add_f32 v[30:31], v[30:31], 1.0 op_sel_hi:[1,0]
	v_mfma_f32_16x16x32_bf16 v[20:23], v[134:137], v[152:155], v[68:71]
	v_rcp_f32_e32 v30, v30
	v_rcp_f32_e32 v31, v31
	v_pk_mul_f32 v[24:25], v[24:25], v[32:33]
	v_cndmask_b32_e32 v28, v29, v28, vcc
	v_cvt_pk_bf16_f32 v24, v24, v25
	v_pk_mul_f32 v[26:27], v[26:27], v[30:31]
	ds_bpermute_b32 v24, v44, v24
	v_cvt_pk_bf16_f32 v25, v26, v27
	ds_bpermute_b32 v25, v44, v25
	v_ashrrev_i32_e32 v29, 31, v28
	v_lshlrev_b64 v[26:27], 9, v[28:29]
	v_lshl_add_u64 v[26:27], s[8:9], 0, v[26:27]
	v_lshl_add_u64 v[26:27], v[26:27], 0, v[172:173]
	v_pk_mul_f32 v[28:29], v[20:21], v[20:21]
	s_waitcnt lgkmcnt(0)
	global_store_dwordx2 v[26:27], v[24:25], off
	v_pk_mul_f32 v[26:27], v[22:23], v[22:23]
	v_pk_mul_f32 v[28:29], v[20:21], v[28:29]
	v_pk_mul_f32 v[26:27], v[22:23], v[26:27]
	v_pk_fma_f32 v[28:29], v[28:29], s[42:43], v[20:21] op_sel_hi:[1,0,1]
	v_pk_fma_f32 v[26:27], v[26:27], s[42:43], v[22:23] op_sel_hi:[1,0,1]
	v_pk_mul_f32 v[28:29], v[28:29], s[96:97] op_sel_hi:[1,0]
	v_pk_mul_f32 v[26:27], v[26:27], s[96:97] op_sel_hi:[1,0]
	v_exp_f32_e32 v28, v28
	v_exp_f32_e32 v29, v29
	v_exp_f32_e32 v26, v26
	v_exp_f32_e32 v27, v27
	v_add_u32_e32 v24, s4, v39
	v_pk_add_f32 v[28:29], v[28:29], 1.0 op_sel_hi:[1,0]
	v_add_u32_e32 v25, s5, v38
	v_rcp_f32_e32 v28, v28
	v_rcp_f32_e32 v29, v29
	v_pk_add_f32 v[26:27], v[26:27], 1.0 op_sel_hi:[1,0]
	v_mfma_f32_16x16x32_bf16 v[16:19], v[148:151], v[152:155], v[56:59]
	v_rcp_f32_e32 v26, v26
	v_rcp_f32_e32 v27, v27
	v_pk_mul_f32 v[20:21], v[20:21], v[28:29]
	v_cndmask_b32_e32 v24, v25, v24, vcc
	v_cvt_pk_bf16_f32 v20, v20, v21
	v_pk_mul_f32 v[22:23], v[22:23], v[26:27]
	ds_bpermute_b32 v20, v44, v20
	v_cvt_pk_bf16_f32 v21, v22, v23
	ds_bpermute_b32 v21, v44, v21
	v_ashrrev_i32_e32 v25, 31, v24
	v_lshlrev_b64 v[22:23], 9, v[24:25]
	v_lshl_add_u64 v[22:23], s[8:9], 0, v[22:23]
	v_lshl_add_u64 v[22:23], v[22:23], 0, v[172:173]
	v_pk_mul_f32 v[24:25], v[16:17], v[16:17]
	s_waitcnt lgkmcnt(0)
	global_store_dwordx2 v[22:23], v[20:21], off
	v_pk_mul_f32 v[22:23], v[18:19], v[18:19]
	v_pk_mul_f32 v[24:25], v[16:17], v[24:25]
	v_pk_mul_f32 v[22:23], v[18:19], v[22:23]
	v_pk_fma_f32 v[24:25], v[24:25], s[42:43], v[16:17] op_sel_hi:[1,0,1]
	v_pk_fma_f32 v[22:23], v[22:23], s[42:43], v[18:19] op_sel_hi:[1,0,1]
	v_pk_mul_f32 v[24:25], v[24:25], s[96:97] op_sel_hi:[1,0]
	v_pk_mul_f32 v[22:23], v[22:23], s[96:97] op_sel_hi:[1,0]
	v_exp_f32_e32 v24, v24
	v_exp_f32_e32 v25, v25
	v_exp_f32_e32 v22, v22
	v_exp_f32_e32 v23, v23
	v_add_u32_e32 v20, s6, v39
	v_pk_add_f32 v[24:25], v[24:25], 1.0 op_sel_hi:[1,0]
	v_add_u32_e32 v21, s7, v38
	v_rcp_f32_e32 v24, v24
	v_rcp_f32_e32 v25, v25
	v_pk_add_f32 v[22:23], v[22:23], 1.0 op_sel_hi:[1,0]
	v_cndmask_b32_e32 v20, v21, v20, vcc
	v_rcp_f32_e32 v22, v22
	v_rcp_f32_e32 v23, v23
	v_pk_mul_f32 v[16:17], v[16:17], v[24:25]
	v_ashrrev_i32_e32 v21, 31, v20
	v_cvt_pk_bf16_f32 v16, v16, v17
	v_pk_mul_f32 v[18:19], v[18:19], v[22:23]
	ds_bpermute_b32 v16, v44, v16
	v_cvt_pk_bf16_f32 v17, v18, v19
	ds_bpermute_b32 v17, v44, v17
	v_lshlrev_b64 v[18:19], 9, v[20:21]
	v_lshl_add_u64 v[18:19], s[8:9], 0, v[18:19]
	v_lshl_add_u64 v[18:19], v[18:19], 0, v[172:173]
	v_mfma_f32_16x16x32_bf16 v[12:15], v[140:143], v[164:167], v[0:3]
	s_waitcnt lgkmcnt(0)
	global_store_dwordx2 v[18:19], v[16:17], off
	v_add_u32_e32 v16, 32, v45
	v_mul_hi_i32 v17, v16, s10
	v_lshrrev_b32_e32 v18, 31, v17
	v_ashrrev_i32_e32 v17, 4, v17
	v_add_u32_e32 v17, v17, v18
	v_mul_lo_u32 v18, v17, s72
	v_sub_u32_e32 v16, v16, v18
	v_lshlrev_b32_e32 v18, 11, v17
	v_pk_mul_f32 v[20:21], v[12:13], v[12:13]
	v_add3_u32 v22, v16, v18, s11
	v_pk_mul_f32 v[18:19], v[14:15], v[14:15]
	v_pk_mul_f32 v[20:21], v[12:13], v[20:21]
	v_pk_mul_f32 v[18:19], v[14:15], v[18:19]
	v_pk_fma_f32 v[20:21], v[20:21], s[42:43], v[12:13] op_sel_hi:[1,0,1]
	v_pk_fma_f32 v[18:19], v[18:19], s[42:43], v[14:15] op_sel_hi:[1,0,1]
	v_pk_mul_f32 v[20:21], v[20:21], s[96:97] op_sel_hi:[1,0]
	v_pk_mul_f32 v[18:19], v[18:19], s[96:97] op_sel_hi:[1,0]
	v_exp_f32_e32 v20, v20
	v_exp_f32_e32 v21, v21
	v_exp_f32_e32 v18, v18
	v_exp_f32_e32 v19, v19
	v_cmp_gt_i32_e32 vcc, 8, v16
	v_pk_add_f32 v[20:21], v[20:21], 1.0 op_sel_hi:[1,0]
	v_lshlrev_b32_e32 v16, 5, v16
	v_rcp_f32_e32 v20, v20
	v_rcp_f32_e32 v21, v21
	v_pk_add_f32 v[18:19], v[18:19], 1.0 op_sel_hi:[1,0]
	v_lshl_add_u32 v23, v17, 8, v16
	v_rcp_f32_e32 v18, v18
	v_rcp_f32_e32 v19, v19
	v_pk_mul_f32 v[12:13], v[12:13], v[20:21]
	v_add_u32_e32 v16, s0, v23
	v_add_u32_e32 v17, s1, v22
	v_pk_mul_f32 v[14:15], v[14:15], v[18:19]
	v_cvt_pk_bf16_f32 v12, v12, v13
	v_mfma_f32_16x16x32_bf16 v[8:11], v[144:147], v[164:167], v[4:7]
	v_cvt_pk_bf16_f32 v13, v14, v15
	v_cndmask_b32_e32 v16, v17, v16, vcc
	ds_bpermute_b32 v12, v44, v12
	ds_bpermute_b32 v13, v44, v13
	v_ashrrev_i32_e32 v17, 31, v16
	v_lshlrev_b64 v[14:15], 9, v[16:17]
	v_lshl_add_u64 v[14:15], s[8:9], 0, v[14:15]
	v_lshl_add_u64 v[14:15], v[14:15], 0, v[172:173]
	s_nop 0
	v_pk_mul_f32 v[16:17], v[8:9], v[8:9]
	s_waitcnt lgkmcnt(0)
	global_store_dwordx2 v[14:15], v[12:13], off
	v_pk_mul_f32 v[14:15], v[10:11], v[10:11]
	v_pk_mul_f32 v[16:17], v[8:9], v[16:17]
	v_pk_mul_f32 v[14:15], v[10:11], v[14:15]
	v_pk_fma_f32 v[16:17], v[16:17], s[42:43], v[8:9] op_sel_hi:[1,0,1]
	v_pk_fma_f32 v[14:15], v[14:15], s[42:43], v[10:11] op_sel_hi:[1,0,1]
	v_pk_mul_f32 v[16:17], v[16:17], s[96:97] op_sel_hi:[1,0]
	v_pk_mul_f32 v[14:15], v[14:15], s[96:97] op_sel_hi:[1,0]
	v_exp_f32_e32 v16, v16
	v_exp_f32_e32 v17, v17
	v_exp_f32_e32 v14, v14
	v_exp_f32_e32 v15, v15
	v_add_u32_e32 v12, s2, v23
	v_pk_add_f32 v[16:17], v[16:17], 1.0 op_sel_hi:[1,0]
	v_add_u32_e32 v13, s3, v22
	v_rcp_f32_e32 v16, v16
	v_rcp_f32_e32 v17, v17
	v_pk_add_f32 v[14:15], v[14:15], 1.0 op_sel_hi:[1,0]
	v_mfma_f32_16x16x32_bf16 v[4:7], v[134:137], v[164:167], v[72:75]
	v_rcp_f32_e32 v14, v14
	v_rcp_f32_e32 v15, v15
	v_pk_mul_f32 v[8:9], v[8:9], v[16:17]
	v_cndmask_b32_e32 v12, v13, v12, vcc
	v_cvt_pk_bf16_f32 v8, v8, v9
	v_pk_mul_f32 v[10:11], v[10:11], v[14:15]
	ds_bpermute_b32 v8, v44, v8
	v_cvt_pk_bf16_f32 v9, v10, v11
	ds_bpermute_b32 v9, v44, v9
	v_ashrrev_i32_e32 v13, 31, v12
	v_lshlrev_b64 v[10:11], 9, v[12:13]
	v_lshl_add_u64 v[10:11], s[8:9], 0, v[10:11]
	v_lshl_add_u64 v[10:11], v[10:11], 0, v[172:173]
	v_pk_mul_f32 v[12:13], v[4:5], v[4:5]
	s_waitcnt lgkmcnt(0)
	global_store_dwordx2 v[10:11], v[8:9], off
	v_pk_mul_f32 v[10:11], v[6:7], v[6:7]
	v_pk_mul_f32 v[12:13], v[4:5], v[12:13]
	v_pk_mul_f32 v[10:11], v[6:7], v[10:11]
	v_pk_fma_f32 v[12:13], v[12:13], s[42:43], v[4:5] op_sel_hi:[1,0,1]
	v_pk_fma_f32 v[10:11], v[10:11], s[42:43], v[6:7] op_sel_hi:[1,0,1]
	v_pk_mul_f32 v[12:13], v[12:13], s[96:97] op_sel_hi:[1,0]
	v_pk_mul_f32 v[10:11], v[10:11], s[96:97] op_sel_hi:[1,0]
	v_exp_f32_e32 v12, v12
	v_exp_f32_e32 v13, v13
	v_exp_f32_e32 v10, v10
	v_exp_f32_e32 v11, v11
	v_add_u32_e32 v8, s4, v23
	v_pk_add_f32 v[12:13], v[12:13], 1.0 op_sel_hi:[1,0]
	v_add_u32_e32 v9, s5, v22
	v_rcp_f32_e32 v12, v12
	v_rcp_f32_e32 v13, v13
	v_pk_add_f32 v[10:11], v[10:11], 1.0 op_sel_hi:[1,0]
	v_mfma_f32_16x16x32_bf16 v[0:3], v[148:151], v[164:167], v[76:79]
	v_rcp_f32_e32 v10, v10
	v_rcp_f32_e32 v11, v11
	v_pk_mul_f32 v[4:5], v[4:5], v[12:13]
	v_cndmask_b32_e32 v8, v9, v8, vcc
	v_cvt_pk_bf16_f32 v4, v4, v5
	v_pk_mul_f32 v[6:7], v[6:7], v[10:11]
	ds_bpermute_b32 v4, v44, v4
	v_cvt_pk_bf16_f32 v5, v6, v7
	ds_bpermute_b32 v5, v44, v5
	v_ashrrev_i32_e32 v9, 31, v8
	v_lshlrev_b64 v[6:7], 9, v[8:9]
	v_lshl_add_u64 v[6:7], s[8:9], 0, v[6:7]
	v_lshl_add_u64 v[6:7], v[6:7], 0, v[172:173]
	v_pk_mul_f32 v[8:9], v[0:1], v[0:1]
	s_waitcnt lgkmcnt(0)
	global_store_dwordx2 v[6:7], v[4:5], off
	v_pk_mul_f32 v[6:7], v[2:3], v[2:3]
	v_pk_mul_f32 v[8:9], v[0:1], v[8:9]
	v_pk_mul_f32 v[6:7], v[2:3], v[6:7]
	v_pk_fma_f32 v[8:9], v[8:9], s[42:43], v[0:1] op_sel_hi:[1,0,1]
	v_pk_fma_f32 v[6:7], v[6:7], s[42:43], v[2:3] op_sel_hi:[1,0,1]
	v_pk_mul_f32 v[8:9], v[8:9], s[96:97] op_sel_hi:[1,0]
	v_pk_mul_f32 v[6:7], v[6:7], s[96:97] op_sel_hi:[1,0]
	v_exp_f32_e32 v8, v8
	v_exp_f32_e32 v9, v9
	v_exp_f32_e32 v6, v6
	v_exp_f32_e32 v7, v7
	v_add_u32_e32 v4, s6, v23
	v_pk_add_f32 v[8:9], v[8:9], 1.0 op_sel_hi:[1,0]
	v_add_u32_e32 v5, s7, v22
	v_rcp_f32_e32 v8, v8
	v_rcp_f32_e32 v9, v9
	v_pk_add_f32 v[6:7], v[6:7], 1.0 op_sel_hi:[1,0]
	v_cndmask_b32_e32 v4, v5, v4, vcc
	v_rcp_f32_e32 v6, v6
	v_rcp_f32_e32 v7, v7
	v_pk_mul_f32 v[0:1], v[0:1], v[8:9]
	v_ashrrev_i32_e32 v5, 31, v4
	v_cvt_pk_bf16_f32 v0, v0, v1
	v_pk_mul_f32 v[2:3], v[2:3], v[6:7]
	ds_bpermute_b32 v0, v44, v0
	v_cvt_pk_bf16_f32 v1, v2, v3
	ds_bpermute_b32 v1, v44, v1
	v_lshlrev_b64 v[2:3], 9, v[4:5]
	v_lshl_add_u64 v[2:3], s[8:9], 0, v[2:3]
	v_lshl_add_u64 v[2:3], v[2:3], 0, v[172:173]
	s_waitcnt lgkmcnt(0)
	global_store_dwordx2 v[2:3], v[0:1], off
	s_barrier

.LBB0_1227:
	v_readlane_b32 s0, v250, 4
	s_waitcnt lgkmcnt(0)
	s_mov_b32 s2, s100
	s_cmp_le_i32 s2, s1
	s_cselect_b64 s[2:3], -1, 0
	s_mov_b32 s4, s101
	s_cmp_lt_i32 s1, s4
	s_cselect_b64 s[6:7], -1, 0
	s_and_b64 s[6:7], s[2:3], s[6:7]
	s_mov_b64 s[2:3], -1
	s_and_b64 vcc, exec, s[6:7]
	s_cbranch_vccnz .LBB0_1229
	v_readlane_b32 s0, v255, 35
	s_add_i32 s1, s0, 9
	s_mov_b64 s[2:3], 0

.LBB0_1232:
	v_lshl_add_u64 v[16:17], s[60:61], 0, v[128:129]
	v_add_co_u32_e32 v0, vcc, 0x4c3ab000, v16
	s_nop 1
	v_addc_co_u32_e32 v1, vcc, 0, v17, vcc
	v_add_co_u32_e32 v4, vcc, 0x4c3ad000, v16
	s_nop 1
	v_addc_co_u32_e32 v5, vcc, 0, v17, vcc
	v_add_co_u32_e32 v8, vcc, 0x4c3af000, v16
	global_load_dwordx4 v[0:3], v[0:1], off offset:1536
	s_nop 0
	global_load_dwordx4 v[4:7], v[4:5], off offset:1536
	v_addc_co_u32_e32 v9, vcc, 0, v17, vcc
	v_add_co_u32_e32 v12, vcc, 0x4c3b1000, v16
	s_nop 1
	v_addc_co_u32_e32 v13, vcc, 0, v17, vcc
	v_add_co_u32_e32 v18, vcc, 0x4c3b3000, v16
	global_load_dwordx4 v[8:11], v[8:9], off offset:1536
	s_nop 0
	global_load_dwordx4 v[12:15], v[12:13], off offset:1536
	v_addc_co_u32_e32 v19, vcc, 0, v17, vcc
	v_add_co_u32_e32 v20, vcc, 0x4c3b5000, v16
	s_nop 1
	v_addc_co_u32_e32 v21, vcc, 0, v17, vcc
	global_load_dwordx4 v[16:19], v[18:19], off offset:1536
	s_nop 0
	global_load_dwordx4 v[20:23], v[20:21], off offset:1536
	s_waitcnt vmcnt(5)
	ds_write_b128 v132, v[0:3]
	s_waitcnt vmcnt(4)
	ds_write_b128 v132, v[4:7] offset:8448
	s_waitcnt vmcnt(3)
	ds_write_b128 v132, v[8:11] offset:16896
	s_waitcnt vmcnt(2)
	ds_write_b128 v132, v[12:15] offset:25344
	s_waitcnt vmcnt(1)
	ds_write_b128 v132, v[16:19] offset:33792
	s_waitcnt vmcnt(0)
	ds_write_b128 v132, v[20:23] offset:42240
	s_waitcnt lgkmcnt(0)
	s_barrier
	global_load_dwordx4 v[0:3], v[64:65], off
	global_load_dwordx4 v[4:7], v[66:67], off
	global_load_dwordx4 v[8:11], v[60:61], off
	global_load_dwordx4 v[12:15], v[60:61], off offset:1024
	global_load_dwordx4 v[16:19], v[68:69], off
	global_load_dwordx4 v[20:23], v[70:71], off
	global_load_dwordx4 v[24:27], v[62:63], off
	global_load_dwordx4 v[28:31], v[60:61], off offset:2048
	global_load_dwordx4 v[32:35], v[72:73], off
	global_load_dwordx4 v[36:39], v[74:75], off
	global_load_dwordx4 v[40:43], v[76:77], off
	global_load_dwordx4 v[44:47], v[78:79], off
	ds_read_b128 v[48:51], v135
	ds_read_b128 v[52:55], v135 offset:64
	ds_read_b128 v[56:59], v135 offset:16896
	ds_read_b128 v[138:141], v135 offset:16960
	ds_read_b128 v[142:145], v135 offset:8448
	ds_read_b128 v[146:149], v135 offset:128
	ds_read_b128 v[150:153], v135 offset:8512
	ds_read_b128 v[154:157], v135 offset:8576
	ds_read_b128 v[158:161], v135 offset:17024
	global_load_dwordx4 v[162:165], v[60:61], off offset:3072
	global_load_dwordx4 v[166:169], v[80:81], off
	global_load_dwordx4 v[174:177], v[82:83], off
	global_load_dwordx4 v[178:181], v[84:85], off
	ds_read_b128 v[182:185], v135 offset:192
	ds_read_b128 v[186:189], v135 offset:8640
	ds_read_b128 v[190:193], v135 offset:17088
	s_waitcnt vmcnt(13) lgkmcnt(11)
	v_mfma_f32_16x16x32_bf16 v[194:197], v[8:11], v[48:51], 0
	s_waitcnt vmcnt(9)
	v_mfma_f32_16x16x32_bf16 v[204:207], v[24:27], v[48:51], 0
	v_mfma_f32_16x16x32_bf16 v[208:211], v[0:3], v[48:51], 0
	v_mfma_f32_16x16x32_bf16 v[48:51], v[4:7], v[48:51], 0
	s_waitcnt lgkmcnt(7)
	v_mfma_f32_16x16x32_bf16 v[214:217], v[8:11], v[142:145], 0
	v_mfma_f32_16x16x32_bf16 v[218:221], v[24:27], v[142:145], 0
	v_mfma_f32_16x16x32_bf16 v[222:225], v[0:3], v[142:145], 0
	v_mfma_f32_16x16x32_bf16 v[142:145], v[4:7], v[142:145], 0
	v_mfma_f32_16x16x32_bf16 v[8:11], v[8:11], v[56:59], 0
	v_mfma_f32_16x16x32_bf16 v[24:27], v[24:27], v[56:59], 0
	v_mfma_f32_16x16x32_bf16 v[0:3], v[0:3], v[56:59], 0
	v_mfma_f32_16x16x32_bf16 v[4:7], v[4:7], v[56:59], 0
	global_load_dwordx4 v[56:59], v[86:87], off
	global_load_dwordx4 v[226:229], v[88:89], off
	global_load_dwordx4 v[230:233], v[90:91], off
	global_load_dwordx4 v[234:237], v[92:93], off
	ds_read_b128 v[238:241], v135 offset:256
	ds_read_b128 v[242:245], v135 offset:8704
	ds_read_b128 v[246:249], v135 offset:17152
	v_mfma_f32_16x16x32_bf16 v[194:197], v[12:15], v[52:55], v[194:197]
	v_mfma_f32_16x16x32_bf16 v[204:207], v[16:19], v[52:55], v[204:207]
	v_mfma_f32_16x16x32_bf16 v[208:211], v[20:23], v[52:55], v[208:211]
	s_waitcnt vmcnt(11)
	v_mfma_f32_16x16x32_bf16 v[48:51], v[32:35], v[52:55], v[48:51]
	s_waitcnt lgkmcnt(8)
	v_mfma_f32_16x16x32_bf16 v[52:55], v[12:15], v[150:153], v[214:217]
	v_mfma_f32_16x16x32_bf16 v[214:217], v[16:19], v[150:153], v[218:221]
	v_mfma_f32_16x16x32_bf16 v[218:221], v[20:23], v[150:153], v[222:225]
	v_mfma_f32_16x16x32_bf16 v[142:145], v[32:35], v[150:153], v[142:145]
	v_mfma_f32_16x16x32_bf16 v[8:11], v[12:15], v[138:141], v[8:11]
	v_mfma_f32_16x16x32_bf16 v[12:15], v[16:19], v[138:141], v[24:27]
	v_mfma_f32_16x16x32_bf16 v[0:3], v[20:23], v[138:141], v[0:3]
	v_mfma_f32_16x16x32_bf16 v[4:7], v[32:35], v[138:141], v[4:7]
	global_load_dwordx4 v[16:19], v[94:95], off
	global_load_dwordx4 v[20:23], v[96:97], off
	global_load_dwordx4 v[24:27], v[98:99], off
	global_load_dwordx4 v[32:35], v[100:101], off
	ds_read_b128 v[138:141], v135 offset:320
	ds_read_b128 v[150:153], v135 offset:8768
	ds_read_b128 v[222:225], v135 offset:17216
	v_mfma_f32_16x16x32_bf16 v[194:197], v[28:31], v[146:149], v[194:197]
	s_waitcnt vmcnt(14)
	v_mfma_f32_16x16x32_bf16 v[204:207], v[36:39], v[146:149], v[204:207]
	s_waitcnt vmcnt(13)
	v_mfma_f32_16x16x32_bf16 v[208:211], v[40:43], v[146:149], v[208:211]
	s_waitcnt vmcnt(12)
	v_mfma_f32_16x16x32_bf16 v[48:51], v[44:47], v[146:149], v[48:51]
	s_waitcnt lgkmcnt(10)
	v_mfma_f32_16x16x32_bf16 v[52:55], v[28:31], v[154:157], v[52:55]
	v_mfma_f32_16x16x32_bf16 v[146:149], v[36:39], v[154:157], v[214:217]
	v_mfma_f32_16x16x32_bf16 v[214:217], v[40:43], v[154:157], v[218:221]
	v_mfma_f32_16x16x32_bf16 v[142:145], v[44:47], v[154:157], v[142:145]
	s_waitcnt lgkmcnt(9)
	v_mfma_f32_16x16x32_bf16 v[8:11], v[28:31], v[158:161], v[8:11]
	v_mfma_f32_16x16x32_bf16 v[12:15], v[36:39], v[158:161], v[12:15]
	v_mfma_f32_16x16x32_bf16 v[0:3], v[40:43], v[158:161], v[0:3]
	v_mfma_f32_16x16x32_bf16 v[4:7], v[44:47], v[158:161], v[4:7]
	global_load_dwordx4 v[28:31], v[102:103], off
	global_load_dwordx4 v[36:39], v[104:105], off
	global_load_dwordx4 v[40:43], v[106:107], off
	global_load_dwordx4 v[44:47], v[108:109], off
	ds_read_b128 v[154:157], v135 offset:384
	ds_read_b128 v[158:161], v135 offset:8832
	ds_read_b128 v[218:221], v135 offset:17280
	s_waitcnt vmcnt(15) lgkmcnt(11)
	v_mfma_f32_16x16x32_bf16 v[194:197], v[162:165], v[182:185], v[194:197]
	s_waitcnt vmcnt(14)
	v_mfma_f32_16x16x32_bf16 v[204:207], v[166:169], v[182:185], v[204:207]
	s_waitcnt vmcnt(13)
	v_mfma_f32_16x16x32_bf16 v[208:211], v[174:177], v[182:185], v[208:211]
	s_waitcnt vmcnt(12)
	v_mfma_f32_16x16x32_bf16 v[48:51], v[178:181], v[182:185], v[48:51]
	s_waitcnt lgkmcnt(10)
	v_mfma_f32_16x16x32_bf16 v[52:55], v[162:165], v[186:189], v[52:55]
	v_mfma_f32_16x16x32_bf16 v[146:149], v[166:169], v[186:189], v[146:149]
	v_mfma_f32_16x16x32_bf16 v[182:185], v[174:177], v[186:189], v[214:217]
	v_mfma_f32_16x16x32_bf16 v[142:145], v[178:181], v[186:189], v[142:145]
	s_waitcnt lgkmcnt(9)
	v_mfma_f32_16x16x32_bf16 v[8:11], v[162:165], v[190:193], v[8:11]
	v_mfma_f32_16x16x32_bf16 v[12:15], v[166:169], v[190:193], v[12:15]
	v_mfma_f32_16x16x32_bf16 v[0:3], v[174:177], v[190:193], v[0:3]
	v_mfma_f32_16x16x32_bf16 v[4:7], v[178:181], v[190:193], v[4:7]
	global_load_dwordx4 v[162:165], v[110:111], off
	global_load_dwordx4 v[166:169], v[112:113], off
	global_load_dwordx4 v[174:177], v[114:115], off
	global_load_dwordx4 v[178:181], v[116:117], off
	ds_read_b128 v[186:189], v135 offset:448
	ds_read_b128 v[190:193], v135 offset:8896
	ds_read_b128 v[214:217], v135 offset:17344
	s_waitcnt vmcnt(15) lgkmcnt(11)
	v_mfma_f32_16x16x32_bf16 v[194:197], v[56:59], v[238:241], v[194:197]
	s_waitcnt vmcnt(14)
	v_mfma_f32_16x16x32_bf16 v[204:207], v[226:229], v[238:241], v[204:207]
	s_waitcnt vmcnt(13)
	v_mfma_f32_16x16x32_bf16 v[208:211], v[230:233], v[238:241], v[208:211]
	s_waitcnt vmcnt(12)
	v_mfma_f32_16x16x32_bf16 v[48:51], v[234:237], v[238:241], v[48:51]
	s_waitcnt lgkmcnt(10)
	v_mfma_f32_16x16x32_bf16 v[52:55], v[56:59], v[242:245], v[52:55]
	v_mfma_f32_16x16x32_bf16 v[146:149], v[226:229], v[242:245], v[146:149]
	v_mfma_f32_16x16x32_bf16 v[182:185], v[230:233], v[242:245], v[182:185]
	v_mfma_f32_16x16x32_bf16 v[142:145], v[234:237], v[242:245], v[142:145]
	s_waitcnt lgkmcnt(9)
	v_mfma_f32_16x16x32_bf16 v[8:11], v[56:59], v[246:249], v[8:11]
	v_mfma_f32_16x16x32_bf16 v[12:15], v[226:229], v[246:249], v[12:15]
	v_mfma_f32_16x16x32_bf16 v[0:3], v[230:233], v[246:249], v[0:3]
	v_mfma_f32_16x16x32_bf16 v[4:7], v[234:237], v[246:249], v[4:7]
	s_waitcnt vmcnt(11) lgkmcnt(8)
	v_mfma_f32_16x16x32_bf16 v[56:59], v[16:19], v[138:141], v[194:197]
	s_waitcnt vmcnt(10)
	v_mfma_f32_16x16x32_bf16 v[194:197], v[20:23], v[138:141], v[204:207]
	s_waitcnt vmcnt(9)
	v_mfma_f32_16x16x32_bf16 v[204:207], v[24:27], v[138:141], v[208:211]
	s_waitcnt vmcnt(8)
	v_mfma_f32_16x16x32_bf16 v[48:51], v[32:35], v[138:141], v[48:51]
	s_waitcnt lgkmcnt(7)
	v_mfma_f32_16x16x32_bf16 v[52:55], v[16:19], v[150:153], v[52:55]
	v_mfma_f32_16x16x32_bf16 v[138:141], v[20:23], v[150:153], v[146:149]
	v_mfma_f32_16x16x32_bf16 v[146:149], v[24:27], v[150:153], v[182:185]
	v_mfma_f32_16x16x32_bf16 v[142:145], v[32:35], v[150:153], v[142:145]
	s_waitcnt lgkmcnt(6)
	v_mfma_f32_16x16x32_bf16 v[8:11], v[16:19], v[222:225], v[8:11]
	v_mfma_f32_16x16x32_bf16 v[12:15], v[20:23], v[222:225], v[12:15]
	v_mfma_f32_16x16x32_bf16 v[0:3], v[24:27], v[222:225], v[0:3]
	v_mfma_f32_16x16x32_bf16 v[4:7], v[32:35], v[222:225], v[4:7]
	s_waitcnt vmcnt(7) lgkmcnt(5)
	v_mfma_f32_16x16x32_bf16 v[16:19], v[28:31], v[154:157], v[56:59]
	s_waitcnt vmcnt(6)
	v_mfma_f32_16x16x32_bf16 v[20:23], v[36:39], v[154:157], v[194:197]
	s_waitcnt vmcnt(5)
	v_mfma_f32_16x16x32_bf16 v[24:27], v[40:43], v[154:157], v[204:207]
	s_waitcnt vmcnt(4)
	v_mfma_f32_16x16x32_bf16 v[48:51], v[44:47], v[154:157], v[48:51]
	s_waitcnt lgkmcnt(4)
	v_mfma_f32_16x16x32_bf16 v[52:55], v[28:31], v[158:161], v[52:55]
	v_mfma_f32_16x16x32_bf16 v[138:141], v[36:39], v[158:161], v[138:141]
	v_mfma_f32_16x16x32_bf16 v[146:149], v[40:43], v[158:161], v[146:149]
	v_mfma_f32_16x16x32_bf16 v[142:145], v[44:47], v[158:161], v[142:145]
	s_waitcnt lgkmcnt(3)
	v_mfma_f32_16x16x32_bf16 v[150:153], v[28:31], v[218:221], v[8:11]
	v_mfma_f32_16x16x32_bf16 v[12:15], v[36:39], v[218:221], v[12:15]
	v_mfma_f32_16x16x32_bf16 v[0:3], v[40:43], v[218:221], v[0:3]
	v_mfma_f32_16x16x32_bf16 v[36:39], v[44:47], v[218:221], v[4:7]
	s_waitcnt vmcnt(0) lgkmcnt(2)
	v_mfma_f32_16x16x32_bf16 v[8:11], v[178:181], v[186:189], v[48:51]
	s_nop 2
	global_load_dwordx4 v[48:51], v[118:119], off
	global_load_dwordx4 v[40:43], v[120:121], off offset:3072
	s_mov_b32 s1, 0x4ccab000
	v_add_u32_e32 v137, 0x2000, v136
	v_mfma_f32_16x16x32_bf16 v[154:157], v[162:165], v[186:189], v[16:19]
	s_add_i32 s2, s2, s37
	v_lshl_add_u64 v[128:129], v[128:129], 0, s[10:11]
	s_cmpk_lt_i32 s2, 0xc0
	v_mfma_f32_16x16x32_bf16 v[32:35], v[166:169], v[186:189], v[20:23]
	v_mfma_f32_16x16x32_bf16 v[20:23], v[174:177], v[186:189], v[24:27]
	s_waitcnt lgkmcnt(0)
	v_mfma_f32_16x16x32_bf16 v[24:27], v[166:169], v[214:217], v[12:15]
	v_mfma_f32_16x16x32_bf16 v[12:15], v[174:177], v[214:217], v[0:3]
	v_mfma_f32_16x16x32_bf16 v[0:3], v[178:181], v[214:217], v[36:39]
	v_mfma_f32_16x16x32_bf16 v[56:59], v[162:165], v[190:193], v[52:55]
	s_waitcnt vmcnt(1)
	s_nop 0
	v_add_f32_e32 v36, v154, v48
	v_mul_f32_e32 v36, 0xbfb8aa3b, v36
	v_exp_f32_e32 v36, v36
	v_mfma_f32_16x16x32_bf16 v[28:31], v[166:169], v[190:193], v[138:141]
	s_nop 1
	v_add_f32_e32 v56, v56, v48
	v_add_f32_e32 v57, v57, v49
	v_add_f32_e32 v36, 1.0, v36
	v_rcp_f32_e32 v52, v36
	v_add_f32_e32 v36, v155, v49
	v_mul_f32_e32 v36, 0xbfb8aa3b, v36
	v_exp_f32_e32 v36, v36
	v_mul_f32_e32 v56, 0xbfb8aa3b, v56
	v_mul_f32_e32 v57, 0xbfb8aa3b, v57
	v_exp_f32_e32 v56, v56
	v_add_f32_e32 v36, 1.0, v36
	v_rcp_f32_e32 v53, v36
	ds_read2_b64 v[36:39], v136 offset1:4
	v_exp_f32_e32 v57, v57
	v_add_f32_e32 v56, 1.0, v56
	v_rcp_f32_e32 v56, v56
	v_mfma_f32_16x16x32_bf16 v[44:47], v[162:165], v[214:217], v[150:153]
	s_waitcnt lgkmcnt(0)
	v_lshlrev_b32_e32 v54, 16, v36
	v_and_b32_e32 v55, 0xffff0000, v36
	v_add_f32_e32 v36, v156, v50
	v_mul_f32_e32 v36, 0xbfb8aa3b, v36
	v_exp_f32_e32 v36, v36
	v_pk_mul_f32 v[52:53], v[52:53], v[54:55]
	v_add_f32_e32 v57, 1.0, v57
	v_pk_mul_f32 v[54:55], v[52:53], v[52:53]
	v_add_f32_e32 v36, 1.0, v36
	v_rcp_f32_e32 v131, v36
	v_add_f32_e32 v36, v157, v51
	v_mul_f32_e32 v36, 0xbfb8aa3b, v36
	v_exp_f32_e32 v36, v36
	v_add_f32_e32 v54, v54, v55
	v_rcp_f32_e32 v57, v57
	v_add_f32_e32 v46, v46, v50
	v_add_f32_e32 v36, 1.0, v36
	v_rcp_f32_e32 v130, v36
	v_and_b32_e32 v36, 0xffff0000, v37
	v_lshlrev_b32_e32 v37, 16, v37
	v_mul_f32_e32 v46, 0xbfb8aa3b, v46
	v_pk_mul_f32 v[36:37], v[130:131], v[36:37]
	v_exp_f32_e32 v46, v46
	v_pk_mul_f32 v[130:131], v[36:37], v[36:37]
	v_add_f32_e32 v44, v44, v48
	v_add_f32_e32 v54, v131, v54
	v_add_f32_e32 v54, v130, v54
	ds_swizzle_b32 v55, v54 offset:swizzle(SWAP,16)
	v_lshl_add_u64 v[130:131], s[60:61], 0, v[126:127]
	v_add_f32_e32 v45, v45, v49
	v_add_f32_e32 v46, 1.0, v46
	v_mul_f32_e32 v44, 0xbfb8aa3b, v44
	s_waitcnt lgkmcnt(0)
	v_add_f32_e32 v54, v54, v55
	ds_bpermute_b32 v55, v134, v54
	v_mul_f32_e32 v45, 0xbfb8aa3b, v45
	v_exp_f32_e32 v44, v44
	v_exp_f32_e32 v45, v45
	v_mfma_f32_16x16x32_bf16 v[16:19], v[174:177], v[190:193], v[146:149]
	s_waitcnt lgkmcnt(0)
	v_add_f32_e32 v54, v54, v55
	v_fmamk_f32 v54, v54, 0x3d800000, v198
	v_cmp_gt_f32_e32 vcc, s0, v54
	v_mul_f32_e32 v55, 0x4b800000, v54
	s_mov_b32 s0, 0x800000
	v_cndmask_b32_e32 v54, v54, v55, vcc
	v_rsq_f32_e32 v54, v54
	v_add_f32_e32 v44, 1.0, v44
	v_add_f32_e32 v45, 1.0, v45
	v_rcp_f32_e32 v44, v44
	v_mul_f32_e32 v55, 0x45800000, v54
	v_cndmask_b32_e32 v54, v54, v55, vcc
	v_mul_f32_e32 v52, v52, v54
	s_waitcnt vmcnt(0)
	v_mul_f32_e32 v52, v40, v52
	v_mul_f32_e32 v53, v53, v54
	v_mul_f32_e32 v36, v36, v54
	v_mul_f32_e32 v53, v41, v53
	v_cvt_pk_bf16_f32 v52, v52, v53
	v_mul_f32_e32 v37, v37, v54
	v_mul_f32_e32 v36, v43, v36
	ds_bpermute_b32 v52, v133, v52
	v_mul_f32_e32 v37, v42, v37
	v_cvt_pk_bf16_f32 v36, v37, v36
	ds_bpermute_b32 v53, v133, v36
	v_add_co_u32_e32 v36, vcc, s1, v130
	s_mov_b32 s1, 0x4ccb3000
	s_nop 0
	v_addc_co_u32_e32 v37, vcc, 0, v131, vcc
	s_waitcnt lgkmcnt(0)
	global_store_dwordx2 v[36:37], v[52:53], off offset:3072
	ds_read2_b64 v[52:55], v137 offset0:32 offset1:36
	v_rcp_f32_e32 v45, v45
	v_mfma_f32_16x16x32_bf16 v[4:7], v[178:181], v[190:193], v[142:145]
	v_lshl_add_u64 v[126:127], v[126:127], 0, s[8:9]
	s_waitcnt lgkmcnt(0)
	v_lshlrev_b32_e32 v138, 16, v52
	v_and_b32_e32 v139, 0xffff0000, v52
	v_add_f32_e32 v52, v58, v50
	v_mul_f32_e32 v52, 0xbfb8aa3b, v52
	v_exp_f32_e32 v52, v52
	v_pk_mul_f32 v[56:57], v[56:57], v[138:139]
	v_add_f32_e32 v52, 1.0, v52
	v_rcp_f32_e32 v141, v52
	v_add_f32_e32 v52, v59, v51
	v_mul_f32_e32 v52, 0xbfb8aa3b, v52
	v_exp_f32_e32 v52, v52
	v_pk_mul_f32 v[138:139], v[56:57], v[56:57]
	v_add_f32_e32 v52, 1.0, v52
	v_rcp_f32_e32 v140, v52
	v_and_b32_e32 v52, 0xffff0000, v53
	v_lshlrev_b32_e32 v53, 16, v53
	v_add_f32_e32 v138, v138, v139
	v_pk_mul_f32 v[52:53], v[140:141], v[52:53]
	v_rcp_f32_e32 v141, v46
	v_pk_mul_f32 v[58:59], v[52:53], v[52:53]
	v_add_f32_e32 v46, v47, v51
	v_add_f32_e32 v59, v59, v138
	v_add_f32_e32 v58, v58, v59
	ds_swizzle_b32 v59, v58 offset:swizzle(SWAP,16)
	v_mul_f32_e32 v46, 0xbfb8aa3b, v46
	v_exp_f32_e32 v46, v46
	v_add_u32_e32 v138, 0x4000, v136
	s_waitcnt lgkmcnt(0)
	v_add_f32_e32 v58, v58, v59
	ds_bpermute_b32 v59, v134, v58
	v_add_f32_e32 v46, 1.0, v46
	v_rcp_f32_e32 v140, v46
	s_waitcnt lgkmcnt(0)
	v_add_f32_e32 v58, v58, v59
	v_fmamk_f32 v58, v58, 0x3d800000, v198
	v_cmp_gt_f32_e32 vcc, s0, v58
	v_mul_f32_e32 v59, 0x4b800000, v58
	s_nop 0
	v_cndmask_b32_e32 v58, v58, v59, vcc
	v_rsq_f32_e32 v58, v58
	s_nop 0
	v_mul_f32_e32 v59, 0x45800000, v58
	v_cndmask_b32_e32 v58, v58, v59, vcc
	v_mul_f32_e32 v56, v56, v58
	v_mul_f32_e32 v56, v40, v56
	v_mul_f32_e32 v57, v57, v58
	v_mul_f32_e32 v52, v52, v58
	v_mul_f32_e32 v57, v41, v57
	v_cvt_pk_bf16_f32 v56, v56, v57
	v_mul_f32_e32 v53, v53, v58
	v_mul_f32_e32 v52, v43, v52
	ds_bpermute_b32 v56, v133, v56
	v_mul_f32_e32 v53, v42, v53
	v_cvt_pk_bf16_f32 v52, v53, v52
	ds_bpermute_b32 v57, v133, v52
	v_add_co_u32_e32 v52, vcc, s1, v130
	s_mov_b32 s1, 0x4ccbb000
	s_nop 0
	v_addc_co_u32_e32 v53, vcc, 0, v131, vcc
	s_waitcnt lgkmcnt(0)
	global_store_dwordx2 v[52:53], v[56:57], off offset:3072
	ds_read2_b64 v[56:59], v138 offset0:64 offset1:68
	s_waitcnt lgkmcnt(0)
	v_lshlrev_b32_e32 v48, 16, v56
	v_and_b32_e32 v49, 0xffff0000, v56
	v_pk_mul_f32 v[44:45], v[44:45], v[48:49]
	v_and_b32_e32 v46, 0xffff0000, v57
	v_lshlrev_b32_e32 v47, 16, v57
	v_pk_mul_f32 v[48:49], v[44:45], v[44:45]
	v_pk_mul_f32 v[46:47], v[140:141], v[46:47]
	v_add_f32_e32 v48, v48, v49
	v_pk_mul_f32 v[50:51], v[46:47], v[46:47]
	s_nop 0
	v_add_f32_e32 v48, v51, v48
	v_add_f32_e32 v48, v50, v48
	ds_swizzle_b32 v49, v48 offset:swizzle(SWAP,16)
	v_lshlrev_b32_e32 v50, 16, v38
	v_and_b32_e32 v51, 0xffff0000, v38
	s_waitcnt lgkmcnt(0)
	v_add_f32_e32 v48, v48, v49
	ds_bpermute_b32 v49, v134, v48
	s_waitcnt lgkmcnt(0)
	v_add_f32_e32 v48, v48, v49
	v_fmamk_f32 v48, v48, 0x3d800000, v198
	v_cmp_gt_f32_e32 vcc, s0, v48
	v_mul_f32_e32 v49, 0x4b800000, v48
	s_nop 0
	v_cndmask_b32_e32 v48, v48, v49, vcc
	v_rsq_f32_e32 v48, v48
	s_nop 0
	v_mul_f32_e32 v49, 0x45800000, v48
	v_cndmask_b32_e32 v48, v48, v49, vcc
	v_mul_f32_e32 v44, v44, v48
	v_mul_f32_e32 v40, v40, v44
	v_mul_f32_e32 v44, v45, v48
	v_mul_f32_e32 v41, v41, v44
	v_cvt_pk_bf16_f32 v40, v40, v41
	ds_bpermute_b32 v44, v133, v40
	v_mul_f32_e32 v40, v47, v48
	v_mul_f32_e32 v40, v42, v40
	v_mul_f32_e32 v41, v46, v48
	v_mul_f32_e32 v41, v43, v41
	v_cvt_pk_bf16_f32 v40, v40, v41
	ds_bpermute_b32 v45, v133, v40
	v_add_co_u32_e32 v40, vcc, s1, v130
	s_nop 1
	v_addc_co_u32_e32 v41, vcc, 0, v131, vcc
	s_waitcnt lgkmcnt(0)
	global_store_dwordx2 v[40:41], v[44:45], off offset:3072
	global_load_dwordx4 v[42:45], v[122:123], off offset:64
	s_nop 0
	global_load_dwordx4 v[46:49], v[124:125], off offset:3136
	s_waitcnt vmcnt(1)
	v_add_f32_e32 v34, v34, v44
	v_mul_f32_e32 v34, 0xbfb8aa3b, v34
	v_exp_f32_e32 v34, v34
	v_add_f32_e32 v32, v32, v42
	v_add_f32_e32 v33, v33, v43
	v_mul_f32_e32 v32, 0xbfb8aa3b, v32
	v_add_f32_e32 v34, 1.0, v34
	v_mul_f32_e32 v33, 0xbfb8aa3b, v33
	v_rcp_f32_e32 v57, v34
	v_add_f32_e32 v34, v35, v45
	v_exp_f32_e32 v32, v32
	v_exp_f32_e32 v33, v33
	v_mul_f32_e32 v34, 0xbfb8aa3b, v34
	v_exp_f32_e32 v34, v34
	v_add_f32_e32 v32, 1.0, v32
	v_add_f32_e32 v33, 1.0, v33
	v_rcp_f32_e32 v32, v32
	v_rcp_f32_e32 v33, v33
	v_add_f32_e32 v34, 1.0, v34
	v_rcp_f32_e32 v56, v34
	v_and_b32_e32 v34, 0xffff0000, v39
	v_pk_mul_f32 v[32:33], v[32:33], v[50:51]
	v_lshlrev_b32_e32 v35, 16, v39
	v_pk_mul_f32 v[50:51], v[32:33], v[32:33]
	v_pk_mul_f32 v[34:35], v[56:57], v[34:35]
	v_add_f32_e32 v50, v50, v51
	v_pk_mul_f32 v[38:39], v[34:35], v[34:35]
	v_add_f32_e32 v30, v30, v44
	v_add_f32_e32 v39, v39, v50
	v_add_f32_e32 v38, v38, v39
	ds_swizzle_b32 v39, v38 offset:swizzle(SWAP,16)
	v_mul_f32_e32 v30, 0xbfb8aa3b, v30
	v_exp_f32_e32 v30, v30
	v_add_f32_e32 v28, v28, v42
	v_add_f32_e32 v29, v29, v43
	s_waitcnt lgkmcnt(0)
	v_add_f32_e32 v38, v38, v39
	ds_bpermute_b32 v39, v134, v38
	v_add_f32_e32 v30, 1.0, v30
	v_mul_f32_e32 v28, 0xbfb8aa3b, v28
	v_mul_f32_e32 v29, 0xbfb8aa3b, v29
	v_exp_f32_e32 v28, v28
	s_waitcnt lgkmcnt(0)
	v_add_f32_e32 v38, v38, v39
	v_fmamk_f32 v38, v38, 0x3d800000, v198
	v_cmp_gt_f32_e32 vcc, s0, v38
	v_mul_f32_e32 v39, 0x4b800000, v38
	v_exp_f32_e32 v29, v29
	v_cndmask_b32_e32 v38, v38, v39, vcc
	v_rsq_f32_e32 v38, v38
	v_add_f32_e32 v28, 1.0, v28
	v_add_f32_e32 v29, 1.0, v29
	v_rcp_f32_e32 v28, v28
	v_mul_f32_e32 v39, 0x45800000, v38
	v_cndmask_b32_e32 v38, v38, v39, vcc
	v_mul_f32_e32 v32, v32, v38
	v_mul_f32_e32 v33, v33, v38
	s_waitcnt vmcnt(0)
	v_mul_f32_e32 v32, v46, v32
	v_mul_f32_e32 v33, v47, v33
	v_cvt_pk_bf16_f32 v32, v32, v33
	v_mul_f32_e32 v33, v35, v38
	v_rcp_f32_e32 v35, v30
	v_add_f32_e32 v30, v31, v45
	v_mul_f32_e32 v30, 0xbfb8aa3b, v30
	v_mul_f32_e32 v33, v48, v33
	v_mul_f32_e32 v34, v34, v38
	v_exp_f32_e32 v30, v30
	v_mul_f32_e32 v34, v49, v34
	v_cvt_pk_bf16_f32 v33, v33, v34
	ds_bpermute_b32 v32, v133, v32
	ds_bpermute_b32 v33, v133, v33
	v_rcp_f32_e32 v29, v29
	v_add_f32_e32 v30, 1.0, v30
	v_rcp_f32_e32 v34, v30
	v_and_b32_e32 v30, 0xffff0000, v55
	s_waitcnt lgkmcnt(0)
	global_store_dwordx2 v[36:37], v[32:33], off offset:3104
	v_lshlrev_b32_e32 v32, 16, v54
	v_and_b32_e32 v33, 0xffff0000, v54
	v_pk_mul_f32 v[28:29], v[28:29], v[32:33]
	v_lshlrev_b32_e32 v31, 16, v55
	v_pk_mul_f32 v[32:33], v[28:29], v[28:29]
	v_pk_mul_f32 v[30:31], v[34:35], v[30:31]
	v_add_f32_e32 v32, v32, v33
	v_pk_mul_f32 v[34:35], v[30:31], v[30:31]
	v_add_f32_e32 v26, v26, v44
	v_add_f32_e32 v32, v35, v32
	v_add_f32_e32 v32, v34, v32
	ds_swizzle_b32 v33, v32 offset:swizzle(SWAP,16)
	v_mul_f32_e32 v26, 0xbfb8aa3b, v26
	v_exp_f32_e32 v26, v26
	v_add_f32_e32 v24, v24, v42
	v_add_f32_e32 v25, v25, v43
	s_waitcnt lgkmcnt(0)
	v_add_f32_e32 v32, v32, v33
	ds_bpermute_b32 v33, v134, v32
	v_add_f32_e32 v26, 1.0, v26
	v_mul_f32_e32 v24, 0xbfb8aa3b, v24
	v_mul_f32_e32 v25, 0xbfb8aa3b, v25
	v_exp_f32_e32 v24, v24
	s_waitcnt lgkmcnt(0)
	v_add_f32_e32 v32, v32, v33
	v_fmamk_f32 v32, v32, 0x3d800000, v198
	v_cmp_gt_f32_e32 vcc, s0, v32
	v_mul_f32_e32 v33, 0x4b800000, v32
	v_exp_f32_e32 v25, v25
	v_cndmask_b32_e32 v32, v32, v33, vcc
	v_rsq_f32_e32 v32, v32
	v_add_f32_e32 v24, 1.0, v24
	v_add_f32_e32 v25, 1.0, v25
	v_rcp_f32_e32 v24, v24
	v_mul_f32_e32 v33, 0x45800000, v32
	v_cndmask_b32_e32 v32, v32, v33, vcc
	v_mul_f32_e32 v28, v28, v32
	v_mul_f32_e32 v29, v29, v32
	v_mul_f32_e32 v28, v46, v28
	v_mul_f32_e32 v29, v47, v29
	v_cvt_pk_bf16_f32 v28, v28, v29
	v_mul_f32_e32 v29, v31, v32
	v_rcp_f32_e32 v31, v26
	v_add_f32_e32 v26, v27, v45
	v_mul_f32_e32 v26, 0xbfb8aa3b, v26
	v_mul_f32_e32 v29, v48, v29
	v_mul_f32_e32 v30, v30, v32
	v_exp_f32_e32 v26, v26
	v_mul_f32_e32 v30, v49, v30
	v_cvt_pk_bf16_f32 v29, v29, v30
	ds_bpermute_b32 v28, v133, v28
	ds_bpermute_b32 v29, v133, v29
	v_rcp_f32_e32 v25, v25
	v_add_f32_e32 v26, 1.0, v26
	v_rcp_f32_e32 v30, v26
	v_and_b32_e32 v26, 0xffff0000, v59
	s_waitcnt lgkmcnt(0)
	global_store_dwordx2 v[52:53], v[28:29], off offset:3104
	v_lshlrev_b32_e32 v28, 16, v58
	v_and_b32_e32 v29, 0xffff0000, v58
	v_pk_mul_f32 v[24:25], v[24:25], v[28:29]
	v_lshlrev_b32_e32 v27, 16, v59
	v_pk_mul_f32 v[28:29], v[24:25], v[24:25]
	v_pk_mul_f32 v[26:27], v[30:31], v[26:27]
	v_add_f32_e32 v28, v28, v29
	v_pk_mul_f32 v[30:31], v[26:27], v[26:27]
	s_nop 0
	v_add_f32_e32 v28, v31, v28
	v_add_f32_e32 v28, v30, v28
	ds_swizzle_b32 v29, v28 offset:swizzle(SWAP,16)
	s_waitcnt lgkmcnt(0)
	v_add_f32_e32 v28, v28, v29
	ds_bpermute_b32 v29, v134, v28
	s_waitcnt lgkmcnt(0)
	v_add_f32_e32 v28, v28, v29
	v_fmamk_f32 v28, v28, 0x3d800000, v198
	v_cmp_gt_f32_e32 vcc, s0, v28
	v_mul_f32_e32 v29, 0x4b800000, v28
	s_nop 0
	v_cndmask_b32_e32 v28, v28, v29, vcc
	v_rsq_f32_e32 v28, v28
	s_nop 0
	v_mul_f32_e32 v29, 0x45800000, v28
	v_cndmask_b32_e32 v28, v28, v29, vcc
	v_mul_f32_e32 v24, v24, v28
	v_mul_f32_e32 v25, v25, v28
	v_mul_f32_e32 v24, v46, v24
	v_mul_f32_e32 v25, v47, v25
	v_cvt_pk_bf16_f32 v24, v24, v25
	v_mul_f32_e32 v25, v27, v28
	v_mul_f32_e32 v25, v48, v25
	v_mul_f32_e32 v26, v26, v28
	v_mul_f32_e32 v26, v49, v26
	v_cvt_pk_bf16_f32 v25, v25, v26
	ds_bpermute_b32 v24, v133, v24
	ds_bpermute_b32 v25, v133, v25
	s_waitcnt lgkmcnt(0)
	global_store_dwordx2 v[40:41], v[24:25], off offset:3104
	global_load_dwordx4 v[28:31], v[122:123], off offset:128
	s_nop 0
	global_load_dwordx4 v[24:27], v[124:125], off offset:3200
	ds_read2_b64 v[32:35], v136 offset0:8 offset1:12
	s_waitcnt lgkmcnt(0)
	v_lshlrev_b32_e32 v38, 16, v32
	v_and_b32_e32 v39, 0xffff0000, v32
	s_waitcnt vmcnt(1)
	v_add_f32_e32 v22, v22, v30
	v_mul_f32_e32 v22, 0xbfb8aa3b, v22
	v_exp_f32_e32 v22, v22
	v_add_f32_e32 v20, v20, v28
	v_add_f32_e32 v21, v21, v29
	v_mul_f32_e32 v20, 0xbfb8aa3b, v20
	v_add_f32_e32 v22, 1.0, v22
	v_mul_f32_e32 v21, 0xbfb8aa3b, v21
	v_rcp_f32_e32 v43, v22
	v_add_f32_e32 v22, v23, v31
	v_exp_f32_e32 v20, v20
	v_exp_f32_e32 v21, v21
	v_mul_f32_e32 v22, 0xbfb8aa3b, v22
	v_exp_f32_e32 v22, v22
	v_add_f32_e32 v20, 1.0, v20
	v_add_f32_e32 v21, 1.0, v21
	v_rcp_f32_e32 v20, v20
	v_rcp_f32_e32 v21, v21
	v_add_f32_e32 v22, 1.0, v22
	v_rcp_f32_e32 v42, v22
	v_and_b32_e32 v22, 0xffff0000, v33
	v_pk_mul_f32 v[20:21], v[20:21], v[38:39]
	v_lshlrev_b32_e32 v23, 16, v33
	v_pk_mul_f32 v[38:39], v[20:21], v[20:21]
	v_pk_mul_f32 v[22:23], v[42:43], v[22:23]
	v_add_f32_e32 v38, v38, v39
	v_pk_mul_f32 v[32:33], v[22:23], v[22:23]
	v_add_f32_e32 v18, v18, v30
	v_add_f32_e32 v33, v33, v38
	v_add_f32_e32 v32, v32, v33
	ds_swizzle_b32 v33, v32 offset:swizzle(SWAP,16)
	v_mul_f32_e32 v18, 0xbfb8aa3b, v18
	v_exp_f32_e32 v18, v18
	v_add_f32_e32 v16, v16, v28
	v_add_f32_e32 v17, v17, v29
	s_waitcnt lgkmcnt(0)
	v_add_f32_e32 v32, v32, v33
	ds_bpermute_b32 v33, v134, v32
	v_add_f32_e32 v18, 1.0, v18
	v_mul_f32_e32 v16, 0xbfb8aa3b, v16
	v_mul_f32_e32 v17, 0xbfb8aa3b, v17
	v_rcp_f32_e32 v39, v18
	s_waitcnt lgkmcnt(0)
	v_add_f32_e32 v32, v32, v33
	v_fmamk_f32 v32, v32, 0x3d800000, v198
	v_cmp_gt_f32_e32 vcc, s0, v32
	v_mul_f32_e32 v33, 0x4b800000, v32
	v_add_f32_e32 v18, v19, v31
	v_cndmask_b32_e32 v32, v32, v33, vcc
	v_rsq_f32_e32 v32, v32
	v_exp_f32_e32 v16, v16
	v_exp_f32_e32 v17, v17
	v_mul_f32_e32 v18, 0xbfb8aa3b, v18
	v_mul_f32_e32 v33, 0x45800000, v32
	v_cndmask_b32_e32 v32, v32, v33, vcc
	v_mul_f32_e32 v20, v20, v32
	v_mul_f32_e32 v21, v21, v32
	s_waitcnt vmcnt(0)
	v_mul_f32_e32 v20, v24, v20
	v_mul_f32_e32 v21, v25, v21
	v_cvt_pk_bf16_f32 v20, v20, v21
	v_mul_f32_e32 v21, v23, v32
	v_mul_f32_e32 v21, v26, v21
	v_mul_f32_e32 v22, v22, v32
	v_mul_f32_e32 v22, v27, v22
	v_cvt_pk_bf16_f32 v21, v21, v22
	ds_bpermute_b32 v20, v133, v20
	ds_bpermute_b32 v21, v133, v21
	v_exp_f32_e32 v18, v18
	v_add_f32_e32 v16, 1.0, v16
	v_add_f32_e32 v17, 1.0, v17
	v_rcp_f32_e32 v16, v16
	s_waitcnt lgkmcnt(0)
	global_store_dwordx2 v[36:37], v[20:21], off offset:3136
	ds_read2_b64 v[20:23], v137 offset0:40 offset1:44
	v_rcp_f32_e32 v17, v17
	v_add_f32_e32 v18, 1.0, v18
	v_rcp_f32_e32 v38, v18
	v_add_f32_e32 v14, v14, v30
	s_waitcnt lgkmcnt(0)
	v_lshlrev_b32_e32 v32, 16, v20
	v_and_b32_e32 v33, 0xffff0000, v20
	v_pk_mul_f32 v[16:17], v[16:17], v[32:33]
	v_and_b32_e32 v18, 0xffff0000, v21
	v_lshlrev_b32_e32 v19, 16, v21
	v_pk_mul_f32 v[32:33], v[16:17], v[16:17]
	v_pk_mul_f32 v[18:19], v[38:39], v[18:19]
	v_add_f32_e32 v32, v32, v33
	v_pk_mul_f32 v[20:21], v[18:19], v[18:19]
	v_mul_f32_e32 v14, 0xbfb8aa3b, v14
	v_add_f32_e32 v21, v21, v32
	v_add_f32_e32 v20, v20, v21
	ds_swizzle_b32 v21, v20 offset:swizzle(SWAP,16)
	v_exp_f32_e32 v14, v14
	v_add_f32_e32 v12, v12, v28
	v_add_f32_e32 v13, v13, v29
	v_mul_f32_e32 v12, 0xbfb8aa3b, v12
	s_waitcnt lgkmcnt(0)
	v_add_f32_e32 v20, v20, v21
	ds_bpermute_b32 v21, v134, v20
	v_add_f32_e32 v14, 1.0, v14
	v_mul_f32_e32 v13, 0xbfb8aa3b, v13
	v_rcp_f32_e32 v29, v14
	v_add_f32_e32 v14, v15, v31
	s_waitcnt lgkmcnt(0)
	v_add_f32_e32 v20, v20, v21
	v_fmamk_f32 v20, v20, 0x3d800000, v198
	v_cmp_gt_f32_e32 vcc, s0, v20
	v_mul_f32_e32 v21, 0x4b800000, v20
	v_exp_f32_e32 v12, v12
	v_cndmask_b32_e32 v20, v20, v21, vcc
	v_rsq_f32_e32 v20, v20
	v_exp_f32_e32 v13, v13
	v_mul_f32_e32 v14, 0xbfb8aa3b, v14
	v_exp_f32_e32 v14, v14
	v_mul_f32_e32 v21, 0x45800000, v20
	v_cndmask_b32_e32 v20, v20, v21, vcc
	v_mul_f32_e32 v16, v16, v20
	v_mul_f32_e32 v17, v17, v20
	v_mul_f32_e32 v16, v24, v16
	v_mul_f32_e32 v17, v25, v17
	v_cvt_pk_bf16_f32 v16, v16, v17
	v_mul_f32_e32 v17, v19, v20
	v_mul_f32_e32 v17, v26, v17
	v_mul_f32_e32 v18, v18, v20
	v_mul_f32_e32 v18, v27, v18
	v_cvt_pk_bf16_f32 v17, v17, v18
	ds_bpermute_b32 v16, v133, v16
	ds_bpermute_b32 v17, v133, v17
	v_add_f32_e32 v12, 1.0, v12
	v_add_f32_e32 v13, 1.0, v13
	v_rcp_f32_e32 v12, v12
	v_rcp_f32_e32 v13, v13
	s_waitcnt lgkmcnt(0)
	global_store_dwordx2 v[52:53], v[16:17], off offset:3136
	ds_read2_b64 v[16:19], v138 offset0:72 offset1:76
	v_add_f32_e32 v14, 1.0, v14
	v_rcp_f32_e32 v28, v14
	s_waitcnt lgkmcnt(0)
	v_lshlrev_b32_e32 v20, 16, v16
	v_and_b32_e32 v21, 0xffff0000, v16
	v_pk_mul_f32 v[12:13], v[12:13], v[20:21]
	v_and_b32_e32 v14, 0xffff0000, v17
	v_lshlrev_b32_e32 v15, 16, v17
	v_pk_mul_f32 v[20:21], v[12:13], v[12:13]
	v_pk_mul_f32 v[14:15], v[28:29], v[14:15]
	v_add_f32_e32 v20, v20, v21
	v_pk_mul_f32 v[16:17], v[14:15], v[14:15]
	s_nop 0
	v_add_f32_e32 v17, v17, v20
	v_add_f32_e32 v16, v16, v17
	ds_swizzle_b32 v17, v16 offset:swizzle(SWAP,16)
	s_waitcnt lgkmcnt(0)
	v_add_f32_e32 v16, v16, v17
	ds_bpermute_b32 v17, v134, v16
	s_waitcnt lgkmcnt(0)
	v_add_f32_e32 v16, v16, v17
	v_fmamk_f32 v16, v16, 0x3d800000, v198
	v_cmp_gt_f32_e32 vcc, s0, v16
	v_mul_f32_e32 v17, 0x4b800000, v16
	s_nop 0
	v_cndmask_b32_e32 v16, v16, v17, vcc
	v_rsq_f32_e32 v16, v16
	s_nop 0
	v_mul_f32_e32 v17, 0x45800000, v16
	v_cndmask_b32_e32 v16, v16, v17, vcc
	v_mul_f32_e32 v12, v12, v16
	v_mul_f32_e32 v13, v13, v16
	v_mul_f32_e32 v12, v24, v12
	v_mul_f32_e32 v13, v25, v13
	v_cvt_pk_bf16_f32 v12, v12, v13
	v_mul_f32_e32 v13, v15, v16
	v_mul_f32_e32 v13, v26, v13
	v_mul_f32_e32 v14, v14, v16
	v_mul_f32_e32 v14, v27, v14
	v_cvt_pk_bf16_f32 v13, v13, v14
	ds_bpermute_b32 v12, v133, v12
	ds_bpermute_b32 v13, v133, v13
	v_lshlrev_b32_e32 v16, 16, v34
	v_and_b32_e32 v17, 0xffff0000, v34
	s_waitcnt lgkmcnt(0)
	global_store_dwordx2 v[40:41], v[12:13], off offset:3136
	global_load_dwordx4 v[12:15], v[122:123], off offset:192
	s_nop 0
	global_load_dwordx4 v[24:27], v[124:125], off offset:3264
	s_waitcnt vmcnt(1)
	v_add_f32_e32 v10, v10, v14
	v_mul_f32_e32 v10, 0xbfb8aa3b, v10
	v_exp_f32_e32 v10, v10
	v_add_f32_e32 v8, v8, v12
	v_add_f32_e32 v9, v9, v13
	v_mul_f32_e32 v8, 0xbfb8aa3b, v8
	v_add_f32_e32 v10, 1.0, v10
	v_mul_f32_e32 v9, 0xbfb8aa3b, v9
	v_rcp_f32_e32 v21, v10
	v_add_f32_e32 v10, v11, v15
	v_exp_f32_e32 v8, v8
	v_exp_f32_e32 v9, v9
	v_mul_f32_e32 v10, 0xbfb8aa3b, v10
	v_exp_f32_e32 v10, v10
	v_add_f32_e32 v8, 1.0, v8
	v_add_f32_e32 v9, 1.0, v9
	v_rcp_f32_e32 v8, v8
	v_rcp_f32_e32 v9, v9
	v_add_f32_e32 v10, 1.0, v10
	v_rcp_f32_e32 v20, v10
	v_and_b32_e32 v10, 0xffff0000, v35
	v_pk_mul_f32 v[8:9], v[8:9], v[16:17]
	v_lshlrev_b32_e32 v11, 16, v35
	v_pk_mul_f32 v[16:17], v[8:9], v[8:9]
	v_pk_mul_f32 v[10:11], v[20:21], v[10:11]
	v_add_f32_e32 v16, v16, v17
	v_pk_mul_f32 v[20:21], v[10:11], v[10:11]
	v_add_f32_e32 v6, v6, v14
	v_add_f32_e32 v16, v21, v16
	v_add_f32_e32 v16, v20, v16
	ds_swizzle_b32 v17, v16 offset:swizzle(SWAP,16)
	v_mul_f32_e32 v6, 0xbfb8aa3b, v6
	v_exp_f32_e32 v6, v6
	v_add_f32_e32 v4, v4, v12
	v_add_f32_e32 v5, v5, v13
	s_waitcnt lgkmcnt(0)
	v_add_f32_e32 v16, v16, v17
	ds_bpermute_b32 v17, v134, v16
	v_add_f32_e32 v6, 1.0, v6
	v_mul_f32_e32 v4, 0xbfb8aa3b, v4
	v_mul_f32_e32 v5, 0xbfb8aa3b, v5
	v_exp_f32_e32 v4, v4
	s_waitcnt lgkmcnt(0)
	v_add_f32_e32 v16, v16, v17
	v_fmamk_f32 v16, v16, 0x3d800000, v198
	v_cmp_gt_f32_e32 vcc, s0, v16
	v_mul_f32_e32 v17, 0x4b800000, v16
	v_exp_f32_e32 v5, v5
	v_cndmask_b32_e32 v16, v16, v17, vcc
	v_rsq_f32_e32 v16, v16
	v_add_f32_e32 v4, 1.0, v4
	v_add_f32_e32 v5, 1.0, v5
	v_rcp_f32_e32 v4, v4
	v_mul_f32_e32 v17, 0x45800000, v16
	v_cndmask_b32_e32 v16, v16, v17, vcc
	v_mul_f32_e32 v8, v8, v16
	v_mul_f32_e32 v9, v9, v16
	s_waitcnt vmcnt(0)
	v_mul_f32_e32 v8, v24, v8
	v_mul_f32_e32 v9, v25, v9
	v_cvt_pk_bf16_f32 v8, v8, v9
	v_mul_f32_e32 v9, v11, v16
	v_rcp_f32_e32 v11, v6
	v_add_f32_e32 v6, v7, v15
	v_mul_f32_e32 v6, 0xbfb8aa3b, v6
	v_mul_f32_e32 v9, v26, v9
	v_mul_f32_e32 v10, v10, v16
	v_exp_f32_e32 v6, v6
	v_mul_f32_e32 v10, v27, v10
	v_cvt_pk_bf16_f32 v9, v9, v10
	ds_bpermute_b32 v8, v133, v8
	ds_bpermute_b32 v9, v133, v9
	v_rcp_f32_e32 v5, v5
	v_add_f32_e32 v6, 1.0, v6
	v_rcp_f32_e32 v10, v6
	v_and_b32_e32 v6, 0xffff0000, v23
	s_waitcnt lgkmcnt(0)
	global_store_dwordx2 v[36:37], v[8:9], off offset:3168
	v_lshlrev_b32_e32 v8, 16, v22
	v_and_b32_e32 v9, 0xffff0000, v22
	v_pk_mul_f32 v[4:5], v[4:5], v[8:9]
	v_lshlrev_b32_e32 v7, 16, v23
	v_pk_mul_f32 v[8:9], v[4:5], v[4:5]
	v_pk_mul_f32 v[6:7], v[10:11], v[6:7]
	v_add_f32_e32 v8, v8, v9
	v_pk_mul_f32 v[10:11], v[6:7], v[6:7]
	v_add_f32_e32 v2, v2, v14
	v_add_f32_e32 v8, v11, v8
	v_add_f32_e32 v8, v10, v8
	ds_swizzle_b32 v9, v8 offset:swizzle(SWAP,16)
	v_mul_f32_e32 v2, 0xbfb8aa3b, v2
	v_exp_f32_e32 v2, v2
	v_add_f32_e32 v0, v0, v12
	v_add_f32_e32 v1, v1, v13
	s_waitcnt lgkmcnt(0)
	v_add_f32_e32 v8, v8, v9
	ds_bpermute_b32 v9, v134, v8
	v_add_f32_e32 v2, 1.0, v2
	v_mul_f32_e32 v0, 0xbfb8aa3b, v0
	v_mul_f32_e32 v1, 0xbfb8aa3b, v1
	v_exp_f32_e32 v0, v0
	s_waitcnt lgkmcnt(0)
	v_add_f32_e32 v8, v8, v9
	v_fmamk_f32 v8, v8, 0x3d800000, v198
	v_cmp_gt_f32_e32 vcc, s0, v8
	v_mul_f32_e32 v9, 0x4b800000, v8
	v_exp_f32_e32 v1, v1
	v_cndmask_b32_e32 v8, v8, v9, vcc
	v_rsq_f32_e32 v8, v8
	v_add_f32_e32 v0, 1.0, v0
	v_add_f32_e32 v1, 1.0, v1
	v_rcp_f32_e32 v0, v0
	v_mul_f32_e32 v9, 0x45800000, v8
	v_cndmask_b32_e32 v8, v8, v9, vcc
	v_mul_f32_e32 v4, v4, v8
	v_mul_f32_e32 v5, v5, v8
	v_mul_f32_e32 v4, v24, v4
	v_mul_f32_e32 v5, v25, v5
	v_cvt_pk_bf16_f32 v4, v4, v5
	v_mul_f32_e32 v5, v7, v8
	v_rcp_f32_e32 v7, v2
	v_add_f32_e32 v2, v3, v15
	v_mul_f32_e32 v2, 0xbfb8aa3b, v2
	v_mul_f32_e32 v5, v26, v5
	v_mul_f32_e32 v6, v6, v8
	v_exp_f32_e32 v2, v2
	v_mul_f32_e32 v6, v27, v6
	v_cvt_pk_bf16_f32 v5, v5, v6
	ds_bpermute_b32 v4, v133, v4
	ds_bpermute_b32 v5, v133, v5
	v_rcp_f32_e32 v1, v1
	v_add_f32_e32 v2, 1.0, v2
	v_rcp_f32_e32 v6, v2
	v_and_b32_e32 v2, 0xffff0000, v19
	s_waitcnt lgkmcnt(0)
	global_store_dwordx2 v[52:53], v[4:5], off offset:3168
	v_lshlrev_b32_e32 v4, 16, v18
	v_and_b32_e32 v5, 0xffff0000, v18
	v_pk_mul_f32 v[0:1], v[0:1], v[4:5]
	v_lshlrev_b32_e32 v3, 16, v19
	v_pk_mul_f32 v[4:5], v[0:1], v[0:1]
	v_pk_mul_f32 v[2:3], v[6:7], v[2:3]
	v_add_f32_e32 v4, v4, v5
	v_pk_mul_f32 v[6:7], v[2:3], v[2:3]
	s_nop 0
	v_add_f32_e32 v4, v7, v4
	v_add_f32_e32 v4, v6, v4
	ds_swizzle_b32 v5, v4 offset:swizzle(SWAP,16)
	s_waitcnt lgkmcnt(0)
	v_add_f32_e32 v4, v4, v5
	ds_bpermute_b32 v5, v134, v4
	s_waitcnt lgkmcnt(0)
	v_add_f32_e32 v4, v4, v5
	v_fmamk_f32 v4, v4, 0x3d800000, v198
	v_cmp_gt_f32_e32 vcc, s0, v4
	v_mul_f32_e32 v5, 0x4b800000, v4
	s_nop 0
	v_cndmask_b32_e32 v4, v4, v5, vcc
	v_rsq_f32_e32 v4, v4
	s_nop 0
	v_mul_f32_e32 v5, 0x45800000, v4
	v_cndmask_b32_e32 v4, v4, v5, vcc
	v_mul_f32_e32 v0, v0, v4
	v_mul_f32_e32 v1, v1, v4
	v_mul_f32_e32 v0, v24, v0
	v_mul_f32_e32 v1, v25, v1
	v_cvt_pk_bf16_f32 v0, v0, v1
	v_mul_f32_e32 v1, v3, v4
	v_mul_f32_e32 v1, v26, v1
	v_mul_f32_e32 v2, v2, v4
	v_mul_f32_e32 v2, v27, v2
	v_cvt_pk_bf16_f32 v1, v1, v2
	ds_bpermute_b32 v0, v133, v0
	ds_bpermute_b32 v1, v133, v1
	s_waitcnt lgkmcnt(0)
	global_store_dwordx2 v[40:41], v[0:1], off offset:3168
	s_barrier
	s_cbranch_scc1 .LBB0_1232

.LBB0_1287:
	v_readlane_b32 s0, v250, 4
	s_waitcnt lgkmcnt(0)
	s_mov_b32 s2, s100
	s_cmp_le_i32 s2, s1
	s_cselect_b64 s[2:3], -1, 0
	s_mov_b32 s25, s101
	s_cmp_lt_i32 s1, s25
	s_cselect_b64 s[4:5], -1, 0
	s_and_b64 s[4:5], s[2:3], s[4:5]
	s_mov_b64 s[2:3], -1
	s_and_b64 vcc, exec, s[4:5]
	s_cbranch_vccnz .LBB0_1289
	v_readlane_b32 s0, v255, 35
	s_add_i32 s1, s0, 10
	s_mov_b64 s[2:3], 0

.Lpeel_out:
	s_mov_b64 s[28:29], 0
	v_mov_b64_e32 v[136:137], v[132:133]
	v_mov_b64_e32 v[138:139], v[128:129]
	v_mov_b32_e32 v172, v130
	v_mov_b32_e32 v140, v134
	ds_read_b128 v[142:145], v186
	ds_read_b128 v[146:149], v186 offset:1024
	ds_read_b128 v[150:153], v186 offset:2048
	ds_read_b128 v[162:165], v186 offset:3072
	s_add_u32 s30, s26, 0x80
	s_addc_u32 s31, s27, 0
	s_and_b64 s[28:29], s[28:29], exec
	s_cselect_b32 s31, s19, s31
	s_cselect_b32 s30, s18, s30
	s_cselect_b32 s29, s17, s15
	s_cselect_b32 s28, s16, s9
	v_lshl_add_u64 v[154:155], s[26:27], 0, v[128:129]
	s_add_i32 m0, s23, 0xc000
	ds_read_b128 v[166:169], v185
	ds_read_b128 v[174:177], v185 offset:1024
	ds_read_b128 v[178:181], v185 offset:2048
	ds_read_b128 v[204:207], v185 offset:3072
	ds_read_b128 v[208:211], v185 offset:4096
	ds_read_b128 v[214:217], v185 offset:5120
	ds_read_b128 v[218:221], v185 offset:6144
	ds_read_b128 v[222:225], v185 offset:7168
	global_load_lds_dwordx4 v[154:155], off
	v_lshl_add_u64 v[154:155], s[26:27], 0, v[132:133]
	s_add_i32 m0, s23, 0xe000
	s_nop 0
	global_load_lds_dwordx4 v[154:155], off
	s_waitcnt lgkmcnt(8)
	s_barrier
	s_waitcnt lgkmcnt(0)
	s_setprio 1
	v_mfma_f32_16x16x32_bf16 v[124:127], v[142:145], v[166:169], 0
	v_mfma_f32_16x16x32_bf16 v[120:123], v[150:153], v[166:169], 0
	v_mfma_f32_16x16x32_bf16 v[116:119], v[142:145], v[178:181], 0
	v_mfma_f32_16x16x32_bf16 v[112:115], v[150:153], v[178:181], 0
	v_mfma_f32_16x16x32_bf16 v[108:111], v[142:145], v[208:211], 0
	v_mfma_f32_16x16x32_bf16 v[104:107], v[150:153], v[208:211], 0
	v_mfma_f32_16x16x32_bf16 v[100:103], v[142:145], v[218:221], 0
	v_mfma_f32_16x16x32_bf16 v[96:99], v[150:153], v[218:221], 0
	v_mfma_f32_16x16x32_bf16 v[124:127], v[146:149], v[174:177], v[124:127]
	v_mfma_f32_16x16x32_bf16 v[120:123], v[162:165], v[174:177], v[120:123]
	v_mfma_f32_16x16x32_bf16 v[116:119], v[146:149], v[204:207], v[116:119]
	v_mfma_f32_16x16x32_bf16 v[112:115], v[162:165], v[204:207], v[112:115]
	v_mfma_f32_16x16x32_bf16 v[108:111], v[146:149], v[214:217], v[108:111]
	v_mfma_f32_16x16x32_bf16 v[104:107], v[162:165], v[214:217], v[104:107]
	v_mfma_f32_16x16x32_bf16 v[100:103], v[146:149], v[222:225], v[100:103]
	v_mfma_f32_16x16x32_bf16 v[96:99], v[162:165], v[222:225], v[96:99]
	s_setprio 0
	s_barrier
	s_mov_b32 m0, s25
	v_lshl_add_u64 v[170:171], s[28:29], 0, v[158:159]
	ds_read_b128 v[226:229], v186 offset:16384
	ds_read_b128 v[230:233], v186 offset:17408
	ds_read_b128 v[234:237], v186 offset:18432
	ds_read_b128 v[238:241], v186 offset:19456
	global_load_lds_dwordx4 v[170:171], off
	v_lshl_add_u64 v[182:183], s[28:29], 0, v[160:161]
	s_mov_b32 m0, s51
	s_nop 0
	global_load_lds_dwordx4 v[182:183], off
	s_barrier
	s_waitcnt lgkmcnt(0)
	s_setprio 1
	v_mfma_f32_16x16x32_bf16 v[68:71], v[226:229], v[166:169], 0
	v_mfma_f32_16x16x32_bf16 v[64:67], v[234:237], v[166:169], 0
	v_mfma_f32_16x16x32_bf16 v[52:55], v[226:229], v[178:181], 0
	v_mfma_f32_16x16x32_bf16 v[48:51], v[234:237], v[178:181], 0
	v_mfma_f32_16x16x32_bf16 v[44:47], v[226:229], v[208:211], 0
	v_mfma_f32_16x16x32_bf16 v[40:43], v[234:237], v[208:211], 0
	v_mfma_f32_16x16x32_bf16 v[36:39], v[226:229], v[218:221], 0
	v_mfma_f32_16x16x32_bf16 v[32:35], v[234:237], v[218:221], 0
	v_mfma_f32_16x16x32_bf16 v[68:71], v[230:233], v[174:177], v[68:71]
	v_mfma_f32_16x16x32_bf16 v[64:67], v[238:241], v[174:177], v[64:67]
	v_mfma_f32_16x16x32_bf16 v[52:55], v[230:233], v[204:207], v[52:55]
	v_mfma_f32_16x16x32_bf16 v[48:51], v[238:241], v[204:207], v[48:51]
	v_mfma_f32_16x16x32_bf16 v[44:47], v[230:233], v[214:217], v[44:47]
	v_mfma_f32_16x16x32_bf16 v[40:43], v[238:241], v[214:217], v[40:43]
	v_mfma_f32_16x16x32_bf16 v[36:39], v[230:233], v[222:225], v[36:39]
	v_mfma_f32_16x16x32_bf16 v[32:35], v[238:241], v[222:225], v[32:35]
	s_setprio 0
	s_mov_b32 m0, s23
	s_barrier
	ds_read_b128 v[166:169], v185 offset:16384
	ds_read_b128 v[174:177], v185 offset:17408
	ds_read_b128 v[178:181], v185 offset:18432
	ds_read_b128 v[204:207], v185 offset:19456
	ds_read_b128 v[208:211], v185 offset:20480
	ds_read_b128 v[214:217], v185 offset:21504
	ds_read_b128 v[218:221], v185 offset:22528
	ds_read_b128 v[222:225], v185 offset:23552
	global_load_lds_dwordx4 v172, s[30:31]
	s_mov_b32 m0, s56
	v_mov_b32_e32 v141, v173
	global_load_lds_dwordx4 v140, s[30:31]
	s_barrier
	s_waitcnt lgkmcnt(0)
	v_lshl_add_u64 v[196:197], s[30:31], 0, v[172:173]
	v_lshl_add_u64 v[242:243], s[30:31], 0, v[140:141]
	s_setprio 1
	v_mfma_f32_16x16x32_bf16 v[92:95], v[142:145], v[166:169], 0
	v_mfma_f32_16x16x32_bf16 v[88:91], v[150:153], v[166:169], 0
	v_mfma_f32_16x16x32_bf16 v[84:87], v[142:145], v[178:181], 0
	v_mfma_f32_16x16x32_bf16 v[80:83], v[150:153], v[178:181], 0
	v_mfma_f32_16x16x32_bf16 v[76:79], v[142:145], v[208:211], 0
	v_mfma_f32_16x16x32_bf16 v[72:75], v[150:153], v[208:211], 0
	v_mfma_f32_16x16x32_bf16 v[60:63], v[142:145], v[218:221], 0
	v_mfma_f32_16x16x32_bf16 v[56:59], v[150:153], v[218:221], 0
	v_mfma_f32_16x16x32_bf16 v[92:95], v[146:149], v[174:177], v[92:95]
	v_mfma_f32_16x16x32_bf16 v[88:91], v[162:165], v[174:177], v[88:91]
	v_mfma_f32_16x16x32_bf16 v[84:87], v[146:149], v[204:207], v[84:87]
	v_mfma_f32_16x16x32_bf16 v[80:83], v[162:165], v[204:207], v[80:83]
	v_mfma_f32_16x16x32_bf16 v[76:79], v[146:149], v[214:217], v[76:79]
	v_mfma_f32_16x16x32_bf16 v[72:75], v[162:165], v[214:217], v[72:75]
	v_mfma_f32_16x16x32_bf16 v[60:63], v[146:149], v[222:225], v[60:63]
	v_mfma_f32_16x16x32_bf16 v[56:59], v[162:165], v[222:225], v[56:59]
	s_setprio 0
	s_barrier
	s_add_u32 s94, s28, 0x40000
	s_addc_u32 s95, s29, 0
	s_mov_b32 m0, s65
	v_lshl_add_u64 v[140:141], s[94:95], 0, v[158:159]
	global_load_lds_dwordx4 v[140:141], off
	v_lshl_add_u64 v[140:141], s[94:95], 0, v[160:161]
	s_mov_b32 m0, s70
	s_nop 0
	global_load_lds_dwordx4 v[140:141], off
	s_waitcnt vmcnt(6)
	s_barrier
	s_setprio 1
	v_mfma_f32_16x16x32_bf16 v[28:31], v[226:229], v[166:169], 0
	v_mfma_f32_16x16x32_bf16 v[24:27], v[234:237], v[166:169], 0
	v_mfma_f32_16x16x32_bf16 v[20:23], v[226:229], v[178:181], 0
	v_mfma_f32_16x16x32_bf16 v[16:19], v[234:237], v[178:181], 0
	v_mfma_f32_16x16x32_bf16 v[12:15], v[226:229], v[208:211], 0
	v_mfma_f32_16x16x32_bf16 v[8:11], v[234:237], v[208:211], 0
	v_mfma_f32_16x16x32_bf16 v[4:7], v[226:229], v[218:221], 0
	v_mfma_f32_16x16x32_bf16 v[0:3], v[234:237], v[218:221], 0
	v_mfma_f32_16x16x32_bf16 v[28:31], v[230:233], v[174:177], v[28:31]
	v_mfma_f32_16x16x32_bf16 v[24:27], v[238:241], v[174:177], v[24:27]
	v_mfma_f32_16x16x32_bf16 v[20:23], v[230:233], v[204:207], v[20:23]
	v_mfma_f32_16x16x32_bf16 v[16:19], v[238:241], v[204:207], v[16:19]
	v_mfma_f32_16x16x32_bf16 v[12:15], v[230:233], v[214:217], v[12:15]
	v_mfma_f32_16x16x32_bf16 v[8:11], v[238:241], v[214:217], v[8:11]
	v_mfma_f32_16x16x32_bf16 v[4:7], v[230:233], v[222:225], v[4:7]
	v_mfma_f32_16x16x32_bf16 v[0:3], v[238:241], v[222:225], v[0:3]
	s_setprio 0
	s_barrier
	ds_read_b128 v[140:143], v186 offset:32768
	ds_read_b128 v[144:147], v186 offset:33792
	ds_read_b128 v[148:151], v186 offset:34816
	ds_read_b128 v[152:155], v186 offset:35840
	s_mov_b32 m0, s71
	v_lshl_add_u64 v[138:139], s[30:31], 0, v[138:139]
	ds_read_b128 v[162:165], v185 offset:32768
	ds_read_b128 v[166:169], v185 offset:33792
	ds_read_b128 v[174:177], v185 offset:34816
	ds_read_b128 v[178:181], v185 offset:35840
	ds_read_b128 v[204:207], v185 offset:36864
	ds_read_b128 v[208:211], v185 offset:37888
	ds_read_b128 v[214:217], v185 offset:38912
	ds_read_b128 v[218:221], v185 offset:39936
	global_load_lds_dwordx4 v[138:139], off
	v_lshl_add_u64 v[136:137], s[30:31], 0, v[136:137]
	s_mov_b32 m0, s80
	s_nop 0
	global_load_lds_dwordx4 v[136:137], off
	s_waitcnt lgkmcnt(8)
	s_barrier
	s_waitcnt lgkmcnt(0)
	s_setprio 1
	v_mfma_f32_16x16x32_bf16 v[124:127], v[140:143], v[162:165], v[124:127]
	v_mfma_f32_16x16x32_bf16 v[120:123], v[148:151], v[162:165], v[120:123]
	v_mfma_f32_16x16x32_bf16 v[116:119], v[140:143], v[174:177], v[116:119]
	v_mfma_f32_16x16x32_bf16 v[112:115], v[148:151], v[174:177], v[112:115]
	v_mfma_f32_16x16x32_bf16 v[108:111], v[140:143], v[204:207], v[108:111]
	v_mfma_f32_16x16x32_bf16 v[104:107], v[148:151], v[204:207], v[104:107]
	v_mfma_f32_16x16x32_bf16 v[100:103], v[140:143], v[214:217], v[100:103]
	v_mfma_f32_16x16x32_bf16 v[96:99], v[148:151], v[214:217], v[96:99]
	v_mfma_f32_16x16x32_bf16 v[124:127], v[144:147], v[166:169], v[124:127]
	v_mfma_f32_16x16x32_bf16 v[120:123], v[152:155], v[166:169], v[120:123]
	v_mfma_f32_16x16x32_bf16 v[116:119], v[144:147], v[178:181], v[116:119]
	v_mfma_f32_16x16x32_bf16 v[112:115], v[152:155], v[178:181], v[112:115]
	v_mfma_f32_16x16x32_bf16 v[108:111], v[144:147], v[208:211], v[108:111]
	v_mfma_f32_16x16x32_bf16 v[104:107], v[152:155], v[208:211], v[104:107]
	v_mfma_f32_16x16x32_bf16 v[100:103], v[144:147], v[218:221], v[100:103]
	v_mfma_f32_16x16x32_bf16 v[96:99], v[152:155], v[218:221], v[96:99]
	s_setprio 0
	s_barrier
	s_mov_b32 m0, s81
	v_lshl_add_u64 v[170:171], v[170:171], 0, s[40:41]
	ds_read_b128 v[136:139], v186 offset:49152
	ds_read_b128 v[222:225], v186 offset:50176
	ds_read_b128 v[226:229], v186 offset:51200
	ds_read_b128 v[230:233], v186 offset:52224
	global_load_lds_dwordx4 v[170:171], off
	v_lshl_add_u64 v[170:171], v[182:183], 0, s[40:41]
	s_mov_b32 m0, s82
	s_nop 0
	global_load_lds_dwordx4 v[170:171], off
	s_barrier
	s_waitcnt lgkmcnt(0)
	s_setprio 1
	v_mfma_f32_16x16x32_bf16 v[68:71], v[136:139], v[162:165], v[68:71]
	v_mfma_f32_16x16x32_bf16 v[64:67], v[226:229], v[162:165], v[64:67]
	v_mfma_f32_16x16x32_bf16 v[52:55], v[136:139], v[174:177], v[52:55]
	v_mfma_f32_16x16x32_bf16 v[48:51], v[226:229], v[174:177], v[48:51]
	v_mfma_f32_16x16x32_bf16 v[44:47], v[136:139], v[204:207], v[44:47]
	v_mfma_f32_16x16x32_bf16 v[40:43], v[226:229], v[204:207], v[40:43]
	v_mfma_f32_16x16x32_bf16 v[36:39], v[136:139], v[214:217], v[36:39]
	v_mfma_f32_16x16x32_bf16 v[32:35], v[226:229], v[214:217], v[32:35]
	v_mfma_f32_16x16x32_bf16 v[68:71], v[222:225], v[166:169], v[68:71]
	v_mfma_f32_16x16x32_bf16 v[64:67], v[230:233], v[166:169], v[64:67]
	v_mfma_f32_16x16x32_bf16 v[52:55], v[222:225], v[178:181], v[52:55]
	v_mfma_f32_16x16x32_bf16 v[48:51], v[230:233], v[178:181], v[48:51]
	v_mfma_f32_16x16x32_bf16 v[44:47], v[222:225], v[208:211], v[44:47]
	v_mfma_f32_16x16x32_bf16 v[40:43], v[230:233], v[208:211], v[40:43]
	v_mfma_f32_16x16x32_bf16 v[36:39], v[222:225], v[218:221], v[36:39]
	v_mfma_f32_16x16x32_bf16 v[32:35], v[230:233], v[218:221], v[32:35]
	s_setprio 0
	s_mov_b32 m0, s83
	v_lshl_add_u64 v[170:171], v[196:197], 0, s[40:41]
	s_barrier
	ds_read_b128 v[162:165], v185 offset:49152
	ds_read_b128 v[166:169], v185 offset:50176
	ds_read_b128 v[174:177], v185 offset:51200
	ds_read_b128 v[178:181], v185 offset:52224
	ds_read_b128 v[204:207], v185 offset:53248
	ds_read_b128 v[208:211], v185 offset:54272
	ds_read_b128 v[214:217], v185 offset:55296
	ds_read_b128 v[218:221], v185 offset:56320
	global_load_lds_dwordx4 v[170:171], off
	v_lshl_add_u64 v[170:171], v[242:243], 0, s[40:41]
	s_mov_b32 m0, s85
	s_nop 0
	global_load_lds_dwordx4 v[170:171], off
	s_barrier
	s_waitcnt lgkmcnt(0)
	s_setprio 1
	v_mfma_f32_16x16x32_bf16 v[92:95], v[140:143], v[162:165], v[92:95]
	v_mfma_f32_16x16x32_bf16 v[88:91], v[148:151], v[162:165], v[88:91]
	v_mfma_f32_16x16x32_bf16 v[84:87], v[140:143], v[174:177], v[84:87]
	v_mfma_f32_16x16x32_bf16 v[80:83], v[148:151], v[174:177], v[80:83]
	v_mfma_f32_16x16x32_bf16 v[76:79], v[140:143], v[204:207], v[76:79]
	v_mfma_f32_16x16x32_bf16 v[72:75], v[148:151], v[204:207], v[72:75]
	v_mfma_f32_16x16x32_bf16 v[60:63], v[140:143], v[214:217], v[60:63]
	v_mfma_f32_16x16x32_bf16 v[56:59], v[148:151], v[214:217], v[56:59]
	v_mfma_f32_16x16x32_bf16 v[92:95], v[144:147], v[166:169], v[92:95]
	v_mfma_f32_16x16x32_bf16 v[88:91], v[152:155], v[166:169], v[88:91]
	v_mfma_f32_16x16x32_bf16 v[84:87], v[144:147], v[178:181], v[84:87]
	v_mfma_f32_16x16x32_bf16 v[80:83], v[152:155], v[178:181], v[80:83]
	v_mfma_f32_16x16x32_bf16 v[76:79], v[144:147], v[208:211], v[76:79]
	v_mfma_f32_16x16x32_bf16 v[72:75], v[152:155], v[208:211], v[72:75]
	v_mfma_f32_16x16x32_bf16 v[60:63], v[144:147], v[218:221], v[60:63]
	v_mfma_f32_16x16x32_bf16 v[56:59], v[152:155], v[218:221], v[56:59]
	s_setprio 0
	s_barrier
	s_add_u32 s28, s28, 0x40080
	s_addc_u32 s29, s29, 0
	s_mov_b32 m0, s87
	v_lshl_add_u64 v[140:141], s[28:29], 0, v[158:159]
	global_load_lds_dwordx4 v[140:141], off
	v_lshl_add_u64 v[140:141], s[28:29], 0, v[160:161]
	s_mov_b32 m0, s44
	s_nop 0
	global_load_lds_dwordx4 v[140:141], off
	s_waitcnt vmcnt(6)
	s_barrier
	s_setprio 1
	v_mfma_f32_16x16x32_bf16 v[28:31], v[136:139], v[162:165], v[28:31]
	v_mfma_f32_16x16x32_bf16 v[24:27], v[226:229], v[162:165], v[24:27]
	v_mfma_f32_16x16x32_bf16 v[20:23], v[136:139], v[174:177], v[20:23]
	v_mfma_f32_16x16x32_bf16 v[16:19], v[226:229], v[174:177], v[16:19]
	v_mfma_f32_16x16x32_bf16 v[12:15], v[136:139], v[204:207], v[12:15]
	v_mfma_f32_16x16x32_bf16 v[8:11], v[226:229], v[204:207], v[8:11]
	v_mfma_f32_16x16x32_bf16 v[4:7], v[136:139], v[214:217], v[4:7]
	v_mfma_f32_16x16x32_bf16 v[0:3], v[226:229], v[214:217], v[0:3]
	v_mfma_f32_16x16x32_bf16 v[28:31], v[222:225], v[166:169], v[28:31]
	v_mfma_f32_16x16x32_bf16 v[24:27], v[230:233], v[166:169], v[24:27]
	v_mfma_f32_16x16x32_bf16 v[20:23], v[222:225], v[178:181], v[20:23]
	v_mfma_f32_16x16x32_bf16 v[16:19], v[230:233], v[178:181], v[16:19]
	v_mfma_f32_16x16x32_bf16 v[12:15], v[222:225], v[208:211], v[12:15]
	v_mfma_f32_16x16x32_bf16 v[8:11], v[230:233], v[208:211], v[8:11]
	v_mfma_f32_16x16x32_bf16 v[4:7], v[222:225], v[218:221], v[4:7]
	v_mfma_f32_16x16x32_bf16 v[0:3], v[230:233], v[218:221], v[0:3]
	s_setprio 0
	s_add_i32 vcc_lo, vcc_lo, 2
	s_add_u32 s26, s26, 0x100
	s_addc_u32 s27, s27, 0
	s_add_u32 s9, s9, 0x100
	s_addc_u32 s15, s15, 0
	s_cmp_gt_u32 vcc_lo, 13
	s_barrier
	s_branch .LBB0_1320
.LBB0_1319:
	ds_read_b128 v[142:145], v186
	ds_read_b128 v[146:149], v186 offset:1024
	ds_read_b128 v[150:153], v186 offset:2048
	ds_read_b128 v[162:165], v186 offset:3072
	s_add_u32 s30, s26, 0x80
	s_addc_u32 s31, s27, 0
	s_and_b64 s[28:29], s[28:29], exec
	s_cselect_b32 s31, s19, s31
	s_cselect_b32 s30, s18, s30
	s_cselect_b32 s29, s17, s15
	s_cselect_b32 s28, s16, s9
	v_lshl_add_u64 v[154:155], s[26:27], 0, v[128:129]
	s_add_i32 m0, s23, 0xc000
	ds_read_b128 v[166:169], v185
	ds_read_b128 v[174:177], v185 offset:1024
	ds_read_b128 v[178:181], v185 offset:2048
	ds_read_b128 v[204:207], v185 offset:3072
	ds_read_b128 v[208:211], v185 offset:4096
	ds_read_b128 v[214:217], v185 offset:5120
	ds_read_b128 v[218:221], v185 offset:6144
	ds_read_b128 v[222:225], v185 offset:7168
	global_load_lds_dwordx4 v[154:155], off
	v_lshl_add_u64 v[154:155], s[26:27], 0, v[132:133]
	s_add_i32 m0, s23, 0xe000
	s_nop 0
	global_load_lds_dwordx4 v[154:155], off
	s_waitcnt lgkmcnt(8)
	s_barrier
	s_waitcnt lgkmcnt(0)
	s_setprio 1
	v_mfma_f32_16x16x32_bf16 v[124:127], v[142:145], v[166:169], v[124:127]
	v_mfma_f32_16x16x32_bf16 v[120:123], v[150:153], v[166:169], v[120:123]
	v_mfma_f32_16x16x32_bf16 v[116:119], v[142:145], v[178:181], v[116:119]
	v_mfma_f32_16x16x32_bf16 v[112:115], v[150:153], v[178:181], v[112:115]
	v_mfma_f32_16x16x32_bf16 v[108:111], v[142:145], v[208:211], v[108:111]
	v_mfma_f32_16x16x32_bf16 v[104:107], v[150:153], v[208:211], v[104:107]
	v_mfma_f32_16x16x32_bf16 v[100:103], v[142:145], v[218:221], v[100:103]
	v_mfma_f32_16x16x32_bf16 v[96:99], v[150:153], v[218:221], v[96:99]
	v_mfma_f32_16x16x32_bf16 v[124:127], v[146:149], v[174:177], v[124:127]
	v_mfma_f32_16x16x32_bf16 v[120:123], v[162:165], v[174:177], v[120:123]
	v_mfma_f32_16x16x32_bf16 v[116:119], v[146:149], v[204:207], v[116:119]
	v_mfma_f32_16x16x32_bf16 v[112:115], v[162:165], v[204:207], v[112:115]
	v_mfma_f32_16x16x32_bf16 v[108:111], v[146:149], v[214:217], v[108:111]
	v_mfma_f32_16x16x32_bf16 v[104:107], v[162:165], v[214:217], v[104:107]
	v_mfma_f32_16x16x32_bf16 v[100:103], v[146:149], v[222:225], v[100:103]
	v_mfma_f32_16x16x32_bf16 v[96:99], v[162:165], v[222:225], v[96:99]
	s_setprio 0
	s_barrier
	s_mov_b32 m0, s25
	v_lshl_add_u64 v[170:171], s[28:29], 0, v[158:159]
	ds_read_b128 v[226:229], v186 offset:16384
	ds_read_b128 v[230:233], v186 offset:17408
	ds_read_b128 v[234:237], v186 offset:18432
	ds_read_b128 v[238:241], v186 offset:19456
	global_load_lds_dwordx4 v[170:171], off
	v_lshl_add_u64 v[182:183], s[28:29], 0, v[160:161]
	s_mov_b32 m0, s51
	s_nop 0
	global_load_lds_dwordx4 v[182:183], off
	s_barrier
	s_waitcnt lgkmcnt(0)
	s_setprio 1
	v_mfma_f32_16x16x32_bf16 v[68:71], v[226:229], v[166:169], v[68:71]
	v_mfma_f32_16x16x32_bf16 v[64:67], v[234:237], v[166:169], v[64:67]
	v_mfma_f32_16x16x32_bf16 v[52:55], v[226:229], v[178:181], v[52:55]
	v_mfma_f32_16x16x32_bf16 v[48:51], v[234:237], v[178:181], v[48:51]
	v_mfma_f32_16x16x32_bf16 v[44:47], v[226:229], v[208:211], v[44:47]
	v_mfma_f32_16x16x32_bf16 v[40:43], v[234:237], v[208:211], v[40:43]
	v_mfma_f32_16x16x32_bf16 v[36:39], v[226:229], v[218:221], v[36:39]
	v_mfma_f32_16x16x32_bf16 v[32:35], v[234:237], v[218:221], v[32:35]
	v_mfma_f32_16x16x32_bf16 v[68:71], v[230:233], v[174:177], v[68:71]
	v_mfma_f32_16x16x32_bf16 v[64:67], v[238:241], v[174:177], v[64:67]
	v_mfma_f32_16x16x32_bf16 v[52:55], v[230:233], v[204:207], v[52:55]
	v_mfma_f32_16x16x32_bf16 v[48:51], v[238:241], v[204:207], v[48:51]
	v_mfma_f32_16x16x32_bf16 v[44:47], v[230:233], v[214:217], v[44:47]
	v_mfma_f32_16x16x32_bf16 v[40:43], v[238:241], v[214:217], v[40:43]
	v_mfma_f32_16x16x32_bf16 v[36:39], v[230:233], v[222:225], v[36:39]
	v_mfma_f32_16x16x32_bf16 v[32:35], v[238:241], v[222:225], v[32:35]
	s_setprio 0
	s_mov_b32 m0, s23
	s_barrier
	ds_read_b128 v[166:169], v185 offset:16384
	ds_read_b128 v[174:177], v185 offset:17408
	ds_read_b128 v[178:181], v185 offset:18432
	ds_read_b128 v[204:207], v185 offset:19456
	ds_read_b128 v[208:211], v185 offset:20480
	ds_read_b128 v[214:217], v185 offset:21504
	ds_read_b128 v[218:221], v185 offset:22528
	ds_read_b128 v[222:225], v185 offset:23552
	global_load_lds_dwordx4 v172, s[30:31]
	s_mov_b32 m0, s56
	v_mov_b32_e32 v141, v173
	global_load_lds_dwordx4 v140, s[30:31]
	s_barrier
	s_waitcnt lgkmcnt(0)
	v_lshl_add_u64 v[196:197], s[30:31], 0, v[172:173]
	v_lshl_add_u64 v[242:243], s[30:31], 0, v[140:141]
	s_setprio 1
	v_mfma_f32_16x16x32_bf16 v[92:95], v[142:145], v[166:169], v[92:95]
	v_mfma_f32_16x16x32_bf16 v[88:91], v[150:153], v[166:169], v[88:91]
	v_mfma_f32_16x16x32_bf16 v[84:87], v[142:145], v[178:181], v[84:87]
	v_mfma_f32_16x16x32_bf16 v[80:83], v[150:153], v[178:181], v[80:83]
	v_mfma_f32_16x16x32_bf16 v[76:79], v[142:145], v[208:211], v[76:79]
	v_mfma_f32_16x16x32_bf16 v[72:75], v[150:153], v[208:211], v[72:75]
	v_mfma_f32_16x16x32_bf16 v[60:63], v[142:145], v[218:221], v[60:63]
	v_mfma_f32_16x16x32_bf16 v[56:59], v[150:153], v[218:221], v[56:59]
	v_mfma_f32_16x16x32_bf16 v[92:95], v[146:149], v[174:177], v[92:95]
	v_mfma_f32_16x16x32_bf16 v[88:91], v[162:165], v[174:177], v[88:91]
	v_mfma_f32_16x16x32_bf16 v[84:87], v[146:149], v[204:207], v[84:87]
	v_mfma_f32_16x16x32_bf16 v[80:83], v[162:165], v[204:207], v[80:83]
	v_mfma_f32_16x16x32_bf16 v[76:79], v[146:149], v[214:217], v[76:79]
	v_mfma_f32_16x16x32_bf16 v[72:75], v[162:165], v[214:217], v[72:75]
	v_mfma_f32_16x16x32_bf16 v[60:63], v[146:149], v[222:225], v[60:63]
	v_mfma_f32_16x16x32_bf16 v[56:59], v[162:165], v[222:225], v[56:59]
	s_setprio 0
	s_barrier
	s_add_u32 s94, s28, 0x40000
	s_addc_u32 s95, s29, 0
	s_mov_b32 m0, s65
	v_lshl_add_u64 v[140:141], s[94:95], 0, v[158:159]
	global_load_lds_dwordx4 v[140:141], off
	v_lshl_add_u64 v[140:141], s[94:95], 0, v[160:161]
	s_mov_b32 m0, s70
	s_nop 0
	global_load_lds_dwordx4 v[140:141], off
	s_waitcnt vmcnt(6)
	s_barrier
	s_setprio 1
	v_mfma_f32_16x16x32_bf16 v[28:31], v[226:229], v[166:169], v[28:31]
	v_mfma_f32_16x16x32_bf16 v[24:27], v[234:237], v[166:169], v[24:27]
	v_mfma_f32_16x16x32_bf16 v[20:23], v[226:229], v[178:181], v[20:23]
	v_mfma_f32_16x16x32_bf16 v[16:19], v[234:237], v[178:181], v[16:19]
	v_mfma_f32_16x16x32_bf16 v[12:15], v[226:229], v[208:211], v[12:15]
	v_mfma_f32_16x16x32_bf16 v[8:11], v[234:237], v[208:211], v[8:11]
	v_mfma_f32_16x16x32_bf16 v[4:7], v[226:229], v[218:221], v[4:7]
	v_mfma_f32_16x16x32_bf16 v[0:3], v[234:237], v[218:221], v[0:3]
	v_mfma_f32_16x16x32_bf16 v[28:31], v[230:233], v[174:177], v[28:31]
	v_mfma_f32_16x16x32_bf16 v[24:27], v[238:241], v[174:177], v[24:27]
	v_mfma_f32_16x16x32_bf16 v[20:23], v[230:233], v[204:207], v[20:23]
	v_mfma_f32_16x16x32_bf16 v[16:19], v[238:241], v[204:207], v[16:19]
	v_mfma_f32_16x16x32_bf16 v[12:15], v[230:233], v[214:217], v[12:15]
	v_mfma_f32_16x16x32_bf16 v[8:11], v[238:241], v[214:217], v[8:11]
	v_mfma_f32_16x16x32_bf16 v[4:7], v[230:233], v[222:225], v[4:7]
	v_mfma_f32_16x16x32_bf16 v[0:3], v[238:241], v[222:225], v[0:3]
	s_setprio 0
	s_barrier
	ds_read_b128 v[140:143], v186 offset:32768
	ds_read_b128 v[144:147], v186 offset:33792
	ds_read_b128 v[148:151], v186 offset:34816
	ds_read_b128 v[152:155], v186 offset:35840
	s_mov_b32 m0, s71
	v_lshl_add_u64 v[138:139], s[30:31], 0, v[138:139]
	ds_read_b128 v[162:165], v185 offset:32768
	ds_read_b128 v[166:169], v185 offset:33792
	ds_read_b128 v[174:177], v185 offset:34816
	ds_read_b128 v[178:181], v185 offset:35840
	ds_read_b128 v[204:207], v185 offset:36864
	ds_read_b128 v[208:211], v185 offset:37888
	ds_read_b128 v[214:217], v185 offset:38912
	ds_read_b128 v[218:221], v185 offset:39936
	global_load_lds_dwordx4 v[138:139], off
	v_lshl_add_u64 v[136:137], s[30:31], 0, v[136:137]
	s_mov_b32 m0, s80
	s_nop 0
	global_load_lds_dwordx4 v[136:137], off
	s_waitcnt lgkmcnt(8)
	s_barrier
	s_waitcnt lgkmcnt(0)
	s_setprio 1
	v_mfma_f32_16x16x32_bf16 v[124:127], v[140:143], v[162:165], v[124:127]
	v_mfma_f32_16x16x32_bf16 v[120:123], v[148:151], v[162:165], v[120:123]
	v_mfma_f32_16x16x32_bf16 v[116:119], v[140:143], v[174:177], v[116:119]
	v_mfma_f32_16x16x32_bf16 v[112:115], v[148:151], v[174:177], v[112:115]
	v_mfma_f32_16x16x32_bf16 v[108:111], v[140:143], v[204:207], v[108:111]
	v_mfma_f32_16x16x32_bf16 v[104:107], v[148:151], v[204:207], v[104:107]
	v_mfma_f32_16x16x32_bf16 v[100:103], v[140:143], v[214:217], v[100:103]
	v_mfma_f32_16x16x32_bf16 v[96:99], v[148:151], v[214:217], v[96:99]
	v_mfma_f32_16x16x32_bf16 v[124:127], v[144:147], v[166:169], v[124:127]
	v_mfma_f32_16x16x32_bf16 v[120:123], v[152:155], v[166:169], v[120:123]
	v_mfma_f32_16x16x32_bf16 v[116:119], v[144:147], v[178:181], v[116:119]
	v_mfma_f32_16x16x32_bf16 v[112:115], v[152:155], v[178:181], v[112:115]
	v_mfma_f32_16x16x32_bf16 v[108:111], v[144:147], v[208:211], v[108:111]
	v_mfma_f32_16x16x32_bf16 v[104:107], v[152:155], v[208:211], v[104:107]
	v_mfma_f32_16x16x32_bf16 v[100:103], v[144:147], v[218:221], v[100:103]
	v_mfma_f32_16x16x32_bf16 v[96:99], v[152:155], v[218:221], v[96:99]
	s_setprio 0
	s_barrier
	s_mov_b32 m0, s81
	v_lshl_add_u64 v[170:171], v[170:171], 0, s[40:41]
	ds_read_b128 v[136:139], v186 offset:49152
	ds_read_b128 v[222:225], v186 offset:50176
	ds_read_b128 v[226:229], v186 offset:51200
	ds_read_b128 v[230:233], v186 offset:52224
	global_load_lds_dwordx4 v[170:171], off
	v_lshl_add_u64 v[170:171], v[182:183], 0, s[40:41]
	s_mov_b32 m0, s82
	s_nop 0
	global_load_lds_dwordx4 v[170:171], off
	s_barrier
	s_waitcnt lgkmcnt(0)
	s_setprio 1
	v_mfma_f32_16x16x32_bf16 v[68:71], v[136:139], v[162:165], v[68:71]
	v_mfma_f32_16x16x32_bf16 v[64:67], v[226:229], v[162:165], v[64:67]
	v_mfma_f32_16x16x32_bf16 v[52:55], v[136:139], v[174:177], v[52:55]
	v_mfma_f32_16x16x32_bf16 v[48:51], v[226:229], v[174:177], v[48:51]
	v_mfma_f32_16x16x32_bf16 v[44:47], v[136:139], v[204:207], v[44:47]
	v_mfma_f32_16x16x32_bf16 v[40:43], v[226:229], v[204:207], v[40:43]
	v_mfma_f32_16x16x32_bf16 v[36:39], v[136:139], v[214:217], v[36:39]
	v_mfma_f32_16x16x32_bf16 v[32:35], v[226:229], v[214:217], v[32:35]
	v_mfma_f32_16x16x32_bf16 v[68:71], v[222:225], v[166:169], v[68:71]
	v_mfma_f32_16x16x32_bf16 v[64:67], v[230:233], v[166:169], v[64:67]
	v_mfma_f32_16x16x32_bf16 v[52:55], v[222:225], v[178:181], v[52:55]
	v_mfma_f32_16x16x32_bf16 v[48:51], v[230:233], v[178:181], v[48:51]
	v_mfma_f32_16x16x32_bf16 v[44:47], v[222:225], v[208:211], v[44:47]
	v_mfma_f32_16x16x32_bf16 v[40:43], v[230:233], v[208:211], v[40:43]
	v_mfma_f32_16x16x32_bf16 v[36:39], v[222:225], v[218:221], v[36:39]
	v_mfma_f32_16x16x32_bf16 v[32:35], v[230:233], v[218:221], v[32:35]
	s_setprio 0
	s_mov_b32 m0, s83
	v_lshl_add_u64 v[170:171], v[196:197], 0, s[40:41]
	s_barrier
	ds_read_b128 v[162:165], v185 offset:49152
	ds_read_b128 v[166:169], v185 offset:50176
	ds_read_b128 v[174:177], v185 offset:51200
	ds_read_b128 v[178:181], v185 offset:52224
	ds_read_b128 v[204:207], v185 offset:53248
	ds_read_b128 v[208:211], v185 offset:54272
	ds_read_b128 v[214:217], v185 offset:55296
	ds_read_b128 v[218:221], v185 offset:56320
	global_load_lds_dwordx4 v[170:171], off
	v_lshl_add_u64 v[170:171], v[242:243], 0, s[40:41]
	s_mov_b32 m0, s85
	s_nop 0
	global_load_lds_dwordx4 v[170:171], off
	s_barrier
	s_waitcnt lgkmcnt(0)
	s_setprio 1
	v_mfma_f32_16x16x32_bf16 v[92:95], v[140:143], v[162:165], v[92:95]
	v_mfma_f32_16x16x32_bf16 v[88:91], v[148:151], v[162:165], v[88:91]
	v_mfma_f32_16x16x32_bf16 v[84:87], v[140:143], v[174:177], v[84:87]
	v_mfma_f32_16x16x32_bf16 v[80:83], v[148:151], v[174:177], v[80:83]
	v_mfma_f32_16x16x32_bf16 v[76:79], v[140:143], v[204:207], v[76:79]
	v_mfma_f32_16x16x32_bf16 v[72:75], v[148:151], v[204:207], v[72:75]
	v_mfma_f32_16x16x32_bf16 v[60:63], v[140:143], v[214:217], v[60:63]
	v_mfma_f32_16x16x32_bf16 v[56:59], v[148:151], v[214:217], v[56:59]
	v_mfma_f32_16x16x32_bf16 v[92:95], v[144:147], v[166:169], v[92:95]
	v_mfma_f32_16x16x32_bf16 v[88:91], v[152:155], v[166:169], v[88:91]
	v_mfma_f32_16x16x32_bf16 v[84:87], v[144:147], v[178:181], v[84:87]
	v_mfma_f32_16x16x32_bf16 v[80:83], v[152:155], v[178:181], v[80:83]
	v_mfma_f32_16x16x32_bf16 v[76:79], v[144:147], v[208:211], v[76:79]
	v_mfma_f32_16x16x32_bf16 v[72:75], v[152:155], v[208:211], v[72:75]
	v_mfma_f32_16x16x32_bf16 v[60:63], v[144:147], v[218:221], v[60:63]
	v_mfma_f32_16x16x32_bf16 v[56:59], v[152:155], v[218:221], v[56:59]
	s_setprio 0
	s_barrier
	s_add_u32 s28, s28, 0x40080
	s_addc_u32 s29, s29, 0
	s_mov_b32 m0, s87
	v_lshl_add_u64 v[140:141], s[28:29], 0, v[158:159]
	global_load_lds_dwordx4 v[140:141], off
	v_lshl_add_u64 v[140:141], s[28:29], 0, v[160:161]
	s_mov_b32 m0, s44
	s_nop 0
	global_load_lds_dwordx4 v[140:141], off
	s_waitcnt vmcnt(6)
	s_barrier
	s_setprio 1
	v_mfma_f32_16x16x32_bf16 v[28:31], v[136:139], v[162:165], v[28:31]
	v_mfma_f32_16x16x32_bf16 v[24:27], v[226:229], v[162:165], v[24:27]
	v_mfma_f32_16x16x32_bf16 v[20:23], v[136:139], v[174:177], v[20:23]
	v_mfma_f32_16x16x32_bf16 v[16:19], v[226:229], v[174:177], v[16:19]
	v_mfma_f32_16x16x32_bf16 v[12:15], v[136:139], v[204:207], v[12:15]
	v_mfma_f32_16x16x32_bf16 v[8:11], v[226:229], v[204:207], v[8:11]
	v_mfma_f32_16x16x32_bf16 v[4:7], v[136:139], v[214:217], v[4:7]
	v_mfma_f32_16x16x32_bf16 v[0:3], v[226:229], v[214:217], v[0:3]
	v_mfma_f32_16x16x32_bf16 v[28:31], v[222:225], v[166:169], v[28:31]
	v_mfma_f32_16x16x32_bf16 v[24:27], v[230:233], v[166:169], v[24:27]
	v_mfma_f32_16x16x32_bf16 v[20:23], v[222:225], v[178:181], v[20:23]
	v_mfma_f32_16x16x32_bf16 v[16:19], v[230:233], v[178:181], v[16:19]
	v_mfma_f32_16x16x32_bf16 v[12:15], v[222:225], v[208:211], v[12:15]
	v_mfma_f32_16x16x32_bf16 v[8:11], v[230:233], v[208:211], v[8:11]
	v_mfma_f32_16x16x32_bf16 v[4:7], v[222:225], v[218:221], v[4:7]
	v_mfma_f32_16x16x32_bf16 v[0:3], v[230:233], v[218:221], v[0:3]
	s_setprio 0
	s_add_i32 vcc_lo, vcc_lo, 2
	s_add_u32 s26, s26, 0x100
	s_addc_u32 s27, s27, 0
	s_add_u32 s9, s9, 0x100
	s_addc_u32 s15, s15, 0
	s_cmp_gt_u32 vcc_lo, 13
	s_barrier
	s_cbranch_scc1 .LBB0_1303

.LBB0_1328:
	v_add_u32_e32 v12, s12, v88
	v_add_u32_e32 v4, 0x45, v12
	v_ashrrev_i32_e32 v13, 31, v12
	v_ashrrev_i32_e32 v5, 31, v4
	v_lshlrev_b64 v[0:1], 13, v[12:13]
	v_lshlrev_b64 v[4:5], 13, v[4:5]
	v_lshl_add_u64 v[0:1], v[64:65], 0, v[0:1]
	v_lshl_add_u64 v[4:5], v[64:65], 0, v[4:5]
	global_load_dwordx4 v[48:51], v[0:1], off nt
	v_add_u32_e32 v8, 0x46, v12
	global_load_dwordx4 v[4:7], v[4:5], off nt
	v_or_b32_e32 v0, 1, v12
	v_ashrrev_i32_e32 v1, 31, v0
	v_ashrrev_i32_e32 v9, 31, v8
	v_lshlrev_b64 v[0:1], 13, v[0:1]
	v_lshlrev_b64 v[8:9], 13, v[8:9]
	v_lshl_add_u64 v[0:1], v[64:65], 0, v[0:1]
	v_lshl_add_u64 v[8:9], v[64:65], 0, v[8:9]
	global_load_dwordx4 v[52:55], v[0:1], off nt
	global_load_dwordx4 v[8:11], v[8:9], off nt
	v_or_b32_e32 v0, 2, v12
	v_ashrrev_i32_e32 v1, 31, v0
	v_lshlrev_b64 v[0:1], 13, v[0:1]
	v_lshl_add_u64 v[0:1], v[64:65], 0, v[0:1]
	global_load_dwordx4 v[56:59], v[0:1], off nt
	v_or_b32_e32 v0, 3, v12
	v_ashrrev_i32_e32 v1, 31, v0
	v_lshlrev_b64 v[0:1], 13, v[0:1]
	v_lshl_add_u64 v[0:1], v[64:65], 0, v[0:1]
	global_load_dwordx4 v[60:63], v[0:1], off nt
	v_or_b32_e32 v0, 4, v12
	v_ashrrev_i32_e32 v1, 31, v0
	v_lshlrev_b64 v[0:1], 13, v[0:1]
	v_lshl_add_u64 v[0:1], v[64:65], 0, v[0:1]
	global_load_dwordx4 v[32:35], v[0:1], off nt
	v_or_b32_e32 v0, 5, v12
	v_ashrrev_i32_e32 v1, 31, v0
	v_lshlrev_b64 v[0:1], 13, v[0:1]
	v_lshl_add_u64 v[0:1], v[64:65], 0, v[0:1]
	global_load_dwordx4 v[36:39], v[0:1], off nt
	v_or_b32_e32 v0, 6, v12
	v_ashrrev_i32_e32 v1, 31, v0
	v_lshlrev_b64 v[0:1], 13, v[0:1]
	v_lshl_add_u64 v[0:1], v[64:65], 0, v[0:1]
	global_load_dwordx4 v[40:43], v[0:1], off nt
	v_or_b32_e32 v0, 7, v12
	v_ashrrev_i32_e32 v1, 31, v0
	v_lshlrev_b64 v[0:1], 13, v[0:1]
	v_lshl_add_u64 v[0:1], v[64:65], 0, v[0:1]
	global_load_dwordx4 v[44:47], v[0:1], off nt
	v_add_u32_e32 v0, 64, v12
	v_ashrrev_i32_e32 v1, 31, v0
	v_lshlrev_b64 v[0:1], 13, v[0:1]
	v_lshl_add_u64 v[0:1], v[64:65], 0, v[0:1]
	global_load_dwordx4 v[16:19], v[0:1], off nt
	v_add_u32_e32 v0, 0x41, v12
	v_ashrrev_i32_e32 v1, 31, v0
	v_lshlrev_b64 v[0:1], 13, v[0:1]
	v_lshl_add_u64 v[0:1], v[64:65], 0, v[0:1]
	global_load_dwordx4 v[20:23], v[0:1], off nt
	v_add_u32_e32 v0, 0x42, v12
	v_ashrrev_i32_e32 v1, 31, v0
	v_lshlrev_b64 v[0:1], 13, v[0:1]
	v_lshl_add_u64 v[0:1], v[64:65], 0, v[0:1]
	global_load_dwordx4 v[24:27], v[0:1], off nt
	v_add_u32_e32 v0, 0x43, v12
	v_ashrrev_i32_e32 v1, 31, v0
	v_lshlrev_b64 v[0:1], 13, v[0:1]
	v_lshl_add_u64 v[0:1], v[64:65], 0, v[0:1]
	global_load_dwordx4 v[28:31], v[0:1], off nt
	v_add_u32_e32 v0, 0x44, v12
	v_ashrrev_i32_e32 v1, 31, v0
	v_lshlrev_b64 v[0:1], 13, v[0:1]
	v_lshl_add_u64 v[0:1], v[64:65], 0, v[0:1]
	global_load_dwordx4 v[0:3], v[0:1], off nt
	v_add_u32_e32 v12, 0x47, v12
	v_ashrrev_i32_e32 v13, 31, v12
	v_lshlrev_b64 v[12:13], 13, v[12:13]
	v_lshl_add_u64 v[12:13], v[64:65], 0, v[12:13]
	global_load_dwordx4 v[12:15], v[12:13], off nt
	s_and_b64 vcc, exec, s[10:11]
	s_mov_b64 s[10:11], 0
	s_waitcnt vmcnt(15)
	v_mul_f32_e32 v48, 0x42000000, v48
	s_waitcnt vmcnt(14)
	v_mul_f32_e32 v4, 0x42000000, v4
	v_mul_f32_e32 v5, 0x42000000, v5
	s_waitcnt vmcnt(13)
	v_mul_f32_e32 v52, 0x42000000, v52
	v_cvt_pk_fp8_f32 v66, v48, v52
	s_waitcnt vmcnt(12)
	v_mul_f32_e32 v8, 0x42000000, v8
	s_waitcnt vmcnt(11)
	v_mul_f32_e32 v48, 0x42000000, v57
	v_mul_f32_e32 v56, 0x42000000, v56
	s_waitcnt vmcnt(10)
	v_mul_f32_e32 v60, 0x42000000, v60
	v_cvt_pk_fp8_f32 v66, v56, v60 op_sel:[0,0,1]
	s_waitcnt vmcnt(9)
	v_mul_f32_e32 v32, 0x42000000, v32
	s_waitcnt vmcnt(8)
	v_mul_f32_e32 v36, 0x42000000, v36
	v_cvt_pk_fp8_f32 v67, v32, v36
	v_mul_f32_e32 v32, 0x42000000, v49
	v_mul_f32_e32 v36, 0x42000000, v53
	v_mul_f32_e32 v49, 0x42000000, v61
	s_waitcnt vmcnt(7)
	v_mul_f32_e32 v40, 0x42000000, v40
	s_waitcnt vmcnt(6)
	v_mul_f32_e32 v44, 0x42000000, v44
	v_cvt_pk_fp8_f32 v67, v40, v44 op_sel:[0,0,1]
	v_cvt_pk_fp8_f32 v40, v32, v36
	v_mul_f32_e32 v32, 0x42000000, v33
	v_mul_f32_e32 v33, 0x42000000, v37
	v_mul_f32_e32 v36, 0x42000000, v41
	v_cvt_pk_fp8_f32 v41, v32, v33
	v_mul_f32_e32 v37, 0x42000000, v45
	v_mul_f32_e32 v32, 0x42000000, v50
	v_mul_f32_e32 v33, 0x42000000, v54
	v_cvt_pk_fp8_f32 v41, v36, v37 op_sel:[0,0,1]
	v_cvt_pk_fp8_f32 v36, v32, v33
	v_mul_f32_e32 v37, 0x42000000, v58
	v_mul_f32_e32 v45, 0x42000000, v62
	v_mul_f32_e32 v32, 0x42000000, v34
	v_cvt_pk_fp8_f32 v36, v37, v45 op_sel:[0,0,1]
	v_mul_f32_e32 v33, 0x42000000, v38
	v_cvt_pk_fp8_f32 v37, v32, v33
	v_mul_f32_e32 v34, 0x42000000, v42
	v_mul_f32_e32 v38, 0x42000000, v46
	v_mul_f32_e32 v33, 0x42000000, v51
	v_cvt_pk_fp8_f32 v37, v34, v38 op_sel:[0,0,1]
	v_mul_f32_e32 v34, 0x42000000, v55
	v_cvt_pk_fp8_f32 v32, v33, v34
	v_mul_f32_e32 v34, 0x42000000, v35
	v_mul_f32_e32 v35, 0x42000000, v39
	v_cvt_pk_fp8_f32 v33, v34, v35
	s_waitcnt vmcnt(1)
	v_mul_f32_e32 v0, 0x42000000, v0
	v_cvt_pk_fp8_f32 v35, v0, v4
	s_waitcnt vmcnt(0)
	v_mul_f32_e32 v12, 0x42000000, v12
	v_mul_f32_e32 v4, 0x42000000, v17
	v_cvt_pk_fp8_f32 v35, v8, v12 op_sel:[0,0,1]
	v_mul_f32_e32 v8, 0x42000000, v21
	v_cvt_pk_fp8_f32 v0, v4, v8
	v_mul_f32_e32 v4, 0x42000000, v1
	v_cvt_pk_fp8_f32 v1, v4, v5
	v_mul_f32_e32 v16, 0x42000000, v16
	v_mul_f32_e32 v20, 0x42000000, v20
	v_cvt_pk_fp8_f32 v34, v16, v20
	v_mul_f32_e32 v12, 0x42000000, v25
	v_mul_f32_e32 v16, 0x42000000, v29
	v_mul_f32_e32 v8, 0x42000000, v9
	v_mul_f32_e32 v9, 0x42000000, v13
	v_cvt_pk_fp8_f32 v40, v48, v49 op_sel:[0,0,1]
	v_cvt_pk_fp8_f32 v0, v12, v16 op_sel:[0,0,1]
	v_cvt_pk_fp8_f32 v1, v8, v9 op_sel:[0,0,1]
	v_add_u32_e32 v44, s12, v79
	v_mul_f32_e32 v4, 0x42000000, v22
	v_mul_f32_e32 v2, 0x42000000, v2
	ds_write2_b64 v44, v[40:41], v[0:1] offset0:34 offset1:42
	v_mul_f32_e32 v1, 0x42000000, v18
	v_cvt_pk_fp8_f32 v0, v1, v4
	v_mul_f32_e32 v4, 0x42000000, v6
	v_cvt_pk_fp8_f32 v1, v2, v4
	v_mul_f32_e32 v5, 0x42000000, v26
	v_mul_f32_e32 v8, 0x42000000, v30
	v_cvt_pk_fp8_f32 v0, v5, v8 op_sel:[0,0,1]
	v_mul_f32_e32 v5, 0x42000000, v10
	v_mul_f32_e32 v6, 0x42000000, v14
	v_cvt_pk_fp8_f32 v1, v5, v6 op_sel:[0,0,1]
	v_mul_f32_e32 v2, 0x42000000, v23
	v_mul_f32_e32 v38, 0x42000000, v59
	v_mul_f32_e32 v42, 0x42000000, v63
	ds_write2_b64 v44, v[36:37], v[0:1] offset0:68 offset1:76
	v_mul_f32_e32 v1, 0x42000000, v19
	v_cvt_pk_fp8_f32 v0, v1, v2
	v_mul_f32_e32 v2, 0x42000000, v3
	v_mul_f32_e32 v3, 0x42000000, v7
	v_cvt_pk_fp8_f32 v1, v2, v3
	v_mul_f32_e32 v4, 0x42000000, v27
	v_mul_f32_e32 v5, 0x42000000, v31
	v_cvt_pk_fp8_f32 v32, v38, v42 op_sel:[0,0,1]
	v_mul_f32_e32 v38, 0x42000000, v43
	v_mul_f32_e32 v39, 0x42000000, v47
	v_mul_f32_e32 v24, 0x42000000, v24
	v_mul_f32_e32 v28, 0x42000000, v28
	v_cvt_pk_fp8_f32 v0, v4, v5 op_sel:[0,0,1]
	v_mul_f32_e32 v4, 0x42000000, v11
	v_mul_f32_e32 v5, 0x42000000, v15
	v_cvt_pk_fp8_f32 v33, v38, v39 op_sel:[0,0,1]
	v_cvt_pk_fp8_f32 v34, v24, v28 op_sel:[0,0,1]
	v_cvt_pk_fp8_f32 v1, v4, v5 op_sel:[0,0,1]
	s_movk_i32 s12, 0x80
	ds_write2_b64 v44, v[66:67], v[34:35] offset1:8
	ds_write2_b64 v44, v[32:33], v[0:1] offset0:102 offset1:110
	s_cbranch_vccnz .LBB0_1328
	s_lshl_b64 s[8:9], s[8:9], 21
	s_add_u32 s8, s95, s8
	s_addc_u32 s9, s97, s9
	s_lshl_b32 s10, s2, 8
	s_waitcnt lgkmcnt(0)
	s_barrier
	s_ashr_i32 s11, s3, 31
	ds_read_b128 v[0:3], v80
	v_add_u32_e32 v4, s10, v71
	s_add_u32 s2, s8, s3
	v_ashrrev_i32_e32 v5, 31, v4
	s_addc_u32 s3, s9, s11
	v_lshlrev_b64 v[4:5], 10, v[4:5]
	v_lshl_add_u64 v[4:5], s[2:3], 0, v[4:5]
	v_lshl_add_u64 v[4:5], v[4:5], 0, v[172:173]
	s_waitcnt lgkmcnt(0)
	global_store_dwordx4 v[4:5], v[0:3], off sc1
	ds_read_b128 v[0:3], v81
	v_add_u32_e32 v4, s10, v72
	v_ashrrev_i32_e32 v5, 31, v4
	v_lshlrev_b64 v[4:5], 10, v[4:5]
	v_lshl_add_u64 v[4:5], s[2:3], 0, v[4:5]
	v_lshl_add_u64 v[4:5], v[4:5], 0, v[172:173]
	s_waitcnt lgkmcnt(0)
	global_store_dwordx4 v[4:5], v[0:3], off sc1
	ds_read_b128 v[0:3], v82
	v_add_u32_e32 v4, s10, v73
	v_ashrrev_i32_e32 v5, 31, v4
	v_lshlrev_b64 v[4:5], 10, v[4:5]
	v_lshl_add_u64 v[4:5], s[2:3], 0, v[4:5]
	v_lshl_add_u64 v[4:5], v[4:5], 0, v[172:173]
	s_waitcnt lgkmcnt(0)
	global_store_dwordx4 v[4:5], v[0:3], off sc1
	ds_read_b128 v[0:3], v83
	v_add_u32_e32 v4, s10, v74
	v_ashrrev_i32_e32 v5, 31, v4
	v_lshlrev_b64 v[4:5], 10, v[4:5]
	v_lshl_add_u64 v[4:5], s[2:3], 0, v[4:5]
	v_lshl_add_u64 v[4:5], v[4:5], 0, v[172:173]
	s_waitcnt lgkmcnt(0)
	global_store_dwordx4 v[4:5], v[0:3], off sc1
	ds_read_b128 v[0:3], v84
	v_add_u32_e32 v4, s10, v75
	v_ashrrev_i32_e32 v5, 31, v4
	v_lshlrev_b64 v[4:5], 10, v[4:5]
	v_lshl_add_u64 v[4:5], s[2:3], 0, v[4:5]
	v_lshl_add_u64 v[4:5], v[4:5], 0, v[172:173]
	s_waitcnt lgkmcnt(0)
	global_store_dwordx4 v[4:5], v[0:3], off sc1
	ds_read_b128 v[0:3], v85
	v_add_u32_e32 v4, s10, v76
	v_ashrrev_i32_e32 v5, 31, v4
	v_lshlrev_b64 v[4:5], 10, v[4:5]
	v_lshl_add_u64 v[4:5], s[2:3], 0, v[4:5]
	v_lshl_add_u64 v[4:5], v[4:5], 0, v[172:173]
	s_waitcnt lgkmcnt(0)
	global_store_dwordx4 v[4:5], v[0:3], off sc1
	ds_read_b128 v[0:3], v86
	v_add_u32_e32 v4, s10, v77
	v_ashrrev_i32_e32 v5, 31, v4
	v_lshlrev_b64 v[4:5], 10, v[4:5]
	v_lshl_add_u64 v[4:5], s[2:3], 0, v[4:5]
	v_lshl_add_u64 v[4:5], v[4:5], 0, v[172:173]
	s_waitcnt lgkmcnt(0)
	global_store_dwordx4 v[4:5], v[0:3], off sc1
	ds_read_b128 v[0:3], v87
	v_add_u32_e32 v4, s10, v78
	v_ashrrev_i32_e32 v5, 31, v4
	v_lshlrev_b64 v[4:5], 10, v[4:5]
	v_lshl_add_u64 v[4:5], s[2:3], 0, v[4:5]
	v_lshl_add_u64 v[4:5], v[4:5], 0, v[172:173]
	s_waitcnt lgkmcnt(0)
	global_store_dwordx4 v[4:5], v[0:3], off sc1
	s_barrier
	s_movk_i32 s8, 0xc0
	s_mov_b64 s[2:3], 0
	s_andn2_b64 vcc, exec, s[6:7]
	s_cbranch_vccnz .LBB0_1327

.LBB0_1384:
	v_readlane_b32 s0, v250, 4
	s_waitcnt lgkmcnt(0)
	s_mov_b32 s2, s100
	s_cmp_le_i32 s2, s1
	s_cselect_b64 s[2:3], -1, 0
	s_mov_b32 s12, s101
	s_cmp_lt_i32 s1, s12
	s_cselect_b64 s[4:5], -1, 0
	s_and_b64 s[4:5], s[2:3], s[4:5]
	s_mov_b64 s[2:3], -1
	s_and_b64 vcc, exec, s[4:5]
	s_cbranch_vccnz .LBB0_1386
	v_readlane_b32 s0, v255, 35
	s_add_i32 s1, s0, 11
	s_mov_b64 s[2:3], 0

.LBB0_1503:
	v_readlane_b32 s0, v250, 4
	s_waitcnt lgkmcnt(0)
	s_mov_b32 s2, s100
	s_cmp_le_i32 s2, s1
	s_cselect_b64 s[2:3], -1, 0
	s_mov_b32 s28, s101
	s_cmp_lt_i32 s1, s28
	s_cselect_b64 s[4:5], -1, 0
	s_and_b64 s[4:5], s[2:3], s[4:5]
	s_mov_b64 s[2:3], -1
	s_and_b64 vcc, exec, s[4:5]
	s_cbranch_vccnz .LBB0_1505
	v_readlane_b32 s0, v255, 35
	s_add_i32 s22, s0, 12
	s_mov_b64 s[2:3], 0

.Lpeel_gu:
	s_mov_b64 s[24:25], 0
	v_mov_b32_e32 v186, v166
	v_mov_b32_e32 v184, v170
	v_mov_b64_e32 v[178:179], v[168:169]
	v_mov_b64_e32 v[176:177], v[174:175]
	ds_read_b128 v[0:3], v191
	ds_read_b128 v[8:11], v191 offset:2048
	ds_read_b128 v[4:7], v193
	ds_read_b128 v[12:15], v193 offset:2048
	s_add_u32 s26, s22, 0x80
	s_addc_u32 s27, s23, 0
	s_and_b64 s[24:25], s[24:25], exec
	s_cselect_b32 s27, s19, s27
	s_cselect_b32 s26, s18, s26
	s_cselect_b32 s25, s17, s3
	s_cselect_b32 s24, s16, s2
	v_lshl_add_u64 v[16:17], s[22:23], 0, v[168:169]
	s_add_i32 m0, s44, 0xc000
	ds_read_b128 v[226:229], v190
	ds_read_b128 v[234:237], v190 offset:2048
	ds_read_b128 v[230:233], v192
	ds_read_b128 v[238:241], v192 offset:2048
	ds_read_b128 v[242:245], v190 offset:4096
	ds_read_b128 v[204:207], v190 offset:6144
	ds_read_b128 v[246:249], v192 offset:4096
	ds_read_b128 v[208:211], v192 offset:6144
	global_load_lds_dwordx4 v[16:17], off
	v_lshl_add_u64 v[16:17], s[22:23], 0, v[174:175]
	s_add_i32 m0, s44, 0xe000
	s_nop 0
	global_load_lds_dwordx4 v[16:17], off
	s_waitcnt lgkmcnt(8)
	s_barrier
	s_waitcnt lgkmcnt(0)
	s_setprio 1
	v_mfma_scale_f32_16x16x128_f8f6f4 v[156:159], v[0:7], v[226:233], 0, v189, v189 op_sel_hi:[0,0,0]
	v_mfma_scale_f32_16x16x128_f8f6f4 v[148:151], v[8:15], v[226:233], 0, v189, v189 op_sel_hi:[0,0,0]
	v_mfma_scale_f32_16x16x128_f8f6f4 v[140:143], v[0:7], v[234:241], 0, v189, v189 op_sel_hi:[0,0,0]
	v_mfma_scale_f32_16x16x128_f8f6f4 v[132:135], v[8:15], v[234:241], 0, v189, v189 op_sel_hi:[0,0,0]
	v_mfma_scale_f32_16x16x128_f8f6f4 v[124:127], v[0:7], v[242:249], 0, v189, v189 op_sel_hi:[0,0,0]
	v_mfma_scale_f32_16x16x128_f8f6f4 v[116:119], v[8:15], v[242:249], 0, v189, v189 op_sel_hi:[0,0,0]
	v_mfma_scale_f32_16x16x128_f8f6f4 v[108:111], v[0:7], v[204:211], 0, v189, v189 op_sel_hi:[0,0,0]
	v_mfma_scale_f32_16x16x128_f8f6f4 v[100:103], v[8:15], v[204:211], 0, v189, v189 op_sel_hi:[0,0,0]
	s_setprio 0
	s_barrier
	s_mov_b32 m0, s46
	v_lshl_add_u64 v[180:181], s[24:25], 0, v[160:161]
	ds_read_b128 v[16:19], v191 offset:16384
	ds_read_b128 v[24:27], v191 offset:18432
	ds_read_b128 v[20:23], v193 offset:16384
	ds_read_b128 v[28:31], v193 offset:18432
	global_load_lds_dwordx4 v[180:181], off
	v_lshl_add_u64 v[182:183], s[24:25], 0, v[162:163]
	s_mov_b32 m0, s47
	s_nop 0
	global_load_lds_dwordx4 v[182:183], off
	s_barrier
	s_waitcnt lgkmcnt(0)
	s_setprio 1
	v_mfma_scale_f32_16x16x128_f8f6f4 v[152:155], v[16:23], v[226:233], 0, v189, v189 op_sel_hi:[0,0,0]
	v_mfma_scale_f32_16x16x128_f8f6f4 v[144:147], v[24:31], v[226:233], 0, v189, v189 op_sel_hi:[0,0,0]
	v_mfma_scale_f32_16x16x128_f8f6f4 v[136:139], v[16:23], v[234:241], 0, v189, v189 op_sel_hi:[0,0,0]
	v_mfma_scale_f32_16x16x128_f8f6f4 v[128:131], v[24:31], v[234:241], 0, v189, v189 op_sel_hi:[0,0,0]
	v_mfma_scale_f32_16x16x128_f8f6f4 v[120:123], v[16:23], v[242:249], 0, v189, v189 op_sel_hi:[0,0,0]
	v_mfma_scale_f32_16x16x128_f8f6f4 v[112:115], v[24:31], v[242:249], 0, v189, v189 op_sel_hi:[0,0,0]
	v_mfma_scale_f32_16x16x128_f8f6f4 v[104:107], v[16:23], v[204:211], 0, v189, v189 op_sel_hi:[0,0,0]
	v_mfma_scale_f32_16x16x128_f8f6f4 v[96:99], v[24:31], v[204:211], 0, v189, v189 op_sel_hi:[0,0,0]
	s_setprio 0
	s_mov_b32 m0, s44
	s_barrier
	ds_read_b128 v[204:207], v190 offset:16384
	ds_read_b128 v[226:229], v190 offset:18432
	ds_read_b128 v[208:211], v192 offset:16384
	ds_read_b128 v[230:233], v192 offset:18432
	ds_read_b128 v[234:237], v190 offset:20480
	ds_read_b128 v[242:245], v190 offset:22528
	ds_read_b128 v[238:241], v192 offset:20480
	ds_read_b128 v[246:249], v192 offset:22528
	global_load_lds_dwordx4 v186, s[26:27]
	s_mov_b32 m0, s50
	v_mov_b32_e32 v187, v173
	global_load_lds_dwordx4 v184, s[26:27]
	s_barrier
	s_waitcnt lgkmcnt(0)
	v_mov_b32_e32 v185, v173
	v_lshl_add_u64 v[186:187], s[26:27], 0, v[186:187]
	v_lshl_add_u64 v[184:185], s[26:27], 0, v[184:185]
	s_setprio 1
	v_mfma_scale_f32_16x16x128_f8f6f4 v[92:95], v[0:7], v[204:211], 0, v189, v189 op_sel_hi:[0,0,0]
	v_mfma_scale_f32_16x16x128_f8f6f4 v[84:87], v[8:15], v[204:211], 0, v189, v189 op_sel_hi:[0,0,0]
	v_mfma_scale_f32_16x16x128_f8f6f4 v[76:79], v[0:7], v[226:233], 0, v189, v189 op_sel_hi:[0,0,0]
	v_mfma_scale_f32_16x16x128_f8f6f4 v[68:71], v[8:15], v[226:233], 0, v189, v189 op_sel_hi:[0,0,0]
	v_mfma_scale_f32_16x16x128_f8f6f4 v[60:63], v[0:7], v[234:241], 0, v189, v189 op_sel_hi:[0,0,0]
	v_mfma_scale_f32_16x16x128_f8f6f4 v[52:55], v[8:15], v[234:241], 0, v189, v189 op_sel_hi:[0,0,0]
	v_mfma_scale_f32_16x16x128_f8f6f4 v[44:47], v[0:7], v[242:249], 0, v189, v189 op_sel_hi:[0,0,0]
	v_mfma_scale_f32_16x16x128_f8f6f4 v[36:39], v[8:15], v[242:249], 0, v189, v189 op_sel_hi:[0,0,0]
	s_setprio 0
	s_barrier
	s_add_u32 s72, s24, 0x20000
	s_addc_u32 s73, s25, 0
	s_mov_b32 m0, s51
	v_lshl_add_u64 v[0:1], s[72:73], 0, v[160:161]
	global_load_lds_dwordx4 v[0:1], off
	v_lshl_add_u64 v[0:1], s[72:73], 0, v[162:163]
	s_mov_b32 m0, s56
	s_nop 0
	global_load_lds_dwordx4 v[0:1], off
	s_waitcnt vmcnt(6)
	s_barrier
	s_setprio 1
	v_mfma_scale_f32_16x16x128_f8f6f4 v[88:91], v[16:23], v[204:211], 0, v189, v189 op_sel_hi:[0,0,0]
	v_mfma_scale_f32_16x16x128_f8f6f4 v[80:83], v[24:31], v[204:211], 0, v189, v189 op_sel_hi:[0,0,0]
	v_mfma_scale_f32_16x16x128_f8f6f4 v[72:75], v[16:23], v[226:233], 0, v189, v189 op_sel_hi:[0,0,0]
	v_mfma_scale_f32_16x16x128_f8f6f4 v[64:67], v[24:31], v[226:233], 0, v189, v189 op_sel_hi:[0,0,0]
	v_mfma_scale_f32_16x16x128_f8f6f4 v[56:59], v[16:23], v[234:241], 0, v189, v189 op_sel_hi:[0,0,0]
	v_mfma_scale_f32_16x16x128_f8f6f4 v[48:51], v[24:31], v[234:241], 0, v189, v189 op_sel_hi:[0,0,0]
	v_mfma_scale_f32_16x16x128_f8f6f4 v[40:43], v[16:23], v[242:249], 0, v189, v189 op_sel_hi:[0,0,0]
	v_mfma_scale_f32_16x16x128_f8f6f4 v[32:35], v[24:31], v[242:249], 0, v189, v189 op_sel_hi:[0,0,0]
	s_setprio 0
	s_barrier
	ds_read_b128 v[0:3], v191 offset:32768
	ds_read_b128 v[8:11], v191 offset:34816
	ds_read_b128 v[4:7], v193 offset:32768
	ds_read_b128 v[12:15], v193 offset:34816
	s_mov_b32 m0, s65
	v_lshl_add_u64 v[178:179], s[26:27], 0, v[178:179]
	ds_read_b128 v[16:19], v190 offset:32768
	ds_read_b128 v[24:27], v190 offset:34816
	ds_read_b128 v[20:23], v192 offset:32768
	ds_read_b128 v[28:31], v192 offset:34816
	ds_read_b128 v[204:207], v190 offset:36864
	ds_read_b128 v[226:229], v190 offset:38912
	ds_read_b128 v[208:211], v192 offset:36864
	ds_read_b128 v[230:233], v192 offset:38912
	global_load_lds_dwordx4 v[178:179], off
	v_lshl_add_u64 v[176:177], s[26:27], 0, v[176:177]
	s_mov_b32 m0, s70
	s_nop 0
	global_load_lds_dwordx4 v[176:177], off
	s_waitcnt lgkmcnt(8)
	s_barrier
	s_waitcnt lgkmcnt(0)
	s_setprio 1
	v_mfma_scale_f32_16x16x128_f8f6f4 v[156:159], v[0:7], v[16:23], v[156:159], v189, v189 op_sel_hi:[0,0,0]
	v_mfma_scale_f32_16x16x128_f8f6f4 v[148:151], v[8:15], v[16:23], v[148:151], v189, v189 op_sel_hi:[0,0,0]
	v_mfma_scale_f32_16x16x128_f8f6f4 v[140:143], v[0:7], v[24:31], v[140:143], v189, v189 op_sel_hi:[0,0,0]
	v_mfma_scale_f32_16x16x128_f8f6f4 v[132:135], v[8:15], v[24:31], v[132:135], v189, v189 op_sel_hi:[0,0,0]
	v_mfma_scale_f32_16x16x128_f8f6f4 v[124:127], v[0:7], v[204:211], v[124:127], v189, v189 op_sel_hi:[0,0,0]
	v_mfma_scale_f32_16x16x128_f8f6f4 v[116:119], v[8:15], v[204:211], v[116:119], v189, v189 op_sel_hi:[0,0,0]
	v_mfma_scale_f32_16x16x128_f8f6f4 v[108:111], v[0:7], v[226:233], v[108:111], v189, v189 op_sel_hi:[0,0,0]
	v_mfma_scale_f32_16x16x128_f8f6f4 v[100:103], v[8:15], v[226:233], v[100:103], v189, v189 op_sel_hi:[0,0,0]
	s_setprio 0
	s_barrier
	s_mov_b32 m0, s71
	v_lshl_add_u64 v[176:177], v[180:181], 0, s[40:41]
	ds_read_b128 v[234:237], v191 offset:49152
	ds_read_b128 v[242:245], v191 offset:51200
	ds_read_b128 v[238:241], v193 offset:49152
	ds_read_b128 v[246:249], v193 offset:51200
	global_load_lds_dwordx4 v[176:177], off
	v_lshl_add_u64 v[176:177], v[182:183], 0, s[40:41]
	s_mov_b32 m0, s80
	s_nop 0
	global_load_lds_dwordx4 v[176:177], off
	s_barrier
	s_waitcnt lgkmcnt(0)
	s_setprio 1
	v_mfma_scale_f32_16x16x128_f8f6f4 v[152:155], v[234:241], v[16:23], v[152:155], v189, v189 op_sel_hi:[0,0,0]
	v_mfma_scale_f32_16x16x128_f8f6f4 v[144:147], v[242:249], v[16:23], v[144:147], v189, v189 op_sel_hi:[0,0,0]
	v_mfma_scale_f32_16x16x128_f8f6f4 v[136:139], v[234:241], v[24:31], v[136:139], v189, v189 op_sel_hi:[0,0,0]
	v_mfma_scale_f32_16x16x128_f8f6f4 v[128:131], v[242:249], v[24:31], v[128:131], v189, v189 op_sel_hi:[0,0,0]
	v_mfma_scale_f32_16x16x128_f8f6f4 v[120:123], v[234:241], v[204:211], v[120:123], v189, v189 op_sel_hi:[0,0,0]
	v_mfma_scale_f32_16x16x128_f8f6f4 v[112:115], v[242:249], v[204:211], v[112:115], v189, v189 op_sel_hi:[0,0,0]
	v_mfma_scale_f32_16x16x128_f8f6f4 v[104:107], v[234:241], v[226:233], v[104:107], v189, v189 op_sel_hi:[0,0,0]
	v_mfma_scale_f32_16x16x128_f8f6f4 v[96:99], v[242:249], v[226:233], v[96:99], v189, v189 op_sel_hi:[0,0,0]
	s_setprio 0
	s_mov_b32 m0, s81
	v_lshl_add_u64 v[186:187], v[186:187], 0, s[40:41]
	s_barrier
	ds_read_b128 v[16:19], v190 offset:49152
	ds_read_b128 v[24:27], v190 offset:51200
	ds_read_b128 v[20:23], v192 offset:49152
	ds_read_b128 v[28:31], v192 offset:51200
	ds_read_b128 v[176:179], v190 offset:53248
	ds_read_b128 v[204:207], v190 offset:55296
	ds_read_b128 v[180:183], v192 offset:53248
	ds_read_b128 v[208:211], v192 offset:55296
	global_load_lds_dwordx4 v[186:187], off
	v_lshl_add_u64 v[184:185], v[184:185], 0, s[40:41]
	s_mov_b32 m0, s82
	s_nop 0
	global_load_lds_dwordx4 v[184:185], off
	s_barrier
	s_waitcnt lgkmcnt(0)
	s_setprio 1
	v_mfma_scale_f32_16x16x128_f8f6f4 v[92:95], v[0:7], v[16:23], v[92:95], v189, v189 op_sel_hi:[0,0,0]
	v_mfma_scale_f32_16x16x128_f8f6f4 v[84:87], v[8:15], v[16:23], v[84:87], v189, v189 op_sel_hi:[0,0,0]
	v_mfma_scale_f32_16x16x128_f8f6f4 v[76:79], v[0:7], v[24:31], v[76:79], v189, v189 op_sel_hi:[0,0,0]
	v_mfma_scale_f32_16x16x128_f8f6f4 v[68:71], v[8:15], v[24:31], v[68:71], v189, v189 op_sel_hi:[0,0,0]
	v_mfma_scale_f32_16x16x128_f8f6f4 v[60:63], v[0:7], v[176:183], v[60:63], v189, v189 op_sel_hi:[0,0,0]
	v_mfma_scale_f32_16x16x128_f8f6f4 v[52:55], v[8:15], v[176:183], v[52:55], v189, v189 op_sel_hi:[0,0,0]
	v_mfma_scale_f32_16x16x128_f8f6f4 v[44:47], v[0:7], v[204:211], v[44:47], v189, v189 op_sel_hi:[0,0,0]
	v_mfma_scale_f32_16x16x128_f8f6f4 v[36:39], v[8:15], v[204:211], v[36:39], v189, v189 op_sel_hi:[0,0,0]
	s_setprio 0
	s_barrier
	s_add_u32 s24, s24, 0x20080
	s_addc_u32 s25, s25, 0
	s_mov_b32 m0, s83
	v_lshl_add_u64 v[0:1], s[24:25], 0, v[160:161]
	global_load_lds_dwordx4 v[0:1], off
	v_lshl_add_u64 v[0:1], s[24:25], 0, v[162:163]
	s_mov_b32 m0, s85
	s_nop 0
	global_load_lds_dwordx4 v[0:1], off
	s_waitcnt vmcnt(6)
	s_barrier
	s_setprio 1
	v_mfma_scale_f32_16x16x128_f8f6f4 v[88:91], v[234:241], v[16:23], v[88:91], v189, v189 op_sel_hi:[0,0,0]
	v_mfma_scale_f32_16x16x128_f8f6f4 v[80:83], v[242:249], v[16:23], v[80:83], v189, v189 op_sel_hi:[0,0,0]
	v_mfma_scale_f32_16x16x128_f8f6f4 v[72:75], v[234:241], v[24:31], v[72:75], v189, v189 op_sel_hi:[0,0,0]
	v_mfma_scale_f32_16x16x128_f8f6f4 v[64:67], v[242:249], v[24:31], v[64:67], v189, v189 op_sel_hi:[0,0,0]
	v_mfma_scale_f32_16x16x128_f8f6f4 v[56:59], v[234:241], v[176:183], v[56:59], v189, v189 op_sel_hi:[0,0,0]
	v_mfma_scale_f32_16x16x128_f8f6f4 v[48:51], v[242:249], v[176:183], v[48:51], v189, v189 op_sel_hi:[0,0,0]
	v_mfma_scale_f32_16x16x128_f8f6f4 v[40:43], v[234:241], v[204:211], v[40:43], v189, v189 op_sel_hi:[0,0,0]
	v_mfma_scale_f32_16x16x128_f8f6f4 v[32:35], v[242:249], v[204:211], v[32:35], v189, v189 op_sel_hi:[0,0,0]
	s_setprio 0
	s_add_i32 s64, s64, 2
	s_add_u32 s22, s22, 0x100
	s_addc_u32 s23, s23, 0
	s_add_u32 s2, s2, 0x100
	s_addc_u32 s3, s3, 0
	s_cmp_gt_u32 s64, 5
	s_barrier
	s_branch .LBB0_1556

.LBB0_1555:
	ds_read_b128 v[0:3], v191
	ds_read_b128 v[8:11], v191 offset:2048
	ds_read_b128 v[4:7], v193
	ds_read_b128 v[12:15], v193 offset:2048
	s_add_u32 s26, s22, 0x80
	s_addc_u32 s27, s23, 0
	s_and_b64 s[24:25], s[24:25], exec
	s_cselect_b32 s27, s19, s27
	s_cselect_b32 s26, s18, s26
	s_cselect_b32 s25, s17, s3
	s_cselect_b32 s24, s16, s2
	v_lshl_add_u64 v[16:17], s[22:23], 0, v[168:169]
	s_add_i32 m0, s44, 0xc000
	ds_read_b128 v[226:229], v190
	ds_read_b128 v[234:237], v190 offset:2048
	ds_read_b128 v[230:233], v192
	ds_read_b128 v[238:241], v192 offset:2048
	ds_read_b128 v[242:245], v190 offset:4096
	ds_read_b128 v[204:207], v190 offset:6144
	ds_read_b128 v[246:249], v192 offset:4096
	ds_read_b128 v[208:211], v192 offset:6144
	global_load_lds_dwordx4 v[16:17], off
	v_lshl_add_u64 v[16:17], s[22:23], 0, v[174:175]
	s_add_i32 m0, s44, 0xe000
	s_nop 0
	global_load_lds_dwordx4 v[16:17], off
	s_waitcnt lgkmcnt(8)
	s_barrier
	s_waitcnt lgkmcnt(0)
	s_setprio 1
	v_mfma_scale_f32_16x16x128_f8f6f4 v[156:159], v[0:7], v[226:233], v[156:159], v189, v189 op_sel_hi:[0,0,0]
	v_mfma_scale_f32_16x16x128_f8f6f4 v[148:151], v[8:15], v[226:233], v[148:151], v189, v189 op_sel_hi:[0,0,0]
	v_mfma_scale_f32_16x16x128_f8f6f4 v[140:143], v[0:7], v[234:241], v[140:143], v189, v189 op_sel_hi:[0,0,0]
	v_mfma_scale_f32_16x16x128_f8f6f4 v[132:135], v[8:15], v[234:241], v[132:135], v189, v189 op_sel_hi:[0,0,0]
	v_mfma_scale_f32_16x16x128_f8f6f4 v[124:127], v[0:7], v[242:249], v[124:127], v189, v189 op_sel_hi:[0,0,0]
	v_mfma_scale_f32_16x16x128_f8f6f4 v[116:119], v[8:15], v[242:249], v[116:119], v189, v189 op_sel_hi:[0,0,0]
	v_mfma_scale_f32_16x16x128_f8f6f4 v[108:111], v[0:7], v[204:211], v[108:111], v189, v189 op_sel_hi:[0,0,0]
	v_mfma_scale_f32_16x16x128_f8f6f4 v[100:103], v[8:15], v[204:211], v[100:103], v189, v189 op_sel_hi:[0,0,0]
	s_setprio 0
	s_barrier
	s_mov_b32 m0, s46
	v_lshl_add_u64 v[180:181], s[24:25], 0, v[160:161]
	ds_read_b128 v[16:19], v191 offset:16384
	ds_read_b128 v[24:27], v191 offset:18432
	ds_read_b128 v[20:23], v193 offset:16384
	ds_read_b128 v[28:31], v193 offset:18432
	global_load_lds_dwordx4 v[180:181], off
	v_lshl_add_u64 v[182:183], s[24:25], 0, v[162:163]
	s_mov_b32 m0, s47
	s_nop 0
	global_load_lds_dwordx4 v[182:183], off
	s_barrier
	s_waitcnt lgkmcnt(0)
	s_setprio 1
	v_mfma_scale_f32_16x16x128_f8f6f4 v[152:155], v[16:23], v[226:233], v[152:155], v189, v189 op_sel_hi:[0,0,0]
	v_mfma_scale_f32_16x16x128_f8f6f4 v[144:147], v[24:31], v[226:233], v[144:147], v189, v189 op_sel_hi:[0,0,0]
	v_mfma_scale_f32_16x16x128_f8f6f4 v[136:139], v[16:23], v[234:241], v[136:139], v189, v189 op_sel_hi:[0,0,0]
	v_mfma_scale_f32_16x16x128_f8f6f4 v[128:131], v[24:31], v[234:241], v[128:131], v189, v189 op_sel_hi:[0,0,0]
	v_mfma_scale_f32_16x16x128_f8f6f4 v[120:123], v[16:23], v[242:249], v[120:123], v189, v189 op_sel_hi:[0,0,0]
	v_mfma_scale_f32_16x16x128_f8f6f4 v[112:115], v[24:31], v[242:249], v[112:115], v189, v189 op_sel_hi:[0,0,0]
	v_mfma_scale_f32_16x16x128_f8f6f4 v[104:107], v[16:23], v[204:211], v[104:107], v189, v189 op_sel_hi:[0,0,0]
	v_mfma_scale_f32_16x16x128_f8f6f4 v[96:99], v[24:31], v[204:211], v[96:99], v189, v189 op_sel_hi:[0,0,0]
	s_setprio 0
	s_mov_b32 m0, s44
	s_barrier
	ds_read_b128 v[204:207], v190 offset:16384
	ds_read_b128 v[226:229], v190 offset:18432
	ds_read_b128 v[208:211], v192 offset:16384
	ds_read_b128 v[230:233], v192 offset:18432
	ds_read_b128 v[234:237], v190 offset:20480
	ds_read_b128 v[242:245], v190 offset:22528
	ds_read_b128 v[238:241], v192 offset:20480
	ds_read_b128 v[246:249], v192 offset:22528
	global_load_lds_dwordx4 v186, s[26:27]
	s_mov_b32 m0, s50
	v_mov_b32_e32 v187, v173
	global_load_lds_dwordx4 v184, s[26:27]
	s_barrier
	s_waitcnt lgkmcnt(0)
	v_mov_b32_e32 v185, v173
	v_lshl_add_u64 v[186:187], s[26:27], 0, v[186:187]
	v_lshl_add_u64 v[184:185], s[26:27], 0, v[184:185]
	s_setprio 1
	v_mfma_scale_f32_16x16x128_f8f6f4 v[92:95], v[0:7], v[204:211], v[92:95], v189, v189 op_sel_hi:[0,0,0]
	v_mfma_scale_f32_16x16x128_f8f6f4 v[84:87], v[8:15], v[204:211], v[84:87], v189, v189 op_sel_hi:[0,0,0]
	v_mfma_scale_f32_16x16x128_f8f6f4 v[76:79], v[0:7], v[226:233], v[76:79], v189, v189 op_sel_hi:[0,0,0]
	v_mfma_scale_f32_16x16x128_f8f6f4 v[68:71], v[8:15], v[226:233], v[68:71], v189, v189 op_sel_hi:[0,0,0]
	v_mfma_scale_f32_16x16x128_f8f6f4 v[60:63], v[0:7], v[234:241], v[60:63], v189, v189 op_sel_hi:[0,0,0]
	v_mfma_scale_f32_16x16x128_f8f6f4 v[52:55], v[8:15], v[234:241], v[52:55], v189, v189 op_sel_hi:[0,0,0]
	v_mfma_scale_f32_16x16x128_f8f6f4 v[44:47], v[0:7], v[242:249], v[44:47], v189, v189 op_sel_hi:[0,0,0]
	v_mfma_scale_f32_16x16x128_f8f6f4 v[36:39], v[8:15], v[242:249], v[36:39], v189, v189 op_sel_hi:[0,0,0]
	s_setprio 0
	s_barrier
	s_add_u32 s72, s24, 0x20000
	s_addc_u32 s73, s25, 0
	s_mov_b32 m0, s51
	v_lshl_add_u64 v[0:1], s[72:73], 0, v[160:161]
	global_load_lds_dwordx4 v[0:1], off
	v_lshl_add_u64 v[0:1], s[72:73], 0, v[162:163]
	s_mov_b32 m0, s56
	s_nop 0
	global_load_lds_dwordx4 v[0:1], off
	s_waitcnt vmcnt(6)
	s_barrier
	s_setprio 1
	v_mfma_scale_f32_16x16x128_f8f6f4 v[88:91], v[16:23], v[204:211], v[88:91], v189, v189 op_sel_hi:[0,0,0]
	v_mfma_scale_f32_16x16x128_f8f6f4 v[80:83], v[24:31], v[204:211], v[80:83], v189, v189 op_sel_hi:[0,0,0]
	v_mfma_scale_f32_16x16x128_f8f6f4 v[72:75], v[16:23], v[226:233], v[72:75], v189, v189 op_sel_hi:[0,0,0]
	v_mfma_scale_f32_16x16x128_f8f6f4 v[64:67], v[24:31], v[226:233], v[64:67], v189, v189 op_sel_hi:[0,0,0]
	v_mfma_scale_f32_16x16x128_f8f6f4 v[56:59], v[16:23], v[234:241], v[56:59], v189, v189 op_sel_hi:[0,0,0]
	v_mfma_scale_f32_16x16x128_f8f6f4 v[48:51], v[24:31], v[234:241], v[48:51], v189, v189 op_sel_hi:[0,0,0]
	v_mfma_scale_f32_16x16x128_f8f6f4 v[40:43], v[16:23], v[242:249], v[40:43], v189, v189 op_sel_hi:[0,0,0]
	v_mfma_scale_f32_16x16x128_f8f6f4 v[32:35], v[24:31], v[242:249], v[32:35], v189, v189 op_sel_hi:[0,0,0]
	s_setprio 0
	s_barrier
	ds_read_b128 v[0:3], v191 offset:32768
	ds_read_b128 v[8:11], v191 offset:34816
	ds_read_b128 v[4:7], v193 offset:32768
	ds_read_b128 v[12:15], v193 offset:34816
	s_mov_b32 m0, s65
	v_lshl_add_u64 v[178:179], s[26:27], 0, v[178:179]
	ds_read_b128 v[16:19], v190 offset:32768
	ds_read_b128 v[24:27], v190 offset:34816
	ds_read_b128 v[20:23], v192 offset:32768
	ds_read_b128 v[28:31], v192 offset:34816
	ds_read_b128 v[204:207], v190 offset:36864
	ds_read_b128 v[226:229], v190 offset:38912
	ds_read_b128 v[208:211], v192 offset:36864
	ds_read_b128 v[230:233], v192 offset:38912
	global_load_lds_dwordx4 v[178:179], off
	v_lshl_add_u64 v[176:177], s[26:27], 0, v[176:177]
	s_mov_b32 m0, s70
	s_nop 0
	global_load_lds_dwordx4 v[176:177], off
	s_waitcnt lgkmcnt(8)
	s_barrier
	s_waitcnt lgkmcnt(0)
	s_setprio 1
	v_mfma_scale_f32_16x16x128_f8f6f4 v[156:159], v[0:7], v[16:23], v[156:159], v189, v189 op_sel_hi:[0,0,0]
	v_mfma_scale_f32_16x16x128_f8f6f4 v[148:151], v[8:15], v[16:23], v[148:151], v189, v189 op_sel_hi:[0,0,0]
	v_mfma_scale_f32_16x16x128_f8f6f4 v[140:143], v[0:7], v[24:31], v[140:143], v189, v189 op_sel_hi:[0,0,0]
	v_mfma_scale_f32_16x16x128_f8f6f4 v[132:135], v[8:15], v[24:31], v[132:135], v189, v189 op_sel_hi:[0,0,0]
	v_mfma_scale_f32_16x16x128_f8f6f4 v[124:127], v[0:7], v[204:211], v[124:127], v189, v189 op_sel_hi:[0,0,0]
	v_mfma_scale_f32_16x16x128_f8f6f4 v[116:119], v[8:15], v[204:211], v[116:119], v189, v189 op_sel_hi:[0,0,0]
	v_mfma_scale_f32_16x16x128_f8f6f4 v[108:111], v[0:7], v[226:233], v[108:111], v189, v189 op_sel_hi:[0,0,0]
	v_mfma_scale_f32_16x16x128_f8f6f4 v[100:103], v[8:15], v[226:233], v[100:103], v189, v189 op_sel_hi:[0,0,0]
	s_setprio 0
	s_barrier
	s_mov_b32 m0, s71
	v_lshl_add_u64 v[176:177], v[180:181], 0, s[40:41]
	ds_read_b128 v[234:237], v191 offset:49152
	ds_read_b128 v[242:245], v191 offset:51200
	ds_read_b128 v[238:241], v193 offset:49152
	ds_read_b128 v[246:249], v193 offset:51200
	global_load_lds_dwordx4 v[176:177], off
	v_lshl_add_u64 v[176:177], v[182:183], 0, s[40:41]
	s_mov_b32 m0, s80
	s_nop 0
	global_load_lds_dwordx4 v[176:177], off
	s_barrier
	s_waitcnt lgkmcnt(0)
	s_setprio 1
	v_mfma_scale_f32_16x16x128_f8f6f4 v[152:155], v[234:241], v[16:23], v[152:155], v189, v189 op_sel_hi:[0,0,0]
	v_mfma_scale_f32_16x16x128_f8f6f4 v[144:147], v[242:249], v[16:23], v[144:147], v189, v189 op_sel_hi:[0,0,0]
	v_mfma_scale_f32_16x16x128_f8f6f4 v[136:139], v[234:241], v[24:31], v[136:139], v189, v189 op_sel_hi:[0,0,0]
	v_mfma_scale_f32_16x16x128_f8f6f4 v[128:131], v[242:249], v[24:31], v[128:131], v189, v189 op_sel_hi:[0,0,0]
	v_mfma_scale_f32_16x16x128_f8f6f4 v[120:123], v[234:241], v[204:211], v[120:123], v189, v189 op_sel_hi:[0,0,0]
	v_mfma_scale_f32_16x16x128_f8f6f4 v[112:115], v[242:249], v[204:211], v[112:115], v189, v189 op_sel_hi:[0,0,0]
	v_mfma_scale_f32_16x16x128_f8f6f4 v[104:107], v[234:241], v[226:233], v[104:107], v189, v189 op_sel_hi:[0,0,0]
	v_mfma_scale_f32_16x16x128_f8f6f4 v[96:99], v[242:249], v[226:233], v[96:99], v189, v189 op_sel_hi:[0,0,0]
	s_setprio 0
	s_mov_b32 m0, s81
	v_lshl_add_u64 v[186:187], v[186:187], 0, s[40:41]
	s_barrier
	ds_read_b128 v[16:19], v190 offset:49152
	ds_read_b128 v[24:27], v190 offset:51200
	ds_read_b128 v[20:23], v192 offset:49152
	ds_read_b128 v[28:31], v192 offset:51200
	ds_read_b128 v[176:179], v190 offset:53248
	ds_read_b128 v[204:207], v190 offset:55296
	ds_read_b128 v[180:183], v192 offset:53248
	ds_read_b128 v[208:211], v192 offset:55296
	global_load_lds_dwordx4 v[186:187], off
	v_lshl_add_u64 v[184:185], v[184:185], 0, s[40:41]
	s_mov_b32 m0, s82
	s_nop 0
	global_load_lds_dwordx4 v[184:185], off
	s_barrier
	s_waitcnt lgkmcnt(0)
	s_setprio 1
	v_mfma_scale_f32_16x16x128_f8f6f4 v[92:95], v[0:7], v[16:23], v[92:95], v189, v189 op_sel_hi:[0,0,0]
	v_mfma_scale_f32_16x16x128_f8f6f4 v[84:87], v[8:15], v[16:23], v[84:87], v189, v189 op_sel_hi:[0,0,0]
	v_mfma_scale_f32_16x16x128_f8f6f4 v[76:79], v[0:7], v[24:31], v[76:79], v189, v189 op_sel_hi:[0,0,0]
	v_mfma_scale_f32_16x16x128_f8f6f4 v[68:71], v[8:15], v[24:31], v[68:71], v189, v189 op_sel_hi:[0,0,0]
	v_mfma_scale_f32_16x16x128_f8f6f4 v[60:63], v[0:7], v[176:183], v[60:63], v189, v189 op_sel_hi:[0,0,0]
	v_mfma_scale_f32_16x16x128_f8f6f4 v[52:55], v[8:15], v[176:183], v[52:55], v189, v189 op_sel_hi:[0,0,0]
	v_mfma_scale_f32_16x16x128_f8f6f4 v[44:47], v[0:7], v[204:211], v[44:47], v189, v189 op_sel_hi:[0,0,0]
	v_mfma_scale_f32_16x16x128_f8f6f4 v[36:39], v[8:15], v[204:211], v[36:39], v189, v189 op_sel_hi:[0,0,0]
	s_setprio 0
	s_barrier
	s_add_u32 s24, s24, 0x20080
	s_addc_u32 s25, s25, 0
	s_mov_b32 m0, s83
	v_lshl_add_u64 v[0:1], s[24:25], 0, v[160:161]
	global_load_lds_dwordx4 v[0:1], off
	v_lshl_add_u64 v[0:1], s[24:25], 0, v[162:163]
	s_mov_b32 m0, s85
	s_nop 0
	global_load_lds_dwordx4 v[0:1], off
	s_waitcnt vmcnt(6)
	s_barrier
	s_setprio 1
	v_mfma_scale_f32_16x16x128_f8f6f4 v[88:91], v[234:241], v[16:23], v[88:91], v189, v189 op_sel_hi:[0,0,0]
	v_mfma_scale_f32_16x16x128_f8f6f4 v[80:83], v[242:249], v[16:23], v[80:83], v189, v189 op_sel_hi:[0,0,0]
	v_mfma_scale_f32_16x16x128_f8f6f4 v[72:75], v[234:241], v[24:31], v[72:75], v189, v189 op_sel_hi:[0,0,0]
	v_mfma_scale_f32_16x16x128_f8f6f4 v[64:67], v[242:249], v[24:31], v[64:67], v189, v189 op_sel_hi:[0,0,0]
	v_mfma_scale_f32_16x16x128_f8f6f4 v[56:59], v[234:241], v[176:183], v[56:59], v189, v189 op_sel_hi:[0,0,0]
	v_mfma_scale_f32_16x16x128_f8f6f4 v[48:51], v[242:249], v[176:183], v[48:51], v189, v189 op_sel_hi:[0,0,0]
	v_mfma_scale_f32_16x16x128_f8f6f4 v[40:43], v[234:241], v[204:211], v[40:43], v189, v189 op_sel_hi:[0,0,0]
	v_mfma_scale_f32_16x16x128_f8f6f4 v[32:35], v[242:249], v[204:211], v[32:35], v189, v189 op_sel_hi:[0,0,0]
	s_setprio 0
	s_add_i32 s64, s64, 2
	s_add_u32 s22, s22, 0x100
	s_addc_u32 s23, s23, 0
	s_add_u32 s2, s2, 0x100
	s_addc_u32 s3, s3, 0
	s_cmp_gt_u32 s64, 5
	s_barrier
	s_cbranch_scc1 .LBB0_1540

.LBB0_1620:
	v_readlane_b32 s0, v250, 4
	s_waitcnt lgkmcnt(0)
	s_mov_b32 s2, s100
	s_cmp_le_i32 s2, s22
	s_cselect_b64 s[2:3], -1, 0
	s_mov_b32 s1, s101
	s_cmp_lt_i32 s22, s1
	s_cselect_b64 s[4:5], -1, 0
	s_and_b64 s[2:3], s[2:3], s[4:5]
	s_andn2_b64 vcc, exec, s[2:3]
	s_cbranch_vccz .LBB0_1621
	s_getpc_b64 s[98:99]

.Lpeel_dn:
	s_mov_b64 s[24:25], 0
	v_mov_b64_e32 v[176:177], v[170:171]
	v_mov_b64_e32 v[178:179], v[166:167]
	v_mov_b32_e32 v184, v174
	v_mov_b32_e32 v172, v168
	ds_read_b128 v[0:3], v190
	ds_read_b128 v[8:11], v190 offset:2048
	ds_read_b128 v[4:7], v192
	ds_read_b128 v[12:15], v192 offset:2048
	s_add_u32 s26, s22, 0x80
	s_addc_u32 s27, s23, 0
	s_and_b64 s[24:25], s[24:25], exec
	s_cselect_b32 s27, s19, s27
	s_cselect_b32 s26, s18, s26
	s_cselect_b32 s25, s17, s83
	s_cselect_b32 s24, s16, s7
	v_lshl_add_u64 v[16:17], s[22:23], 0, v[166:167]
	s_add_i32 m0, s13, 0xc000
	ds_read_b128 v[204:207], v189
	ds_read_b128 v[216:219], v189 offset:2048
	ds_read_b128 v[208:211], v191
	ds_read_b128 v[220:223], v191 offset:2048
	ds_read_b128 v[224:227], v189 offset:4096
	ds_read_b128 v[232:235], v189 offset:6144
	ds_read_b128 v[228:231], v191 offset:4096
	ds_read_b128 v[236:239], v191 offset:6144
	global_load_lds_dwordx4 v[16:17], off
	v_lshl_add_u64 v[16:17], s[22:23], 0, v[170:171]
	s_add_i32 m0, s13, 0xe000
	s_nop 0
	global_load_lds_dwordx4 v[16:17], off
	s_waitcnt lgkmcnt(8)
	s_barrier
	s_waitcnt lgkmcnt(0)
	s_setprio 1
	v_mfma_scale_f32_16x16x128_f8f6f4 v[156:159], v[0:7], v[204:211], 0, v188, v188 op_sel_hi:[0,0,0]
	v_mfma_scale_f32_16x16x128_f8f6f4 v[152:155], v[8:15], v[204:211], 0, v188, v188 op_sel_hi:[0,0,0]
	v_mfma_scale_f32_16x16x128_f8f6f4 v[148:151], v[0:7], v[216:223], 0, v188, v188 op_sel_hi:[0,0,0]
	v_mfma_scale_f32_16x16x128_f8f6f4 v[144:147], v[8:15], v[216:223], 0, v188, v188 op_sel_hi:[0,0,0]
	v_mfma_scale_f32_16x16x128_f8f6f4 v[140:143], v[0:7], v[224:231], 0, v188, v188 op_sel_hi:[0,0,0]
	v_mfma_scale_f32_16x16x128_f8f6f4 v[136:139], v[8:15], v[224:231], 0, v188, v188 op_sel_hi:[0,0,0]
	v_mfma_scale_f32_16x16x128_f8f6f4 v[132:135], v[0:7], v[232:239], 0, v188, v188 op_sel_hi:[0,0,0]
	v_mfma_scale_f32_16x16x128_f8f6f4 v[128:131], v[8:15], v[232:239], 0, v188, v188 op_sel_hi:[0,0,0]
	s_setprio 0
	s_barrier
	s_mov_b32 m0, s15
	v_lshl_add_u64 v[180:181], s[24:25], 0, v[162:163]
	ds_read_b128 v[16:19], v190 offset:16384
	ds_read_b128 v[24:27], v190 offset:18432
	ds_read_b128 v[20:23], v192 offset:16384
	ds_read_b128 v[28:31], v192 offset:18432
	global_load_lds_dwordx4 v[180:181], off
	v_lshl_add_u64 v[182:183], s[24:25], 0, v[164:165]
	s_mov_b32 m0, s31
	s_nop 0
	global_load_lds_dwordx4 v[182:183], off
	s_barrier
	s_waitcnt lgkmcnt(0)
	s_setprio 1
	v_mfma_scale_f32_16x16x128_f8f6f4 v[100:103], v[16:23], v[204:211], 0, v188, v188 op_sel_hi:[0,0,0]
	v_mfma_scale_f32_16x16x128_f8f6f4 v[96:99], v[24:31], v[204:211], 0, v188, v188 op_sel_hi:[0,0,0]
	v_mfma_scale_f32_16x16x128_f8f6f4 v[84:87], v[16:23], v[216:223], 0, v188, v188 op_sel_hi:[0,0,0]
	v_mfma_scale_f32_16x16x128_f8f6f4 v[80:83], v[24:31], v[216:223], 0, v188, v188 op_sel_hi:[0,0,0]
	v_mfma_scale_f32_16x16x128_f8f6f4 v[76:79], v[16:23], v[224:231], 0, v188, v188 op_sel_hi:[0,0,0]
	v_mfma_scale_f32_16x16x128_f8f6f4 v[72:75], v[24:31], v[224:231], 0, v188, v188 op_sel_hi:[0,0,0]
	v_mfma_scale_f32_16x16x128_f8f6f4 v[68:71], v[16:23], v[232:239], 0, v188, v188 op_sel_hi:[0,0,0]
	v_mfma_scale_f32_16x16x128_f8f6f4 v[64:67], v[24:31], v[232:239], 0, v188, v188 op_sel_hi:[0,0,0]
	s_setprio 0
	s_mov_b32 m0, s13
	s_barrier
	ds_read_b128 v[204:207], v189 offset:16384
	ds_read_b128 v[216:219], v189 offset:18432
	ds_read_b128 v[208:211], v191 offset:16384
	ds_read_b128 v[220:223], v191 offset:18432
	ds_read_b128 v[224:227], v189 offset:20480
	ds_read_b128 v[232:235], v189 offset:22528
	ds_read_b128 v[228:231], v191 offset:20480
	ds_read_b128 v[236:239], v191 offset:22528
	global_load_lds_dwordx4 v172, s[26:27]
	s_mov_b32 m0, s44
	v_mov_b32_e32 v185, v173
	global_load_lds_dwordx4 v184, s[26:27]
	s_barrier
	s_waitcnt lgkmcnt(0)
	v_lshl_add_u64 v[186:187], s[26:27], 0, v[172:173]
	v_lshl_add_u64 v[184:185], s[26:27], 0, v[184:185]
	s_setprio 1
	v_mfma_scale_f32_16x16x128_f8f6f4 v[124:127], v[0:7], v[204:211], 0, v188, v188 op_sel_hi:[0,0,0]
	v_mfma_scale_f32_16x16x128_f8f6f4 v[120:123], v[8:15], v[204:211], 0, v188, v188 op_sel_hi:[0,0,0]
	v_mfma_scale_f32_16x16x128_f8f6f4 v[116:119], v[0:7], v[216:223], 0, v188, v188 op_sel_hi:[0,0,0]
	v_mfma_scale_f32_16x16x128_f8f6f4 v[112:115], v[8:15], v[216:223], 0, v188, v188 op_sel_hi:[0,0,0]
	v_mfma_scale_f32_16x16x128_f8f6f4 v[108:111], v[0:7], v[224:231], 0, v188, v188 op_sel_hi:[0,0,0]
	v_mfma_scale_f32_16x16x128_f8f6f4 v[104:107], v[8:15], v[224:231], 0, v188, v188 op_sel_hi:[0,0,0]
	v_mfma_scale_f32_16x16x128_f8f6f4 v[92:95], v[0:7], v[232:239], 0, v188, v188 op_sel_hi:[0,0,0]
	v_mfma_scale_f32_16x16x128_f8f6f4 v[88:91], v[8:15], v[232:239], 0, v188, v188 op_sel_hi:[0,0,0]
	s_setprio 0
	s_barrier
	s_add_u32 s90, s24, 0x20000
	s_addc_u32 s91, s25, 0
	s_mov_b32 m0, s46
	v_lshl_add_u64 v[0:1], s[90:91], 0, v[162:163]
	global_load_lds_dwordx4 v[0:1], off
	v_lshl_add_u64 v[0:1], s[90:91], 0, v[164:165]
	s_mov_b32 m0, s47
	s_nop 0
	global_load_lds_dwordx4 v[0:1], off
	s_waitcnt vmcnt(6)
	s_barrier
	s_setprio 1
	v_mfma_scale_f32_16x16x128_f8f6f4 v[60:63], v[16:23], v[204:211], 0, v188, v188 op_sel_hi:[0,0,0]
	v_mfma_scale_f32_16x16x128_f8f6f4 v[56:59], v[24:31], v[204:211], 0, v188, v188 op_sel_hi:[0,0,0]
	v_mfma_scale_f32_16x16x128_f8f6f4 v[52:55], v[16:23], v[216:223], 0, v188, v188 op_sel_hi:[0,0,0]
	v_mfma_scale_f32_16x16x128_f8f6f4 v[48:51], v[24:31], v[216:223], 0, v188, v188 op_sel_hi:[0,0,0]
	v_mfma_scale_f32_16x16x128_f8f6f4 v[44:47], v[16:23], v[224:231], 0, v188, v188 op_sel_hi:[0,0,0]
	v_mfma_scale_f32_16x16x128_f8f6f4 v[40:43], v[24:31], v[224:231], 0, v188, v188 op_sel_hi:[0,0,0]
	v_mfma_scale_f32_16x16x128_f8f6f4 v[36:39], v[16:23], v[232:239], 0, v188, v188 op_sel_hi:[0,0,0]
	v_mfma_scale_f32_16x16x128_f8f6f4 v[32:35], v[24:31], v[232:239], 0, v188, v188 op_sel_hi:[0,0,0]
	s_setprio 0
	s_barrier
	ds_read_b128 v[0:3], v190 offset:32768
	ds_read_b128 v[8:11], v190 offset:34816
	ds_read_b128 v[4:7], v192 offset:32768
	ds_read_b128 v[12:15], v192 offset:34816
	s_mov_b32 m0, s50
	v_lshl_add_u64 v[178:179], s[26:27], 0, v[178:179]
	ds_read_b128 v[16:19], v189 offset:32768
	ds_read_b128 v[24:27], v189 offset:34816
	ds_read_b128 v[20:23], v191 offset:32768
	ds_read_b128 v[28:31], v191 offset:34816
	ds_read_b128 v[204:207], v189 offset:36864
	ds_read_b128 v[216:219], v189 offset:38912
	ds_read_b128 v[208:211], v191 offset:36864
	ds_read_b128 v[220:223], v191 offset:38912
	global_load_lds_dwordx4 v[178:179], off
	v_lshl_add_u64 v[176:177], s[26:27], 0, v[176:177]
	s_mov_b32 m0, s51
	s_nop 0
	global_load_lds_dwordx4 v[176:177], off
	s_waitcnt lgkmcnt(8)
	s_barrier
	s_waitcnt lgkmcnt(0)
	s_setprio 1
	v_mfma_scale_f32_16x16x128_f8f6f4 v[156:159], v[0:7], v[16:23], v[156:159], v188, v188 op_sel_hi:[0,0,0]
	v_mfma_scale_f32_16x16x128_f8f6f4 v[152:155], v[8:15], v[16:23], v[152:155], v188, v188 op_sel_hi:[0,0,0]
	v_mfma_scale_f32_16x16x128_f8f6f4 v[148:151], v[0:7], v[24:31], v[148:151], v188, v188 op_sel_hi:[0,0,0]
	v_mfma_scale_f32_16x16x128_f8f6f4 v[144:147], v[8:15], v[24:31], v[144:147], v188, v188 op_sel_hi:[0,0,0]
	v_mfma_scale_f32_16x16x128_f8f6f4 v[140:143], v[0:7], v[204:211], v[140:143], v188, v188 op_sel_hi:[0,0,0]
	v_mfma_scale_f32_16x16x128_f8f6f4 v[136:139], v[8:15], v[204:211], v[136:139], v188, v188 op_sel_hi:[0,0,0]
	v_mfma_scale_f32_16x16x128_f8f6f4 v[132:135], v[0:7], v[216:223], v[132:135], v188, v188 op_sel_hi:[0,0,0]
	v_mfma_scale_f32_16x16x128_f8f6f4 v[128:131], v[8:15], v[216:223], v[128:131], v188, v188 op_sel_hi:[0,0,0]
	s_setprio 0
	s_barrier
	s_mov_b32 m0, s56
	v_lshl_add_u64 v[176:177], v[180:181], 0, s[40:41]
	ds_read_b128 v[224:227], v190 offset:49152
	ds_read_b128 v[232:235], v190 offset:51200
	ds_read_b128 v[228:231], v192 offset:49152
	ds_read_b128 v[236:239], v192 offset:51200
	global_load_lds_dwordx4 v[176:177], off
	v_lshl_add_u64 v[176:177], v[182:183], 0, s[40:41]
	s_mov_b32 m0, s57
	s_nop 0
	global_load_lds_dwordx4 v[176:177], off
	s_barrier
	s_waitcnt lgkmcnt(0)
	s_setprio 1
	v_mfma_scale_f32_16x16x128_f8f6f4 v[100:103], v[224:231], v[16:23], v[100:103], v188, v188 op_sel_hi:[0,0,0]
	v_mfma_scale_f32_16x16x128_f8f6f4 v[96:99], v[232:239], v[16:23], v[96:99], v188, v188 op_sel_hi:[0,0,0]
	v_mfma_scale_f32_16x16x128_f8f6f4 v[84:87], v[224:231], v[24:31], v[84:87], v188, v188 op_sel_hi:[0,0,0]
	v_mfma_scale_f32_16x16x128_f8f6f4 v[80:83], v[232:239], v[24:31], v[80:83], v188, v188 op_sel_hi:[0,0,0]
	v_mfma_scale_f32_16x16x128_f8f6f4 v[76:79], v[224:231], v[204:211], v[76:79], v188, v188 op_sel_hi:[0,0,0]
	v_mfma_scale_f32_16x16x128_f8f6f4 v[72:75], v[232:239], v[204:211], v[72:75], v188, v188 op_sel_hi:[0,0,0]
	v_mfma_scale_f32_16x16x128_f8f6f4 v[68:71], v[224:231], v[216:223], v[68:71], v188, v188 op_sel_hi:[0,0,0]
	v_mfma_scale_f32_16x16x128_f8f6f4 v[64:67], v[232:239], v[216:223], v[64:67], v188, v188 op_sel_hi:[0,0,0]
	s_setprio 0
	s_mov_b32 m0, s64
	v_lshl_add_u64 v[186:187], v[186:187], 0, s[40:41]
	s_barrier
	ds_read_b128 v[16:19], v189 offset:49152
	ds_read_b128 v[24:27], v189 offset:51200
	ds_read_b128 v[20:23], v191 offset:49152
	ds_read_b128 v[28:31], v191 offset:51200
	ds_read_b128 v[176:179], v189 offset:53248
	ds_read_b128 v[204:207], v189 offset:55296
	ds_read_b128 v[180:183], v191 offset:53248
	ds_read_b128 v[208:211], v191 offset:55296
	global_load_lds_dwordx4 v[186:187], off
	v_lshl_add_u64 v[184:185], v[184:185], 0, s[40:41]
	s_mov_b32 m0, s65
	s_nop 0
	global_load_lds_dwordx4 v[184:185], off
	s_barrier
	s_waitcnt lgkmcnt(0)
	s_setprio 1
	v_mfma_scale_f32_16x16x128_f8f6f4 v[124:127], v[0:7], v[16:23], v[124:127], v188, v188 op_sel_hi:[0,0,0]
	v_mfma_scale_f32_16x16x128_f8f6f4 v[120:123], v[8:15], v[16:23], v[120:123], v188, v188 op_sel_hi:[0,0,0]
	v_mfma_scale_f32_16x16x128_f8f6f4 v[116:119], v[0:7], v[24:31], v[116:119], v188, v188 op_sel_hi:[0,0,0]
	v_mfma_scale_f32_16x16x128_f8f6f4 v[112:115], v[8:15], v[24:31], v[112:115], v188, v188 op_sel_hi:[0,0,0]
	v_mfma_scale_f32_16x16x128_f8f6f4 v[108:111], v[0:7], v[176:183], v[108:111], v188, v188 op_sel_hi:[0,0,0]
	v_mfma_scale_f32_16x16x128_f8f6f4 v[104:107], v[8:15], v[176:183], v[104:107], v188, v188 op_sel_hi:[0,0,0]
	v_mfma_scale_f32_16x16x128_f8f6f4 v[92:95], v[0:7], v[204:211], v[92:95], v188, v188 op_sel_hi:[0,0,0]
	v_mfma_scale_f32_16x16x128_f8f6f4 v[88:91], v[8:15], v[204:211], v[88:91], v188, v188 op_sel_hi:[0,0,0]
	s_setprio 0
	s_barrier
	s_add_u32 s24, s24, 0x20080
	s_addc_u32 s25, s25, 0
	s_mov_b32 m0, s70
	v_lshl_add_u64 v[0:1], s[24:25], 0, v[162:163]
	global_load_lds_dwordx4 v[0:1], off
	v_lshl_add_u64 v[0:1], s[24:25], 0, v[164:165]
	s_mov_b32 m0, s71
	s_nop 0
	global_load_lds_dwordx4 v[0:1], off
	s_waitcnt vmcnt(6)
	s_barrier
	s_setprio 1
	v_mfma_scale_f32_16x16x128_f8f6f4 v[60:63], v[224:231], v[16:23], v[60:63], v188, v188 op_sel_hi:[0,0,0]
	v_mfma_scale_f32_16x16x128_f8f6f4 v[56:59], v[232:239], v[16:23], v[56:59], v188, v188 op_sel_hi:[0,0,0]
	v_mfma_scale_f32_16x16x128_f8f6f4 v[52:55], v[224:231], v[24:31], v[52:55], v188, v188 op_sel_hi:[0,0,0]
	v_mfma_scale_f32_16x16x128_f8f6f4 v[48:51], v[232:239], v[24:31], v[48:51], v188, v188 op_sel_hi:[0,0,0]
	v_mfma_scale_f32_16x16x128_f8f6f4 v[44:47], v[224:231], v[176:183], v[44:47], v188, v188 op_sel_hi:[0,0,0]
	v_mfma_scale_f32_16x16x128_f8f6f4 v[40:43], v[232:239], v[176:183], v[40:43], v188, v188 op_sel_hi:[0,0,0]
	v_mfma_scale_f32_16x16x128_f8f6f4 v[36:39], v[224:231], v[204:211], v[36:39], v188, v188 op_sel_hi:[0,0,0]
	v_mfma_scale_f32_16x16x128_f8f6f4 v[32:35], v[232:239], v[204:211], v[32:35], v188, v188 op_sel_hi:[0,0,0]
	s_setprio 0
	s_add_i32 s85, s85, 2
	s_add_u32 s22, s22, 0x100
	s_addc_u32 s23, s23, 0
	s_add_u32 s7, s7, 0x100
	s_addc_u32 s83, s83, 0
	s_cmp_gt_u32 s85, 5
	s_barrier
	s_branch .LBB0_1667
.LBB0_1666:
	ds_read_b128 v[0:3], v190
	ds_read_b128 v[8:11], v190 offset:2048
	ds_read_b128 v[4:7], v192
	ds_read_b128 v[12:15], v192 offset:2048
	s_add_u32 s26, s22, 0x80
	s_addc_u32 s27, s23, 0
	s_and_b64 s[24:25], s[24:25], exec
	s_cselect_b32 s27, s19, s27
	s_cselect_b32 s26, s18, s26
	s_cselect_b32 s25, s17, s83
	s_cselect_b32 s24, s16, s7
	v_lshl_add_u64 v[16:17], s[22:23], 0, v[166:167]
	s_add_i32 m0, s13, 0xc000
	ds_read_b128 v[204:207], v189
	ds_read_b128 v[216:219], v189 offset:2048
	ds_read_b128 v[208:211], v191
	ds_read_b128 v[220:223], v191 offset:2048
	ds_read_b128 v[224:227], v189 offset:4096
	ds_read_b128 v[232:235], v189 offset:6144
	ds_read_b128 v[228:231], v191 offset:4096
	ds_read_b128 v[236:239], v191 offset:6144
	global_load_lds_dwordx4 v[16:17], off
	v_lshl_add_u64 v[16:17], s[22:23], 0, v[170:171]
	s_add_i32 m0, s13, 0xe000
	s_nop 0
	global_load_lds_dwordx4 v[16:17], off
	s_waitcnt lgkmcnt(8)
	s_barrier
	s_waitcnt lgkmcnt(0)
	s_setprio 1
	v_mfma_scale_f32_16x16x128_f8f6f4 v[156:159], v[0:7], v[204:211], v[156:159], v188, v188 op_sel_hi:[0,0,0]
	v_mfma_scale_f32_16x16x128_f8f6f4 v[152:155], v[8:15], v[204:211], v[152:155], v188, v188 op_sel_hi:[0,0,0]
	v_mfma_scale_f32_16x16x128_f8f6f4 v[148:151], v[0:7], v[216:223], v[148:151], v188, v188 op_sel_hi:[0,0,0]
	v_mfma_scale_f32_16x16x128_f8f6f4 v[144:147], v[8:15], v[216:223], v[144:147], v188, v188 op_sel_hi:[0,0,0]
	v_mfma_scale_f32_16x16x128_f8f6f4 v[140:143], v[0:7], v[224:231], v[140:143], v188, v188 op_sel_hi:[0,0,0]
	v_mfma_scale_f32_16x16x128_f8f6f4 v[136:139], v[8:15], v[224:231], v[136:139], v188, v188 op_sel_hi:[0,0,0]
	v_mfma_scale_f32_16x16x128_f8f6f4 v[132:135], v[0:7], v[232:239], v[132:135], v188, v188 op_sel_hi:[0,0,0]
	v_mfma_scale_f32_16x16x128_f8f6f4 v[128:131], v[8:15], v[232:239], v[128:131], v188, v188 op_sel_hi:[0,0,0]
	s_setprio 0
	s_barrier
	s_mov_b32 m0, s15
	v_lshl_add_u64 v[180:181], s[24:25], 0, v[162:163]
	ds_read_b128 v[16:19], v190 offset:16384
	ds_read_b128 v[24:27], v190 offset:18432
	ds_read_b128 v[20:23], v192 offset:16384
	ds_read_b128 v[28:31], v192 offset:18432
	global_load_lds_dwordx4 v[180:181], off
	v_lshl_add_u64 v[182:183], s[24:25], 0, v[164:165]
	s_mov_b32 m0, s31
	s_nop 0
	global_load_lds_dwordx4 v[182:183], off
	s_barrier
	s_waitcnt lgkmcnt(0)
	s_setprio 1
	v_mfma_scale_f32_16x16x128_f8f6f4 v[100:103], v[16:23], v[204:211], v[100:103], v188, v188 op_sel_hi:[0,0,0]
	v_mfma_scale_f32_16x16x128_f8f6f4 v[96:99], v[24:31], v[204:211], v[96:99], v188, v188 op_sel_hi:[0,0,0]
	v_mfma_scale_f32_16x16x128_f8f6f4 v[84:87], v[16:23], v[216:223], v[84:87], v188, v188 op_sel_hi:[0,0,0]
	v_mfma_scale_f32_16x16x128_f8f6f4 v[80:83], v[24:31], v[216:223], v[80:83], v188, v188 op_sel_hi:[0,0,0]
	v_mfma_scale_f32_16x16x128_f8f6f4 v[76:79], v[16:23], v[224:231], v[76:79], v188, v188 op_sel_hi:[0,0,0]
	v_mfma_scale_f32_16x16x128_f8f6f4 v[72:75], v[24:31], v[224:231], v[72:75], v188, v188 op_sel_hi:[0,0,0]
	v_mfma_scale_f32_16x16x128_f8f6f4 v[68:71], v[16:23], v[232:239], v[68:71], v188, v188 op_sel_hi:[0,0,0]
	v_mfma_scale_f32_16x16x128_f8f6f4 v[64:67], v[24:31], v[232:239], v[64:67], v188, v188 op_sel_hi:[0,0,0]
	s_setprio 0
	s_mov_b32 m0, s13
	s_barrier
	ds_read_b128 v[204:207], v189 offset:16384
	ds_read_b128 v[216:219], v189 offset:18432
	ds_read_b128 v[208:211], v191 offset:16384
	ds_read_b128 v[220:223], v191 offset:18432
	ds_read_b128 v[224:227], v189 offset:20480
	ds_read_b128 v[232:235], v189 offset:22528
	ds_read_b128 v[228:231], v191 offset:20480
	ds_read_b128 v[236:239], v191 offset:22528
	global_load_lds_dwordx4 v172, s[26:27]
	s_mov_b32 m0, s44
	v_mov_b32_e32 v185, v173
	global_load_lds_dwordx4 v184, s[26:27]
	s_barrier
	s_waitcnt lgkmcnt(0)
	v_lshl_add_u64 v[186:187], s[26:27], 0, v[172:173]
	v_lshl_add_u64 v[184:185], s[26:27], 0, v[184:185]
	s_setprio 1
	v_mfma_scale_f32_16x16x128_f8f6f4 v[124:127], v[0:7], v[204:211], v[124:127], v188, v188 op_sel_hi:[0,0,0]
	v_mfma_scale_f32_16x16x128_f8f6f4 v[120:123], v[8:15], v[204:211], v[120:123], v188, v188 op_sel_hi:[0,0,0]
	v_mfma_scale_f32_16x16x128_f8f6f4 v[116:119], v[0:7], v[216:223], v[116:119], v188, v188 op_sel_hi:[0,0,0]
	v_mfma_scale_f32_16x16x128_f8f6f4 v[112:115], v[8:15], v[216:223], v[112:115], v188, v188 op_sel_hi:[0,0,0]
	v_mfma_scale_f32_16x16x128_f8f6f4 v[108:111], v[0:7], v[224:231], v[108:111], v188, v188 op_sel_hi:[0,0,0]
	v_mfma_scale_f32_16x16x128_f8f6f4 v[104:107], v[8:15], v[224:231], v[104:107], v188, v188 op_sel_hi:[0,0,0]
	v_mfma_scale_f32_16x16x128_f8f6f4 v[92:95], v[0:7], v[232:239], v[92:95], v188, v188 op_sel_hi:[0,0,0]
	v_mfma_scale_f32_16x16x128_f8f6f4 v[88:91], v[8:15], v[232:239], v[88:91], v188, v188 op_sel_hi:[0,0,0]
	s_setprio 0
	s_barrier
	s_add_u32 s90, s24, 0x20000
	s_addc_u32 s91, s25, 0
	s_mov_b32 m0, s46
	v_lshl_add_u64 v[0:1], s[90:91], 0, v[162:163]
	global_load_lds_dwordx4 v[0:1], off
	v_lshl_add_u64 v[0:1], s[90:91], 0, v[164:165]
	s_mov_b32 m0, s47
	s_nop 0
	global_load_lds_dwordx4 v[0:1], off
	s_waitcnt vmcnt(6)
	s_barrier
	s_setprio 1
	v_mfma_scale_f32_16x16x128_f8f6f4 v[60:63], v[16:23], v[204:211], v[60:63], v188, v188 op_sel_hi:[0,0,0]
	v_mfma_scale_f32_16x16x128_f8f6f4 v[56:59], v[24:31], v[204:211], v[56:59], v188, v188 op_sel_hi:[0,0,0]
	v_mfma_scale_f32_16x16x128_f8f6f4 v[52:55], v[16:23], v[216:223], v[52:55], v188, v188 op_sel_hi:[0,0,0]
	v_mfma_scale_f32_16x16x128_f8f6f4 v[48:51], v[24:31], v[216:223], v[48:51], v188, v188 op_sel_hi:[0,0,0]
	v_mfma_scale_f32_16x16x128_f8f6f4 v[44:47], v[16:23], v[224:231], v[44:47], v188, v188 op_sel_hi:[0,0,0]
	v_mfma_scale_f32_16x16x128_f8f6f4 v[40:43], v[24:31], v[224:231], v[40:43], v188, v188 op_sel_hi:[0,0,0]
	v_mfma_scale_f32_16x16x128_f8f6f4 v[36:39], v[16:23], v[232:239], v[36:39], v188, v188 op_sel_hi:[0,0,0]
	v_mfma_scale_f32_16x16x128_f8f6f4 v[32:35], v[24:31], v[232:239], v[32:35], v188, v188 op_sel_hi:[0,0,0]
	s_setprio 0
	s_barrier
	ds_read_b128 v[0:3], v190 offset:32768
	ds_read_b128 v[8:11], v190 offset:34816
	ds_read_b128 v[4:7], v192 offset:32768
	ds_read_b128 v[12:15], v192 offset:34816
	s_mov_b32 m0, s50
	v_lshl_add_u64 v[178:179], s[26:27], 0, v[178:179]
	ds_read_b128 v[16:19], v189 offset:32768
	ds_read_b128 v[24:27], v189 offset:34816
	ds_read_b128 v[20:23], v191 offset:32768
	ds_read_b128 v[28:31], v191 offset:34816
	ds_read_b128 v[204:207], v189 offset:36864
	ds_read_b128 v[216:219], v189 offset:38912
	ds_read_b128 v[208:211], v191 offset:36864
	ds_read_b128 v[220:223], v191 offset:38912
	global_load_lds_dwordx4 v[178:179], off
	v_lshl_add_u64 v[176:177], s[26:27], 0, v[176:177]
	s_mov_b32 m0, s51
	s_nop 0
	global_load_lds_dwordx4 v[176:177], off
	s_waitcnt lgkmcnt(8)
	s_barrier
	s_waitcnt lgkmcnt(0)
	s_setprio 1
	v_mfma_scale_f32_16x16x128_f8f6f4 v[156:159], v[0:7], v[16:23], v[156:159], v188, v188 op_sel_hi:[0,0,0]
	v_mfma_scale_f32_16x16x128_f8f6f4 v[152:155], v[8:15], v[16:23], v[152:155], v188, v188 op_sel_hi:[0,0,0]
	v_mfma_scale_f32_16x16x128_f8f6f4 v[148:151], v[0:7], v[24:31], v[148:151], v188, v188 op_sel_hi:[0,0,0]
	v_mfma_scale_f32_16x16x128_f8f6f4 v[144:147], v[8:15], v[24:31], v[144:147], v188, v188 op_sel_hi:[0,0,0]
	v_mfma_scale_f32_16x16x128_f8f6f4 v[140:143], v[0:7], v[204:211], v[140:143], v188, v188 op_sel_hi:[0,0,0]
	v_mfma_scale_f32_16x16x128_f8f6f4 v[136:139], v[8:15], v[204:211], v[136:139], v188, v188 op_sel_hi:[0,0,0]
	v_mfma_scale_f32_16x16x128_f8f6f4 v[132:135], v[0:7], v[216:223], v[132:135], v188, v188 op_sel_hi:[0,0,0]
	v_mfma_scale_f32_16x16x128_f8f6f4 v[128:131], v[8:15], v[216:223], v[128:131], v188, v188 op_sel_hi:[0,0,0]
	s_setprio 0
	s_barrier
	s_mov_b32 m0, s56
	v_lshl_add_u64 v[176:177], v[180:181], 0, s[40:41]
	ds_read_b128 v[224:227], v190 offset:49152
	ds_read_b128 v[232:235], v190 offset:51200
	ds_read_b128 v[228:231], v192 offset:49152
	ds_read_b128 v[236:239], v192 offset:51200
	global_load_lds_dwordx4 v[176:177], off
	v_lshl_add_u64 v[176:177], v[182:183], 0, s[40:41]
	s_mov_b32 m0, s57
	s_nop 0
	global_load_lds_dwordx4 v[176:177], off
	s_barrier
	s_waitcnt lgkmcnt(0)
	s_setprio 1
	v_mfma_scale_f32_16x16x128_f8f6f4 v[100:103], v[224:231], v[16:23], v[100:103], v188, v188 op_sel_hi:[0,0,0]
	v_mfma_scale_f32_16x16x128_f8f6f4 v[96:99], v[232:239], v[16:23], v[96:99], v188, v188 op_sel_hi:[0,0,0]
	v_mfma_scale_f32_16x16x128_f8f6f4 v[84:87], v[224:231], v[24:31], v[84:87], v188, v188 op_sel_hi:[0,0,0]
	v_mfma_scale_f32_16x16x128_f8f6f4 v[80:83], v[232:239], v[24:31], v[80:83], v188, v188 op_sel_hi:[0,0,0]
	v_mfma_scale_f32_16x16x128_f8f6f4 v[76:79], v[224:231], v[204:211], v[76:79], v188, v188 op_sel_hi:[0,0,0]
	v_mfma_scale_f32_16x16x128_f8f6f4 v[72:75], v[232:239], v[204:211], v[72:75], v188, v188 op_sel_hi:[0,0,0]
	v_mfma_scale_f32_16x16x128_f8f6f4 v[68:71], v[224:231], v[216:223], v[68:71], v188, v188 op_sel_hi:[0,0,0]
	v_mfma_scale_f32_16x16x128_f8f6f4 v[64:67], v[232:239], v[216:223], v[64:67], v188, v188 op_sel_hi:[0,0,0]
	s_setprio 0
	s_mov_b32 m0, s64
	v_lshl_add_u64 v[186:187], v[186:187], 0, s[40:41]
	s_barrier
	ds_read_b128 v[16:19], v189 offset:49152
	ds_read_b128 v[24:27], v189 offset:51200
	ds_read_b128 v[20:23], v191 offset:49152
	ds_read_b128 v[28:31], v191 offset:51200
	ds_read_b128 v[176:179], v189 offset:53248
	ds_read_b128 v[204:207], v189 offset:55296
	ds_read_b128 v[180:183], v191 offset:53248
	ds_read_b128 v[208:211], v191 offset:55296
	global_load_lds_dwordx4 v[186:187], off
	v_lshl_add_u64 v[184:185], v[184:185], 0, s[40:41]
	s_mov_b32 m0, s65
	s_nop 0
	global_load_lds_dwordx4 v[184:185], off
	s_barrier
	s_waitcnt lgkmcnt(0)
	s_setprio 1
	v_mfma_scale_f32_16x16x128_f8f6f4 v[124:127], v[0:7], v[16:23], v[124:127], v188, v188 op_sel_hi:[0,0,0]
	v_mfma_scale_f32_16x16x128_f8f6f4 v[120:123], v[8:15], v[16:23], v[120:123], v188, v188 op_sel_hi:[0,0,0]
	v_mfma_scale_f32_16x16x128_f8f6f4 v[116:119], v[0:7], v[24:31], v[116:119], v188, v188 op_sel_hi:[0,0,0]
	v_mfma_scale_f32_16x16x128_f8f6f4 v[112:115], v[8:15], v[24:31], v[112:115], v188, v188 op_sel_hi:[0,0,0]
	v_mfma_scale_f32_16x16x128_f8f6f4 v[108:111], v[0:7], v[176:183], v[108:111], v188, v188 op_sel_hi:[0,0,0]
	v_mfma_scale_f32_16x16x128_f8f6f4 v[104:107], v[8:15], v[176:183], v[104:107], v188, v188 op_sel_hi:[0,0,0]
	v_mfma_scale_f32_16x16x128_f8f6f4 v[92:95], v[0:7], v[204:211], v[92:95], v188, v188 op_sel_hi:[0,0,0]
	v_mfma_scale_f32_16x16x128_f8f6f4 v[88:91], v[8:15], v[204:211], v[88:91], v188, v188 op_sel_hi:[0,0,0]
	s_setprio 0
	s_barrier
	s_add_u32 s24, s24, 0x20080
	s_addc_u32 s25, s25, 0
	s_mov_b32 m0, s70
	v_lshl_add_u64 v[0:1], s[24:25], 0, v[162:163]
	global_load_lds_dwordx4 v[0:1], off
	v_lshl_add_u64 v[0:1], s[24:25], 0, v[164:165]
	s_mov_b32 m0, s71
	s_nop 0
	global_load_lds_dwordx4 v[0:1], off
	s_waitcnt vmcnt(6)
	s_barrier
	s_setprio 1
	v_mfma_scale_f32_16x16x128_f8f6f4 v[60:63], v[224:231], v[16:23], v[60:63], v188, v188 op_sel_hi:[0,0,0]
	v_mfma_scale_f32_16x16x128_f8f6f4 v[56:59], v[232:239], v[16:23], v[56:59], v188, v188 op_sel_hi:[0,0,0]
	v_mfma_scale_f32_16x16x128_f8f6f4 v[52:55], v[224:231], v[24:31], v[52:55], v188, v188 op_sel_hi:[0,0,0]
	v_mfma_scale_f32_16x16x128_f8f6f4 v[48:51], v[232:239], v[24:31], v[48:51], v188, v188 op_sel_hi:[0,0,0]
	v_mfma_scale_f32_16x16x128_f8f6f4 v[44:47], v[224:231], v[176:183], v[44:47], v188, v188 op_sel_hi:[0,0,0]
	v_mfma_scale_f32_16x16x128_f8f6f4 v[40:43], v[232:239], v[176:183], v[40:43], v188, v188 op_sel_hi:[0,0,0]
	v_mfma_scale_f32_16x16x128_f8f6f4 v[36:39], v[224:231], v[204:211], v[36:39], v188, v188 op_sel_hi:[0,0,0]
	v_mfma_scale_f32_16x16x128_f8f6f4 v[32:35], v[232:239], v[204:211], v[32:35], v188, v188 op_sel_hi:[0,0,0]
	s_setprio 0
	s_add_i32 s85, s85, 2
	s_add_u32 s22, s22, 0x100
	s_addc_u32 s23, s23, 0
	s_add_u32 s7, s7, 0x100
	s_addc_u32 s83, s83, 0
	s_cmp_gt_u32 s85, 5
	s_barrier
	s_cbranch_scc1 .LBB0_1655
